# v99: remaining first-level DMA address adds eliminated (saddr form with SGPR base copy / reordered base update): 2 VALU per K iteration left
# baseline (speedup 1.0000x reference)
; #define PG8_STAGE_A(b, h, ptr, NX) do { if constexpr (Sched::GATHER) { unsigned gs_[2]; gs_[0] = ((NX) && last_) ? gN[h][0] : gA[h][0]; gs_[1] = ((NX) && last_) ? gN[h][1] : gA[h][1]; PG8_STAGE(PG8_SA(b, h), ptr, gs_); } \
;         else PG8_STAGE(PG8_SA(b, h), (ptr) + ((h) ? hstep : (size_t)0), voffA); } while (0)
; #define PG8_STAGE(bufoff, gbase, voff) do { _Pragma("unroll") for (int _i = 0; _i < 2; ++_i) \
;         __builtin_amdgcn_global_load_lds((const unsigned*)((const char*)(gbase) + (voff)[_i]), (PG8_LAS unsigned*)(lds + (bufoff) + ldsw + _i * 8192), 16, 0, 0); } while (0)
; #define PG8_LDA(dst, b, h) do { _Pragma("unroll") for (int m = 0; m < 4; ++m) _Pragma("unroll") for (int k = 0; k < 2; ++k) dst[m][k] = *(const PG8_LAS bf16x8*)(lds + PG8_SA(b, h) + aoff + m * 2048 + k * 1024); } while (0)
; #define PG8_LDB(dst, b, h) do { _Pragma("unroll") for (int n = 0; n < 2; ++n) _Pragma("unroll") for (int k = 0; k < 2; ++k) dst[n][k] = *(const PG8_LAS bf16x8*)(lds + PG8_SB(b, h) + boff + n * 2048 + k * 1024); } while (0)
; #define PG8_WAIT_V(n) asm volatile("s_waitcnt vmcnt(" #n ")" ::: "memory")
; template <class Epi, class Sched, bool ALIGN_EPI = false, bool SP2 = false>
; __device__ __forceinline__ void gemm_phase(PG8_LAS unsigned char* lds, const Gemm g, const Sched& S, const Epi& E, const bool skip_epi = false) {
;     ...
;         const char* nA = has_next ? (const char*)g.A + (size_t)nxt.pm * pmstepA + nxt.ko : cA; const char* nB = has_next ? (const char*)g.Bt + (size_t)nxt.pn * tstep + nxt.ko : cB;
;         for (int t = 0; t < nt; t += 2) {
;             const bool last = (t == nt - 2); last_ = last && has_next;
;             const char* a1 = cA + (size_t)(t + 1) * kstep;
;             const char* a2 = last ? nA : cA + (size_t)(t + 2) * kstep; const char* b2 = last ? nB : cB + (size_t)(t + 2) * kstep;
;             const char* a3 = a2 + kstep; const char* b3 = b2 + kstep;
;             if (last && has_next) S.a_ready(nxt);
;             if constexpr (SP2) {
;             PG8_LDB(B0, 0, 0); PG8_LDB(B1, 0, 1); PG8_SCHED; PG8_LDA(At, 0, 0); PG8_STAGE_A(1, 1, a1, false);
;             PG8_WAIT_V(8); PG8_WAIT_L(0); PG8_BAR; PG8_MMA(0, 0, At, B0); PG8_MMA(0, 1, At, B1); PG8_BAR; PG8_SCHED;
;             PG8_LDA(At, 0, 1); PG8_STAGE(PG8_SB(0, 0), b2, voffB); PG8_STAGE(PG8_SB(0, 1), b2 + hstep, voffB); PG8_STAGE_A(0, 0, a2, true);
.LBB0_252:
	s_ashr_i32 s17, s16, 31
	s_lshl_b64 s[18:19], s[16:17], 19
	s_add_u32 s18, s86, s18
	s_addc_u32 s19, s87, s19
	s_and_b64 s[20:21], s[4:5], exec
	s_cselect_b32 s17, s19, s25
	s_cselect_b32 s56, s18, s24
	s_ashr_i32 s15, s14, 31
	s_lshl_b64 s[20:21], s[14:15], 19
	v_readlane_b32 s28, v254, 36
	v_readlane_b32 s29, v254, 37
	s_add_u32 s20, s28, s20
	s_addc_u32 s21, s29, s21
	s_and_b64 s[28:29], s[4:5], exec
	s_cselect_b32 s15, s21, s27
	s_cselect_b32 s57, s20, s26
	s_add_u32 s24, s24, 0x40080
	s_addc_u32 s25, s25, 0
	s_add_u32 s58, s26, 0x100
	s_addc_u32 s59, s27, 0
	s_mov_b32 s60, -2
	s_waitcnt vmcnt(0)
	ds_read_b128 v[148:151], v170
	ds_read_b128 v[152:155], v170 offset:1024
	ds_read_b128 v[156:159], v170 offset:2048
	ds_read_b128 v[160:163], v170 offset:3072
	ds_read_b128 v[176:179], v171
	ds_read_b128 v[180:183], v171 offset:1024
	ds_read_b128 v[184:187], v171 offset:2048
	ds_read_b128 v[188:191], v171 offset:3072
	s_add_u32 s26, s24, 0xfffc0080
	s_addc_u32 s27, s25, -1
	s_cmp_eq_u32 s60, 12
	s_cselect_b32 s29, s17, s27
	s_cselect_b32 s28, s56, s26
	s_cselect_b32 s27, s15, s59
	s_cselect_b32 s26, s57, s58
	s_add_i32 m0, s23, 0xc000
	ds_read_b128 v[192:195], v172
	ds_read_b128 v[196:199], v172 offset:1024
	ds_read_b128 v[200:203], v172 offset:2048
	ds_read_b128 v[204:207], v172 offset:3072
	ds_read_b128 v[208:211], v172 offset:4096
	ds_read_b128 v[212:215], v172 offset:5120
	ds_read_b128 v[216:219], v172 offset:6144
	ds_read_b128 v[220:223], v172 offset:7168
	global_load_lds_dwordx4 v140, s[24:25]
	s_add_i32 m0, s23, 0xe000
	s_nop 0
	global_load_lds_dwordx4 v142, s[24:25]
	s_waitcnt vmcnt(8)
	s_waitcnt lgkmcnt(0)
	s_barrier
	s_setprio 3
	s_waitcnt lgkmcnt(0)
	v_mfma_f32_16x16x32_bf16 v[126:129], v[148:151], v[192:195], 0
	v_mfma_f32_16x16x32_bf16 v[122:125], v[156:159], v[192:195], 0
	v_mfma_f32_16x16x32_bf16 v[114:117], v[148:151], v[200:203], 0
	v_mfma_f32_16x16x32_bf16 v[106:109], v[156:159], v[200:203], 0
	v_mfma_f32_16x16x32_bf16 v[98:101], v[148:151], v[208:211], 0
	v_mfma_f32_16x16x32_bf16 v[90:93], v[156:159], v[208:211], 0
	v_mfma_f32_16x16x32_bf16 v[82:85], v[148:151], v[216:219], 0
	v_mfma_f32_16x16x32_bf16 v[74:77], v[156:159], v[216:219], 0
	v_mfma_f32_16x16x32_bf16 v[126:129], v[152:155], v[196:199], v[126:129]
	v_mfma_f32_16x16x32_bf16 v[122:125], v[160:163], v[196:199], v[122:125]
	v_mfma_f32_16x16x32_bf16 v[114:117], v[152:155], v[204:207], v[114:117]
	v_mfma_f32_16x16x32_bf16 v[106:109], v[160:163], v[204:207], v[106:109]
	v_mfma_f32_16x16x32_bf16 v[98:101], v[152:155], v[212:215], v[98:101]
	v_mfma_f32_16x16x32_bf16 v[90:93], v[160:163], v[212:215], v[90:93]
	v_mfma_f32_16x16x32_bf16 v[82:85], v[152:155], v[220:223], v[82:85]
	v_mfma_f32_16x16x32_bf16 v[74:77], v[160:163], v[220:223], v[74:77]
	s_setprio 0
	s_setprio 3
	v_mfma_f32_16x16x32_bf16 v[118:121], v[176:179], v[192:195], 0
	v_mfma_f32_16x16x32_bf16 v[110:113], v[184:187], v[192:195], 0
	v_mfma_f32_16x16x32_bf16 v[102:105], v[176:179], v[200:203], 0
	v_mfma_f32_16x16x32_bf16 v[94:97], v[184:187], v[200:203], 0
	v_mfma_f32_16x16x32_bf16 v[86:89], v[176:179], v[208:211], 0
	v_mfma_f32_16x16x32_bf16 v[78:81], v[184:187], v[208:211], 0
	v_mfma_f32_16x16x32_bf16 v[70:73], v[176:179], v[216:219], 0
	v_mfma_f32_16x16x32_bf16 v[66:69], v[184:187], v[216:219], 0
	v_mfma_f32_16x16x32_bf16 v[118:121], v[180:183], v[196:199], v[118:121]
	v_mfma_f32_16x16x32_bf16 v[110:113], v[188:191], v[196:199], v[110:113]
	v_mfma_f32_16x16x32_bf16 v[102:105], v[180:183], v[204:207], v[102:105]
	v_mfma_f32_16x16x32_bf16 v[94:97], v[188:191], v[204:207], v[94:97]
	v_mfma_f32_16x16x32_bf16 v[86:89], v[180:183], v[212:215], v[86:89]
	v_mfma_f32_16x16x32_bf16 v[78:81], v[188:191], v[212:215], v[78:81]
	v_mfma_f32_16x16x32_bf16 v[70:73], v[180:183], v[220:223], v[70:73]
	v_mfma_f32_16x16x32_bf16 v[66:69], v[188:191], v[220:223], v[66:69]
	s_setprio 0
	s_barrier
	s_add_i32 s61, s46, s2
	s_mov_b32 m0, s61
	ds_read_b128 v[192:195], v172 offset:16384
	ds_read_b128 v[196:199], v172 offset:17408
	ds_read_b128 v[200:203], v172 offset:18432
	ds_read_b128 v[204:207], v172 offset:19456
	ds_read_b128 v[208:211], v172 offset:20480
	ds_read_b128 v[212:215], v172 offset:21504
	ds_read_b128 v[216:219], v172 offset:22528
	ds_read_b128 v[220:223], v172 offset:23552
	global_load_lds_dwordx4 v134, s[26:27]
	s_add_i32 m0, s61, 0x2000
	s_add_u32 s62, s26, 0x40000
	s_addc_u32 s63, s27, 0
	s_add_i32 s61, s47, s2
	global_load_lds_dwordx4 v130, s[26:27]
	s_mov_b32 m0, s61
	s_mov_b64 s[98:99], s[28:29]
	global_load_lds_dwordx4 v134, s[62:63]
	s_add_i32 m0, s61, 0x2000
	s_nop 0
	global_load_lds_dwordx4 v130, s[62:63]
	s_mov_b32 m0, s23
	s_nop 0
	global_load_lds_dwordx4 v136, s[28:29]
	s_mov_b32 m0, s31
	s_nop 0
	global_load_lds_dwordx4 v132, s[28:29]
	s_waitcnt vmcnt(8)
	s_waitcnt lgkmcnt(0)
	s_barrier
; #define PG8_STAGE_A(b, h, ptr, NX) do { if constexpr (Sched::GATHER) { unsigned gs_[2]; gs_[0] = ((NX) && last_) ? gN[h][0] : gA[h][0]; gs_[1] = ((NX) && last_) ? gN[h][1] : gA[h][1]; PG8_STAGE(PG8_SA(b, h), ptr, gs_); } \
;         else PG8_STAGE(PG8_SA(b, h), (ptr) + ((h) ? hstep : (size_t)0), voffA); } while (0)
; #define PG8_LDA(dst, b, h) do { _Pragma("unroll") for (int m = 0; m < 4; ++m) _Pragma("unroll") for (int k = 0; k < 2; ++k) dst[m][k] = *(const PG8_LAS bf16x8*)(lds + PG8_SA(b, h) + aoff + m * 2048 + k * 1024); } while (0)
; #define PG8_LDB(dst, b, h) do { _Pragma("unroll") for (int n = 0; n < 2; ++n) _Pragma("unroll") for (int k = 0; k < 2; ++k) dst[n][k] = *(const PG8_LAS bf16x8*)(lds + PG8_SB(b, h) + boff + n * 2048 + k * 1024); } while (0)
; #define PG8_MMA(ai, bj, At, Bt) do { __builtin_amdgcn_s_setprio(1); _Pragma("unroll") for (int m = 0; m < 4; ++m) _Pragma("unroll") for (int n = 0; n < 2; ++n) _Pragma("unroll") for (int k = 0; k < 2; ++k) \
;         acc[ai][bj][m][n] = __builtin_amdgcn_mfma_f32_16x16x32_bf16(Bt[n][k], At[m][k], acc[ai][bj][m][n], 0, 0, 0); __builtin_amdgcn_s_setprio(0); } while (0)
; #define PG8_WAIT_V(n) asm volatile("s_waitcnt vmcnt(" #n ")" ::: "memory")
; #define PG8_WAIT_L(n) asm volatile("s_waitcnt lgkmcnt(" #n ")" ::: "memory")
; #define PG8_BAR __builtin_amdgcn_s_barrier()
; #define PG8_SCHED __builtin_amdgcn_sched_barrier(0)
; template <class Epi, class Sched, bool ALIGN_EPI = false, bool SP2 = false>
; __device__ __forceinline__ void gemm_phase(PG8_LAS unsigned char* lds, const Gemm g, const Sched& S, const Epi& E, const bool skip_epi = false) {
;     ...
;             PG8_WAIT_V(8); PG8_WAIT_L(0); PG8_BAR; PG8_MMA(1, 0, At, B0); PG8_MMA(1, 1, At, B1); PG8_BAR; PG8_SCHED;
;             PG8_LDB(B0, 1, 0); PG8_LDB(B1, 1, 1); PG8_SCHED; PG8_LDA(At, 1, 0); PG8_STAGE_A(0, 1, a2, true);
;             PG8_WAIT_V(8); PG8_WAIT_L(0); PG8_BAR; PG8_MMA(0, 0, At, B0); PG8_MMA(0, 1, At, B1); PG8_BAR; PG8_SCHED;
	s_setprio 3
	s_waitcnt lgkmcnt(0)
	v_mfma_f32_16x16x32_bf16 v[62:65], v[148:151], v[192:195], 0
	v_mfma_f32_16x16x32_bf16 v[58:61], v[156:159], v[192:195], 0
	v_mfma_f32_16x16x32_bf16 v[50:53], v[148:151], v[200:203], 0
	v_mfma_f32_16x16x32_bf16 v[42:45], v[156:159], v[200:203], 0
	v_mfma_f32_16x16x32_bf16 v[34:37], v[148:151], v[208:211], 0
	v_mfma_f32_16x16x32_bf16 v[26:29], v[156:159], v[208:211], 0
	v_mfma_f32_16x16x32_bf16 v[18:21], v[148:151], v[216:219], 0
	v_mfma_f32_16x16x32_bf16 v[10:13], v[156:159], v[216:219], 0
	v_mfma_f32_16x16x32_bf16 v[62:65], v[152:155], v[196:199], v[62:65]
	v_mfma_f32_16x16x32_bf16 v[58:61], v[160:163], v[196:199], v[58:61]
	v_mfma_f32_16x16x32_bf16 v[50:53], v[152:155], v[204:207], v[50:53]
	v_mfma_f32_16x16x32_bf16 v[42:45], v[160:163], v[204:207], v[42:45]
	v_mfma_f32_16x16x32_bf16 v[34:37], v[152:155], v[212:215], v[34:37]
	v_mfma_f32_16x16x32_bf16 v[26:29], v[160:163], v[212:215], v[26:29]
	v_mfma_f32_16x16x32_bf16 v[18:21], v[152:155], v[220:223], v[18:21]
	v_mfma_f32_16x16x32_bf16 v[10:13], v[160:163], v[220:223], v[10:13]
	s_setprio 0
	s_setprio 3
	v_mfma_f32_16x16x32_bf16 v[54:57], v[176:179], v[192:195], 0
	v_mfma_f32_16x16x32_bf16 v[46:49], v[184:187], v[192:195], 0
	v_mfma_f32_16x16x32_bf16 v[38:41], v[176:179], v[200:203], 0
	v_mfma_f32_16x16x32_bf16 v[30:33], v[184:187], v[200:203], 0
	v_mfma_f32_16x16x32_bf16 v[22:25], v[176:179], v[208:211], 0
	v_mfma_f32_16x16x32_bf16 v[14:17], v[184:187], v[208:211], 0
	v_mfma_f32_16x16x32_bf16 v[6:9], v[176:179], v[216:219], 0
	v_mfma_f32_16x16x32_bf16 v[2:5], v[184:187], v[216:219], 0
	v_mfma_f32_16x16x32_bf16 v[54:57], v[180:183], v[196:199], v[54:57]
	v_mfma_f32_16x16x32_bf16 v[46:49], v[188:191], v[196:199], v[46:49]
	v_mfma_f32_16x16x32_bf16 v[38:41], v[180:183], v[204:207], v[38:41]
	v_mfma_f32_16x16x32_bf16 v[30:33], v[188:191], v[204:207], v[30:33]
	v_mfma_f32_16x16x32_bf16 v[22:25], v[180:183], v[212:215], v[22:25]
	v_mfma_f32_16x16x32_bf16 v[14:17], v[188:191], v[212:215], v[14:17]
	v_mfma_f32_16x16x32_bf16 v[6:9], v[180:183], v[220:223], v[6:9]
	v_mfma_f32_16x16x32_bf16 v[2:5], v[188:191], v[220:223], v[2:5]
	s_setprio 0
	s_barrier
	s_add_i32 s61, 0, 0x18000
	s_add_i32 s62, 0, 0x1c000
	v_add_u32_e32 v160, s61, v1
	v_add_u32_e32 v188, s62, v1
	ds_read_b128 v[148:151], v160
	ds_read_b128 v[152:155], v160 offset:1024
	ds_read_b128 v[156:159], v160 offset:2048
	ds_read_b128 v[160:163], v160 offset:3072
	ds_read_b128 v[176:179], v188
	ds_read_b128 v[180:183], v188 offset:1024
	ds_read_b128 v[184:187], v188 offset:2048
	ds_read_b128 v[188:191], v188 offset:3072
	s_add_u32 s28, s28, 0x40000
	s_addc_u32 s29, s29, 0
	s_mov_b32 m0, s34
	ds_read_b128 v[192:195], v172 offset:32768
	ds_read_b128 v[196:199], v172 offset:33792
	ds_read_b128 v[200:203], v172 offset:34816
	ds_read_b128 v[204:207], v172 offset:35840
	ds_read_b128 v[208:211], v172 offset:36864
	ds_read_b128 v[212:215], v172 offset:37888
	ds_read_b128 v[216:219], v172 offset:38912
	ds_read_b128 v[220:223], v172 offset:39936
	global_load_lds_dwordx4 v136, s[28:29]
	s_mov_b32 m0, s35
	s_nop 0
	global_load_lds_dwordx4 v132, s[28:29]
	s_waitcnt vmcnt(8)
	s_waitcnt lgkmcnt(0)
	s_barrier
	s_setprio 3
	s_waitcnt lgkmcnt(0)
	v_mfma_f32_16x16x32_bf16 v[126:129], v[148:151], v[192:195], v[126:129]
	v_mfma_f32_16x16x32_bf16 v[122:125], v[156:159], v[192:195], v[122:125]
	v_mfma_f32_16x16x32_bf16 v[114:117], v[148:151], v[200:203], v[114:117]
	v_mfma_f32_16x16x32_bf16 v[106:109], v[156:159], v[200:203], v[106:109]
	v_mfma_f32_16x16x32_bf16 v[98:101], v[148:151], v[208:211], v[98:101]
	v_mfma_f32_16x16x32_bf16 v[90:93], v[156:159], v[208:211], v[90:93]
	v_mfma_f32_16x16x32_bf16 v[82:85], v[148:151], v[216:219], v[82:85]
	v_mfma_f32_16x16x32_bf16 v[74:77], v[156:159], v[216:219], v[74:77]
	v_mfma_f32_16x16x32_bf16 v[126:129], v[152:155], v[196:199], v[126:129]
	v_mfma_f32_16x16x32_bf16 v[122:125], v[160:163], v[196:199], v[122:125]
	v_mfma_f32_16x16x32_bf16 v[114:117], v[152:155], v[204:207], v[114:117]
	v_mfma_f32_16x16x32_bf16 v[106:109], v[160:163], v[204:207], v[106:109]
	v_mfma_f32_16x16x32_bf16 v[98:101], v[152:155], v[212:215], v[98:101]
	v_mfma_f32_16x16x32_bf16 v[90:93], v[160:163], v[212:215], v[90:93]
	v_mfma_f32_16x16x32_bf16 v[82:85], v[152:155], v[220:223], v[82:85]
	v_mfma_f32_16x16x32_bf16 v[74:77], v[160:163], v[220:223], v[74:77]
	s_setprio 0
	s_setprio 3
	v_mfma_f32_16x16x32_bf16 v[118:121], v[176:179], v[192:195], v[118:121]
	v_mfma_f32_16x16x32_bf16 v[110:113], v[184:187], v[192:195], v[110:113]
	v_mfma_f32_16x16x32_bf16 v[102:105], v[176:179], v[200:203], v[102:105]
	v_mfma_f32_16x16x32_bf16 v[94:97], v[184:187], v[200:203], v[94:97]
	v_mfma_f32_16x16x32_bf16 v[86:89], v[176:179], v[208:211], v[86:89]
	v_mfma_f32_16x16x32_bf16 v[78:81], v[184:187], v[208:211], v[78:81]
	v_mfma_f32_16x16x32_bf16 v[70:73], v[176:179], v[216:219], v[70:73]
	v_mfma_f32_16x16x32_bf16 v[66:69], v[184:187], v[216:219], v[66:69]
	v_mfma_f32_16x16x32_bf16 v[118:121], v[180:183], v[196:199], v[118:121]
	v_mfma_f32_16x16x32_bf16 v[110:113], v[188:191], v[196:199], v[110:113]
	v_mfma_f32_16x16x32_bf16 v[102:105], v[180:183], v[204:207], v[102:105]
	v_mfma_f32_16x16x32_bf16 v[94:97], v[188:191], v[204:207], v[94:97]
	v_mfma_f32_16x16x32_bf16 v[86:89], v[180:183], v[212:215], v[86:89]
	v_mfma_f32_16x16x32_bf16 v[78:81], v[188:191], v[212:215], v[78:81]
	v_mfma_f32_16x16x32_bf16 v[70:73], v[180:183], v[220:223], v[70:73]
	v_mfma_f32_16x16x32_bf16 v[66:69], v[188:191], v[220:223], v[66:69]
	s_setprio 0
	s_barrier
; #define PG8_STAGE_A(b, h, ptr, NX) do { if constexpr (Sched::GATHER) { unsigned gs_[2]; gs_[0] = ((NX) && last_) ? gN[h][0] : gA[h][0]; gs_[1] = ((NX) && last_) ? gN[h][1] : gA[h][1]; PG8_STAGE(PG8_SA(b, h), ptr, gs_); } \
;         else PG8_STAGE(PG8_SA(b, h), (ptr) + ((h) ? hstep : (size_t)0), voffA); } while (0)
; #define PG8_STAGE(bufoff, gbase, voff) do { _Pragma("unroll") for (int _i = 0; _i < 2; ++_i) \
;         __builtin_amdgcn_global_load_lds((const unsigned*)((const char*)(gbase) + (voff)[_i]), (PG8_LAS unsigned*)(lds + (bufoff) + ldsw + _i * 8192), 16, 0, 0); } while (0)
; #define PG8_LDA(dst, b, h) do { _Pragma("unroll") for (int m = 0; m < 4; ++m) _Pragma("unroll") for (int k = 0; k < 2; ++k) dst[m][k] = *(const PG8_LAS bf16x8*)(lds + PG8_SA(b, h) + aoff + m * 2048 + k * 1024); } while (0)
; #define PG8_MMA(ai, bj, At, Bt) do { __builtin_amdgcn_s_setprio(1); _Pragma("unroll") for (int m = 0; m < 4; ++m) _Pragma("unroll") for (int n = 0; n < 2; ++n) _Pragma("unroll") for (int k = 0; k < 2; ++k) \
;         acc[ai][bj][m][n] = __builtin_amdgcn_mfma_f32_16x16x32_bf16(Bt[n][k], At[m][k], acc[ai][bj][m][n], 0, 0, 0); __builtin_amdgcn_s_setprio(0); } while (0)
; #define PG8_WAIT_V(n) asm volatile("s_waitcnt vmcnt(" #n ")" ::: "memory")
; #define PG8_WAIT_L(n) asm volatile("s_waitcnt lgkmcnt(" #n ")" ::: "memory")
; #define PG8_BAR __builtin_amdgcn_s_barrier()
; #define PG8_SCHED __builtin_amdgcn_sched_barrier(0)
; template <class Epi, class Sched, bool ALIGN_EPI = false, bool SP2 = false>
; __device__ __forceinline__ void gemm_phase(PG8_LAS unsigned char* lds, const Gemm g, const Sched& S, const Epi& E, const bool skip_epi = false) {
;     ...
;             PG8_LDA(At, 1, 1); PG8_STAGE(PG8_SB(1, 0), b3, voffB); PG8_STAGE(PG8_SB(1, 1), b3 + hstep, voffB); PG8_STAGE_A(1, 0, a3, true);
;             PG8_WAIT_V(8); PG8_WAIT_L(0); PG8_BAR; PG8_MMA(1, 0, At, B0); PG8_MMA(1, 1, At, B1); PG8_BAR; PG8_SCHED;
	s_add_i32 s28, s61, s2
	s_add_i32 m0, s28, 0xffffff80
	ds_read_b128 v[192:195], v172 offset:49152
	ds_read_b128 v[196:199], v172 offset:50176
	ds_read_b128 v[200:203], v172 offset:51200
	ds_read_b128 v[204:207], v172 offset:52224
	ds_read_b128 v[208:211], v172 offset:53248
	ds_read_b128 v[212:215], v172 offset:54272
	ds_read_b128 v[216:219], v172 offset:55296
	ds_read_b128 v[220:223], v172 offset:56320
	global_load_lds_dwordx4 v134, s[26:27] offset:128
	s_add_i32 m0, s28, 0x1f80
	s_add_i32 s28, s62, s2
	global_load_lds_dwordx4 v130, s[26:27] offset:128
	s_add_u32 s26, s26, 0x40080
	s_addc_u32 s27, s27, 0
	s_mov_b32 m0, s28
	s_nop 0
	global_load_lds_dwordx4 v134, s[26:27]
	s_add_i32 m0, s28, 0x2000
	s_nop 0
	global_load_lds_dwordx4 v130, s[26:27]
	s_add_i32 m0, s37, 0xffffff80
	s_nop 0
	global_load_lds_dwordx4 v136, s[98:99] offset:128
	s_add_i32 m0, s38, 0xffffff80
	s_nop 0
	global_load_lds_dwordx4 v132, s[98:99] offset:128
	s_waitcnt vmcnt(8)
	s_waitcnt lgkmcnt(0)
	s_barrier
	s_setprio 3
	s_waitcnt lgkmcnt(0)
	v_mfma_f32_16x16x32_bf16 v[62:65], v[148:151], v[192:195], v[62:65]
	v_mfma_f32_16x16x32_bf16 v[58:61], v[156:159], v[192:195], v[58:61]
	v_mfma_f32_16x16x32_bf16 v[50:53], v[148:151], v[200:203], v[50:53]
	v_mfma_f32_16x16x32_bf16 v[42:45], v[156:159], v[200:203], v[42:45]
	v_mfma_f32_16x16x32_bf16 v[34:37], v[148:151], v[208:211], v[34:37]
	v_mfma_f32_16x16x32_bf16 v[26:29], v[156:159], v[208:211], v[26:29]
	v_mfma_f32_16x16x32_bf16 v[18:21], v[148:151], v[216:219], v[18:21]
	v_mfma_f32_16x16x32_bf16 v[10:13], v[156:159], v[216:219], v[10:13]
	v_mfma_f32_16x16x32_bf16 v[62:65], v[152:155], v[196:199], v[62:65]
	v_mfma_f32_16x16x32_bf16 v[58:61], v[160:163], v[196:199], v[58:61]
	v_mfma_f32_16x16x32_bf16 v[50:53], v[152:155], v[204:207], v[50:53]
	v_mfma_f32_16x16x32_bf16 v[42:45], v[160:163], v[204:207], v[42:45]
	v_mfma_f32_16x16x32_bf16 v[34:37], v[152:155], v[212:215], v[34:37]
	v_mfma_f32_16x16x32_bf16 v[26:29], v[160:163], v[212:215], v[26:29]
	v_mfma_f32_16x16x32_bf16 v[18:21], v[152:155], v[220:223], v[18:21]
	v_mfma_f32_16x16x32_bf16 v[10:13], v[160:163], v[220:223], v[10:13]
	s_setprio 0
	s_setprio 3
	v_mfma_f32_16x16x32_bf16 v[54:57], v[176:179], v[192:195], v[54:57]
	v_mfma_f32_16x16x32_bf16 v[46:49], v[184:187], v[192:195], v[46:49]
	v_mfma_f32_16x16x32_bf16 v[38:41], v[176:179], v[200:203], v[38:41]
	v_mfma_f32_16x16x32_bf16 v[30:33], v[184:187], v[200:203], v[30:33]
	v_mfma_f32_16x16x32_bf16 v[22:25], v[176:179], v[208:211], v[22:25]
	v_mfma_f32_16x16x32_bf16 v[14:17], v[184:187], v[208:211], v[14:17]
	v_mfma_f32_16x16x32_bf16 v[6:9], v[176:179], v[216:219], v[6:9]
	v_mfma_f32_16x16x32_bf16 v[2:5], v[184:187], v[216:219], v[2:5]
	v_mfma_f32_16x16x32_bf16 v[54:57], v[180:183], v[196:199], v[54:57]
	v_mfma_f32_16x16x32_bf16 v[46:49], v[188:191], v[196:199], v[46:49]
	v_mfma_f32_16x16x32_bf16 v[38:41], v[180:183], v[204:207], v[38:41]
	v_mfma_f32_16x16x32_bf16 v[30:33], v[188:191], v[204:207], v[30:33]
	v_mfma_f32_16x16x32_bf16 v[22:25], v[180:183], v[212:215], v[22:25]
	v_mfma_f32_16x16x32_bf16 v[14:17], v[188:191], v[212:215], v[14:17]
	v_mfma_f32_16x16x32_bf16 v[6:9], v[180:183], v[220:223], v[6:9]
	v_mfma_f32_16x16x32_bf16 v[2:5], v[188:191], v[220:223], v[2:5]
	s_setprio 0
	s_barrier
	s_add_i32 s60, s60, 2
	s_add_u32 s24, s24, 0x100
	s_addc_u32 s25, s25, 0
	s_add_u32 s58, s58, 0x100
	s_addc_u32 s59, s59, 0
	s_cmp_gt_u32 s60, 13
.LBB0_253:
	ds_read_b128 v[148:151], v170
	ds_read_b128 v[152:155], v170 offset:1024
	ds_read_b128 v[156:159], v170 offset:2048
	ds_read_b128 v[160:163], v170 offset:3072
	ds_read_b128 v[176:179], v171
	ds_read_b128 v[180:183], v171 offset:1024
	ds_read_b128 v[184:187], v171 offset:2048
	ds_read_b128 v[188:191], v171 offset:3072
	s_add_u32 s26, s24, 0xfffc0080
	s_addc_u32 s27, s25, -1
	s_cmp_eq_u32 s60, 12
	s_cselect_b32 s29, s17, s27
	s_cselect_b32 s28, s56, s26
	s_cselect_b32 s27, s15, s59
	s_cselect_b32 s26, s57, s58
	s_add_i32 m0, s23, 0xc000
	ds_read_b128 v[192:195], v172
	ds_read_b128 v[196:199], v172 offset:1024
	ds_read_b128 v[200:203], v172 offset:2048
	ds_read_b128 v[204:207], v172 offset:3072
	ds_read_b128 v[208:211], v172 offset:4096
	ds_read_b128 v[212:215], v172 offset:5120
	ds_read_b128 v[216:219], v172 offset:6144
	ds_read_b128 v[220:223], v172 offset:7168
	global_load_lds_dwordx4 v140, s[24:25]
	s_add_i32 m0, s23, 0xe000
	s_nop 0
	global_load_lds_dwordx4 v142, s[24:25]
	s_waitcnt vmcnt(8)
	s_waitcnt lgkmcnt(0)
	s_barrier
; #define PG8_STAGE_A(b, h, ptr, NX) do { if constexpr (Sched::GATHER) { unsigned gs_[2]; gs_[0] = ((NX) && last_) ? gN[h][0] : gA[h][0]; gs_[1] = ((NX) && last_) ? gN[h][1] : gA[h][1]; PG8_STAGE(PG8_SA(b, h), ptr, gs_); } \
;         else PG8_STAGE(PG8_SA(b, h), (ptr) + ((h) ? hstep : (size_t)0), voffA); } while (0)
; #define PG8_STAGE(bufoff, gbase, voff) do { _Pragma("unroll") for (int _i = 0; _i < 2; ++_i) \
;         __builtin_amdgcn_global_load_lds((const unsigned*)((const char*)(gbase) + (voff)[_i]), (PG8_LAS unsigned*)(lds + (bufoff) + ldsw + _i * 8192), 16, 0, 0); } while (0)
; #define PG8_LDA(dst, b, h) do { _Pragma("unroll") for (int m = 0; m < 4; ++m) _Pragma("unroll") for (int k = 0; k < 2; ++k) dst[m][k] = *(const PG8_LAS bf16x8*)(lds + PG8_SA(b, h) + aoff + m * 2048 + k * 1024); } while (0)
; #define PG8_LDB(dst, b, h) do { _Pragma("unroll") for (int n = 0; n < 2; ++n) _Pragma("unroll") for (int k = 0; k < 2; ++k) dst[n][k] = *(const PG8_LAS bf16x8*)(lds + PG8_SB(b, h) + boff + n * 2048 + k * 1024); } while (0)
; #define PG8_MMA(ai, bj, At, Bt) do { __builtin_amdgcn_s_setprio(1); _Pragma("unroll") for (int m = 0; m < 4; ++m) _Pragma("unroll") for (int n = 0; n < 2; ++n) _Pragma("unroll") for (int k = 0; k < 2; ++k) \
;         acc[ai][bj][m][n] = __builtin_amdgcn_mfma_f32_16x16x32_bf16(Bt[n][k], At[m][k], acc[ai][bj][m][n], 0, 0, 0); __builtin_amdgcn_s_setprio(0); } while (0)
; #define PG8_WAIT_V(n) asm volatile("s_waitcnt vmcnt(" #n ")" ::: "memory")
; #define PG8_WAIT_L(n) asm volatile("s_waitcnt lgkmcnt(" #n ")" ::: "memory")
; #define PG8_BAR __builtin_amdgcn_s_barrier()
; #define PG8_SCHED __builtin_amdgcn_sched_barrier(0)
; template <class Epi, class Sched, bool ALIGN_EPI = false, bool SP2 = false>
; __device__ __forceinline__ void gemm_phase(PG8_LAS unsigned char* lds, const Gemm g, const Sched& S, const Epi& E, const bool skip_epi = false) {
;     ...
;             PG8_LDB(B0, 0, 0); PG8_LDB(B1, 0, 1); PG8_SCHED; PG8_LDA(At, 0, 0); PG8_STAGE_A(1, 1, a1, false);
;             PG8_WAIT_V(8); PG8_WAIT_L(0); PG8_BAR; PG8_MMA(0, 0, At, B0); PG8_MMA(0, 1, At, B1); PG8_BAR; PG8_SCHED;
;             PG8_LDA(At, 0, 1); PG8_STAGE(PG8_SB(0, 0), b2, voffB); PG8_STAGE(PG8_SB(0, 1), b2 + hstep, voffB); PG8_STAGE_A(0, 0, a2, true);
;             PG8_WAIT_V(8); PG8_WAIT_L(0); PG8_BAR; PG8_MMA(1, 0, At, B0); PG8_MMA(1, 1, At, B1); PG8_BAR; PG8_SCHED;
	s_setprio 3
	s_waitcnt lgkmcnt(0)
	v_mfma_f32_16x16x32_bf16 v[126:129], v[148:151], v[192:195], v[126:129]
	v_mfma_f32_16x16x32_bf16 v[122:125], v[156:159], v[192:195], v[122:125]
	v_mfma_f32_16x16x32_bf16 v[114:117], v[148:151], v[200:203], v[114:117]
	v_mfma_f32_16x16x32_bf16 v[106:109], v[156:159], v[200:203], v[106:109]
	v_mfma_f32_16x16x32_bf16 v[98:101], v[148:151], v[208:211], v[98:101]
	v_mfma_f32_16x16x32_bf16 v[90:93], v[156:159], v[208:211], v[90:93]
	v_mfma_f32_16x16x32_bf16 v[82:85], v[148:151], v[216:219], v[82:85]
	v_mfma_f32_16x16x32_bf16 v[74:77], v[156:159], v[216:219], v[74:77]
	v_mfma_f32_16x16x32_bf16 v[126:129], v[152:155], v[196:199], v[126:129]
	v_mfma_f32_16x16x32_bf16 v[122:125], v[160:163], v[196:199], v[122:125]
	v_mfma_f32_16x16x32_bf16 v[114:117], v[152:155], v[204:207], v[114:117]
	v_mfma_f32_16x16x32_bf16 v[106:109], v[160:163], v[204:207], v[106:109]
	v_mfma_f32_16x16x32_bf16 v[98:101], v[152:155], v[212:215], v[98:101]
	v_mfma_f32_16x16x32_bf16 v[90:93], v[160:163], v[212:215], v[90:93]
	v_mfma_f32_16x16x32_bf16 v[82:85], v[152:155], v[220:223], v[82:85]
	v_mfma_f32_16x16x32_bf16 v[74:77], v[160:163], v[220:223], v[74:77]
	s_setprio 0
	s_setprio 3
	v_mfma_f32_16x16x32_bf16 v[118:121], v[176:179], v[192:195], v[118:121]
	v_mfma_f32_16x16x32_bf16 v[110:113], v[184:187], v[192:195], v[110:113]
	v_mfma_f32_16x16x32_bf16 v[102:105], v[176:179], v[200:203], v[102:105]
	v_mfma_f32_16x16x32_bf16 v[94:97], v[184:187], v[200:203], v[94:97]
	v_mfma_f32_16x16x32_bf16 v[86:89], v[176:179], v[208:211], v[86:89]
	v_mfma_f32_16x16x32_bf16 v[78:81], v[184:187], v[208:211], v[78:81]
	v_mfma_f32_16x16x32_bf16 v[70:73], v[176:179], v[216:219], v[70:73]
	v_mfma_f32_16x16x32_bf16 v[66:69], v[184:187], v[216:219], v[66:69]
	v_mfma_f32_16x16x32_bf16 v[118:121], v[180:183], v[196:199], v[118:121]
	v_mfma_f32_16x16x32_bf16 v[110:113], v[188:191], v[196:199], v[110:113]
	v_mfma_f32_16x16x32_bf16 v[102:105], v[180:183], v[204:207], v[102:105]
	v_mfma_f32_16x16x32_bf16 v[94:97], v[188:191], v[204:207], v[94:97]
	v_mfma_f32_16x16x32_bf16 v[86:89], v[180:183], v[212:215], v[86:89]
	v_mfma_f32_16x16x32_bf16 v[78:81], v[188:191], v[212:215], v[78:81]
	v_mfma_f32_16x16x32_bf16 v[70:73], v[180:183], v[220:223], v[70:73]
	v_mfma_f32_16x16x32_bf16 v[66:69], v[188:191], v[220:223], v[66:69]
	s_setprio 0
	s_barrier
	s_add_i32 s61, s46, s2
	s_mov_b32 m0, s61
	ds_read_b128 v[192:195], v172 offset:16384
	ds_read_b128 v[196:199], v172 offset:17408
	ds_read_b128 v[200:203], v172 offset:18432
	ds_read_b128 v[204:207], v172 offset:19456
	ds_read_b128 v[208:211], v172 offset:20480
	ds_read_b128 v[212:215], v172 offset:21504
	ds_read_b128 v[216:219], v172 offset:22528
	ds_read_b128 v[220:223], v172 offset:23552
	global_load_lds_dwordx4 v134, s[26:27]
	s_add_i32 m0, s61, 0x2000
	s_add_u32 s62, s26, 0x40000
	s_addc_u32 s63, s27, 0
	s_add_i32 s61, s47, s2
	global_load_lds_dwordx4 v130, s[26:27]
	s_mov_b32 m0, s61
	s_mov_b64 s[98:99], s[28:29]
	global_load_lds_dwordx4 v134, s[62:63]
	s_add_i32 m0, s61, 0x2000
	s_nop 0
	global_load_lds_dwordx4 v130, s[62:63]
	s_mov_b32 m0, s23
	s_nop 0
	global_load_lds_dwordx4 v136, s[28:29]
	s_mov_b32 m0, s31
	s_nop 0
	global_load_lds_dwordx4 v132, s[28:29]
	s_waitcnt vmcnt(8)
	s_waitcnt lgkmcnt(0)
	s_barrier
	s_setprio 3
	s_waitcnt lgkmcnt(0)
	v_mfma_f32_16x16x32_bf16 v[62:65], v[148:151], v[192:195], v[62:65]
	v_mfma_f32_16x16x32_bf16 v[58:61], v[156:159], v[192:195], v[58:61]
	v_mfma_f32_16x16x32_bf16 v[50:53], v[148:151], v[200:203], v[50:53]
	v_mfma_f32_16x16x32_bf16 v[42:45], v[156:159], v[200:203], v[42:45]
	v_mfma_f32_16x16x32_bf16 v[34:37], v[148:151], v[208:211], v[34:37]
	v_mfma_f32_16x16x32_bf16 v[26:29], v[156:159], v[208:211], v[26:29]
	v_mfma_f32_16x16x32_bf16 v[18:21], v[148:151], v[216:219], v[18:21]
	v_mfma_f32_16x16x32_bf16 v[10:13], v[156:159], v[216:219], v[10:13]
	v_mfma_f32_16x16x32_bf16 v[62:65], v[152:155], v[196:199], v[62:65]
	v_mfma_f32_16x16x32_bf16 v[58:61], v[160:163], v[196:199], v[58:61]
	v_mfma_f32_16x16x32_bf16 v[50:53], v[152:155], v[204:207], v[50:53]
	v_mfma_f32_16x16x32_bf16 v[42:45], v[160:163], v[204:207], v[42:45]
	v_mfma_f32_16x16x32_bf16 v[34:37], v[152:155], v[212:215], v[34:37]
	v_mfma_f32_16x16x32_bf16 v[26:29], v[160:163], v[212:215], v[26:29]
	v_mfma_f32_16x16x32_bf16 v[18:21], v[152:155], v[220:223], v[18:21]
	v_mfma_f32_16x16x32_bf16 v[10:13], v[160:163], v[220:223], v[10:13]
	s_setprio 0
	s_setprio 3
	v_mfma_f32_16x16x32_bf16 v[54:57], v[176:179], v[192:195], v[54:57]
	v_mfma_f32_16x16x32_bf16 v[46:49], v[184:187], v[192:195], v[46:49]
	v_mfma_f32_16x16x32_bf16 v[38:41], v[176:179], v[200:203], v[38:41]
	v_mfma_f32_16x16x32_bf16 v[30:33], v[184:187], v[200:203], v[30:33]
	v_mfma_f32_16x16x32_bf16 v[22:25], v[176:179], v[208:211], v[22:25]
	v_mfma_f32_16x16x32_bf16 v[14:17], v[184:187], v[208:211], v[14:17]
	v_mfma_f32_16x16x32_bf16 v[6:9], v[176:179], v[216:219], v[6:9]
	v_mfma_f32_16x16x32_bf16 v[2:5], v[184:187], v[216:219], v[2:5]
	v_mfma_f32_16x16x32_bf16 v[54:57], v[180:183], v[196:199], v[54:57]
	v_mfma_f32_16x16x32_bf16 v[46:49], v[188:191], v[196:199], v[46:49]
	v_mfma_f32_16x16x32_bf16 v[38:41], v[180:183], v[204:207], v[38:41]
	v_mfma_f32_16x16x32_bf16 v[30:33], v[188:191], v[204:207], v[30:33]
	v_mfma_f32_16x16x32_bf16 v[22:25], v[180:183], v[212:215], v[22:25]
	v_mfma_f32_16x16x32_bf16 v[14:17], v[188:191], v[212:215], v[14:17]
	v_mfma_f32_16x16x32_bf16 v[6:9], v[180:183], v[220:223], v[6:9]
	v_mfma_f32_16x16x32_bf16 v[2:5], v[188:191], v[220:223], v[2:5]
	s_setprio 0
	s_barrier
; #define PG8_STAGE_A(b, h, ptr, NX) do { if constexpr (Sched::GATHER) { unsigned gs_[2]; gs_[0] = ((NX) && last_) ? gN[h][0] : gA[h][0]; gs_[1] = ((NX) && last_) ? gN[h][1] : gA[h][1]; PG8_STAGE(PG8_SA(b, h), ptr, gs_); } \
;         else PG8_STAGE(PG8_SA(b, h), (ptr) + ((h) ? hstep : (size_t)0), voffA); } while (0)
; #define PG8_LDA(dst, b, h) do { _Pragma("unroll") for (int m = 0; m < 4; ++m) _Pragma("unroll") for (int k = 0; k < 2; ++k) dst[m][k] = *(const PG8_LAS bf16x8*)(lds + PG8_SA(b, h) + aoff + m * 2048 + k * 1024); } while (0)
; #define PG8_LDB(dst, b, h) do { _Pragma("unroll") for (int n = 0; n < 2; ++n) _Pragma("unroll") for (int k = 0; k < 2; ++k) dst[n][k] = *(const PG8_LAS bf16x8*)(lds + PG8_SB(b, h) + boff + n * 2048 + k * 1024); } while (0)
; #define PG8_MMA(ai, bj, At, Bt) do { __builtin_amdgcn_s_setprio(1); _Pragma("unroll") for (int m = 0; m < 4; ++m) _Pragma("unroll") for (int n = 0; n < 2; ++n) _Pragma("unroll") for (int k = 0; k < 2; ++k) \
;         acc[ai][bj][m][n] = __builtin_amdgcn_mfma_f32_16x16x32_bf16(Bt[n][k], At[m][k], acc[ai][bj][m][n], 0, 0, 0); __builtin_amdgcn_s_setprio(0); } while (0)
; #define PG8_WAIT_V(n) asm volatile("s_waitcnt vmcnt(" #n ")" ::: "memory")
; #define PG8_WAIT_L(n) asm volatile("s_waitcnt lgkmcnt(" #n ")" ::: "memory")
; #define PG8_BAR __builtin_amdgcn_s_barrier()
; #define PG8_SCHED __builtin_amdgcn_sched_barrier(0)
; template <class Epi, class Sched, bool ALIGN_EPI = false, bool SP2 = false>
; __device__ __forceinline__ void gemm_phase(PG8_LAS unsigned char* lds, const Gemm g, const Sched& S, const Epi& E, const bool skip_epi = false) {
;     ...
;             PG8_LDB(B0, 1, 0); PG8_LDB(B1, 1, 1); PG8_SCHED; PG8_LDA(At, 1, 0); PG8_STAGE_A(0, 1, a2, true);
;             PG8_WAIT_V(8); PG8_WAIT_L(0); PG8_BAR; PG8_MMA(0, 0, At, B0); PG8_MMA(0, 1, At, B1); PG8_BAR; PG8_SCHED;
	s_add_i32 s61, 0, 0x18000
	s_add_i32 s62, 0, 0x1c000
	v_add_u32_e32 v160, s61, v1
	v_add_u32_e32 v188, s62, v1
	ds_read_b128 v[148:151], v160
	ds_read_b128 v[152:155], v160 offset:1024
	ds_read_b128 v[156:159], v160 offset:2048
	ds_read_b128 v[160:163], v160 offset:3072
	ds_read_b128 v[176:179], v188
	ds_read_b128 v[180:183], v188 offset:1024
	ds_read_b128 v[184:187], v188 offset:2048
	ds_read_b128 v[188:191], v188 offset:3072
	s_add_u32 s28, s28, 0x40000
	s_addc_u32 s29, s29, 0
	s_mov_b32 m0, s34
	ds_read_b128 v[192:195], v172 offset:32768
	ds_read_b128 v[196:199], v172 offset:33792
	ds_read_b128 v[200:203], v172 offset:34816
	ds_read_b128 v[204:207], v172 offset:35840
	ds_read_b128 v[208:211], v172 offset:36864
	ds_read_b128 v[212:215], v172 offset:37888
	ds_read_b128 v[216:219], v172 offset:38912
	ds_read_b128 v[220:223], v172 offset:39936
	global_load_lds_dwordx4 v136, s[28:29]
	s_mov_b32 m0, s35
	s_nop 0
	global_load_lds_dwordx4 v132, s[28:29]
	s_waitcnt vmcnt(8)
	s_waitcnt lgkmcnt(0)
	s_barrier
	s_setprio 3
	s_waitcnt lgkmcnt(0)
	v_mfma_f32_16x16x32_bf16 v[126:129], v[148:151], v[192:195], v[126:129]
	v_mfma_f32_16x16x32_bf16 v[122:125], v[156:159], v[192:195], v[122:125]
	v_mfma_f32_16x16x32_bf16 v[114:117], v[148:151], v[200:203], v[114:117]
	v_mfma_f32_16x16x32_bf16 v[106:109], v[156:159], v[200:203], v[106:109]
	v_mfma_f32_16x16x32_bf16 v[98:101], v[148:151], v[208:211], v[98:101]
	v_mfma_f32_16x16x32_bf16 v[90:93], v[156:159], v[208:211], v[90:93]
	v_mfma_f32_16x16x32_bf16 v[82:85], v[148:151], v[216:219], v[82:85]
	v_mfma_f32_16x16x32_bf16 v[74:77], v[156:159], v[216:219], v[74:77]
	v_mfma_f32_16x16x32_bf16 v[126:129], v[152:155], v[196:199], v[126:129]
	v_mfma_f32_16x16x32_bf16 v[122:125], v[160:163], v[196:199], v[122:125]
	v_mfma_f32_16x16x32_bf16 v[114:117], v[152:155], v[204:207], v[114:117]
	v_mfma_f32_16x16x32_bf16 v[106:109], v[160:163], v[204:207], v[106:109]
	v_mfma_f32_16x16x32_bf16 v[98:101], v[152:155], v[212:215], v[98:101]
	v_mfma_f32_16x16x32_bf16 v[90:93], v[160:163], v[212:215], v[90:93]
	v_mfma_f32_16x16x32_bf16 v[82:85], v[152:155], v[220:223], v[82:85]
	v_mfma_f32_16x16x32_bf16 v[74:77], v[160:163], v[220:223], v[74:77]
	s_setprio 0
	s_setprio 3
	v_mfma_f32_16x16x32_bf16 v[118:121], v[176:179], v[192:195], v[118:121]
	v_mfma_f32_16x16x32_bf16 v[110:113], v[184:187], v[192:195], v[110:113]
	v_mfma_f32_16x16x32_bf16 v[102:105], v[176:179], v[200:203], v[102:105]
	v_mfma_f32_16x16x32_bf16 v[94:97], v[184:187], v[200:203], v[94:97]
	v_mfma_f32_16x16x32_bf16 v[86:89], v[176:179], v[208:211], v[86:89]
	v_mfma_f32_16x16x32_bf16 v[78:81], v[184:187], v[208:211], v[78:81]
	v_mfma_f32_16x16x32_bf16 v[70:73], v[176:179], v[216:219], v[70:73]
	v_mfma_f32_16x16x32_bf16 v[66:69], v[184:187], v[216:219], v[66:69]
	v_mfma_f32_16x16x32_bf16 v[118:121], v[180:183], v[196:199], v[118:121]
	v_mfma_f32_16x16x32_bf16 v[110:113], v[188:191], v[196:199], v[110:113]
	v_mfma_f32_16x16x32_bf16 v[102:105], v[180:183], v[204:207], v[102:105]
	v_mfma_f32_16x16x32_bf16 v[94:97], v[188:191], v[204:207], v[94:97]
	v_mfma_f32_16x16x32_bf16 v[86:89], v[180:183], v[212:215], v[86:89]
	v_mfma_f32_16x16x32_bf16 v[78:81], v[188:191], v[212:215], v[78:81]
	v_mfma_f32_16x16x32_bf16 v[70:73], v[180:183], v[220:223], v[70:73]
	v_mfma_f32_16x16x32_bf16 v[66:69], v[188:191], v[220:223], v[66:69]
	s_setprio 0
	s_barrier
; #define PG8_STAGE_A(b, h, ptr, NX) do { if constexpr (Sched::GATHER) { unsigned gs_[2]; gs_[0] = ((NX) && last_) ? gN[h][0] : gA[h][0]; gs_[1] = ((NX) && last_) ? gN[h][1] : gA[h][1]; PG8_STAGE(PG8_SA(b, h), ptr, gs_); } \
;         else PG8_STAGE(PG8_SA(b, h), (ptr) + ((h) ? hstep : (size_t)0), voffA); } while (0)
; #define PG8_STAGE(bufoff, gbase, voff) do { _Pragma("unroll") for (int _i = 0; _i < 2; ++_i) \
;         __builtin_amdgcn_global_load_lds((const unsigned*)((const char*)(gbase) + (voff)[_i]), (PG8_LAS unsigned*)(lds + (bufoff) + ldsw + _i * 8192), 16, 0, 0); } while (0)
; #define PG8_LDA(dst, b, h) do { _Pragma("unroll") for (int m = 0; m < 4; ++m) _Pragma("unroll") for (int k = 0; k < 2; ++k) dst[m][k] = *(const PG8_LAS bf16x8*)(lds + PG8_SA(b, h) + aoff + m * 2048 + k * 1024); } while (0)
; #define PG8_MMA(ai, bj, At, Bt) do { __builtin_amdgcn_s_setprio(1); _Pragma("unroll") for (int m = 0; m < 4; ++m) _Pragma("unroll") for (int n = 0; n < 2; ++n) _Pragma("unroll") for (int k = 0; k < 2; ++k) \
;         acc[ai][bj][m][n] = __builtin_amdgcn_mfma_f32_16x16x32_bf16(Bt[n][k], At[m][k], acc[ai][bj][m][n], 0, 0, 0); __builtin_amdgcn_s_setprio(0); } while (0)
; #define PG8_WAIT_V(n) asm volatile("s_waitcnt vmcnt(" #n ")" ::: "memory")
; #define PG8_WAIT_L(n) asm volatile("s_waitcnt lgkmcnt(" #n ")" ::: "memory")
; #define PG8_BAR __builtin_amdgcn_s_barrier()
; #define PG8_SCHED __builtin_amdgcn_sched_barrier(0)
; __device__ __forceinline__ void rstd8(const float* SS, int rowb, int lane, float (&rs)[2][4]) {
;     ...
;     for (int ai = 0; ai < 2; ++ai)
; #pragma unroll
;         for (int m = 0; m < 4; ++m) p[ai][m] = *(const f32x4*)(SS + (size_t)(rowb + HALF * ai + 16 * m + (lane >> 2)) * 16 + 4 * (lane & 3));
; template <class Epi, class Sched, bool ALIGN_EPI = false, bool SP2 = false>
; __device__ __forceinline__ void gemm_phase(PG8_LAS unsigned char* lds, const Gemm g, const Sched& S, const Epi& E, const bool skip_epi = false) {
;     ...
;             PG8_LDA(At, 1, 1); PG8_STAGE(PG8_SB(1, 0), b3, voffB); PG8_STAGE(PG8_SB(1, 1), b3 + hstep, voffB); PG8_STAGE_A(1, 0, a3, true);
;             PG8_WAIT_V(8); PG8_WAIT_L(0); PG8_BAR; PG8_MMA(1, 0, At, B0); PG8_MMA(1, 1, At, B1); PG8_BAR; PG8_SCHED;
	s_add_i32 s28, s61, s2
	s_add_i32 m0, s28, 0xffffff80
	ds_read_b128 v[192:195], v172 offset:49152
	ds_read_b128 v[196:199], v172 offset:50176
	ds_read_b128 v[200:203], v172 offset:51200
	ds_read_b128 v[204:207], v172 offset:52224
	ds_read_b128 v[208:211], v172 offset:53248
	ds_read_b128 v[212:215], v172 offset:54272
	ds_read_b128 v[216:219], v172 offset:55296
	ds_read_b128 v[220:223], v172 offset:56320
	global_load_lds_dwordx4 v134, s[26:27] offset:128
	s_add_i32 m0, s28, 0x1f80
	s_add_i32 s28, s62, s2
	global_load_lds_dwordx4 v130, s[26:27] offset:128
	s_add_u32 s26, s26, 0x40080
	s_addc_u32 s27, s27, 0
	s_mov_b32 m0, s28
	s_nop 0
	global_load_lds_dwordx4 v134, s[26:27]
	s_add_i32 m0, s28, 0x2000
	s_nop 0
	global_load_lds_dwordx4 v130, s[26:27]
	s_add_i32 m0, s37, 0xffffff80
	s_nop 0
	global_load_lds_dwordx4 v136, s[98:99] offset:128
	s_add_i32 m0, s38, 0xffffff80
	s_nop 0
	global_load_lds_dwordx4 v132, s[98:99] offset:128
	s_waitcnt vmcnt(8)
	s_waitcnt lgkmcnt(0)
	s_barrier
	s_setprio 3
	s_waitcnt lgkmcnt(0)
	v_mfma_f32_16x16x32_bf16 v[62:65], v[148:151], v[192:195], v[62:65]
	v_mfma_f32_16x16x32_bf16 v[58:61], v[156:159], v[192:195], v[58:61]
	v_mfma_f32_16x16x32_bf16 v[50:53], v[148:151], v[200:203], v[50:53]
	v_mfma_f32_16x16x32_bf16 v[42:45], v[156:159], v[200:203], v[42:45]
	v_mfma_f32_16x16x32_bf16 v[34:37], v[148:151], v[208:211], v[34:37]
	v_mfma_f32_16x16x32_bf16 v[26:29], v[156:159], v[208:211], v[26:29]
	v_mfma_f32_16x16x32_bf16 v[18:21], v[148:151], v[216:219], v[18:21]
	v_mfma_f32_16x16x32_bf16 v[10:13], v[156:159], v[216:219], v[10:13]
	v_mfma_f32_16x16x32_bf16 v[62:65], v[152:155], v[196:199], v[62:65]
	v_mfma_f32_16x16x32_bf16 v[58:61], v[160:163], v[196:199], v[58:61]
	v_mfma_f32_16x16x32_bf16 v[50:53], v[152:155], v[204:207], v[50:53]
	v_mfma_f32_16x16x32_bf16 v[42:45], v[160:163], v[204:207], v[42:45]
	v_mfma_f32_16x16x32_bf16 v[34:37], v[152:155], v[212:215], v[34:37]
	v_mfma_f32_16x16x32_bf16 v[26:29], v[160:163], v[212:215], v[26:29]
	v_mfma_f32_16x16x32_bf16 v[18:21], v[152:155], v[220:223], v[18:21]
	v_mfma_f32_16x16x32_bf16 v[10:13], v[160:163], v[220:223], v[10:13]
	s_setprio 0
	s_setprio 3
	v_mfma_f32_16x16x32_bf16 v[54:57], v[176:179], v[192:195], v[54:57]
	v_mfma_f32_16x16x32_bf16 v[46:49], v[184:187], v[192:195], v[46:49]
	v_mfma_f32_16x16x32_bf16 v[38:41], v[176:179], v[200:203], v[38:41]
	v_mfma_f32_16x16x32_bf16 v[30:33], v[184:187], v[200:203], v[30:33]
	v_mfma_f32_16x16x32_bf16 v[22:25], v[176:179], v[208:211], v[22:25]
	v_mfma_f32_16x16x32_bf16 v[14:17], v[184:187], v[208:211], v[14:17]
	v_mfma_f32_16x16x32_bf16 v[6:9], v[176:179], v[216:219], v[6:9]
	v_mfma_f32_16x16x32_bf16 v[2:5], v[184:187], v[216:219], v[2:5]
	v_mfma_f32_16x16x32_bf16 v[54:57], v[180:183], v[196:199], v[54:57]
	v_mfma_f32_16x16x32_bf16 v[46:49], v[188:191], v[196:199], v[46:49]
	v_mfma_f32_16x16x32_bf16 v[38:41], v[180:183], v[204:207], v[38:41]
	v_mfma_f32_16x16x32_bf16 v[30:33], v[188:191], v[204:207], v[30:33]
	v_mfma_f32_16x16x32_bf16 v[22:25], v[180:183], v[212:215], v[22:25]
	v_mfma_f32_16x16x32_bf16 v[14:17], v[188:191], v[212:215], v[14:17]
	v_mfma_f32_16x16x32_bf16 v[6:9], v[180:183], v[220:223], v[6:9]
	v_mfma_f32_16x16x32_bf16 v[2:5], v[188:191], v[220:223], v[2:5]
	s_setprio 0
	s_barrier
	s_add_i32 s60, s60, 2
	s_add_u32 s24, s24, 0x100
	s_addc_u32 s25, s25, 0
	s_add_u32 s58, s58, 0x100
	s_addc_u32 s59, s59, 0
	s_cmp_gt_u32 s60, 13
	s_cbranch_scc0 .LBB0_253
	v_lshl_add_u32 v164, s22, 8, v167
	v_ashrrev_i32_e32 v165, 31, v164
	v_lshlrev_b64 v[148:149], 6, v[164:165]
	v_lshl_add_u64 v[148:149], v[138:139], 0, v[148:149]
	v_add_co_u32_e32 v150, vcc, 0x2000, v148
	v_addc_co_u32_e32 v151, vcc, 0, v149, vcc
	global_load_dwordx4 v[176:179], v[148:149], off
	global_load_dwordx4 v[180:183], v[148:149], off offset:1024
	global_load_dwordx4 v[184:187], v[148:149], off offset:2048
	global_load_dwordx4 v[188:191], v[148:149], off offset:3072
	global_load_dwordx4 v[192:195], v[150:151], off
	global_load_dwordx4 v[196:199], v[150:151], off offset:1024
	global_load_dwordx4 v[200:203], v[150:151], off offset:2048
	global_load_dwordx4 v[204:207], v[150:151], off offset:3072
	s_and_b64 vcc, exec, s[12:13]
	s_cbranch_vccz .LBB0_256
	s_barrier

; #define PG8_STAGE_A(b, h, ptr, NX) do { if constexpr (Sched::GATHER) { unsigned gs_[2]; gs_[0] = ((NX) && last_) ? gN[h][0] : gA[h][0]; gs_[1] = ((NX) && last_) ? gN[h][1] : gA[h][1]; PG8_STAGE(PG8_SA(b, h), ptr, gs_); } \
;         else PG8_STAGE(PG8_SA(b, h), (ptr) + ((h) ? hstep : (size_t)0), voffA); } while (0)
; #define PG8_STAGE(bufoff, gbase, voff) do { _Pragma("unroll") for (int _i = 0; _i < 2; ++_i) \
;         __builtin_amdgcn_global_load_lds((const unsigned*)((const char*)(gbase) + (voff)[_i]), (PG8_LAS unsigned*)(lds + (bufoff) + ldsw + _i * 8192), 16, 0, 0); } while (0)
; #define PG8_LDA(dst, b, h) do { _Pragma("unroll") for (int m = 0; m < 4; ++m) _Pragma("unroll") for (int k = 0; k < 2; ++k) dst[m][k] = *(const PG8_LAS bf16x8*)(lds + PG8_SA(b, h) + aoff + m * 2048 + k * 1024); } while (0)
; #define PG8_LDB(dst, b, h) do { _Pragma("unroll") for (int n = 0; n < 2; ++n) _Pragma("unroll") for (int k = 0; k < 2; ++k) dst[n][k] = *(const PG8_LAS bf16x8*)(lds + PG8_SB(b, h) + boff + n * 2048 + k * 1024); } while (0)
; #define PG8_WAIT_V(n) asm volatile("s_waitcnt vmcnt(" #n ")" ::: "memory")
; template <class Epi, class Sched, bool ALIGN_EPI = false, bool SP2 = false>
; __device__ __forceinline__ void gemm_phase(PG8_LAS unsigned char* lds, const Gemm g, const Sched& S, const Epi& E, const bool skip_epi = false) {
;     ...
;         const char* nA = has_next ? (const char*)g.A + (size_t)nxt.pm * pmstepA + nxt.ko : cA; const char* nB = has_next ? (const char*)g.Bt + (size_t)nxt.pn * tstep + nxt.ko : cB;
;         for (int t = 0; t < nt; t += 2) {
;             const bool last = (t == nt - 2); last_ = last && has_next;
;             const char* a1 = cA + (size_t)(t + 1) * kstep;
;             const char* a2 = last ? nA : cA + (size_t)(t + 2) * kstep; const char* b2 = last ? nB : cB + (size_t)(t + 2) * kstep;
;             const char* a3 = a2 + kstep; const char* b3 = b2 + kstep;
;             if (last && has_next) S.a_ready(nxt);
;             if constexpr (SP2) {
;             PG8_LDB(B0, 0, 0); PG8_LDB(B1, 0, 1); PG8_SCHED; PG8_LDA(At, 0, 0); PG8_STAGE_A(1, 1, a1, false);
;             PG8_WAIT_V(8); PG8_WAIT_L(0); PG8_BAR; PG8_MMA(0, 0, At, B0); PG8_MMA(0, 1, At, B1); PG8_BAR; PG8_SCHED;
;             PG8_LDA(At, 0, 1); PG8_STAGE(PG8_SB(0, 0), b2, voffB); PG8_STAGE(PG8_SB(0, 1), b2 + hstep, voffB); PG8_STAGE_A(0, 0, a2, true);
.LBB0_633:
	s_ashr_i32 s19, s18, 31
	s_lshl_b64 s[20:21], s[18:19], 19
	s_add_u32 s20, s46, s20
	s_addc_u32 s21, s47, s21
	s_and_b64 s[22:23], s[6:7], exec
	s_cselect_b32 s19, s21, s27
	s_cselect_b32 s25, s20, s26
	s_ashr_i32 s17, s16, 31
	s_lshl_b64 s[22:23], s[16:17], 19
	v_readlane_b32 s17, v254, 40
	s_add_u32 s22, s17, s22
	v_readlane_b32 s17, v254, 41
	s_addc_u32 s23, s17, s23
	s_and_b64 s[30:31], s[6:7], exec
	s_cselect_b32 s17, s23, s29
	s_cselect_b32 s60, s22, s28
	s_add_u32 s26, s26, 0x40080
	s_addc_u32 s27, s27, 0
	s_add_u32 s61, s28, 0x100
	s_addc_u32 s62, s29, 0
	s_mov_b32 s63, -2
	s_waitcnt lgkmcnt(0)
	ds_read_b128 v[98:101], v234
	ds_read_b128 v[110:113], v234 offset:1024
	ds_read_b128 v[122:125], v234 offset:2048
	ds_read_b128 v[126:129], v234 offset:3072
	ds_read_b128 v[138:141], v235
	ds_read_b128 v[142:145], v235 offset:1024
	ds_read_b128 v[146:149], v235 offset:2048
	ds_read_b128 v[150:153], v235 offset:3072
	s_add_u32 s28, s26, 0xfffc0080
	s_addc_u32 s29, s27, -1
	s_cmp_eq_u32 s63, 12
	s_cselect_b32 s31, s19, s29
	s_cselect_b32 s30, s25, s28
	s_cselect_b32 s29, s17, s62
	s_cselect_b32 s28, s60, s61
	s_add_i32 m0, s3, 0xc000
	ds_read_b128 v[154:157], v236
	ds_read_b128 v[166:169], v236 offset:1024
	ds_read_b128 v[170:173], v236 offset:2048
	ds_read_b128 v[174:177], v236 offset:3072
	ds_read_b128 v[178:181], v236 offset:4096
	ds_read_b128 v[182:185], v236 offset:5120
	ds_read_b128 v[186:189], v236 offset:6144
	ds_read_b128 v[206:209], v236 offset:7168
	global_load_lds_dwordx4 v198, s[26:27]
	s_add_i32 m0, s3, 0xe000
	s_nop 0
	global_load_lds_dwordx4 v200, s[26:27]
	s_waitcnt vmcnt(8)
	s_waitcnt lgkmcnt(0)
	s_barrier
	s_setprio 3
	s_waitcnt lgkmcnt(0)
	v_mfma_f32_16x16x32_bf16 v[162:165], v[98:101], v[154:157], 0
	v_mfma_f32_16x16x32_bf16 v[158:161], v[122:125], v[154:157], 0
	v_mfma_f32_16x16x32_bf16 v[118:121], v[98:101], v[170:173], 0
	v_mfma_f32_16x16x32_bf16 v[114:117], v[122:125], v[170:173], 0
	v_mfma_f32_16x16x32_bf16 v[94:97], v[98:101], v[178:181], 0
	v_mfma_f32_16x16x32_bf16 v[90:93], v[122:125], v[178:181], 0
	v_mfma_f32_16x16x32_bf16 v[78:81], v[98:101], v[186:189], 0
	v_mfma_f32_16x16x32_bf16 v[74:77], v[122:125], v[186:189], 0
	v_mfma_f32_16x16x32_bf16 v[162:165], v[110:113], v[166:169], v[162:165]
	v_mfma_f32_16x16x32_bf16 v[158:161], v[126:129], v[166:169], v[158:161]
	v_mfma_f32_16x16x32_bf16 v[118:121], v[110:113], v[174:177], v[118:121]
	v_mfma_f32_16x16x32_bf16 v[114:117], v[126:129], v[174:177], v[114:117]
	v_mfma_f32_16x16x32_bf16 v[94:97], v[110:113], v[182:185], v[94:97]
	v_mfma_f32_16x16x32_bf16 v[90:93], v[126:129], v[182:185], v[90:93]
	v_mfma_f32_16x16x32_bf16 v[78:81], v[110:113], v[206:209], v[78:81]
	v_mfma_f32_16x16x32_bf16 v[74:77], v[126:129], v[206:209], v[74:77]
	s_setprio 0
	s_setprio 3
	v_mfma_f32_16x16x32_bf16 v[134:137], v[138:141], v[154:157], 0
	v_mfma_f32_16x16x32_bf16 v[130:133], v[146:149], v[154:157], 0
	v_mfma_f32_16x16x32_bf16 v[106:109], v[138:141], v[170:173], 0
	v_mfma_f32_16x16x32_bf16 v[102:105], v[146:149], v[170:173], 0
	v_mfma_f32_16x16x32_bf16 v[86:89], v[138:141], v[178:181], 0
	v_mfma_f32_16x16x32_bf16 v[82:85], v[146:149], v[178:181], 0
	v_mfma_f32_16x16x32_bf16 v[70:73], v[138:141], v[186:189], 0
	v_mfma_f32_16x16x32_bf16 v[66:69], v[146:149], v[186:189], 0
	v_mfma_f32_16x16x32_bf16 v[134:137], v[142:145], v[166:169], v[134:137]
	v_mfma_f32_16x16x32_bf16 v[130:133], v[150:153], v[166:169], v[130:133]
	v_mfma_f32_16x16x32_bf16 v[106:109], v[142:145], v[174:177], v[106:109]
	v_mfma_f32_16x16x32_bf16 v[102:105], v[150:153], v[174:177], v[102:105]
	v_mfma_f32_16x16x32_bf16 v[86:89], v[142:145], v[182:185], v[86:89]
	v_mfma_f32_16x16x32_bf16 v[82:85], v[150:153], v[182:185], v[82:85]
	v_mfma_f32_16x16x32_bf16 v[70:73], v[142:145], v[206:209], v[70:73]
	v_mfma_f32_16x16x32_bf16 v[66:69], v[150:153], v[206:209], v[66:69]
	s_setprio 0
	s_barrier
	s_add_i32 s64, s57, s2
	s_mov_b32 m0, s64
	ds_read_b128 v[154:157], v236 offset:16384
	ds_read_b128 v[166:169], v236 offset:17408
	ds_read_b128 v[170:173], v236 offset:18432
	ds_read_b128 v[174:177], v236 offset:19456
	ds_read_b128 v[178:181], v236 offset:20480
	ds_read_b128 v[182:185], v236 offset:21504
	ds_read_b128 v[186:189], v236 offset:22528
	ds_read_b128 v[206:209], v236 offset:23552
	global_load_lds_dwordx4 v192, s[28:29]
	s_add_i32 m0, s64, 0x2000
	s_add_u32 s64, s28, 0x40000
	s_addc_u32 s65, s29, 0
	s_add_i32 s66, s58, s2
	global_load_lds_dwordx4 v196, s[28:29]
	s_mov_b32 m0, s66
	s_mov_b64 s[98:99], s[30:31]
	global_load_lds_dwordx4 v192, s[64:65]
	s_add_i32 m0, s66, 0x2000
	s_nop 0
	global_load_lds_dwordx4 v196, s[64:65]
	s_mov_b32 m0, s3
	s_nop 0
	global_load_lds_dwordx4 v190, s[30:31]
	s_mov_b32 m0, s34
	s_nop 0
	global_load_lds_dwordx4 v194, s[30:31]
	s_waitcnt vmcnt(8)
	s_waitcnt lgkmcnt(0)
	s_barrier
; #define PG8_STAGE_A(b, h, ptr, NX) do { if constexpr (Sched::GATHER) { unsigned gs_[2]; gs_[0] = ((NX) && last_) ? gN[h][0] : gA[h][0]; gs_[1] = ((NX) && last_) ? gN[h][1] : gA[h][1]; PG8_STAGE(PG8_SA(b, h), ptr, gs_); } \
;         else PG8_STAGE(PG8_SA(b, h), (ptr) + ((h) ? hstep : (size_t)0), voffA); } while (0)
; #define PG8_STAGE(bufoff, gbase, voff) do { _Pragma("unroll") for (int _i = 0; _i < 2; ++_i) \
;         __builtin_amdgcn_global_load_lds((const unsigned*)((const char*)(gbase) + (voff)[_i]), (PG8_LAS unsigned*)(lds + (bufoff) + ldsw + _i * 8192), 16, 0, 0); } while (0)
; #define PG8_LDA(dst, b, h) do { _Pragma("unroll") for (int m = 0; m < 4; ++m) _Pragma("unroll") for (int k = 0; k < 2; ++k) dst[m][k] = *(const PG8_LAS bf16x8*)(lds + PG8_SA(b, h) + aoff + m * 2048 + k * 1024); } while (0)
; #define PG8_LDB(dst, b, h) do { _Pragma("unroll") for (int n = 0; n < 2; ++n) _Pragma("unroll") for (int k = 0; k < 2; ++k) dst[n][k] = *(const PG8_LAS bf16x8*)(lds + PG8_SB(b, h) + boff + n * 2048 + k * 1024); } while (0)
; #define PG8_MMA(ai, bj, At, Bt) do { __builtin_amdgcn_s_setprio(1); _Pragma("unroll") for (int m = 0; m < 4; ++m) _Pragma("unroll") for (int n = 0; n < 2; ++n) _Pragma("unroll") for (int k = 0; k < 2; ++k) \
;         acc[ai][bj][m][n] = __builtin_amdgcn_mfma_f32_16x16x32_bf16(Bt[n][k], At[m][k], acc[ai][bj][m][n], 0, 0, 0); __builtin_amdgcn_s_setprio(0); } while (0)
; #define PG8_WAIT_V(n) asm volatile("s_waitcnt vmcnt(" #n ")" ::: "memory")
; #define PG8_BAR __builtin_amdgcn_s_barrier()
; template <class Epi, class Sched, bool ALIGN_EPI = false, bool SP2 = false>
; __device__ __forceinline__ void gemm_phase(PG8_LAS unsigned char* lds, const Gemm g, const Sched& S, const Epi& E, const bool skip_epi = false) {
;     ...
;             PG8_WAIT_V(8); PG8_WAIT_L(0); PG8_BAR; PG8_MMA(1, 0, At, B0); PG8_MMA(1, 1, At, B1); PG8_BAR; PG8_SCHED;
;             PG8_LDB(B0, 1, 0); PG8_LDB(B1, 1, 1); PG8_SCHED; PG8_LDA(At, 1, 0); PG8_STAGE_A(0, 1, a2, true);
;             PG8_WAIT_V(8); PG8_WAIT_L(0); PG8_BAR; PG8_MMA(0, 0, At, B0); PG8_MMA(0, 1, At, B1); PG8_BAR; PG8_SCHED;
;             PG8_LDA(At, 1, 1); PG8_STAGE(PG8_SB(1, 0), b3, voffB); PG8_STAGE(PG8_SB(1, 1), b3 + hstep, voffB); PG8_STAGE_A(1, 0, a3, true);
;             PG8_WAIT_V(8); PG8_WAIT_L(0); PG8_BAR; PG8_MMA(1, 0, At, B0); PG8_MMA(1, 1, At, B1); PG8_BAR; PG8_SCHED;
	s_setprio 3
	s_waitcnt lgkmcnt(0)
	v_mfma_f32_16x16x32_bf16 v[62:65], v[98:101], v[154:157], 0
	v_mfma_f32_16x16x32_bf16 v[58:61], v[122:125], v[154:157], 0
	v_mfma_f32_16x16x32_bf16 v[46:49], v[98:101], v[170:173], 0
	v_mfma_f32_16x16x32_bf16 v[42:45], v[122:125], v[170:173], 0
	v_mfma_f32_16x16x32_bf16 v[30:33], v[98:101], v[178:181], 0
	v_mfma_f32_16x16x32_bf16 v[26:29], v[122:125], v[178:181], 0
	v_mfma_f32_16x16x32_bf16 v[14:17], v[98:101], v[186:189], 0
	v_mfma_f32_16x16x32_bf16 v[10:13], v[122:125], v[186:189], 0
	v_mfma_f32_16x16x32_bf16 v[62:65], v[110:113], v[166:169], v[62:65]
	v_mfma_f32_16x16x32_bf16 v[58:61], v[126:129], v[166:169], v[58:61]
	v_mfma_f32_16x16x32_bf16 v[46:49], v[110:113], v[174:177], v[46:49]
	v_mfma_f32_16x16x32_bf16 v[42:45], v[126:129], v[174:177], v[42:45]
	v_mfma_f32_16x16x32_bf16 v[30:33], v[110:113], v[182:185], v[30:33]
	v_mfma_f32_16x16x32_bf16 v[26:29], v[126:129], v[182:185], v[26:29]
	v_mfma_f32_16x16x32_bf16 v[14:17], v[110:113], v[206:209], v[14:17]
	v_mfma_f32_16x16x32_bf16 v[10:13], v[126:129], v[206:209], v[10:13]
	s_setprio 0
	s_setprio 3
	v_mfma_f32_16x16x32_bf16 v[54:57], v[138:141], v[154:157], 0
	v_mfma_f32_16x16x32_bf16 v[50:53], v[146:149], v[154:157], 0
	v_mfma_f32_16x16x32_bf16 v[38:41], v[138:141], v[170:173], 0
	v_mfma_f32_16x16x32_bf16 v[34:37], v[146:149], v[170:173], 0
	v_mfma_f32_16x16x32_bf16 v[22:25], v[138:141], v[178:181], 0
	v_mfma_f32_16x16x32_bf16 v[18:21], v[146:149], v[178:181], 0
	v_mfma_f32_16x16x32_bf16 v[6:9], v[138:141], v[186:189], 0
	v_mfma_f32_16x16x32_bf16 v[2:5], v[146:149], v[186:189], 0
	v_mfma_f32_16x16x32_bf16 v[54:57], v[142:145], v[166:169], v[54:57]
	v_mfma_f32_16x16x32_bf16 v[50:53], v[150:153], v[166:169], v[50:53]
	v_mfma_f32_16x16x32_bf16 v[38:41], v[142:145], v[174:177], v[38:41]
	v_mfma_f32_16x16x32_bf16 v[34:37], v[150:153], v[174:177], v[34:37]
	v_mfma_f32_16x16x32_bf16 v[22:25], v[142:145], v[182:185], v[22:25]
	v_mfma_f32_16x16x32_bf16 v[18:21], v[150:153], v[182:185], v[18:21]
	v_mfma_f32_16x16x32_bf16 v[6:9], v[142:145], v[206:209], v[6:9]
	v_mfma_f32_16x16x32_bf16 v[2:5], v[150:153], v[206:209], v[2:5]
	s_setprio 0
	s_barrier
	s_add_i32 s64, 0, 0x18000
	s_add_i32 s65, 0, 0x1c000
	v_add_u32_e32 v126, s64, v229
	v_add_u32_e32 v150, s65, v229
	ds_read_b128 v[98:101], v126
	ds_read_b128 v[110:113], v126 offset:1024
	ds_read_b128 v[122:125], v126 offset:2048
	ds_read_b128 v[126:129], v126 offset:3072
	ds_read_b128 v[138:141], v150
	ds_read_b128 v[142:145], v150 offset:1024
	ds_read_b128 v[146:149], v150 offset:2048
	ds_read_b128 v[150:153], v150 offset:3072
	s_add_u32 s30, s30, 0x40000
	s_addc_u32 s31, s31, 0
	s_mov_b32 m0, s35
	ds_read_b128 v[154:157], v236 offset:32768
	ds_read_b128 v[166:169], v236 offset:33792
	ds_read_b128 v[170:173], v236 offset:34816
	ds_read_b128 v[174:177], v236 offset:35840
	ds_read_b128 v[178:181], v236 offset:36864
	ds_read_b128 v[182:185], v236 offset:37888
	ds_read_b128 v[186:189], v236 offset:38912
	ds_read_b128 v[206:209], v236 offset:39936
	global_load_lds_dwordx4 v190, s[30:31]
	s_mov_b32 m0, s36
	s_nop 0
	global_load_lds_dwordx4 v194, s[30:31]
	s_waitcnt vmcnt(8)
	s_waitcnt lgkmcnt(0)
	s_barrier
	s_setprio 3
	s_waitcnt lgkmcnt(0)
	v_mfma_f32_16x16x32_bf16 v[162:165], v[98:101], v[154:157], v[162:165]
	v_mfma_f32_16x16x32_bf16 v[158:161], v[122:125], v[154:157], v[158:161]
	v_mfma_f32_16x16x32_bf16 v[118:121], v[98:101], v[170:173], v[118:121]
	v_mfma_f32_16x16x32_bf16 v[114:117], v[122:125], v[170:173], v[114:117]
	v_mfma_f32_16x16x32_bf16 v[94:97], v[98:101], v[178:181], v[94:97]
	v_mfma_f32_16x16x32_bf16 v[90:93], v[122:125], v[178:181], v[90:93]
	v_mfma_f32_16x16x32_bf16 v[78:81], v[98:101], v[186:189], v[78:81]
	v_mfma_f32_16x16x32_bf16 v[74:77], v[122:125], v[186:189], v[74:77]
	v_mfma_f32_16x16x32_bf16 v[162:165], v[110:113], v[166:169], v[162:165]
	v_mfma_f32_16x16x32_bf16 v[158:161], v[126:129], v[166:169], v[158:161]
	v_mfma_f32_16x16x32_bf16 v[118:121], v[110:113], v[174:177], v[118:121]
	v_mfma_f32_16x16x32_bf16 v[114:117], v[126:129], v[174:177], v[114:117]
	v_mfma_f32_16x16x32_bf16 v[94:97], v[110:113], v[182:185], v[94:97]
	v_mfma_f32_16x16x32_bf16 v[90:93], v[126:129], v[182:185], v[90:93]
	v_mfma_f32_16x16x32_bf16 v[78:81], v[110:113], v[206:209], v[78:81]
	v_mfma_f32_16x16x32_bf16 v[74:77], v[126:129], v[206:209], v[74:77]
	s_setprio 0
	s_setprio 3
	v_mfma_f32_16x16x32_bf16 v[134:137], v[138:141], v[154:157], v[134:137]
	v_mfma_f32_16x16x32_bf16 v[130:133], v[146:149], v[154:157], v[130:133]
	v_mfma_f32_16x16x32_bf16 v[106:109], v[138:141], v[170:173], v[106:109]
	v_mfma_f32_16x16x32_bf16 v[102:105], v[146:149], v[170:173], v[102:105]
	v_mfma_f32_16x16x32_bf16 v[86:89], v[138:141], v[178:181], v[86:89]
	v_mfma_f32_16x16x32_bf16 v[82:85], v[146:149], v[178:181], v[82:85]
	v_mfma_f32_16x16x32_bf16 v[70:73], v[138:141], v[186:189], v[70:73]
	v_mfma_f32_16x16x32_bf16 v[66:69], v[146:149], v[186:189], v[66:69]
	v_mfma_f32_16x16x32_bf16 v[134:137], v[142:145], v[166:169], v[134:137]
	v_mfma_f32_16x16x32_bf16 v[130:133], v[150:153], v[166:169], v[130:133]
	v_mfma_f32_16x16x32_bf16 v[106:109], v[142:145], v[174:177], v[106:109]
	v_mfma_f32_16x16x32_bf16 v[102:105], v[150:153], v[174:177], v[102:105]
	v_mfma_f32_16x16x32_bf16 v[86:89], v[142:145], v[182:185], v[86:89]
	v_mfma_f32_16x16x32_bf16 v[82:85], v[150:153], v[182:185], v[82:85]
	v_mfma_f32_16x16x32_bf16 v[70:73], v[142:145], v[206:209], v[70:73]
	v_mfma_f32_16x16x32_bf16 v[66:69], v[150:153], v[206:209], v[66:69]
	s_setprio 0
	s_barrier
; #define PG8_STAGE_A(b, h, ptr, NX) do { if constexpr (Sched::GATHER) { unsigned gs_[2]; gs_[0] = ((NX) && last_) ? gN[h][0] : gA[h][0]; gs_[1] = ((NX) && last_) ? gN[h][1] : gA[h][1]; PG8_STAGE(PG8_SA(b, h), ptr, gs_); } \
;         else PG8_STAGE(PG8_SA(b, h), (ptr) + ((h) ? hstep : (size_t)0), voffA); } while (0)
; #define PG8_STAGE(bufoff, gbase, voff) do { _Pragma("unroll") for (int _i = 0; _i < 2; ++_i) \
;         __builtin_amdgcn_global_load_lds((const unsigned*)((const char*)(gbase) + (voff)[_i]), (PG8_LAS unsigned*)(lds + (bufoff) + ldsw + _i * 8192), 16, 0, 0); } while (0)
; #define PG8_LDA(dst, b, h) do { _Pragma("unroll") for (int m = 0; m < 4; ++m) _Pragma("unroll") for (int k = 0; k < 2; ++k) dst[m][k] = *(const PG8_LAS bf16x8*)(lds + PG8_SA(b, h) + aoff + m * 2048 + k * 1024); } while (0)
; #define PG8_LDB(dst, b, h) do { _Pragma("unroll") for (int n = 0; n < 2; ++n) _Pragma("unroll") for (int k = 0; k < 2; ++k) dst[n][k] = *(const PG8_LAS bf16x8*)(lds + PG8_SB(b, h) + boff + n * 2048 + k * 1024); } while (0)
; #define PG8_WAIT_V(n) asm volatile("s_waitcnt vmcnt(" #n ")" ::: "memory")
; #define PG8_WAIT_L(n) asm volatile("s_waitcnt lgkmcnt(" #n ")" ::: "memory")
; #define PG8_BAR __builtin_amdgcn_s_barrier()
; #define PG8_SCHED __builtin_amdgcn_sched_barrier(0)
; template <class Epi, class Sched, bool ALIGN_EPI = false, bool SP2 = false>
; __device__ __forceinline__ void gemm_phase(PG8_LAS unsigned char* lds, const Gemm g, const Sched& S, const Epi& E, const bool skip_epi = false) {
;     ...
;         for (int t = 0; t < nt; t += 2) {
;             const bool last = (t == nt - 2); last_ = last && has_next;
;             const char* a1 = cA + (size_t)(t + 1) * kstep;
;             const char* a2 = last ? nA : cA + (size_t)(t + 2) * kstep; const char* b2 = last ? nB : cB + (size_t)(t + 2) * kstep;
;             const char* a3 = a2 + kstep; const char* b3 = b2 + kstep;
;             if (last && has_next) S.a_ready(nxt);
;             if constexpr (SP2) {
;             PG8_LDB(B0, 0, 0); PG8_LDB(B1, 0, 1); PG8_SCHED; PG8_LDA(At, 0, 0); PG8_STAGE_A(1, 1, a1, false);
;     ...
;             PG8_LDA(At, 1, 1); PG8_STAGE(PG8_SB(1, 0), b3, voffB); PG8_STAGE(PG8_SB(1, 1), b3 + hstep, voffB); PG8_STAGE_A(1, 0, a3, true);
;             PG8_WAIT_V(8); PG8_WAIT_L(0); PG8_BAR; PG8_MMA(1, 0, At, B0); PG8_MMA(1, 1, At, B1); PG8_BAR; PG8_SCHED;
	s_add_i32 s30, s64, s2
	s_add_i32 m0, s30, 0xffffff80
	ds_read_b128 v[154:157], v236 offset:49152
	ds_read_b128 v[166:169], v236 offset:50176
	ds_read_b128 v[170:173], v236 offset:51200
	ds_read_b128 v[174:177], v236 offset:52224
	ds_read_b128 v[178:181], v236 offset:53248
	ds_read_b128 v[182:185], v236 offset:54272
	ds_read_b128 v[186:189], v236 offset:55296
	ds_read_b128 v[206:209], v236 offset:56320
	global_load_lds_dwordx4 v192, s[28:29] offset:128
	s_add_i32 m0, s30, 0x1f80
	s_add_i32 s30, s65, s2
	global_load_lds_dwordx4 v196, s[28:29] offset:128
	s_add_u32 s28, s28, 0x40080
	s_addc_u32 s29, s29, 0
	s_mov_b32 m0, s30
	s_nop 0
	global_load_lds_dwordx4 v192, s[28:29]
	s_add_i32 m0, s30, 0x2000
	s_nop 0
	global_load_lds_dwordx4 v196, s[28:29]
	s_add_i32 m0, s39, 0xffffff80
	s_nop 0
	global_load_lds_dwordx4 v190, s[98:99] offset:128
	s_add_i32 m0, s48, 0xffffff80
	s_nop 0
	global_load_lds_dwordx4 v194, s[98:99] offset:128
	s_waitcnt vmcnt(8)
	s_waitcnt lgkmcnt(0)
	s_barrier
	s_setprio 3
	s_waitcnt lgkmcnt(0)
	v_mfma_f32_16x16x32_bf16 v[62:65], v[98:101], v[154:157], v[62:65]
	v_mfma_f32_16x16x32_bf16 v[58:61], v[122:125], v[154:157], v[58:61]
	v_mfma_f32_16x16x32_bf16 v[46:49], v[98:101], v[170:173], v[46:49]
	v_mfma_f32_16x16x32_bf16 v[42:45], v[122:125], v[170:173], v[42:45]
	v_mfma_f32_16x16x32_bf16 v[30:33], v[98:101], v[178:181], v[30:33]
	v_mfma_f32_16x16x32_bf16 v[26:29], v[122:125], v[178:181], v[26:29]
	v_mfma_f32_16x16x32_bf16 v[14:17], v[98:101], v[186:189], v[14:17]
	v_mfma_f32_16x16x32_bf16 v[10:13], v[122:125], v[186:189], v[10:13]
	v_mfma_f32_16x16x32_bf16 v[62:65], v[110:113], v[166:169], v[62:65]
	v_mfma_f32_16x16x32_bf16 v[58:61], v[126:129], v[166:169], v[58:61]
	v_mfma_f32_16x16x32_bf16 v[46:49], v[110:113], v[174:177], v[46:49]
	v_mfma_f32_16x16x32_bf16 v[42:45], v[126:129], v[174:177], v[42:45]
	v_mfma_f32_16x16x32_bf16 v[30:33], v[110:113], v[182:185], v[30:33]
	v_mfma_f32_16x16x32_bf16 v[26:29], v[126:129], v[182:185], v[26:29]
	v_mfma_f32_16x16x32_bf16 v[14:17], v[110:113], v[206:209], v[14:17]
	v_mfma_f32_16x16x32_bf16 v[10:13], v[126:129], v[206:209], v[10:13]
	s_setprio 0
	s_setprio 3
	v_mfma_f32_16x16x32_bf16 v[54:57], v[138:141], v[154:157], v[54:57]
	v_mfma_f32_16x16x32_bf16 v[50:53], v[146:149], v[154:157], v[50:53]
	v_mfma_f32_16x16x32_bf16 v[38:41], v[138:141], v[170:173], v[38:41]
	v_mfma_f32_16x16x32_bf16 v[34:37], v[146:149], v[170:173], v[34:37]
	v_mfma_f32_16x16x32_bf16 v[22:25], v[138:141], v[178:181], v[22:25]
	v_mfma_f32_16x16x32_bf16 v[18:21], v[146:149], v[178:181], v[18:21]
	v_mfma_f32_16x16x32_bf16 v[6:9], v[138:141], v[186:189], v[6:9]
	v_mfma_f32_16x16x32_bf16 v[2:5], v[146:149], v[186:189], v[2:5]
	v_mfma_f32_16x16x32_bf16 v[54:57], v[142:145], v[166:169], v[54:57]
	v_mfma_f32_16x16x32_bf16 v[50:53], v[150:153], v[166:169], v[50:53]
	v_mfma_f32_16x16x32_bf16 v[38:41], v[142:145], v[174:177], v[38:41]
	v_mfma_f32_16x16x32_bf16 v[34:37], v[150:153], v[174:177], v[34:37]
	v_mfma_f32_16x16x32_bf16 v[22:25], v[142:145], v[182:185], v[22:25]
	v_mfma_f32_16x16x32_bf16 v[18:21], v[150:153], v[182:185], v[18:21]
	v_mfma_f32_16x16x32_bf16 v[6:9], v[142:145], v[206:209], v[6:9]
	v_mfma_f32_16x16x32_bf16 v[2:5], v[150:153], v[206:209], v[2:5]
	s_setprio 0
	s_barrier
	s_add_i32 s63, s63, 2
	s_add_u32 s26, s26, 0x100
	s_addc_u32 s27, s27, 0
	s_add_u32 s61, s61, 0x100
	s_addc_u32 s62, s62, 0
	s_cmp_gt_u32 s63, 13
.LBB0_634:
	ds_read_b128 v[98:101], v234
	ds_read_b128 v[110:113], v234 offset:1024
	ds_read_b128 v[122:125], v234 offset:2048
	ds_read_b128 v[126:129], v234 offset:3072
	ds_read_b128 v[138:141], v235
	ds_read_b128 v[142:145], v235 offset:1024
	ds_read_b128 v[146:149], v235 offset:2048
	ds_read_b128 v[150:153], v235 offset:3072
	s_add_u32 s28, s26, 0xfffc0080
	s_addc_u32 s29, s27, -1
	s_cmp_eq_u32 s63, 12
	s_cselect_b32 s31, s19, s29
	s_cselect_b32 s30, s25, s28
	s_cselect_b32 s29, s17, s62
	s_cselect_b32 s28, s60, s61
	s_add_i32 m0, s3, 0xc000
	ds_read_b128 v[154:157], v236
	ds_read_b128 v[166:169], v236 offset:1024
	ds_read_b128 v[170:173], v236 offset:2048
	ds_read_b128 v[174:177], v236 offset:3072
	ds_read_b128 v[178:181], v236 offset:4096
	ds_read_b128 v[182:185], v236 offset:5120
	ds_read_b128 v[186:189], v236 offset:6144
	ds_read_b128 v[206:209], v236 offset:7168
	global_load_lds_dwordx4 v198, s[26:27]
	s_add_i32 m0, s3, 0xe000
	s_nop 0
	global_load_lds_dwordx4 v200, s[26:27]
	s_waitcnt vmcnt(8)
	s_waitcnt lgkmcnt(0)
	s_barrier
	s_setprio 3
	s_waitcnt lgkmcnt(0)
	v_mfma_f32_16x16x32_bf16 v[162:165], v[98:101], v[154:157], v[162:165]
	v_mfma_f32_16x16x32_bf16 v[158:161], v[122:125], v[154:157], v[158:161]
	v_mfma_f32_16x16x32_bf16 v[118:121], v[98:101], v[170:173], v[118:121]
	v_mfma_f32_16x16x32_bf16 v[114:117], v[122:125], v[170:173], v[114:117]
	v_mfma_f32_16x16x32_bf16 v[94:97], v[98:101], v[178:181], v[94:97]
	v_mfma_f32_16x16x32_bf16 v[90:93], v[122:125], v[178:181], v[90:93]
	v_mfma_f32_16x16x32_bf16 v[78:81], v[98:101], v[186:189], v[78:81]
	v_mfma_f32_16x16x32_bf16 v[74:77], v[122:125], v[186:189], v[74:77]
	v_mfma_f32_16x16x32_bf16 v[162:165], v[110:113], v[166:169], v[162:165]
	v_mfma_f32_16x16x32_bf16 v[158:161], v[126:129], v[166:169], v[158:161]
	v_mfma_f32_16x16x32_bf16 v[118:121], v[110:113], v[174:177], v[118:121]
	v_mfma_f32_16x16x32_bf16 v[114:117], v[126:129], v[174:177], v[114:117]
	v_mfma_f32_16x16x32_bf16 v[94:97], v[110:113], v[182:185], v[94:97]
	v_mfma_f32_16x16x32_bf16 v[90:93], v[126:129], v[182:185], v[90:93]
	v_mfma_f32_16x16x32_bf16 v[78:81], v[110:113], v[206:209], v[78:81]
	v_mfma_f32_16x16x32_bf16 v[74:77], v[126:129], v[206:209], v[74:77]
	s_setprio 0
	s_setprio 3
	v_mfma_f32_16x16x32_bf16 v[134:137], v[138:141], v[154:157], v[134:137]
	v_mfma_f32_16x16x32_bf16 v[130:133], v[146:149], v[154:157], v[130:133]
	v_mfma_f32_16x16x32_bf16 v[106:109], v[138:141], v[170:173], v[106:109]
	v_mfma_f32_16x16x32_bf16 v[102:105], v[146:149], v[170:173], v[102:105]
	v_mfma_f32_16x16x32_bf16 v[86:89], v[138:141], v[178:181], v[86:89]
	v_mfma_f32_16x16x32_bf16 v[82:85], v[146:149], v[178:181], v[82:85]
	v_mfma_f32_16x16x32_bf16 v[70:73], v[138:141], v[186:189], v[70:73]
	v_mfma_f32_16x16x32_bf16 v[66:69], v[146:149], v[186:189], v[66:69]
	v_mfma_f32_16x16x32_bf16 v[134:137], v[142:145], v[166:169], v[134:137]
	v_mfma_f32_16x16x32_bf16 v[130:133], v[150:153], v[166:169], v[130:133]
	v_mfma_f32_16x16x32_bf16 v[106:109], v[142:145], v[174:177], v[106:109]
	v_mfma_f32_16x16x32_bf16 v[102:105], v[150:153], v[174:177], v[102:105]
	v_mfma_f32_16x16x32_bf16 v[86:89], v[142:145], v[182:185], v[86:89]
	v_mfma_f32_16x16x32_bf16 v[82:85], v[150:153], v[182:185], v[82:85]
	v_mfma_f32_16x16x32_bf16 v[70:73], v[142:145], v[206:209], v[70:73]
	v_mfma_f32_16x16x32_bf16 v[66:69], v[150:153], v[206:209], v[66:69]
	s_setprio 0
	s_barrier
; #define PG8_STAGE_A(b, h, ptr, NX) do { if constexpr (Sched::GATHER) { unsigned gs_[2]; gs_[0] = ((NX) && last_) ? gN[h][0] : gA[h][0]; gs_[1] = ((NX) && last_) ? gN[h][1] : gA[h][1]; PG8_STAGE(PG8_SA(b, h), ptr, gs_); } \
;         else PG8_STAGE(PG8_SA(b, h), (ptr) + ((h) ? hstep : (size_t)0), voffA); } while (0)
; #define PG8_STAGE(bufoff, gbase, voff) do { _Pragma("unroll") for (int _i = 0; _i < 2; ++_i) \
;         __builtin_amdgcn_global_load_lds((const unsigned*)((const char*)(gbase) + (voff)[_i]), (PG8_LAS unsigned*)(lds + (bufoff) + ldsw + _i * 8192), 16, 0, 0); } while (0)
; #define PG8_LDA(dst, b, h) do { _Pragma("unroll") for (int m = 0; m < 4; ++m) _Pragma("unroll") for (int k = 0; k < 2; ++k) dst[m][k] = *(const PG8_LAS bf16x8*)(lds + PG8_SA(b, h) + aoff + m * 2048 + k * 1024); } while (0)
; #define PG8_LDB(dst, b, h) do { _Pragma("unroll") for (int n = 0; n < 2; ++n) _Pragma("unroll") for (int k = 0; k < 2; ++k) dst[n][k] = *(const PG8_LAS bf16x8*)(lds + PG8_SB(b, h) + boff + n * 2048 + k * 1024); } while (0)
; #define PG8_MMA(ai, bj, At, Bt) do { __builtin_amdgcn_s_setprio(1); _Pragma("unroll") for (int m = 0; m < 4; ++m) _Pragma("unroll") for (int n = 0; n < 2; ++n) _Pragma("unroll") for (int k = 0; k < 2; ++k) \
;         acc[ai][bj][m][n] = __builtin_amdgcn_mfma_f32_16x16x32_bf16(Bt[n][k], At[m][k], acc[ai][bj][m][n], 0, 0, 0); __builtin_amdgcn_s_setprio(0); } while (0)
; #define PG8_WAIT_V(n) asm volatile("s_waitcnt vmcnt(" #n ")" ::: "memory")
; #define PG8_WAIT_L(n) asm volatile("s_waitcnt lgkmcnt(" #n ")" ::: "memory")
; #define PG8_BAR __builtin_amdgcn_s_barrier()
; #define PG8_SCHED __builtin_amdgcn_sched_barrier(0)
; template <class Epi, class Sched, bool ALIGN_EPI = false, bool SP2 = false>
; __device__ __forceinline__ void gemm_phase(PG8_LAS unsigned char* lds, const Gemm g, const Sched& S, const Epi& E, const bool skip_epi = false) {
;     ...
;             PG8_LDA(At, 0, 1); PG8_STAGE(PG8_SB(0, 0), b2, voffB); PG8_STAGE(PG8_SB(0, 1), b2 + hstep, voffB); PG8_STAGE_A(0, 0, a2, true);
;             PG8_WAIT_V(8); PG8_WAIT_L(0); PG8_BAR; PG8_MMA(1, 0, At, B0); PG8_MMA(1, 1, At, B1); PG8_BAR; PG8_SCHED;
;             PG8_LDB(B0, 1, 0); PG8_LDB(B1, 1, 1); PG8_SCHED; PG8_LDA(At, 1, 0); PG8_STAGE_A(0, 1, a2, true);
;             PG8_WAIT_V(8); PG8_WAIT_L(0); PG8_BAR; PG8_MMA(0, 0, At, B0); PG8_MMA(0, 1, At, B1); PG8_BAR; PG8_SCHED;
	s_add_i32 s64, s57, s2
	s_mov_b32 m0, s64
	ds_read_b128 v[154:157], v236 offset:16384
	ds_read_b128 v[166:169], v236 offset:17408
	ds_read_b128 v[170:173], v236 offset:18432
	ds_read_b128 v[174:177], v236 offset:19456
	ds_read_b128 v[178:181], v236 offset:20480
	ds_read_b128 v[182:185], v236 offset:21504
	ds_read_b128 v[186:189], v236 offset:22528
	ds_read_b128 v[206:209], v236 offset:23552
	global_load_lds_dwordx4 v192, s[28:29]
	s_add_i32 m0, s64, 0x2000
	s_add_u32 s64, s28, 0x40000
	s_addc_u32 s65, s29, 0
	s_add_i32 s66, s58, s2
	global_load_lds_dwordx4 v196, s[28:29]
	s_mov_b32 m0, s66
	s_mov_b64 s[98:99], s[30:31]
	global_load_lds_dwordx4 v192, s[64:65]
	s_add_i32 m0, s66, 0x2000
	s_nop 0
	global_load_lds_dwordx4 v196, s[64:65]
	s_mov_b32 m0, s3
	s_nop 0
	global_load_lds_dwordx4 v190, s[30:31]
	s_mov_b32 m0, s34
	s_nop 0
	global_load_lds_dwordx4 v194, s[30:31]
	s_waitcnt vmcnt(8)
	s_waitcnt lgkmcnt(0)
	s_barrier
	s_setprio 3
	s_waitcnt lgkmcnt(0)
	v_mfma_f32_16x16x32_bf16 v[62:65], v[98:101], v[154:157], v[62:65]
	v_mfma_f32_16x16x32_bf16 v[58:61], v[122:125], v[154:157], v[58:61]
	v_mfma_f32_16x16x32_bf16 v[46:49], v[98:101], v[170:173], v[46:49]
	v_mfma_f32_16x16x32_bf16 v[42:45], v[122:125], v[170:173], v[42:45]
	v_mfma_f32_16x16x32_bf16 v[30:33], v[98:101], v[178:181], v[30:33]
	v_mfma_f32_16x16x32_bf16 v[26:29], v[122:125], v[178:181], v[26:29]
	v_mfma_f32_16x16x32_bf16 v[14:17], v[98:101], v[186:189], v[14:17]
	v_mfma_f32_16x16x32_bf16 v[10:13], v[122:125], v[186:189], v[10:13]
	v_mfma_f32_16x16x32_bf16 v[62:65], v[110:113], v[166:169], v[62:65]
	v_mfma_f32_16x16x32_bf16 v[58:61], v[126:129], v[166:169], v[58:61]
	v_mfma_f32_16x16x32_bf16 v[46:49], v[110:113], v[174:177], v[46:49]
	v_mfma_f32_16x16x32_bf16 v[42:45], v[126:129], v[174:177], v[42:45]
	v_mfma_f32_16x16x32_bf16 v[30:33], v[110:113], v[182:185], v[30:33]
	v_mfma_f32_16x16x32_bf16 v[26:29], v[126:129], v[182:185], v[26:29]
	v_mfma_f32_16x16x32_bf16 v[14:17], v[110:113], v[206:209], v[14:17]
	v_mfma_f32_16x16x32_bf16 v[10:13], v[126:129], v[206:209], v[10:13]
	s_setprio 0
	s_setprio 3
	v_mfma_f32_16x16x32_bf16 v[54:57], v[138:141], v[154:157], v[54:57]
	v_mfma_f32_16x16x32_bf16 v[50:53], v[146:149], v[154:157], v[50:53]
	v_mfma_f32_16x16x32_bf16 v[38:41], v[138:141], v[170:173], v[38:41]
	v_mfma_f32_16x16x32_bf16 v[34:37], v[146:149], v[170:173], v[34:37]
	v_mfma_f32_16x16x32_bf16 v[22:25], v[138:141], v[178:181], v[22:25]
	v_mfma_f32_16x16x32_bf16 v[18:21], v[146:149], v[178:181], v[18:21]
	v_mfma_f32_16x16x32_bf16 v[6:9], v[138:141], v[186:189], v[6:9]
	v_mfma_f32_16x16x32_bf16 v[2:5], v[146:149], v[186:189], v[2:5]
	v_mfma_f32_16x16x32_bf16 v[54:57], v[142:145], v[166:169], v[54:57]
	v_mfma_f32_16x16x32_bf16 v[50:53], v[150:153], v[166:169], v[50:53]
	v_mfma_f32_16x16x32_bf16 v[38:41], v[142:145], v[174:177], v[38:41]
	v_mfma_f32_16x16x32_bf16 v[34:37], v[150:153], v[174:177], v[34:37]
	v_mfma_f32_16x16x32_bf16 v[22:25], v[142:145], v[182:185], v[22:25]
	v_mfma_f32_16x16x32_bf16 v[18:21], v[150:153], v[182:185], v[18:21]
	v_mfma_f32_16x16x32_bf16 v[6:9], v[142:145], v[206:209], v[6:9]
	v_mfma_f32_16x16x32_bf16 v[2:5], v[150:153], v[206:209], v[2:5]
	s_setprio 0
	s_barrier
	s_add_i32 s64, 0, 0x18000
	s_add_i32 s65, 0, 0x1c000
	v_add_u32_e32 v126, s64, v229
	v_add_u32_e32 v150, s65, v229
	ds_read_b128 v[98:101], v126
	ds_read_b128 v[110:113], v126 offset:1024
	ds_read_b128 v[122:125], v126 offset:2048
	ds_read_b128 v[126:129], v126 offset:3072
	ds_read_b128 v[138:141], v150
	ds_read_b128 v[142:145], v150 offset:1024
	ds_read_b128 v[146:149], v150 offset:2048
	ds_read_b128 v[150:153], v150 offset:3072
	s_add_u32 s30, s30, 0x40000
	s_addc_u32 s31, s31, 0
	s_mov_b32 m0, s35
	ds_read_b128 v[154:157], v236 offset:32768
	ds_read_b128 v[166:169], v236 offset:33792
	ds_read_b128 v[170:173], v236 offset:34816
	ds_read_b128 v[174:177], v236 offset:35840
	ds_read_b128 v[178:181], v236 offset:36864
	ds_read_b128 v[182:185], v236 offset:37888
	ds_read_b128 v[186:189], v236 offset:38912
	ds_read_b128 v[206:209], v236 offset:39936
	global_load_lds_dwordx4 v190, s[30:31]
	s_mov_b32 m0, s36
	s_nop 0
	global_load_lds_dwordx4 v194, s[30:31]
	s_waitcnt vmcnt(8)
	s_waitcnt lgkmcnt(0)
	s_barrier
; #define PG8_STAGE_A(b, h, ptr, NX) do { if constexpr (Sched::GATHER) { unsigned gs_[2]; gs_[0] = ((NX) && last_) ? gN[h][0] : gA[h][0]; gs_[1] = ((NX) && last_) ? gN[h][1] : gA[h][1]; PG8_STAGE(PG8_SA(b, h), ptr, gs_); } \
;         else PG8_STAGE(PG8_SA(b, h), (ptr) + ((h) ? hstep : (size_t)0), voffA); } while (0)
; #define PG8_STAGE(bufoff, gbase, voff) do { _Pragma("unroll") for (int _i = 0; _i < 2; ++_i) \
;         __builtin_amdgcn_global_load_lds((const unsigned*)((const char*)(gbase) + (voff)[_i]), (PG8_LAS unsigned*)(lds + (bufoff) + ldsw + _i * 8192), 16, 0, 0); } while (0)
; #define PG8_LDA(dst, b, h) do { _Pragma("unroll") for (int m = 0; m < 4; ++m) _Pragma("unroll") for (int k = 0; k < 2; ++k) dst[m][k] = *(const PG8_LAS bf16x8*)(lds + PG8_SA(b, h) + aoff + m * 2048 + k * 1024); } while (0)
; #define PG8_MMA(ai, bj, At, Bt) do { __builtin_amdgcn_s_setprio(1); _Pragma("unroll") for (int m = 0; m < 4; ++m) _Pragma("unroll") for (int n = 0; n < 2; ++n) _Pragma("unroll") for (int k = 0; k < 2; ++k) \
;         acc[ai][bj][m][n] = __builtin_amdgcn_mfma_f32_16x16x32_bf16(Bt[n][k], At[m][k], acc[ai][bj][m][n], 0, 0, 0); __builtin_amdgcn_s_setprio(0); } while (0)
; #define PG8_WAIT_V(n) asm volatile("s_waitcnt vmcnt(" #n ")" ::: "memory")
; #define PG8_WAIT_L(n) asm volatile("s_waitcnt lgkmcnt(" #n ")" ::: "memory")
; #define PG8_BAR __builtin_amdgcn_s_barrier()
; #define PG8_SCHED __builtin_amdgcn_sched_barrier(0)
; template <class Epi, class Sched, bool ALIGN_EPI = false, bool SP2 = false>
; __device__ __forceinline__ void gemm_phase(PG8_LAS unsigned char* lds, const Gemm g, const Sched& S, const Epi& E, const bool skip_epi = false) {
;     ...
;             PG8_WAIT_V(8); PG8_WAIT_L(0); PG8_BAR; PG8_MMA(0, 0, At, B0); PG8_MMA(0, 1, At, B1); PG8_BAR; PG8_SCHED;
;             PG8_LDA(At, 1, 1); PG8_STAGE(PG8_SB(1, 0), b3, voffB); PG8_STAGE(PG8_SB(1, 1), b3 + hstep, voffB); PG8_STAGE_A(1, 0, a3, true);
;             PG8_WAIT_V(8); PG8_WAIT_L(0); PG8_BAR; PG8_MMA(1, 0, At, B0); PG8_MMA(1, 1, At, B1); PG8_BAR; PG8_SCHED;
;     ...
;         if constexpr (ALIGN_EPI) { if (wr == 0) PG8_BAR; }
	s_setprio 3
	s_waitcnt lgkmcnt(0)
	v_mfma_f32_16x16x32_bf16 v[162:165], v[98:101], v[154:157], v[162:165]
	v_mfma_f32_16x16x32_bf16 v[158:161], v[122:125], v[154:157], v[158:161]
	v_mfma_f32_16x16x32_bf16 v[118:121], v[98:101], v[170:173], v[118:121]
	v_mfma_f32_16x16x32_bf16 v[114:117], v[122:125], v[170:173], v[114:117]
	v_mfma_f32_16x16x32_bf16 v[94:97], v[98:101], v[178:181], v[94:97]
	v_mfma_f32_16x16x32_bf16 v[90:93], v[122:125], v[178:181], v[90:93]
	v_mfma_f32_16x16x32_bf16 v[78:81], v[98:101], v[186:189], v[78:81]
	v_mfma_f32_16x16x32_bf16 v[74:77], v[122:125], v[186:189], v[74:77]
	v_mfma_f32_16x16x32_bf16 v[162:165], v[110:113], v[166:169], v[162:165]
	v_mfma_f32_16x16x32_bf16 v[158:161], v[126:129], v[166:169], v[158:161]
	v_mfma_f32_16x16x32_bf16 v[118:121], v[110:113], v[174:177], v[118:121]
	v_mfma_f32_16x16x32_bf16 v[114:117], v[126:129], v[174:177], v[114:117]
	v_mfma_f32_16x16x32_bf16 v[94:97], v[110:113], v[182:185], v[94:97]
	v_mfma_f32_16x16x32_bf16 v[90:93], v[126:129], v[182:185], v[90:93]
	v_mfma_f32_16x16x32_bf16 v[78:81], v[110:113], v[206:209], v[78:81]
	v_mfma_f32_16x16x32_bf16 v[74:77], v[126:129], v[206:209], v[74:77]
	s_setprio 0
	s_setprio 3
	v_mfma_f32_16x16x32_bf16 v[134:137], v[138:141], v[154:157], v[134:137]
	v_mfma_f32_16x16x32_bf16 v[130:133], v[146:149], v[154:157], v[130:133]
	v_mfma_f32_16x16x32_bf16 v[106:109], v[138:141], v[170:173], v[106:109]
	v_mfma_f32_16x16x32_bf16 v[102:105], v[146:149], v[170:173], v[102:105]
	v_mfma_f32_16x16x32_bf16 v[86:89], v[138:141], v[178:181], v[86:89]
	v_mfma_f32_16x16x32_bf16 v[82:85], v[146:149], v[178:181], v[82:85]
	v_mfma_f32_16x16x32_bf16 v[70:73], v[138:141], v[186:189], v[70:73]
	v_mfma_f32_16x16x32_bf16 v[66:69], v[146:149], v[186:189], v[66:69]
	v_mfma_f32_16x16x32_bf16 v[134:137], v[142:145], v[166:169], v[134:137]
	v_mfma_f32_16x16x32_bf16 v[130:133], v[150:153], v[166:169], v[130:133]
	v_mfma_f32_16x16x32_bf16 v[106:109], v[142:145], v[174:177], v[106:109]
	v_mfma_f32_16x16x32_bf16 v[102:105], v[150:153], v[174:177], v[102:105]
	v_mfma_f32_16x16x32_bf16 v[86:89], v[142:145], v[182:185], v[86:89]
	v_mfma_f32_16x16x32_bf16 v[82:85], v[150:153], v[182:185], v[82:85]
	v_mfma_f32_16x16x32_bf16 v[70:73], v[142:145], v[206:209], v[70:73]
	v_mfma_f32_16x16x32_bf16 v[66:69], v[150:153], v[206:209], v[66:69]
	s_setprio 0
	s_barrier
	s_add_i32 s30, s64, s2
	s_add_i32 m0, s30, 0xffffff80
	ds_read_b128 v[154:157], v236 offset:49152
	ds_read_b128 v[166:169], v236 offset:50176
	ds_read_b128 v[170:173], v236 offset:51200
	ds_read_b128 v[174:177], v236 offset:52224
	ds_read_b128 v[178:181], v236 offset:53248
	ds_read_b128 v[182:185], v236 offset:54272
	ds_read_b128 v[186:189], v236 offset:55296
	ds_read_b128 v[206:209], v236 offset:56320
	global_load_lds_dwordx4 v192, s[28:29] offset:128
	s_add_i32 m0, s30, 0x1f80
	s_add_i32 s30, s65, s2
	global_load_lds_dwordx4 v196, s[28:29] offset:128
	s_add_u32 s28, s28, 0x40080
	s_addc_u32 s29, s29, 0
	s_mov_b32 m0, s30
	s_nop 0
	global_load_lds_dwordx4 v192, s[28:29]
	s_add_i32 m0, s30, 0x2000
	s_nop 0
	global_load_lds_dwordx4 v196, s[28:29]
	s_add_i32 m0, s39, 0xffffff80
	s_nop 0
	global_load_lds_dwordx4 v190, s[98:99] offset:128
	s_add_i32 m0, s48, 0xffffff80
	s_nop 0
	global_load_lds_dwordx4 v194, s[98:99] offset:128
	s_waitcnt vmcnt(8)
	s_waitcnt lgkmcnt(0)
	s_barrier
	s_setprio 3
	s_waitcnt lgkmcnt(0)
	v_mfma_f32_16x16x32_bf16 v[62:65], v[98:101], v[154:157], v[62:65]
	v_mfma_f32_16x16x32_bf16 v[58:61], v[122:125], v[154:157], v[58:61]
	v_mfma_f32_16x16x32_bf16 v[46:49], v[98:101], v[170:173], v[46:49]
	v_mfma_f32_16x16x32_bf16 v[42:45], v[122:125], v[170:173], v[42:45]
	v_mfma_f32_16x16x32_bf16 v[30:33], v[98:101], v[178:181], v[30:33]
	v_mfma_f32_16x16x32_bf16 v[26:29], v[122:125], v[178:181], v[26:29]
	v_mfma_f32_16x16x32_bf16 v[14:17], v[98:101], v[186:189], v[14:17]
	v_mfma_f32_16x16x32_bf16 v[10:13], v[122:125], v[186:189], v[10:13]
	v_mfma_f32_16x16x32_bf16 v[62:65], v[110:113], v[166:169], v[62:65]
	v_mfma_f32_16x16x32_bf16 v[58:61], v[126:129], v[166:169], v[58:61]
	v_mfma_f32_16x16x32_bf16 v[46:49], v[110:113], v[174:177], v[46:49]
	v_mfma_f32_16x16x32_bf16 v[42:45], v[126:129], v[174:177], v[42:45]
	v_mfma_f32_16x16x32_bf16 v[30:33], v[110:113], v[182:185], v[30:33]
	v_mfma_f32_16x16x32_bf16 v[26:29], v[126:129], v[182:185], v[26:29]
	v_mfma_f32_16x16x32_bf16 v[14:17], v[110:113], v[206:209], v[14:17]
	v_mfma_f32_16x16x32_bf16 v[10:13], v[126:129], v[206:209], v[10:13]
	s_setprio 0
	s_setprio 3
	v_mfma_f32_16x16x32_bf16 v[54:57], v[138:141], v[154:157], v[54:57]
	v_mfma_f32_16x16x32_bf16 v[50:53], v[146:149], v[154:157], v[50:53]
	v_mfma_f32_16x16x32_bf16 v[38:41], v[138:141], v[170:173], v[38:41]
	v_mfma_f32_16x16x32_bf16 v[34:37], v[146:149], v[170:173], v[34:37]
	v_mfma_f32_16x16x32_bf16 v[22:25], v[138:141], v[178:181], v[22:25]
	v_mfma_f32_16x16x32_bf16 v[18:21], v[146:149], v[178:181], v[18:21]
	v_mfma_f32_16x16x32_bf16 v[6:9], v[138:141], v[186:189], v[6:9]
	v_mfma_f32_16x16x32_bf16 v[2:5], v[146:149], v[186:189], v[2:5]
	v_mfma_f32_16x16x32_bf16 v[54:57], v[142:145], v[166:169], v[54:57]
	v_mfma_f32_16x16x32_bf16 v[50:53], v[150:153], v[166:169], v[50:53]
	v_mfma_f32_16x16x32_bf16 v[38:41], v[142:145], v[174:177], v[38:41]
	v_mfma_f32_16x16x32_bf16 v[34:37], v[150:153], v[174:177], v[34:37]
	v_mfma_f32_16x16x32_bf16 v[22:25], v[142:145], v[182:185], v[22:25]
	v_mfma_f32_16x16x32_bf16 v[18:21], v[150:153], v[182:185], v[18:21]
	v_mfma_f32_16x16x32_bf16 v[6:9], v[142:145], v[206:209], v[6:9]
	v_mfma_f32_16x16x32_bf16 v[2:5], v[150:153], v[206:209], v[2:5]
	s_setprio 0
	s_barrier
	s_add_i32 s63, s63, 2
	s_add_u32 s26, s26, 0x100
	s_addc_u32 s27, s27, 0
	s_add_u32 s61, s61, 0x100
	s_addc_u32 s62, s62, 0
	s_cmp_gt_u32 s63, 13
	s_cbranch_scc0 .LBB0_634
	s_and_b64 vcc, exec, s[14:15]
	s_cbranch_vccz .LBB0_637
	s_barrier

; #define PG8_STAGE_A(b, h, ptr, NX) do { if constexpr (Sched::GATHER) { unsigned gs_[2]; gs_[0] = ((NX) && last_) ? gN[h][0] : gA[h][0]; gs_[1] = ((NX) && last_) ? gN[h][1] : gA[h][1]; PG8_STAGE(PG8_SA(b, h), ptr, gs_); } \
;         else PG8_STAGE(PG8_SA(b, h), (ptr) + ((h) ? hstep : (size_t)0), voffA); } while (0)
; #define PG8_STAGE(bufoff, gbase, voff) do { _Pragma("unroll") for (int _i = 0; _i < 2; ++_i) \
;         __builtin_amdgcn_global_load_lds((const unsigned*)((const char*)(gbase) + (voff)[_i]), (PG8_LAS unsigned*)(lds + (bufoff) + ldsw + _i * 8192), 16, 0, 0); } while (0)
; #define PG8_LDA(dst, b, h) do { _Pragma("unroll") for (int m = 0; m < 4; ++m) _Pragma("unroll") for (int k = 0; k < 2; ++k) dst[m][k] = *(const PG8_LAS bf16x8*)(lds + PG8_SA(b, h) + aoff + m * 2048 + k * 1024); } while (0)
; #define PG8_LDB(dst, b, h) do { _Pragma("unroll") for (int n = 0; n < 2; ++n) _Pragma("unroll") for (int k = 0; k < 2; ++k) dst[n][k] = *(const PG8_LAS bf16x8*)(lds + PG8_SB(b, h) + boff + n * 2048 + k * 1024); } while (0)
; #define PG8_WAIT_V(n) asm volatile("s_waitcnt vmcnt(" #n ")" ::: "memory")
; template <class Epi, class Sched, bool ALIGN_EPI = false, bool SP2 = false>
; __device__ __forceinline__ void gemm_phase(PG8_LAS unsigned char* lds, const Gemm g, const Sched& S, const Epi& E, const bool skip_epi = false) {
;     ...
;         const char* nA = has_next ? (const char*)g.A + (size_t)nxt.pm * pmstepA + nxt.ko : cA; const char* nB = has_next ? (const char*)g.Bt + (size_t)nxt.pn * tstep + nxt.ko : cB;
;         for (int t = 0; t < nt; t += 2) {
;             const bool last = (t == nt - 2); last_ = last && has_next;
;             const char* a1 = cA + (size_t)(t + 1) * kstep;
;             const char* a2 = last ? nA : cA + (size_t)(t + 2) * kstep; const char* b2 = last ? nB : cB + (size_t)(t + 2) * kstep;
;             const char* a3 = a2 + kstep; const char* b3 = b2 + kstep;
;             if (last && has_next) S.a_ready(nxt);
;             if constexpr (SP2) {
;             PG8_LDB(B0, 0, 0); PG8_LDB(B1, 0, 1); PG8_SCHED; PG8_LDA(At, 0, 0); PG8_STAGE_A(1, 1, a1, false);
;             PG8_WAIT_V(8); PG8_WAIT_L(0); PG8_BAR; PG8_MMA(0, 0, At, B0); PG8_MMA(0, 1, At, B1); PG8_BAR; PG8_SCHED;
;             PG8_LDA(At, 0, 1); PG8_STAGE(PG8_SB(0, 0), b2, voffB); PG8_STAGE(PG8_SB(0, 1), b2 + hstep, voffB); PG8_STAGE_A(0, 0, a2, true);
.LBB0_720:
	s_ashr_i32 s15, s14, 31
	s_lshl_b64 s[16:17], s[14:15], 19
	s_add_u32 s16, s86, s16
	s_addc_u32 s17, s87, s17
	s_and_b64 s[18:19], s[4:5], exec
	s_cselect_b32 s15, s17, s23
	s_cselect_b32 s56, s16, s22
	s_ashr_i32 s13, s12, 31
	s_lshl_b64 s[18:19], s[12:13], 19
	v_readlane_b32 s26, v254, 15
	v_readlane_b32 s27, v254, 16
	s_add_u32 s18, s26, s18
	s_addc_u32 s19, s27, s19
	s_and_b64 s[26:27], s[4:5], exec
	s_cselect_b32 s13, s19, s25
	s_cselect_b32 s57, s18, s24
	s_add_u32 s22, s22, 0x40080
	s_addc_u32 s23, s23, 0
	s_add_u32 s58, s24, 0x100
	s_addc_u32 s59, s25, 0
	s_mov_b32 s60, -2
	s_waitcnt vmcnt(0)
	v_lshl_add_u32 v130, s20, 8, v175
	v_ashrrev_i32_e32 v131, 31, v130
	v_lshlrev_b64 v[130:131], 6, v[130:131]
	v_lshl_add_u64 v[130:131], v[150:151], 0, v[130:131]
	global_load_dwordx4 v[238:241], v[130:131], off
	global_load_dwordx4 v[242:245], v[130:131], off offset:1024
	global_load_dwordx4 v[246:249], v[130:131], off offset:2048
	global_load_dwordx4 v[250:253], v[130:131], off offset:3072
	ds_read_b128 v[130:133], v187
	ds_read_b128 v[134:137], v187 offset:1024
	ds_read_b128 v[138:141], v187 offset:2048
	ds_read_b128 v[160:163], v187 offset:3072
	ds_read_b128 v[164:167], v188
	ds_read_b128 v[182:185], v188 offset:1024
	ds_read_b128 v[192:195], v188 offset:2048
	ds_read_b128 v[196:199], v188 offset:3072
	s_add_u32 s24, s22, 0xfffc0080
	s_addc_u32 s25, s23, -1
	s_cmp_eq_u32 s60, 12
	s_cselect_b32 s27, s15, s25
	s_cselect_b32 s26, s56, s24
	s_cselect_b32 s25, s13, s59
	s_cselect_b32 s24, s57, s58
	s_add_i32 m0, s29, 0xc000
	ds_read_b128 v[200:203], v189
	ds_read_b128 v[204:207], v189 offset:1024
	ds_read_b128 v[208:211], v189 offset:2048
	ds_read_b128 v[212:215], v189 offset:3072
	ds_read_b128 v[216:219], v189 offset:4096
	ds_read_b128 v[220:223], v189 offset:5120
	ds_read_b128 v[224:227], v189 offset:6144
	ds_read_b128 v[230:233], v189 offset:7168
	global_load_lds_dwordx4 v152, s[22:23]
	s_add_i32 m0, s29, 0xe000
	s_nop 0
	global_load_lds_dwordx4 v154, s[22:23]
	s_waitcnt vmcnt(8)
	s_waitcnt lgkmcnt(0)
	s_barrier
	s_setprio 3
	s_waitcnt lgkmcnt(0)
	v_mfma_f32_16x16x32_bf16 v[126:129], v[130:133], v[200:203], 0
	v_mfma_f32_16x16x32_bf16 v[122:125], v[138:141], v[200:203], 0
	v_mfma_f32_16x16x32_bf16 v[110:113], v[130:133], v[208:211], 0
	v_mfma_f32_16x16x32_bf16 v[106:109], v[138:141], v[208:211], 0
	v_mfma_f32_16x16x32_bf16 v[94:97], v[130:133], v[216:219], 0
	v_mfma_f32_16x16x32_bf16 v[90:93], v[138:141], v[216:219], 0
	v_mfma_f32_16x16x32_bf16 v[78:81], v[130:133], v[224:227], 0
	v_mfma_f32_16x16x32_bf16 v[74:77], v[138:141], v[224:227], 0
	v_mfma_f32_16x16x32_bf16 v[126:129], v[134:137], v[204:207], v[126:129]
	v_mfma_f32_16x16x32_bf16 v[122:125], v[160:163], v[204:207], v[122:125]
	v_mfma_f32_16x16x32_bf16 v[110:113], v[134:137], v[212:215], v[110:113]
	v_mfma_f32_16x16x32_bf16 v[106:109], v[160:163], v[212:215], v[106:109]
	v_mfma_f32_16x16x32_bf16 v[94:97], v[134:137], v[220:223], v[94:97]
	v_mfma_f32_16x16x32_bf16 v[90:93], v[160:163], v[220:223], v[90:93]
	v_mfma_f32_16x16x32_bf16 v[78:81], v[134:137], v[230:233], v[78:81]
	v_mfma_f32_16x16x32_bf16 v[74:77], v[160:163], v[230:233], v[74:77]
	s_setprio 0
	s_setprio 3
	v_mfma_f32_16x16x32_bf16 v[118:121], v[164:167], v[200:203], 0
	v_mfma_f32_16x16x32_bf16 v[114:117], v[192:195], v[200:203], 0
	v_mfma_f32_16x16x32_bf16 v[102:105], v[164:167], v[208:211], 0
	v_mfma_f32_16x16x32_bf16 v[98:101], v[192:195], v[208:211], 0
	v_mfma_f32_16x16x32_bf16 v[86:89], v[164:167], v[216:219], 0
	v_mfma_f32_16x16x32_bf16 v[82:85], v[192:195], v[216:219], 0
	v_mfma_f32_16x16x32_bf16 v[70:73], v[164:167], v[224:227], 0
	v_mfma_f32_16x16x32_bf16 v[66:69], v[192:195], v[224:227], 0
	v_mfma_f32_16x16x32_bf16 v[118:121], v[182:185], v[204:207], v[118:121]
	v_mfma_f32_16x16x32_bf16 v[114:117], v[196:199], v[204:207], v[114:117]
	v_mfma_f32_16x16x32_bf16 v[102:105], v[182:185], v[212:215], v[102:105]
	v_mfma_f32_16x16x32_bf16 v[98:101], v[196:199], v[212:215], v[98:101]
	v_mfma_f32_16x16x32_bf16 v[86:89], v[182:185], v[220:223], v[86:89]
	v_mfma_f32_16x16x32_bf16 v[82:85], v[196:199], v[220:223], v[82:85]
	v_mfma_f32_16x16x32_bf16 v[70:73], v[182:185], v[230:233], v[70:73]
	v_mfma_f32_16x16x32_bf16 v[66:69], v[196:199], v[230:233], v[66:69]
	s_setprio 0
	s_barrier
	s_add_i32 s61, s39, s2
	s_mov_b32 m0, s61
	ds_read_b128 v[200:203], v189 offset:16384
	ds_read_b128 v[204:207], v189 offset:17408
	ds_read_b128 v[208:211], v189 offset:18432
	ds_read_b128 v[212:215], v189 offset:19456
	ds_read_b128 v[216:219], v189 offset:20480
	ds_read_b128 v[220:223], v189 offset:21504
	ds_read_b128 v[224:227], v189 offset:22528
	ds_read_b128 v[230:233], v189 offset:23552
	global_load_lds_dwordx4 v146, s[24:25]
	s_add_i32 m0, s61, 0x2000
	s_add_u32 s62, s24, 0x40000
	s_addc_u32 s63, s25, 0
	s_add_i32 s61, s48, s2
	global_load_lds_dwordx4 v142, s[24:25]
	s_mov_b32 m0, s61
	s_mov_b64 s[98:99], s[26:27]
	global_load_lds_dwordx4 v146, s[62:63]
	s_add_i32 m0, s61, 0x2000
	s_nop 0
	global_load_lds_dwordx4 v142, s[62:63]
	s_mov_b32 m0, s29
	s_nop 0
	global_load_lds_dwordx4 v148, s[26:27]
	s_mov_b32 m0, s30
	s_nop 0
	global_load_lds_dwordx4 v144, s[26:27]
	s_waitcnt vmcnt(8)
	s_waitcnt lgkmcnt(0)
	s_barrier
; #define PG8_STAGE_A(b, h, ptr, NX) do { if constexpr (Sched::GATHER) { unsigned gs_[2]; gs_[0] = ((NX) && last_) ? gN[h][0] : gA[h][0]; gs_[1] = ((NX) && last_) ? gN[h][1] : gA[h][1]; PG8_STAGE(PG8_SA(b, h), ptr, gs_); } \
;         else PG8_STAGE(PG8_SA(b, h), (ptr) + ((h) ? hstep : (size_t)0), voffA); } while (0)
; #define PG8_STAGE(bufoff, gbase, voff) do { _Pragma("unroll") for (int _i = 0; _i < 2; ++_i) \
;         __builtin_amdgcn_global_load_lds((const unsigned*)((const char*)(gbase) + (voff)[_i]), (PG8_LAS unsigned*)(lds + (bufoff) + ldsw + _i * 8192), 16, 0, 0); } while (0)
; #define PG8_LDA(dst, b, h) do { _Pragma("unroll") for (int m = 0; m < 4; ++m) _Pragma("unroll") for (int k = 0; k < 2; ++k) dst[m][k] = *(const PG8_LAS bf16x8*)(lds + PG8_SA(b, h) + aoff + m * 2048 + k * 1024); } while (0)
; #define PG8_LDB(dst, b, h) do { _Pragma("unroll") for (int n = 0; n < 2; ++n) _Pragma("unroll") for (int k = 0; k < 2; ++k) dst[n][k] = *(const PG8_LAS bf16x8*)(lds + PG8_SB(b, h) + boff + n * 2048 + k * 1024); } while (0)
; #define PG8_MMA(ai, bj, At, Bt) do { __builtin_amdgcn_s_setprio(1); _Pragma("unroll") for (int m = 0; m < 4; ++m) _Pragma("unroll") for (int n = 0; n < 2; ++n) _Pragma("unroll") for (int k = 0; k < 2; ++k) \
;         acc[ai][bj][m][n] = __builtin_amdgcn_mfma_f32_16x16x32_bf16(Bt[n][k], At[m][k], acc[ai][bj][m][n], 0, 0, 0); __builtin_amdgcn_s_setprio(0); } while (0)
; #define PG8_WAIT_V(n) asm volatile("s_waitcnt vmcnt(" #n ")" ::: "memory")
; #define PG8_WAIT_L(n) asm volatile("s_waitcnt lgkmcnt(" #n ")" ::: "memory")
; #define PG8_BAR __builtin_amdgcn_s_barrier()
; #define PG8_SCHED __builtin_amdgcn_sched_barrier(0)
; template <class Epi, class Sched, bool ALIGN_EPI = false, bool SP2 = false>
; __device__ __forceinline__ void gemm_phase(PG8_LAS unsigned char* lds, const Gemm g, const Sched& S, const Epi& E, const bool skip_epi = false) {
;     ...
;             PG8_WAIT_V(8); PG8_WAIT_L(0); PG8_BAR; PG8_MMA(1, 0, At, B0); PG8_MMA(1, 1, At, B1); PG8_BAR; PG8_SCHED;
;             PG8_LDB(B0, 1, 0); PG8_LDB(B1, 1, 1); PG8_SCHED; PG8_LDA(At, 1, 0); PG8_STAGE_A(0, 1, a2, true);
;             PG8_WAIT_V(8); PG8_WAIT_L(0); PG8_BAR; PG8_MMA(0, 0, At, B0); PG8_MMA(0, 1, At, B1); PG8_BAR; PG8_SCHED;
;             PG8_LDA(At, 1, 1); PG8_STAGE(PG8_SB(1, 0), b3, voffB); PG8_STAGE(PG8_SB(1, 1), b3 + hstep, voffB); PG8_STAGE_A(1, 0, a3, true);
	s_setprio 3
	s_waitcnt lgkmcnt(0)
	v_mfma_f32_16x16x32_bf16 v[62:65], v[130:133], v[200:203], 0
	v_mfma_f32_16x16x32_bf16 v[58:61], v[138:141], v[200:203], 0
	v_mfma_f32_16x16x32_bf16 v[46:49], v[130:133], v[208:211], 0
	v_mfma_f32_16x16x32_bf16 v[42:45], v[138:141], v[208:211], 0
	v_mfma_f32_16x16x32_bf16 v[30:33], v[130:133], v[216:219], 0
	v_mfma_f32_16x16x32_bf16 v[26:29], v[138:141], v[216:219], 0
	v_mfma_f32_16x16x32_bf16 v[14:17], v[130:133], v[224:227], 0
	v_mfma_f32_16x16x32_bf16 v[10:13], v[138:141], v[224:227], 0
	v_mfma_f32_16x16x32_bf16 v[62:65], v[134:137], v[204:207], v[62:65]
	v_mfma_f32_16x16x32_bf16 v[58:61], v[160:163], v[204:207], v[58:61]
	v_mfma_f32_16x16x32_bf16 v[46:49], v[134:137], v[212:215], v[46:49]
	v_mfma_f32_16x16x32_bf16 v[42:45], v[160:163], v[212:215], v[42:45]
	v_mfma_f32_16x16x32_bf16 v[30:33], v[134:137], v[220:223], v[30:33]
	v_mfma_f32_16x16x32_bf16 v[26:29], v[160:163], v[220:223], v[26:29]
	v_mfma_f32_16x16x32_bf16 v[14:17], v[134:137], v[230:233], v[14:17]
	v_mfma_f32_16x16x32_bf16 v[10:13], v[160:163], v[230:233], v[10:13]
	s_setprio 0
	s_setprio 3
	v_mfma_f32_16x16x32_bf16 v[54:57], v[164:167], v[200:203], 0
	v_mfma_f32_16x16x32_bf16 v[50:53], v[192:195], v[200:203], 0
	v_mfma_f32_16x16x32_bf16 v[38:41], v[164:167], v[208:211], 0
	v_mfma_f32_16x16x32_bf16 v[34:37], v[192:195], v[208:211], 0
	v_mfma_f32_16x16x32_bf16 v[22:25], v[164:167], v[216:219], 0
	v_mfma_f32_16x16x32_bf16 v[18:21], v[192:195], v[216:219], 0
	v_mfma_f32_16x16x32_bf16 v[6:9], v[164:167], v[224:227], 0
	v_mfma_f32_16x16x32_bf16 v[2:5], v[192:195], v[224:227], 0
	v_mfma_f32_16x16x32_bf16 v[54:57], v[182:185], v[204:207], v[54:57]
	v_mfma_f32_16x16x32_bf16 v[50:53], v[196:199], v[204:207], v[50:53]
	v_mfma_f32_16x16x32_bf16 v[38:41], v[182:185], v[212:215], v[38:41]
	v_mfma_f32_16x16x32_bf16 v[34:37], v[196:199], v[212:215], v[34:37]
	v_mfma_f32_16x16x32_bf16 v[22:25], v[182:185], v[220:223], v[22:25]
	v_mfma_f32_16x16x32_bf16 v[18:21], v[196:199], v[220:223], v[18:21]
	v_mfma_f32_16x16x32_bf16 v[6:9], v[182:185], v[230:233], v[6:9]
	v_mfma_f32_16x16x32_bf16 v[2:5], v[196:199], v[230:233], v[2:5]
	s_setprio 0
	s_barrier
	s_add_i32 s61, 0, 0x18000
	s_add_i32 s62, 0, 0x1c000
	v_add_u32_e32 v160, s61, v1
	v_add_u32_e32 v170, s62, v1
	ds_read_b128 v[130:133], v160
	ds_read_b128 v[134:137], v160 offset:1024
	ds_read_b128 v[138:141], v160 offset:2048
	ds_read_b128 v[160:163], v160 offset:3072
	ds_read_b128 v[164:167], v170
	ds_read_b128 v[182:185], v170 offset:1024
	ds_read_b128 v[192:195], v170 offset:2048
	ds_read_b128 v[196:199], v170 offset:3072
	s_add_u32 s26, s26, 0x40000
	s_addc_u32 s27, s27, 0
	s_mov_b32 m0, s31
	ds_read_b128 v[200:203], v189 offset:32768
	ds_read_b128 v[204:207], v189 offset:33792
	ds_read_b128 v[208:211], v189 offset:34816
	ds_read_b128 v[212:215], v189 offset:35840
	ds_read_b128 v[216:219], v189 offset:36864
	ds_read_b128 v[220:223], v189 offset:37888
	ds_read_b128 v[224:227], v189 offset:38912
	ds_read_b128 v[230:233], v189 offset:39936
	global_load_lds_dwordx4 v148, s[26:27]
	s_mov_b32 m0, s34
	s_nop 0
	global_load_lds_dwordx4 v144, s[26:27]
	s_waitcnt vmcnt(8)
	s_waitcnt lgkmcnt(0)
	s_barrier
	s_setprio 3
	s_waitcnt lgkmcnt(0)
	v_mfma_f32_16x16x32_bf16 v[126:129], v[130:133], v[200:203], v[126:129]
	v_mfma_f32_16x16x32_bf16 v[122:125], v[138:141], v[200:203], v[122:125]
	v_mfma_f32_16x16x32_bf16 v[110:113], v[130:133], v[208:211], v[110:113]
	v_mfma_f32_16x16x32_bf16 v[106:109], v[138:141], v[208:211], v[106:109]
	v_mfma_f32_16x16x32_bf16 v[94:97], v[130:133], v[216:219], v[94:97]
	v_mfma_f32_16x16x32_bf16 v[90:93], v[138:141], v[216:219], v[90:93]
	v_mfma_f32_16x16x32_bf16 v[78:81], v[130:133], v[224:227], v[78:81]
	v_mfma_f32_16x16x32_bf16 v[74:77], v[138:141], v[224:227], v[74:77]
	v_mfma_f32_16x16x32_bf16 v[126:129], v[134:137], v[204:207], v[126:129]
	v_mfma_f32_16x16x32_bf16 v[122:125], v[160:163], v[204:207], v[122:125]
	v_mfma_f32_16x16x32_bf16 v[110:113], v[134:137], v[212:215], v[110:113]
	v_mfma_f32_16x16x32_bf16 v[106:109], v[160:163], v[212:215], v[106:109]
	v_mfma_f32_16x16x32_bf16 v[94:97], v[134:137], v[220:223], v[94:97]
	v_mfma_f32_16x16x32_bf16 v[90:93], v[160:163], v[220:223], v[90:93]
	v_mfma_f32_16x16x32_bf16 v[78:81], v[134:137], v[230:233], v[78:81]
	v_mfma_f32_16x16x32_bf16 v[74:77], v[160:163], v[230:233], v[74:77]
	s_setprio 0
	s_setprio 3
	v_mfma_f32_16x16x32_bf16 v[118:121], v[164:167], v[200:203], v[118:121]
	v_mfma_f32_16x16x32_bf16 v[114:117], v[192:195], v[200:203], v[114:117]
	v_mfma_f32_16x16x32_bf16 v[102:105], v[164:167], v[208:211], v[102:105]
	v_mfma_f32_16x16x32_bf16 v[98:101], v[192:195], v[208:211], v[98:101]
	v_mfma_f32_16x16x32_bf16 v[86:89], v[164:167], v[216:219], v[86:89]
	v_mfma_f32_16x16x32_bf16 v[82:85], v[192:195], v[216:219], v[82:85]
	v_mfma_f32_16x16x32_bf16 v[70:73], v[164:167], v[224:227], v[70:73]
	v_mfma_f32_16x16x32_bf16 v[66:69], v[192:195], v[224:227], v[66:69]
	v_mfma_f32_16x16x32_bf16 v[118:121], v[182:185], v[204:207], v[118:121]
	v_mfma_f32_16x16x32_bf16 v[114:117], v[196:199], v[204:207], v[114:117]
	v_mfma_f32_16x16x32_bf16 v[102:105], v[182:185], v[212:215], v[102:105]
	v_mfma_f32_16x16x32_bf16 v[98:101], v[196:199], v[212:215], v[98:101]
	v_mfma_f32_16x16x32_bf16 v[86:89], v[182:185], v[220:223], v[86:89]
	v_mfma_f32_16x16x32_bf16 v[82:85], v[196:199], v[220:223], v[82:85]
	v_mfma_f32_16x16x32_bf16 v[70:73], v[182:185], v[230:233], v[70:73]
	v_mfma_f32_16x16x32_bf16 v[66:69], v[196:199], v[230:233], v[66:69]
	s_setprio 0
	s_barrier
; #define PG8_STAGE_A(b, h, ptr, NX) do { if constexpr (Sched::GATHER) { unsigned gs_[2]; gs_[0] = ((NX) && last_) ? gN[h][0] : gA[h][0]; gs_[1] = ((NX) && last_) ? gN[h][1] : gA[h][1]; PG8_STAGE(PG8_SA(b, h), ptr, gs_); } \
;         else PG8_STAGE(PG8_SA(b, h), (ptr) + ((h) ? hstep : (size_t)0), voffA); } while (0)
; #define PG8_STAGE(bufoff, gbase, voff) do { _Pragma("unroll") for (int _i = 0; _i < 2; ++_i) \
;         __builtin_amdgcn_global_load_lds((const unsigned*)((const char*)(gbase) + (voff)[_i]), (PG8_LAS unsigned*)(lds + (bufoff) + ldsw + _i * 8192), 16, 0, 0); } while (0)
; #define PG8_LDA(dst, b, h) do { _Pragma("unroll") for (int m = 0; m < 4; ++m) _Pragma("unroll") for (int k = 0; k < 2; ++k) dst[m][k] = *(const PG8_LAS bf16x8*)(lds + PG8_SA(b, h) + aoff + m * 2048 + k * 1024); } while (0)
; #define PG8_LDB(dst, b, h) do { _Pragma("unroll") for (int n = 0; n < 2; ++n) _Pragma("unroll") for (int k = 0; k < 2; ++k) dst[n][k] = *(const PG8_LAS bf16x8*)(lds + PG8_SB(b, h) + boff + n * 2048 + k * 1024); } while (0)
; #define PG8_WAIT_V(n) asm volatile("s_waitcnt vmcnt(" #n ")" ::: "memory")
; #define PG8_WAIT_L(n) asm volatile("s_waitcnt lgkmcnt(" #n ")" ::: "memory")
; #define PG8_BAR __builtin_amdgcn_s_barrier()
; #define PG8_SCHED __builtin_amdgcn_sched_barrier(0)
; template <class Epi, class Sched, bool ALIGN_EPI = false, bool SP2 = false>
; __device__ __forceinline__ void gemm_phase(PG8_LAS unsigned char* lds, const Gemm g, const Sched& S, const Epi& E, const bool skip_epi = false) {
;     ...
;         for (int t = 0; t < nt; t += 2) {
;             const bool last = (t == nt - 2); last_ = last && has_next;
;             const char* a1 = cA + (size_t)(t + 1) * kstep;
;             const char* a2 = last ? nA : cA + (size_t)(t + 2) * kstep; const char* b2 = last ? nB : cB + (size_t)(t + 2) * kstep;
;             const char* a3 = a2 + kstep; const char* b3 = b2 + kstep;
;             if (last && has_next) S.a_ready(nxt);
;             if constexpr (SP2) {
;             PG8_LDB(B0, 0, 0); PG8_LDB(B1, 0, 1); PG8_SCHED; PG8_LDA(At, 0, 0); PG8_STAGE_A(1, 1, a1, false);
;     ...
;             PG8_LDA(At, 1, 1); PG8_STAGE(PG8_SB(1, 0), b3, voffB); PG8_STAGE(PG8_SB(1, 1), b3 + hstep, voffB); PG8_STAGE_A(1, 0, a3, true);
;             PG8_WAIT_V(8); PG8_WAIT_L(0); PG8_BAR; PG8_MMA(1, 0, At, B0); PG8_MMA(1, 1, At, B1); PG8_BAR; PG8_SCHED;
	s_add_i32 s26, s61, s2
	s_add_i32 m0, s26, 0xffffff80
	ds_read_b128 v[200:203], v189 offset:49152
	ds_read_b128 v[204:207], v189 offset:50176
	ds_read_b128 v[208:211], v189 offset:51200
	ds_read_b128 v[212:215], v189 offset:52224
	ds_read_b128 v[216:219], v189 offset:53248
	ds_read_b128 v[220:223], v189 offset:54272
	ds_read_b128 v[224:227], v189 offset:55296
	ds_read_b128 v[230:233], v189 offset:56320
	global_load_lds_dwordx4 v146, s[24:25] offset:128
	s_add_i32 m0, s26, 0x1f80
	s_add_i32 s26, s62, s2
	global_load_lds_dwordx4 v142, s[24:25] offset:128
	s_add_u32 s24, s24, 0x40080
	s_addc_u32 s25, s25, 0
	s_mov_b32 m0, s26
	s_nop 0
	global_load_lds_dwordx4 v146, s[24:25]
	s_add_i32 m0, s26, 0x2000
	s_nop 0
	global_load_lds_dwordx4 v142, s[24:25]
	s_add_i32 m0, s36, 0xffffff80
	s_nop 0
	global_load_lds_dwordx4 v148, s[98:99] offset:128
	s_add_i32 m0, s37, 0xffffff80
	s_nop 0
	global_load_lds_dwordx4 v144, s[98:99] offset:128
	s_waitcnt vmcnt(8)
	s_waitcnt lgkmcnt(0)
	s_barrier
	s_setprio 3
	s_waitcnt lgkmcnt(0)
	v_mfma_f32_16x16x32_bf16 v[62:65], v[130:133], v[200:203], v[62:65]
	v_mfma_f32_16x16x32_bf16 v[58:61], v[138:141], v[200:203], v[58:61]
	v_mfma_f32_16x16x32_bf16 v[46:49], v[130:133], v[208:211], v[46:49]
	v_mfma_f32_16x16x32_bf16 v[42:45], v[138:141], v[208:211], v[42:45]
	v_mfma_f32_16x16x32_bf16 v[30:33], v[130:133], v[216:219], v[30:33]
	v_mfma_f32_16x16x32_bf16 v[26:29], v[138:141], v[216:219], v[26:29]
	v_mfma_f32_16x16x32_bf16 v[14:17], v[130:133], v[224:227], v[14:17]
	v_mfma_f32_16x16x32_bf16 v[10:13], v[138:141], v[224:227], v[10:13]
	v_mfma_f32_16x16x32_bf16 v[62:65], v[134:137], v[204:207], v[62:65]
	v_mfma_f32_16x16x32_bf16 v[58:61], v[160:163], v[204:207], v[58:61]
	v_mfma_f32_16x16x32_bf16 v[46:49], v[134:137], v[212:215], v[46:49]
	v_mfma_f32_16x16x32_bf16 v[42:45], v[160:163], v[212:215], v[42:45]
	v_mfma_f32_16x16x32_bf16 v[30:33], v[134:137], v[220:223], v[30:33]
	v_mfma_f32_16x16x32_bf16 v[26:29], v[160:163], v[220:223], v[26:29]
	v_mfma_f32_16x16x32_bf16 v[14:17], v[134:137], v[230:233], v[14:17]
	v_mfma_f32_16x16x32_bf16 v[10:13], v[160:163], v[230:233], v[10:13]
	s_setprio 0
	s_setprio 3
	v_mfma_f32_16x16x32_bf16 v[54:57], v[164:167], v[200:203], v[54:57]
	v_mfma_f32_16x16x32_bf16 v[50:53], v[192:195], v[200:203], v[50:53]
	v_mfma_f32_16x16x32_bf16 v[38:41], v[164:167], v[208:211], v[38:41]
	v_mfma_f32_16x16x32_bf16 v[34:37], v[192:195], v[208:211], v[34:37]
	v_mfma_f32_16x16x32_bf16 v[22:25], v[164:167], v[216:219], v[22:25]
	v_mfma_f32_16x16x32_bf16 v[18:21], v[192:195], v[216:219], v[18:21]
	v_mfma_f32_16x16x32_bf16 v[6:9], v[164:167], v[224:227], v[6:9]
	v_mfma_f32_16x16x32_bf16 v[2:5], v[192:195], v[224:227], v[2:5]
	v_mfma_f32_16x16x32_bf16 v[54:57], v[182:185], v[204:207], v[54:57]
	v_mfma_f32_16x16x32_bf16 v[50:53], v[196:199], v[204:207], v[50:53]
	v_mfma_f32_16x16x32_bf16 v[38:41], v[182:185], v[212:215], v[38:41]
	v_mfma_f32_16x16x32_bf16 v[34:37], v[196:199], v[212:215], v[34:37]
	v_mfma_f32_16x16x32_bf16 v[22:25], v[182:185], v[220:223], v[22:25]
	v_mfma_f32_16x16x32_bf16 v[18:21], v[196:199], v[220:223], v[18:21]
	v_mfma_f32_16x16x32_bf16 v[6:9], v[182:185], v[230:233], v[6:9]
	v_mfma_f32_16x16x32_bf16 v[2:5], v[196:199], v[230:233], v[2:5]
	s_setprio 0
	s_barrier
	s_add_i32 s60, s60, 2
	s_add_u32 s22, s22, 0x100
	s_addc_u32 s23, s23, 0
	s_add_u32 s58, s58, 0x100
	s_addc_u32 s59, s59, 0
	s_cmp_gt_u32 s60, 13
.LBB0_721:
	ds_read_b128 v[130:133], v187
	ds_read_b128 v[134:137], v187 offset:1024
	ds_read_b128 v[138:141], v187 offset:2048
	ds_read_b128 v[160:163], v187 offset:3072
	ds_read_b128 v[164:167], v188
	ds_read_b128 v[182:185], v188 offset:1024
	ds_read_b128 v[192:195], v188 offset:2048
	ds_read_b128 v[196:199], v188 offset:3072
	s_add_u32 s24, s22, 0xfffc0080
	s_addc_u32 s25, s23, -1
	s_cmp_eq_u32 s60, 12
	s_cselect_b32 s27, s15, s25
	s_cselect_b32 s26, s56, s24
	s_cselect_b32 s25, s13, s59
	s_cselect_b32 s24, s57, s58
	s_add_i32 m0, s29, 0xc000
	ds_read_b128 v[200:203], v189
	ds_read_b128 v[204:207], v189 offset:1024
	ds_read_b128 v[208:211], v189 offset:2048
	ds_read_b128 v[212:215], v189 offset:3072
	ds_read_b128 v[216:219], v189 offset:4096
	ds_read_b128 v[220:223], v189 offset:5120
	ds_read_b128 v[224:227], v189 offset:6144
	ds_read_b128 v[230:233], v189 offset:7168
	global_load_lds_dwordx4 v152, s[22:23]
	s_add_i32 m0, s29, 0xe000
	s_nop 0
	global_load_lds_dwordx4 v154, s[22:23]
	s_waitcnt vmcnt(8)
	s_waitcnt lgkmcnt(0)
	s_barrier
; #define PG8_STAGE_A(b, h, ptr, NX) do { if constexpr (Sched::GATHER) { unsigned gs_[2]; gs_[0] = ((NX) && last_) ? gN[h][0] : gA[h][0]; gs_[1] = ((NX) && last_) ? gN[h][1] : gA[h][1]; PG8_STAGE(PG8_SA(b, h), ptr, gs_); } \
;         else PG8_STAGE(PG8_SA(b, h), (ptr) + ((h) ? hstep : (size_t)0), voffA); } while (0)
; #define PG8_STAGE(bufoff, gbase, voff) do { _Pragma("unroll") for (int _i = 0; _i < 2; ++_i) \
;         __builtin_amdgcn_global_load_lds((const unsigned*)((const char*)(gbase) + (voff)[_i]), (PG8_LAS unsigned*)(lds + (bufoff) + ldsw + _i * 8192), 16, 0, 0); } while (0)
; #define PG8_LDA(dst, b, h) do { _Pragma("unroll") for (int m = 0; m < 4; ++m) _Pragma("unroll") for (int k = 0; k < 2; ++k) dst[m][k] = *(const PG8_LAS bf16x8*)(lds + PG8_SA(b, h) + aoff + m * 2048 + k * 1024); } while (0)
; #define PG8_LDB(dst, b, h) do { _Pragma("unroll") for (int n = 0; n < 2; ++n) _Pragma("unroll") for (int k = 0; k < 2; ++k) dst[n][k] = *(const PG8_LAS bf16x8*)(lds + PG8_SB(b, h) + boff + n * 2048 + k * 1024); } while (0)
; #define PG8_MMA(ai, bj, At, Bt) do { __builtin_amdgcn_s_setprio(1); _Pragma("unroll") for (int m = 0; m < 4; ++m) _Pragma("unroll") for (int n = 0; n < 2; ++n) _Pragma("unroll") for (int k = 0; k < 2; ++k) \
;         acc[ai][bj][m][n] = __builtin_amdgcn_mfma_f32_16x16x32_bf16(Bt[n][k], At[m][k], acc[ai][bj][m][n], 0, 0, 0); __builtin_amdgcn_s_setprio(0); } while (0)
; #define PG8_WAIT_V(n) asm volatile("s_waitcnt vmcnt(" #n ")" ::: "memory")
; #define PG8_WAIT_L(n) asm volatile("s_waitcnt lgkmcnt(" #n ")" ::: "memory")
; #define PG8_BAR __builtin_amdgcn_s_barrier()
; #define PG8_SCHED __builtin_amdgcn_sched_barrier(0)
; template <class Epi, class Sched, bool ALIGN_EPI = false, bool SP2 = false>
; __device__ __forceinline__ void gemm_phase(PG8_LAS unsigned char* lds, const Gemm g, const Sched& S, const Epi& E, const bool skip_epi = false) {
;     ...
;             PG8_LDB(B0, 0, 0); PG8_LDB(B1, 0, 1); PG8_SCHED; PG8_LDA(At, 0, 0); PG8_STAGE_A(1, 1, a1, false);
;             PG8_WAIT_V(8); PG8_WAIT_L(0); PG8_BAR; PG8_MMA(0, 0, At, B0); PG8_MMA(0, 1, At, B1); PG8_BAR; PG8_SCHED;
;             PG8_LDA(At, 0, 1); PG8_STAGE(PG8_SB(0, 0), b2, voffB); PG8_STAGE(PG8_SB(0, 1), b2 + hstep, voffB); PG8_STAGE_A(0, 0, a2, true);
;             PG8_WAIT_V(8); PG8_WAIT_L(0); PG8_BAR; PG8_MMA(1, 0, At, B0); PG8_MMA(1, 1, At, B1); PG8_BAR; PG8_SCHED;
	s_setprio 3
	s_waitcnt lgkmcnt(0)
	v_mfma_f32_16x16x32_bf16 v[126:129], v[130:133], v[200:203], v[126:129]
	v_mfma_f32_16x16x32_bf16 v[122:125], v[138:141], v[200:203], v[122:125]
	v_mfma_f32_16x16x32_bf16 v[110:113], v[130:133], v[208:211], v[110:113]
	v_mfma_f32_16x16x32_bf16 v[106:109], v[138:141], v[208:211], v[106:109]
	v_mfma_f32_16x16x32_bf16 v[94:97], v[130:133], v[216:219], v[94:97]
	v_mfma_f32_16x16x32_bf16 v[90:93], v[138:141], v[216:219], v[90:93]
	v_mfma_f32_16x16x32_bf16 v[78:81], v[130:133], v[224:227], v[78:81]
	v_mfma_f32_16x16x32_bf16 v[74:77], v[138:141], v[224:227], v[74:77]
	v_mfma_f32_16x16x32_bf16 v[126:129], v[134:137], v[204:207], v[126:129]
	v_mfma_f32_16x16x32_bf16 v[122:125], v[160:163], v[204:207], v[122:125]
	v_mfma_f32_16x16x32_bf16 v[110:113], v[134:137], v[212:215], v[110:113]
	v_mfma_f32_16x16x32_bf16 v[106:109], v[160:163], v[212:215], v[106:109]
	v_mfma_f32_16x16x32_bf16 v[94:97], v[134:137], v[220:223], v[94:97]
	v_mfma_f32_16x16x32_bf16 v[90:93], v[160:163], v[220:223], v[90:93]
	v_mfma_f32_16x16x32_bf16 v[78:81], v[134:137], v[230:233], v[78:81]
	v_mfma_f32_16x16x32_bf16 v[74:77], v[160:163], v[230:233], v[74:77]
	s_setprio 0
	s_setprio 3
	v_mfma_f32_16x16x32_bf16 v[118:121], v[164:167], v[200:203], v[118:121]
	v_mfma_f32_16x16x32_bf16 v[114:117], v[192:195], v[200:203], v[114:117]
	v_mfma_f32_16x16x32_bf16 v[102:105], v[164:167], v[208:211], v[102:105]
	v_mfma_f32_16x16x32_bf16 v[98:101], v[192:195], v[208:211], v[98:101]
	v_mfma_f32_16x16x32_bf16 v[86:89], v[164:167], v[216:219], v[86:89]
	v_mfma_f32_16x16x32_bf16 v[82:85], v[192:195], v[216:219], v[82:85]
	v_mfma_f32_16x16x32_bf16 v[70:73], v[164:167], v[224:227], v[70:73]
	v_mfma_f32_16x16x32_bf16 v[66:69], v[192:195], v[224:227], v[66:69]
	v_mfma_f32_16x16x32_bf16 v[118:121], v[182:185], v[204:207], v[118:121]
	v_mfma_f32_16x16x32_bf16 v[114:117], v[196:199], v[204:207], v[114:117]
	v_mfma_f32_16x16x32_bf16 v[102:105], v[182:185], v[212:215], v[102:105]
	v_mfma_f32_16x16x32_bf16 v[98:101], v[196:199], v[212:215], v[98:101]
	v_mfma_f32_16x16x32_bf16 v[86:89], v[182:185], v[220:223], v[86:89]
	v_mfma_f32_16x16x32_bf16 v[82:85], v[196:199], v[220:223], v[82:85]
	v_mfma_f32_16x16x32_bf16 v[70:73], v[182:185], v[230:233], v[70:73]
	v_mfma_f32_16x16x32_bf16 v[66:69], v[196:199], v[230:233], v[66:69]
	s_setprio 0
	s_barrier
	s_add_i32 s61, s39, s2
	s_mov_b32 m0, s61
	ds_read_b128 v[200:203], v189 offset:16384
	ds_read_b128 v[204:207], v189 offset:17408
	ds_read_b128 v[208:211], v189 offset:18432
	ds_read_b128 v[212:215], v189 offset:19456
	ds_read_b128 v[216:219], v189 offset:20480
	ds_read_b128 v[220:223], v189 offset:21504
	ds_read_b128 v[224:227], v189 offset:22528
	ds_read_b128 v[230:233], v189 offset:23552
	global_load_lds_dwordx4 v146, s[24:25]
	s_add_i32 m0, s61, 0x2000
	s_add_u32 s62, s24, 0x40000
	s_addc_u32 s63, s25, 0
	s_add_i32 s61, s48, s2
	global_load_lds_dwordx4 v142, s[24:25]
	s_mov_b32 m0, s61
	s_mov_b64 s[98:99], s[26:27]
	global_load_lds_dwordx4 v146, s[62:63]
	s_add_i32 m0, s61, 0x2000
	s_nop 0
	global_load_lds_dwordx4 v142, s[62:63]
	s_mov_b32 m0, s29
	s_nop 0
	global_load_lds_dwordx4 v148, s[26:27]
	s_mov_b32 m0, s30
	s_nop 0
	global_load_lds_dwordx4 v144, s[26:27]
	s_waitcnt vmcnt(8)
	s_waitcnt lgkmcnt(0)
	s_barrier
	s_setprio 3
	s_waitcnt lgkmcnt(0)
	v_mfma_f32_16x16x32_bf16 v[62:65], v[130:133], v[200:203], v[62:65]
	v_mfma_f32_16x16x32_bf16 v[58:61], v[138:141], v[200:203], v[58:61]
	v_mfma_f32_16x16x32_bf16 v[46:49], v[130:133], v[208:211], v[46:49]
	v_mfma_f32_16x16x32_bf16 v[42:45], v[138:141], v[208:211], v[42:45]
	v_mfma_f32_16x16x32_bf16 v[30:33], v[130:133], v[216:219], v[30:33]
	v_mfma_f32_16x16x32_bf16 v[26:29], v[138:141], v[216:219], v[26:29]
	v_mfma_f32_16x16x32_bf16 v[14:17], v[130:133], v[224:227], v[14:17]
	v_mfma_f32_16x16x32_bf16 v[10:13], v[138:141], v[224:227], v[10:13]
	v_mfma_f32_16x16x32_bf16 v[62:65], v[134:137], v[204:207], v[62:65]
	v_mfma_f32_16x16x32_bf16 v[58:61], v[160:163], v[204:207], v[58:61]
	v_mfma_f32_16x16x32_bf16 v[46:49], v[134:137], v[212:215], v[46:49]
	v_mfma_f32_16x16x32_bf16 v[42:45], v[160:163], v[212:215], v[42:45]
	v_mfma_f32_16x16x32_bf16 v[30:33], v[134:137], v[220:223], v[30:33]
	v_mfma_f32_16x16x32_bf16 v[26:29], v[160:163], v[220:223], v[26:29]
	v_mfma_f32_16x16x32_bf16 v[14:17], v[134:137], v[230:233], v[14:17]
	v_mfma_f32_16x16x32_bf16 v[10:13], v[160:163], v[230:233], v[10:13]
	s_setprio 0
	s_setprio 3
	v_mfma_f32_16x16x32_bf16 v[54:57], v[164:167], v[200:203], v[54:57]
	v_mfma_f32_16x16x32_bf16 v[50:53], v[192:195], v[200:203], v[50:53]
	v_mfma_f32_16x16x32_bf16 v[38:41], v[164:167], v[208:211], v[38:41]
	v_mfma_f32_16x16x32_bf16 v[34:37], v[192:195], v[208:211], v[34:37]
	v_mfma_f32_16x16x32_bf16 v[22:25], v[164:167], v[216:219], v[22:25]
	v_mfma_f32_16x16x32_bf16 v[18:21], v[192:195], v[216:219], v[18:21]
	v_mfma_f32_16x16x32_bf16 v[6:9], v[164:167], v[224:227], v[6:9]
	v_mfma_f32_16x16x32_bf16 v[2:5], v[192:195], v[224:227], v[2:5]
	v_mfma_f32_16x16x32_bf16 v[54:57], v[182:185], v[204:207], v[54:57]
	v_mfma_f32_16x16x32_bf16 v[50:53], v[196:199], v[204:207], v[50:53]
	v_mfma_f32_16x16x32_bf16 v[38:41], v[182:185], v[212:215], v[38:41]
	v_mfma_f32_16x16x32_bf16 v[34:37], v[196:199], v[212:215], v[34:37]
	v_mfma_f32_16x16x32_bf16 v[22:25], v[182:185], v[220:223], v[22:25]
	v_mfma_f32_16x16x32_bf16 v[18:21], v[196:199], v[220:223], v[18:21]
	v_mfma_f32_16x16x32_bf16 v[6:9], v[182:185], v[230:233], v[6:9]
	v_mfma_f32_16x16x32_bf16 v[2:5], v[196:199], v[230:233], v[2:5]
	s_setprio 0
	s_barrier
; #define PG8_STAGE_A(b, h, ptr, NX) do { if constexpr (Sched::GATHER) { unsigned gs_[2]; gs_[0] = ((NX) && last_) ? gN[h][0] : gA[h][0]; gs_[1] = ((NX) && last_) ? gN[h][1] : gA[h][1]; PG8_STAGE(PG8_SA(b, h), ptr, gs_); } \
;         else PG8_STAGE(PG8_SA(b, h), (ptr) + ((h) ? hstep : (size_t)0), voffA); } while (0)
; #define PG8_STAGE(bufoff, gbase, voff) do { _Pragma("unroll") for (int _i = 0; _i < 2; ++_i) \
;         __builtin_amdgcn_global_load_lds((const unsigned*)((const char*)(gbase) + (voff)[_i]), (PG8_LAS unsigned*)(lds + (bufoff) + ldsw + _i * 8192), 16, 0, 0); } while (0)
; #define PG8_LDA(dst, b, h) do { _Pragma("unroll") for (int m = 0; m < 4; ++m) _Pragma("unroll") for (int k = 0; k < 2; ++k) dst[m][k] = *(const PG8_LAS bf16x8*)(lds + PG8_SA(b, h) + aoff + m * 2048 + k * 1024); } while (0)
; #define PG8_LDB(dst, b, h) do { _Pragma("unroll") for (int n = 0; n < 2; ++n) _Pragma("unroll") for (int k = 0; k < 2; ++k) dst[n][k] = *(const PG8_LAS bf16x8*)(lds + PG8_SB(b, h) + boff + n * 2048 + k * 1024); } while (0)
; #define PG8_MMA(ai, bj, At, Bt) do { __builtin_amdgcn_s_setprio(1); _Pragma("unroll") for (int m = 0; m < 4; ++m) _Pragma("unroll") for (int n = 0; n < 2; ++n) _Pragma("unroll") for (int k = 0; k < 2; ++k) \
;         acc[ai][bj][m][n] = __builtin_amdgcn_mfma_f32_16x16x32_bf16(Bt[n][k], At[m][k], acc[ai][bj][m][n], 0, 0, 0); __builtin_amdgcn_s_setprio(0); } while (0)
; #define PG8_WAIT_V(n) asm volatile("s_waitcnt vmcnt(" #n ")" ::: "memory")
; #define PG8_WAIT_L(n) asm volatile("s_waitcnt lgkmcnt(" #n ")" ::: "memory")
; #define PG8_BAR __builtin_amdgcn_s_barrier()
; template <class Epi, class Sched, bool ALIGN_EPI = false, bool SP2 = false>
; __device__ __forceinline__ void gemm_phase(PG8_LAS unsigned char* lds, const Gemm g, const Sched& S, const Epi& E, const bool skip_epi = false) {
;     ...
;             PG8_LDB(B0, 1, 0); PG8_LDB(B1, 1, 1); PG8_SCHED; PG8_LDA(At, 1, 0); PG8_STAGE_A(0, 1, a2, true);
;             PG8_WAIT_V(8); PG8_WAIT_L(0); PG8_BAR; PG8_MMA(0, 0, At, B0); PG8_MMA(0, 1, At, B1); PG8_BAR; PG8_SCHED;
;             PG8_LDA(At, 1, 1); PG8_STAGE(PG8_SB(1, 0), b3, voffB); PG8_STAGE(PG8_SB(1, 1), b3 + hstep, voffB); PG8_STAGE_A(1, 0, a3, true);
;             PG8_WAIT_V(8); PG8_WAIT_L(0); PG8_BAR; PG8_MMA(1, 0, At, B0); PG8_MMA(1, 1, At, B1); PG8_BAR; PG8_SCHED;
;     ...
;         if constexpr (ALIGN_EPI) { if (wr == 0) PG8_BAR; }
	s_add_i32 s61, 0, 0x18000
	s_add_i32 s62, 0, 0x1c000
	v_add_u32_e32 v160, s61, v1
	v_add_u32_e32 v170, s62, v1
	ds_read_b128 v[130:133], v160
	ds_read_b128 v[134:137], v160 offset:1024
	ds_read_b128 v[138:141], v160 offset:2048
	ds_read_b128 v[160:163], v160 offset:3072
	ds_read_b128 v[164:167], v170
	ds_read_b128 v[182:185], v170 offset:1024
	ds_read_b128 v[192:195], v170 offset:2048
	ds_read_b128 v[196:199], v170 offset:3072
	s_add_u32 s26, s26, 0x40000
	s_addc_u32 s27, s27, 0
	s_mov_b32 m0, s31
	ds_read_b128 v[200:203], v189 offset:32768
	ds_read_b128 v[204:207], v189 offset:33792
	ds_read_b128 v[208:211], v189 offset:34816
	ds_read_b128 v[212:215], v189 offset:35840
	ds_read_b128 v[216:219], v189 offset:36864
	ds_read_b128 v[220:223], v189 offset:37888
	ds_read_b128 v[224:227], v189 offset:38912
	ds_read_b128 v[230:233], v189 offset:39936
	global_load_lds_dwordx4 v148, s[26:27]
	s_mov_b32 m0, s34
	s_nop 0
	global_load_lds_dwordx4 v144, s[26:27]
	s_waitcnt vmcnt(8)
	s_waitcnt lgkmcnt(0)
	s_barrier
	s_setprio 3
	s_waitcnt lgkmcnt(0)
	v_mfma_f32_16x16x32_bf16 v[126:129], v[130:133], v[200:203], v[126:129]
	v_mfma_f32_16x16x32_bf16 v[122:125], v[138:141], v[200:203], v[122:125]
	v_mfma_f32_16x16x32_bf16 v[110:113], v[130:133], v[208:211], v[110:113]
	v_mfma_f32_16x16x32_bf16 v[106:109], v[138:141], v[208:211], v[106:109]
	v_mfma_f32_16x16x32_bf16 v[94:97], v[130:133], v[216:219], v[94:97]
	v_mfma_f32_16x16x32_bf16 v[90:93], v[138:141], v[216:219], v[90:93]
	v_mfma_f32_16x16x32_bf16 v[78:81], v[130:133], v[224:227], v[78:81]
	v_mfma_f32_16x16x32_bf16 v[74:77], v[138:141], v[224:227], v[74:77]
	v_mfma_f32_16x16x32_bf16 v[126:129], v[134:137], v[204:207], v[126:129]
	v_mfma_f32_16x16x32_bf16 v[122:125], v[160:163], v[204:207], v[122:125]
	v_mfma_f32_16x16x32_bf16 v[110:113], v[134:137], v[212:215], v[110:113]
	v_mfma_f32_16x16x32_bf16 v[106:109], v[160:163], v[212:215], v[106:109]
	v_mfma_f32_16x16x32_bf16 v[94:97], v[134:137], v[220:223], v[94:97]
	v_mfma_f32_16x16x32_bf16 v[90:93], v[160:163], v[220:223], v[90:93]
	v_mfma_f32_16x16x32_bf16 v[78:81], v[134:137], v[230:233], v[78:81]
	v_mfma_f32_16x16x32_bf16 v[74:77], v[160:163], v[230:233], v[74:77]
	s_setprio 0
	s_setprio 3
	v_mfma_f32_16x16x32_bf16 v[118:121], v[164:167], v[200:203], v[118:121]
	v_mfma_f32_16x16x32_bf16 v[114:117], v[192:195], v[200:203], v[114:117]
	v_mfma_f32_16x16x32_bf16 v[102:105], v[164:167], v[208:211], v[102:105]
	v_mfma_f32_16x16x32_bf16 v[98:101], v[192:195], v[208:211], v[98:101]
	v_mfma_f32_16x16x32_bf16 v[86:89], v[164:167], v[216:219], v[86:89]
	v_mfma_f32_16x16x32_bf16 v[82:85], v[192:195], v[216:219], v[82:85]
	v_mfma_f32_16x16x32_bf16 v[70:73], v[164:167], v[224:227], v[70:73]
	v_mfma_f32_16x16x32_bf16 v[66:69], v[192:195], v[224:227], v[66:69]
	v_mfma_f32_16x16x32_bf16 v[118:121], v[182:185], v[204:207], v[118:121]
	v_mfma_f32_16x16x32_bf16 v[114:117], v[196:199], v[204:207], v[114:117]
	v_mfma_f32_16x16x32_bf16 v[102:105], v[182:185], v[212:215], v[102:105]
	v_mfma_f32_16x16x32_bf16 v[98:101], v[196:199], v[212:215], v[98:101]
	v_mfma_f32_16x16x32_bf16 v[86:89], v[182:185], v[220:223], v[86:89]
	v_mfma_f32_16x16x32_bf16 v[82:85], v[196:199], v[220:223], v[82:85]
	v_mfma_f32_16x16x32_bf16 v[70:73], v[182:185], v[230:233], v[70:73]
	v_mfma_f32_16x16x32_bf16 v[66:69], v[196:199], v[230:233], v[66:69]
	s_setprio 0
	s_barrier
	s_add_i32 s26, s61, s2
	s_add_i32 m0, s26, 0xffffff80
	ds_read_b128 v[200:203], v189 offset:49152
	ds_read_b128 v[204:207], v189 offset:50176
	ds_read_b128 v[208:211], v189 offset:51200
	ds_read_b128 v[212:215], v189 offset:52224
	ds_read_b128 v[216:219], v189 offset:53248
	ds_read_b128 v[220:223], v189 offset:54272
	ds_read_b128 v[224:227], v189 offset:55296
	ds_read_b128 v[230:233], v189 offset:56320
	global_load_lds_dwordx4 v146, s[24:25] offset:128
	s_add_i32 m0, s26, 0x1f80
	s_add_i32 s26, s62, s2
	global_load_lds_dwordx4 v142, s[24:25] offset:128
	s_add_u32 s24, s24, 0x40080
	s_addc_u32 s25, s25, 0
	s_mov_b32 m0, s26
	s_nop 0
	global_load_lds_dwordx4 v146, s[24:25]
	s_add_i32 m0, s26, 0x2000
	s_nop 0
	global_load_lds_dwordx4 v142, s[24:25]
	s_add_i32 m0, s36, 0xffffff80
	s_nop 0
	global_load_lds_dwordx4 v148, s[98:99] offset:128
	s_add_i32 m0, s37, 0xffffff80
	s_nop 0
	global_load_lds_dwordx4 v144, s[98:99] offset:128
	s_waitcnt vmcnt(8)
	s_waitcnt lgkmcnt(0)
	s_barrier
	s_setprio 3
	s_waitcnt lgkmcnt(0)
	v_mfma_f32_16x16x32_bf16 v[62:65], v[130:133], v[200:203], v[62:65]
	v_mfma_f32_16x16x32_bf16 v[58:61], v[138:141], v[200:203], v[58:61]
	v_mfma_f32_16x16x32_bf16 v[46:49], v[130:133], v[208:211], v[46:49]
	v_mfma_f32_16x16x32_bf16 v[42:45], v[138:141], v[208:211], v[42:45]
	v_mfma_f32_16x16x32_bf16 v[30:33], v[130:133], v[216:219], v[30:33]
	v_mfma_f32_16x16x32_bf16 v[26:29], v[138:141], v[216:219], v[26:29]
	v_mfma_f32_16x16x32_bf16 v[14:17], v[130:133], v[224:227], v[14:17]
	v_mfma_f32_16x16x32_bf16 v[10:13], v[138:141], v[224:227], v[10:13]
	v_mfma_f32_16x16x32_bf16 v[62:65], v[134:137], v[204:207], v[62:65]
	v_mfma_f32_16x16x32_bf16 v[58:61], v[160:163], v[204:207], v[58:61]
	v_mfma_f32_16x16x32_bf16 v[46:49], v[134:137], v[212:215], v[46:49]
	v_mfma_f32_16x16x32_bf16 v[42:45], v[160:163], v[212:215], v[42:45]
	v_mfma_f32_16x16x32_bf16 v[30:33], v[134:137], v[220:223], v[30:33]
	v_mfma_f32_16x16x32_bf16 v[26:29], v[160:163], v[220:223], v[26:29]
	v_mfma_f32_16x16x32_bf16 v[14:17], v[134:137], v[230:233], v[14:17]
	v_mfma_f32_16x16x32_bf16 v[10:13], v[160:163], v[230:233], v[10:13]
	s_setprio 0
	s_setprio 3
	v_mfma_f32_16x16x32_bf16 v[54:57], v[164:167], v[200:203], v[54:57]
	v_mfma_f32_16x16x32_bf16 v[50:53], v[192:195], v[200:203], v[50:53]
	v_mfma_f32_16x16x32_bf16 v[38:41], v[164:167], v[208:211], v[38:41]
	v_mfma_f32_16x16x32_bf16 v[34:37], v[192:195], v[208:211], v[34:37]
	v_mfma_f32_16x16x32_bf16 v[22:25], v[164:167], v[216:219], v[22:25]
	v_mfma_f32_16x16x32_bf16 v[18:21], v[192:195], v[216:219], v[18:21]
	v_mfma_f32_16x16x32_bf16 v[6:9], v[164:167], v[224:227], v[6:9]
	v_mfma_f32_16x16x32_bf16 v[2:5], v[192:195], v[224:227], v[2:5]
	v_mfma_f32_16x16x32_bf16 v[54:57], v[182:185], v[204:207], v[54:57]
	v_mfma_f32_16x16x32_bf16 v[50:53], v[196:199], v[204:207], v[50:53]
	v_mfma_f32_16x16x32_bf16 v[38:41], v[182:185], v[212:215], v[38:41]
	v_mfma_f32_16x16x32_bf16 v[34:37], v[196:199], v[212:215], v[34:37]
	v_mfma_f32_16x16x32_bf16 v[22:25], v[182:185], v[220:223], v[22:25]
	v_mfma_f32_16x16x32_bf16 v[18:21], v[196:199], v[220:223], v[18:21]
	v_mfma_f32_16x16x32_bf16 v[6:9], v[182:185], v[230:233], v[6:9]
	v_mfma_f32_16x16x32_bf16 v[2:5], v[196:199], v[230:233], v[2:5]
	s_setprio 0
	s_barrier
	s_add_i32 s60, s60, 2
	s_add_u32 s22, s22, 0x100
	s_addc_u32 s23, s23, 0
	s_add_u32 s58, s58, 0x100
	s_addc_u32 s59, s59, 0
	s_cmp_gt_u32 s60, 13
	s_cbranch_scc0 .LBB0_721
	s_and_b64 vcc, exec, s[10:11]
	s_cbranch_vccz .LBB0_724
	s_barrier

; #define PG8_STAGE_A(b, h, ptr, NX) do { if constexpr (Sched::GATHER) { unsigned gs_[2]; gs_[0] = ((NX) && last_) ? gN[h][0] : gA[h][0]; gs_[1] = ((NX) && last_) ? gN[h][1] : gA[h][1]; PG8_STAGE(PG8_SA(b, h), ptr, gs_); } \
;         else PG8_STAGE(PG8_SA(b, h), (ptr) + ((h) ? hstep : (size_t)0), voffA); } while (0)
; #define PG8_STAGE(bufoff, gbase, voff) do { _Pragma("unroll") for (int _i = 0; _i < 2; ++_i) \
;         __builtin_amdgcn_global_load_lds((const unsigned*)((const char*)(gbase) + (voff)[_i]), (PG8_LAS unsigned*)(lds + (bufoff) + ldsw + _i * 8192), 16, 0, 0); } while (0)
; #define PG8_LDA(dst, b, h) do { _Pragma("unroll") for (int m = 0; m < 4; ++m) _Pragma("unroll") for (int k = 0; k < 2; ++k) dst[m][k] = *(const PG8_LAS bf16x8*)(lds + PG8_SA(b, h) + aoff + m * 2048 + k * 1024); } while (0)
; #define PG8_WAIT_V(n) asm volatile("s_waitcnt vmcnt(" #n ")" ::: "memory")
; #define PG8_WAIT_L(n) asm volatile("s_waitcnt lgkmcnt(" #n ")" ::: "memory")
; #define PG8_BAR __builtin_amdgcn_s_barrier()
; template <class Epi, class Sched, bool ALIGN_EPI = false, bool SP2 = false>
; __device__ __forceinline__ void gemm_phase(PG8_LAS unsigned char* lds, const Gemm g, const Sched& S, const Epi& E, const bool skip_epi = false) {
;     ...
;         const char* nA = has_next ? (const char*)g.A + (size_t)nxt.pm * pmstepA + nxt.ko : cA; const char* nB = has_next ? (const char*)g.Bt + (size_t)nxt.pn * tstep + nxt.ko : cB;
;         for (int t = 0; t < nt; t += 2) {
;             const bool last = (t == nt - 2); last_ = last && has_next;
;             const char* a1 = cA + (size_t)(t + 1) * kstep;
;             const char* a2 = last ? nA : cA + (size_t)(t + 2) * kstep; const char* b2 = last ? nB : cB + (size_t)(t + 2) * kstep;
;             const char* a3 = a2 + kstep; const char* b3 = b2 + kstep;
;             if (last && has_next) S.a_ready(nxt);
;             if constexpr (SP2) {
;             PG8_LDB(B0, 0, 0); PG8_LDB(B1, 0, 1); PG8_SCHED; PG8_LDA(At, 0, 0); PG8_STAGE_A(1, 1, a1, false);
;             PG8_WAIT_V(8); PG8_WAIT_L(0); PG8_BAR; PG8_MMA(0, 0, At, B0); PG8_MMA(0, 1, At, B1); PG8_BAR; PG8_SCHED;
;             PG8_LDA(At, 0, 1); PG8_STAGE(PG8_SB(0, 0), b2, voffB); PG8_STAGE(PG8_SB(0, 1), b2 + hstep, voffB); PG8_STAGE_A(0, 0, a2, true);
;             PG8_WAIT_V(8); PG8_WAIT_L(0); PG8_BAR; PG8_MMA(1, 0, At, B0); PG8_MMA(1, 1, At, B1); PG8_BAR; PG8_SCHED;
.LBB0_856:
	s_add_u32 s55, s22, 0x100
	s_addc_u32 s56, s23, 0
	s_mov_b32 s57, -2
	s_waitcnt vmcnt(0)
	s_waitcnt lgkmcnt(0)
	ds_read_b128 v[98:101], v234
	ds_read_b128 v[110:113], v234 offset:1024
	ds_read_b128 v[122:125], v234 offset:2048
	ds_read_b128 v[126:129], v234 offset:3072
	ds_read_b128 v[138:141], v235
	ds_read_b128 v[142:145], v235 offset:1024
	ds_read_b128 v[146:149], v235 offset:2048
	ds_read_b128 v[150:153], v235 offset:3072
	s_add_u32 s22, s20, 0x100
	s_addc_u32 s23, s21, 0
	s_cmp_eq_u32 s57, 40
	s_cselect_b32 s27, s9, s23
	s_cselect_b32 s26, s8, s22
	s_cselect_b32 s25, s19, s56
	s_cselect_b32 s24, s18, s55
	v_lshl_add_u64 v[210:211], s[20:21], 0, v[198:199]
	s_add_i32 m0, s3, 0xc000
	ds_read_b128 v[154:157], v236
	ds_read_b128 v[166:169], v236 offset:1024
	ds_read_b128 v[170:173], v236 offset:2048
	ds_read_b128 v[174:177], v236 offset:3072
	ds_read_b128 v[178:181], v236 offset:4096
	ds_read_b128 v[182:185], v236 offset:5120
	ds_read_b128 v[186:189], v236 offset:6144
	ds_read_b128 v[206:209], v236 offset:7168
	global_load_lds_dwordx4 v[210:211], off
	v_lshl_add_u64 v[210:211], s[20:21], 0, v[200:201]
	s_add_i32 m0, s3, 0xe000
	s_nop 0
	global_load_lds_dwordx4 v[210:211], off
	s_waitcnt vmcnt(8)
	s_waitcnt lgkmcnt(0)
	s_barrier
	s_setprio 3
	s_waitcnt lgkmcnt(0)
	v_mfma_f32_16x16x32_bf16 v[162:165], v[98:101], v[154:157], 0
	v_mfma_f32_16x16x32_bf16 v[158:161], v[122:125], v[154:157], 0
	v_mfma_f32_16x16x32_bf16 v[118:121], v[98:101], v[170:173], 0
	v_mfma_f32_16x16x32_bf16 v[114:117], v[122:125], v[170:173], 0
	v_mfma_f32_16x16x32_bf16 v[94:97], v[98:101], v[178:181], 0
	v_mfma_f32_16x16x32_bf16 v[90:93], v[122:125], v[178:181], 0
	v_mfma_f32_16x16x32_bf16 v[78:81], v[98:101], v[186:189], 0
	v_mfma_f32_16x16x32_bf16 v[74:77], v[122:125], v[186:189], 0
	v_mfma_f32_16x16x32_bf16 v[162:165], v[110:113], v[166:169], v[162:165]
	v_mfma_f32_16x16x32_bf16 v[158:161], v[126:129], v[166:169], v[158:161]
	v_mfma_f32_16x16x32_bf16 v[118:121], v[110:113], v[174:177], v[118:121]
	v_mfma_f32_16x16x32_bf16 v[114:117], v[126:129], v[174:177], v[114:117]
	v_mfma_f32_16x16x32_bf16 v[94:97], v[110:113], v[182:185], v[94:97]
	v_mfma_f32_16x16x32_bf16 v[90:93], v[126:129], v[182:185], v[90:93]
	v_mfma_f32_16x16x32_bf16 v[78:81], v[110:113], v[206:209], v[78:81]
	v_mfma_f32_16x16x32_bf16 v[74:77], v[126:129], v[206:209], v[74:77]
	s_setprio 0
	s_setprio 3
	v_mfma_f32_16x16x32_bf16 v[134:137], v[138:141], v[154:157], 0
	v_mfma_f32_16x16x32_bf16 v[130:133], v[146:149], v[154:157], 0
	v_mfma_f32_16x16x32_bf16 v[106:109], v[138:141], v[170:173], 0
	v_mfma_f32_16x16x32_bf16 v[102:105], v[146:149], v[170:173], 0
	v_mfma_f32_16x16x32_bf16 v[86:89], v[138:141], v[178:181], 0
	v_mfma_f32_16x16x32_bf16 v[82:85], v[146:149], v[178:181], 0
	v_mfma_f32_16x16x32_bf16 v[70:73], v[138:141], v[186:189], 0
	v_mfma_f32_16x16x32_bf16 v[66:69], v[146:149], v[186:189], 0
	v_mfma_f32_16x16x32_bf16 v[134:137], v[142:145], v[166:169], v[134:137]
	v_mfma_f32_16x16x32_bf16 v[130:133], v[150:153], v[166:169], v[130:133]
	v_mfma_f32_16x16x32_bf16 v[106:109], v[142:145], v[174:177], v[106:109]
	v_mfma_f32_16x16x32_bf16 v[102:105], v[150:153], v[174:177], v[102:105]
	v_mfma_f32_16x16x32_bf16 v[86:89], v[142:145], v[182:185], v[86:89]
	v_mfma_f32_16x16x32_bf16 v[82:85], v[150:153], v[182:185], v[82:85]
	v_mfma_f32_16x16x32_bf16 v[70:73], v[142:145], v[206:209], v[70:73]
	v_mfma_f32_16x16x32_bf16 v[66:69], v[150:153], v[206:209], v[66:69]
	s_setprio 0
	s_barrier
	s_add_i32 s20, s39, s2
	s_mov_b64 s[98:99], s[24:25]
	s_mov_b32 m0, s20
	ds_read_b128 v[154:157], v236 offset:16384
	ds_read_b128 v[166:169], v236 offset:17408
	ds_read_b128 v[170:173], v236 offset:18432
	ds_read_b128 v[174:177], v236 offset:19456
	ds_read_b128 v[178:181], v236 offset:20480
	ds_read_b128 v[182:185], v236 offset:21504
	ds_read_b128 v[186:189], v236 offset:22528
	ds_read_b128 v[206:209], v236 offset:23552
	global_load_lds_dwordx4 v192, s[24:25]
	s_add_i32 m0, s20, 0x2000
	s_add_u32 s20, s24, 0xb0000
	s_addc_u32 s21, s25, 0
	s_add_i32 s58, s48, s2
	global_load_lds_dwordx4 v196, s[24:25]
	s_mov_b32 m0, s58
	s_nop 0
	global_load_lds_dwordx4 v192, s[20:21]
	s_add_i32 m0, s58, 0x2000
	s_nop 0
	global_load_lds_dwordx4 v196, s[20:21]
	s_mov_b32 m0, s3
	s_nop 0
	global_load_lds_dwordx4 v190, s[26:27]
	s_mov_b32 m0, s28
	s_nop 0
	global_load_lds_dwordx4 v194, s[26:27]
	s_waitcnt vmcnt(8)
	s_waitcnt lgkmcnt(0)
	s_barrier
	s_setprio 3
	s_waitcnt lgkmcnt(0)
	v_mfma_f32_16x16x32_bf16 v[62:65], v[98:101], v[154:157], 0
	v_mfma_f32_16x16x32_bf16 v[58:61], v[122:125], v[154:157], 0
	v_mfma_f32_16x16x32_bf16 v[46:49], v[98:101], v[170:173], 0
	v_mfma_f32_16x16x32_bf16 v[42:45], v[122:125], v[170:173], 0
	v_mfma_f32_16x16x32_bf16 v[30:33], v[98:101], v[178:181], 0
	v_mfma_f32_16x16x32_bf16 v[26:29], v[122:125], v[178:181], 0
	v_mfma_f32_16x16x32_bf16 v[14:17], v[98:101], v[186:189], 0
	v_mfma_f32_16x16x32_bf16 v[10:13], v[122:125], v[186:189], 0
	v_mfma_f32_16x16x32_bf16 v[62:65], v[110:113], v[166:169], v[62:65]
	v_mfma_f32_16x16x32_bf16 v[58:61], v[126:129], v[166:169], v[58:61]
	v_mfma_f32_16x16x32_bf16 v[46:49], v[110:113], v[174:177], v[46:49]
	v_mfma_f32_16x16x32_bf16 v[42:45], v[126:129], v[174:177], v[42:45]
	v_mfma_f32_16x16x32_bf16 v[30:33], v[110:113], v[182:185], v[30:33]
	v_mfma_f32_16x16x32_bf16 v[26:29], v[126:129], v[182:185], v[26:29]
	v_mfma_f32_16x16x32_bf16 v[14:17], v[110:113], v[206:209], v[14:17]
	v_mfma_f32_16x16x32_bf16 v[10:13], v[126:129], v[206:209], v[10:13]
	s_setprio 0
	s_setprio 3
	v_mfma_f32_16x16x32_bf16 v[54:57], v[138:141], v[154:157], 0
	v_mfma_f32_16x16x32_bf16 v[50:53], v[146:149], v[154:157], 0
	v_mfma_f32_16x16x32_bf16 v[38:41], v[138:141], v[170:173], 0
	v_mfma_f32_16x16x32_bf16 v[34:37], v[146:149], v[170:173], 0
	v_mfma_f32_16x16x32_bf16 v[22:25], v[138:141], v[178:181], 0
	v_mfma_f32_16x16x32_bf16 v[18:21], v[146:149], v[178:181], 0
	v_mfma_f32_16x16x32_bf16 v[6:9], v[138:141], v[186:189], 0
	v_mfma_f32_16x16x32_bf16 v[2:5], v[146:149], v[186:189], 0
	v_mfma_f32_16x16x32_bf16 v[54:57], v[142:145], v[166:169], v[54:57]
	v_mfma_f32_16x16x32_bf16 v[50:53], v[150:153], v[166:169], v[50:53]
	v_mfma_f32_16x16x32_bf16 v[38:41], v[142:145], v[174:177], v[38:41]
	v_mfma_f32_16x16x32_bf16 v[34:37], v[150:153], v[174:177], v[34:37]
	v_mfma_f32_16x16x32_bf16 v[22:25], v[142:145], v[182:185], v[22:25]
	v_mfma_f32_16x16x32_bf16 v[18:21], v[150:153], v[182:185], v[18:21]
	v_mfma_f32_16x16x32_bf16 v[6:9], v[142:145], v[206:209], v[6:9]
	v_mfma_f32_16x16x32_bf16 v[2:5], v[150:153], v[206:209], v[2:5]
	s_setprio 0
	s_barrier
; #define PG8_STAGE_A(b, h, ptr, NX) do { if constexpr (Sched::GATHER) { unsigned gs_[2]; gs_[0] = ((NX) && last_) ? gN[h][0] : gA[h][0]; gs_[1] = ((NX) && last_) ? gN[h][1] : gA[h][1]; PG8_STAGE(PG8_SA(b, h), ptr, gs_); } \
;         else PG8_STAGE(PG8_SA(b, h), (ptr) + ((h) ? hstep : (size_t)0), voffA); } while (0)
; #define PG8_STAGE(bufoff, gbase, voff) do { _Pragma("unroll") for (int _i = 0; _i < 2; ++_i) \
;         __builtin_amdgcn_global_load_lds((const unsigned*)((const char*)(gbase) + (voff)[_i]), (PG8_LAS unsigned*)(lds + (bufoff) + ldsw + _i * 8192), 16, 0, 0); } while (0)
; #define PG8_LDA(dst, b, h) do { _Pragma("unroll") for (int m = 0; m < 4; ++m) _Pragma("unroll") for (int k = 0; k < 2; ++k) dst[m][k] = *(const PG8_LAS bf16x8*)(lds + PG8_SA(b, h) + aoff + m * 2048 + k * 1024); } while (0)
; #define PG8_LDB(dst, b, h) do { _Pragma("unroll") for (int n = 0; n < 2; ++n) _Pragma("unroll") for (int k = 0; k < 2; ++k) dst[n][k] = *(const PG8_LAS bf16x8*)(lds + PG8_SB(b, h) + boff + n * 2048 + k * 1024); } while (0)
; #define PG8_MMA(ai, bj, At, Bt) do { __builtin_amdgcn_s_setprio(1); _Pragma("unroll") for (int m = 0; m < 4; ++m) _Pragma("unroll") for (int n = 0; n < 2; ++n) _Pragma("unroll") for (int k = 0; k < 2; ++k) \
;         acc[ai][bj][m][n] = __builtin_amdgcn_mfma_f32_16x16x32_bf16(Bt[n][k], At[m][k], acc[ai][bj][m][n], 0, 0, 0); __builtin_amdgcn_s_setprio(0); } while (0)
; #define PG8_WAIT_V(n) asm volatile("s_waitcnt vmcnt(" #n ")" ::: "memory")
; #define PG8_WAIT_L(n) asm volatile("s_waitcnt lgkmcnt(" #n ")" ::: "memory")
; #define PG8_BAR __builtin_amdgcn_s_barrier()
; #define PG8_SCHED __builtin_amdgcn_sched_barrier(0)
; template <class Epi, class Sched, bool ALIGN_EPI = false, bool SP2 = false>
; __device__ __forceinline__ void gemm_phase(PG8_LAS unsigned char* lds, const Gemm g, const Sched& S, const Epi& E, const bool skip_epi = false) {
;     ...
;             PG8_LDB(B0, 1, 0); PG8_LDB(B1, 1, 1); PG8_SCHED; PG8_LDA(At, 1, 0); PG8_STAGE_A(0, 1, a2, true);
;             PG8_WAIT_V(8); PG8_WAIT_L(0); PG8_BAR; PG8_MMA(0, 0, At, B0); PG8_MMA(0, 1, At, B1); PG8_BAR; PG8_SCHED;
;             PG8_LDA(At, 1, 1); PG8_STAGE(PG8_SB(1, 0), b3, voffB); PG8_STAGE(PG8_SB(1, 1), b3 + hstep, voffB); PG8_STAGE_A(1, 0, a3, true);
;             PG8_WAIT_V(8); PG8_WAIT_L(0); PG8_BAR; PG8_MMA(1, 0, At, B0); PG8_MMA(1, 1, At, B1); PG8_BAR; PG8_SCHED;
	s_add_i32 s58, 0, 0x18000
	s_add_i32 s59, 0, 0x1c000
	v_add_u32_e32 v126, s58, v229
	v_add_u32_e32 v150, s59, v229
	ds_read_b128 v[98:101], v126
	ds_read_b128 v[110:113], v126 offset:1024
	ds_read_b128 v[122:125], v126 offset:2048
	ds_read_b128 v[126:129], v126 offset:3072
	ds_read_b128 v[138:141], v150
	ds_read_b128 v[142:145], v150 offset:1024
	ds_read_b128 v[146:149], v150 offset:2048
	ds_read_b128 v[150:153], v150 offset:3072
	s_add_u32 s20, s26, 0xb0000
	s_addc_u32 s21, s27, 0
	s_mov_b32 m0, s29
	ds_read_b128 v[154:157], v236 offset:32768
	ds_read_b128 v[166:169], v236 offset:33792
	ds_read_b128 v[170:173], v236 offset:34816
	ds_read_b128 v[174:177], v236 offset:35840
	ds_read_b128 v[178:181], v236 offset:36864
	ds_read_b128 v[182:185], v236 offset:37888
	ds_read_b128 v[186:189], v236 offset:38912
	ds_read_b128 v[206:209], v236 offset:39936
	global_load_lds_dwordx4 v190, s[20:21]
	s_mov_b32 m0, s30
	s_nop 0
	global_load_lds_dwordx4 v194, s[20:21]
	s_waitcnt vmcnt(8)
	s_waitcnt lgkmcnt(0)
	s_barrier
	s_setprio 3
	s_waitcnt lgkmcnt(0)
	v_mfma_f32_16x16x32_bf16 v[162:165], v[98:101], v[154:157], v[162:165]
	v_mfma_f32_16x16x32_bf16 v[158:161], v[122:125], v[154:157], v[158:161]
	v_mfma_f32_16x16x32_bf16 v[118:121], v[98:101], v[170:173], v[118:121]
	v_mfma_f32_16x16x32_bf16 v[114:117], v[122:125], v[170:173], v[114:117]
	v_mfma_f32_16x16x32_bf16 v[94:97], v[98:101], v[178:181], v[94:97]
	v_mfma_f32_16x16x32_bf16 v[90:93], v[122:125], v[178:181], v[90:93]
	v_mfma_f32_16x16x32_bf16 v[78:81], v[98:101], v[186:189], v[78:81]
	v_mfma_f32_16x16x32_bf16 v[74:77], v[122:125], v[186:189], v[74:77]
	v_mfma_f32_16x16x32_bf16 v[162:165], v[110:113], v[166:169], v[162:165]
	v_mfma_f32_16x16x32_bf16 v[158:161], v[126:129], v[166:169], v[158:161]
	v_mfma_f32_16x16x32_bf16 v[118:121], v[110:113], v[174:177], v[118:121]
	v_mfma_f32_16x16x32_bf16 v[114:117], v[126:129], v[174:177], v[114:117]
	v_mfma_f32_16x16x32_bf16 v[94:97], v[110:113], v[182:185], v[94:97]
	v_mfma_f32_16x16x32_bf16 v[90:93], v[126:129], v[182:185], v[90:93]
	v_mfma_f32_16x16x32_bf16 v[78:81], v[110:113], v[206:209], v[78:81]
	v_mfma_f32_16x16x32_bf16 v[74:77], v[126:129], v[206:209], v[74:77]
	s_setprio 0
	s_setprio 3
	v_mfma_f32_16x16x32_bf16 v[134:137], v[138:141], v[154:157], v[134:137]
	v_mfma_f32_16x16x32_bf16 v[130:133], v[146:149], v[154:157], v[130:133]
	v_mfma_f32_16x16x32_bf16 v[106:109], v[138:141], v[170:173], v[106:109]
	v_mfma_f32_16x16x32_bf16 v[102:105], v[146:149], v[170:173], v[102:105]
	v_mfma_f32_16x16x32_bf16 v[86:89], v[138:141], v[178:181], v[86:89]
	v_mfma_f32_16x16x32_bf16 v[82:85], v[146:149], v[178:181], v[82:85]
	v_mfma_f32_16x16x32_bf16 v[70:73], v[138:141], v[186:189], v[70:73]
	v_mfma_f32_16x16x32_bf16 v[66:69], v[146:149], v[186:189], v[66:69]
	v_mfma_f32_16x16x32_bf16 v[134:137], v[142:145], v[166:169], v[134:137]
	v_mfma_f32_16x16x32_bf16 v[130:133], v[150:153], v[166:169], v[130:133]
	v_mfma_f32_16x16x32_bf16 v[106:109], v[142:145], v[174:177], v[106:109]
	v_mfma_f32_16x16x32_bf16 v[102:105], v[150:153], v[174:177], v[102:105]
	v_mfma_f32_16x16x32_bf16 v[86:89], v[142:145], v[182:185], v[86:89]
	v_mfma_f32_16x16x32_bf16 v[82:85], v[150:153], v[182:185], v[82:85]
	v_mfma_f32_16x16x32_bf16 v[70:73], v[142:145], v[206:209], v[70:73]
	v_mfma_f32_16x16x32_bf16 v[66:69], v[150:153], v[206:209], v[66:69]
	s_setprio 0
	s_barrier
	s_add_i32 s20, s58, s2
	s_add_i32 m0, s20, 0xffffff80
	ds_read_b128 v[154:157], v236 offset:49152
	ds_read_b128 v[166:169], v236 offset:50176
	ds_read_b128 v[170:173], v236 offset:51200
	ds_read_b128 v[174:177], v236 offset:52224
	ds_read_b128 v[178:181], v236 offset:53248
	ds_read_b128 v[182:185], v236 offset:54272
	ds_read_b128 v[186:189], v236 offset:55296
	ds_read_b128 v[206:209], v236 offset:56320
	global_load_lds_dwordx4 v192, s[24:25] offset:128
	s_add_i32 m0, s20, 0x1f80
	s_add_u32 s20, s24, 0xb0080
	s_addc_u32 s21, s25, 0
	s_add_i32 s24, s59, s2
	global_load_lds_dwordx4 v196, s[98:99] offset:128
	s_mov_b32 m0, s24
	s_nop 0
	global_load_lds_dwordx4 v192, s[20:21]
	s_add_i32 m0, s24, 0x2000
	s_nop 0
	global_load_lds_dwordx4 v196, s[20:21]
	s_add_i32 m0, s35, 0xffffff80
	s_nop 0
	global_load_lds_dwordx4 v190, s[26:27] offset:128
	s_add_i32 m0, s36, 0xffffff80
	s_nop 0
	global_load_lds_dwordx4 v194, s[26:27] offset:128
	s_waitcnt vmcnt(8)
	s_waitcnt lgkmcnt(0)
	s_barrier
	s_setprio 3
	s_waitcnt lgkmcnt(0)
	v_mfma_f32_16x16x32_bf16 v[62:65], v[98:101], v[154:157], v[62:65]
	v_mfma_f32_16x16x32_bf16 v[58:61], v[122:125], v[154:157], v[58:61]
	v_mfma_f32_16x16x32_bf16 v[46:49], v[98:101], v[170:173], v[46:49]
	v_mfma_f32_16x16x32_bf16 v[42:45], v[122:125], v[170:173], v[42:45]
	v_mfma_f32_16x16x32_bf16 v[30:33], v[98:101], v[178:181], v[30:33]
	v_mfma_f32_16x16x32_bf16 v[26:29], v[122:125], v[178:181], v[26:29]
	v_mfma_f32_16x16x32_bf16 v[14:17], v[98:101], v[186:189], v[14:17]
	v_mfma_f32_16x16x32_bf16 v[10:13], v[122:125], v[186:189], v[10:13]
	v_mfma_f32_16x16x32_bf16 v[62:65], v[110:113], v[166:169], v[62:65]
	v_mfma_f32_16x16x32_bf16 v[58:61], v[126:129], v[166:169], v[58:61]
	v_mfma_f32_16x16x32_bf16 v[46:49], v[110:113], v[174:177], v[46:49]
	v_mfma_f32_16x16x32_bf16 v[42:45], v[126:129], v[174:177], v[42:45]
	v_mfma_f32_16x16x32_bf16 v[30:33], v[110:113], v[182:185], v[30:33]
	v_mfma_f32_16x16x32_bf16 v[26:29], v[126:129], v[182:185], v[26:29]
	v_mfma_f32_16x16x32_bf16 v[14:17], v[110:113], v[206:209], v[14:17]
	v_mfma_f32_16x16x32_bf16 v[10:13], v[126:129], v[206:209], v[10:13]
	s_setprio 0
	s_setprio 3
	v_mfma_f32_16x16x32_bf16 v[54:57], v[138:141], v[154:157], v[54:57]
	v_mfma_f32_16x16x32_bf16 v[50:53], v[146:149], v[154:157], v[50:53]
	v_mfma_f32_16x16x32_bf16 v[38:41], v[138:141], v[170:173], v[38:41]
	v_mfma_f32_16x16x32_bf16 v[34:37], v[146:149], v[170:173], v[34:37]
	v_mfma_f32_16x16x32_bf16 v[22:25], v[138:141], v[178:181], v[22:25]
	v_mfma_f32_16x16x32_bf16 v[18:21], v[146:149], v[178:181], v[18:21]
	v_mfma_f32_16x16x32_bf16 v[6:9], v[138:141], v[186:189], v[6:9]
	v_mfma_f32_16x16x32_bf16 v[2:5], v[146:149], v[186:189], v[2:5]
	v_mfma_f32_16x16x32_bf16 v[54:57], v[142:145], v[166:169], v[54:57]
	v_mfma_f32_16x16x32_bf16 v[50:53], v[150:153], v[166:169], v[50:53]
	v_mfma_f32_16x16x32_bf16 v[38:41], v[142:145], v[174:177], v[38:41]
	v_mfma_f32_16x16x32_bf16 v[34:37], v[150:153], v[174:177], v[34:37]
	v_mfma_f32_16x16x32_bf16 v[22:25], v[142:145], v[182:185], v[22:25]
	v_mfma_f32_16x16x32_bf16 v[18:21], v[150:153], v[182:185], v[18:21]
	v_mfma_f32_16x16x32_bf16 v[6:9], v[142:145], v[206:209], v[6:9]
	v_mfma_f32_16x16x32_bf16 v[2:5], v[150:153], v[206:209], v[2:5]
	s_setprio 0
	s_barrier
	s_add_i32 s57, s57, 2
	s_add_u32 s55, s55, 0x100
	s_addc_u32 s56, s56, 0
	s_cmp_gt_u32 s57, 41
	s_mov_b64 s[20:21], s[22:23]
; #define PG8_STAGE_A(b, h, ptr, NX) do { if constexpr (Sched::GATHER) { unsigned gs_[2]; gs_[0] = ((NX) && last_) ? gN[h][0] : gA[h][0]; gs_[1] = ((NX) && last_) ? gN[h][1] : gA[h][1]; PG8_STAGE(PG8_SA(b, h), ptr, gs_); } \
;         else PG8_STAGE(PG8_SA(b, h), (ptr) + ((h) ? hstep : (size_t)0), voffA); } while (0)
; #define PG8_STAGE(bufoff, gbase, voff) do { _Pragma("unroll") for (int _i = 0; _i < 2; ++_i) \
;         __builtin_amdgcn_global_load_lds((const unsigned*)((const char*)(gbase) + (voff)[_i]), (PG8_LAS unsigned*)(lds + (bufoff) + ldsw + _i * 8192), 16, 0, 0); } while (0)
; #define PG8_LDA(dst, b, h) do { _Pragma("unroll") for (int m = 0; m < 4; ++m) _Pragma("unroll") for (int k = 0; k < 2; ++k) dst[m][k] = *(const PG8_LAS bf16x8*)(lds + PG8_SA(b, h) + aoff + m * 2048 + k * 1024); } while (0)
; #define PG8_LDB(dst, b, h) do { _Pragma("unroll") for (int n = 0; n < 2; ++n) _Pragma("unroll") for (int k = 0; k < 2; ++k) dst[n][k] = *(const PG8_LAS bf16x8*)(lds + PG8_SB(b, h) + boff + n * 2048 + k * 1024); } while (0)
; #define PG8_WAIT_V(n) asm volatile("s_waitcnt vmcnt(" #n ")" ::: "memory")
; #define PG8_WAIT_L(n) asm volatile("s_waitcnt lgkmcnt(" #n ")" ::: "memory")
; template <class Epi, class Sched, bool ALIGN_EPI = false, bool SP2 = false>
; __device__ __forceinline__ void gemm_phase(PG8_LAS unsigned char* lds, const Gemm g, const Sched& S, const Epi& E, const bool skip_epi = false) {
;     ...
;         for (int t = 0; t < nt; t += 2) {
;             const bool last = (t == nt - 2); last_ = last && has_next;
;             const char* a1 = cA + (size_t)(t + 1) * kstep;
;             const char* a2 = last ? nA : cA + (size_t)(t + 2) * kstep; const char* b2 = last ? nB : cB + (size_t)(t + 2) * kstep;
;             const char* a3 = a2 + kstep; const char* b3 = b2 + kstep;
;             if (last && has_next) S.a_ready(nxt);
;             if constexpr (SP2) {
;             PG8_LDB(B0, 0, 0); PG8_LDB(B1, 0, 1); PG8_SCHED; PG8_LDA(At, 0, 0); PG8_STAGE_A(1, 1, a1, false);
;             PG8_WAIT_V(8); PG8_WAIT_L(0); PG8_BAR; PG8_MMA(0, 0, At, B0); PG8_MMA(0, 1, At, B1); PG8_BAR; PG8_SCHED;
;             PG8_LDA(At, 0, 1); PG8_STAGE(PG8_SB(0, 0), b2, voffB); PG8_STAGE(PG8_SB(0, 1), b2 + hstep, voffB); PG8_STAGE_A(0, 0, a2, true);
;             PG8_WAIT_V(8); PG8_WAIT_L(0); PG8_BAR; PG8_MMA(1, 0, At, B0); PG8_MMA(1, 1, At, B1); PG8_BAR; PG8_SCHED;
.LBB0_857:
	ds_read_b128 v[98:101], v234
	ds_read_b128 v[110:113], v234 offset:1024
	ds_read_b128 v[122:125], v234 offset:2048
	ds_read_b128 v[126:129], v234 offset:3072
	ds_read_b128 v[138:141], v235
	ds_read_b128 v[142:145], v235 offset:1024
	ds_read_b128 v[146:149], v235 offset:2048
	ds_read_b128 v[150:153], v235 offset:3072
	s_add_u32 s22, s20, 0x100
	s_addc_u32 s23, s21, 0
	s_cmp_eq_u32 s57, 40
	s_cselect_b32 s27, s9, s23
	s_cselect_b32 s26, s8, s22
	s_cselect_b32 s25, s19, s56
	s_cselect_b32 s24, s18, s55
	v_lshl_add_u64 v[210:211], s[20:21], 0, v[198:199]
	s_add_i32 m0, s3, 0xc000
	ds_read_b128 v[154:157], v236
	ds_read_b128 v[166:169], v236 offset:1024
	ds_read_b128 v[170:173], v236 offset:2048
	ds_read_b128 v[174:177], v236 offset:3072
	ds_read_b128 v[178:181], v236 offset:4096
	ds_read_b128 v[182:185], v236 offset:5120
	ds_read_b128 v[186:189], v236 offset:6144
	ds_read_b128 v[206:209], v236 offset:7168
	global_load_lds_dwordx4 v[210:211], off
	v_lshl_add_u64 v[210:211], s[20:21], 0, v[200:201]
	s_add_i32 m0, s3, 0xe000
	s_nop 0
	global_load_lds_dwordx4 v[210:211], off
	s_waitcnt vmcnt(8)
	s_waitcnt lgkmcnt(0)
	s_barrier
	s_setprio 3
	s_waitcnt lgkmcnt(0)
	v_mfma_f32_16x16x32_bf16 v[162:165], v[98:101], v[154:157], v[162:165]
	v_mfma_f32_16x16x32_bf16 v[158:161], v[122:125], v[154:157], v[158:161]
	v_mfma_f32_16x16x32_bf16 v[118:121], v[98:101], v[170:173], v[118:121]
	v_mfma_f32_16x16x32_bf16 v[114:117], v[122:125], v[170:173], v[114:117]
	v_mfma_f32_16x16x32_bf16 v[94:97], v[98:101], v[178:181], v[94:97]
	v_mfma_f32_16x16x32_bf16 v[90:93], v[122:125], v[178:181], v[90:93]
	v_mfma_f32_16x16x32_bf16 v[78:81], v[98:101], v[186:189], v[78:81]
	v_mfma_f32_16x16x32_bf16 v[74:77], v[122:125], v[186:189], v[74:77]
	v_mfma_f32_16x16x32_bf16 v[162:165], v[110:113], v[166:169], v[162:165]
	v_mfma_f32_16x16x32_bf16 v[158:161], v[126:129], v[166:169], v[158:161]
	v_mfma_f32_16x16x32_bf16 v[118:121], v[110:113], v[174:177], v[118:121]
	v_mfma_f32_16x16x32_bf16 v[114:117], v[126:129], v[174:177], v[114:117]
	v_mfma_f32_16x16x32_bf16 v[94:97], v[110:113], v[182:185], v[94:97]
	v_mfma_f32_16x16x32_bf16 v[90:93], v[126:129], v[182:185], v[90:93]
	v_mfma_f32_16x16x32_bf16 v[78:81], v[110:113], v[206:209], v[78:81]
	v_mfma_f32_16x16x32_bf16 v[74:77], v[126:129], v[206:209], v[74:77]
	s_setprio 0
	s_setprio 3
	v_mfma_f32_16x16x32_bf16 v[134:137], v[138:141], v[154:157], v[134:137]
	v_mfma_f32_16x16x32_bf16 v[130:133], v[146:149], v[154:157], v[130:133]
	v_mfma_f32_16x16x32_bf16 v[106:109], v[138:141], v[170:173], v[106:109]
	v_mfma_f32_16x16x32_bf16 v[102:105], v[146:149], v[170:173], v[102:105]
	v_mfma_f32_16x16x32_bf16 v[86:89], v[138:141], v[178:181], v[86:89]
	v_mfma_f32_16x16x32_bf16 v[82:85], v[146:149], v[178:181], v[82:85]
	v_mfma_f32_16x16x32_bf16 v[70:73], v[138:141], v[186:189], v[70:73]
	v_mfma_f32_16x16x32_bf16 v[66:69], v[146:149], v[186:189], v[66:69]
	v_mfma_f32_16x16x32_bf16 v[134:137], v[142:145], v[166:169], v[134:137]
	v_mfma_f32_16x16x32_bf16 v[130:133], v[150:153], v[166:169], v[130:133]
	v_mfma_f32_16x16x32_bf16 v[106:109], v[142:145], v[174:177], v[106:109]
	v_mfma_f32_16x16x32_bf16 v[102:105], v[150:153], v[174:177], v[102:105]
	v_mfma_f32_16x16x32_bf16 v[86:89], v[142:145], v[182:185], v[86:89]
	v_mfma_f32_16x16x32_bf16 v[82:85], v[150:153], v[182:185], v[82:85]
	v_mfma_f32_16x16x32_bf16 v[70:73], v[142:145], v[206:209], v[70:73]
	v_mfma_f32_16x16x32_bf16 v[66:69], v[150:153], v[206:209], v[66:69]
	s_setprio 0
	s_barrier
	s_add_i32 s20, s39, s2
	s_mov_b64 s[98:99], s[24:25]
	s_mov_b32 m0, s20
	ds_read_b128 v[154:157], v236 offset:16384
	ds_read_b128 v[166:169], v236 offset:17408
	ds_read_b128 v[170:173], v236 offset:18432
	ds_read_b128 v[174:177], v236 offset:19456
	ds_read_b128 v[178:181], v236 offset:20480
	ds_read_b128 v[182:185], v236 offset:21504
	ds_read_b128 v[186:189], v236 offset:22528
	ds_read_b128 v[206:209], v236 offset:23552
	global_load_lds_dwordx4 v192, s[24:25]
	s_add_i32 m0, s20, 0x2000
	s_add_u32 s20, s24, 0xb0000
	s_addc_u32 s21, s25, 0
	s_add_i32 s58, s48, s2
	global_load_lds_dwordx4 v196, s[24:25]
	s_mov_b32 m0, s58
	s_nop 0
	global_load_lds_dwordx4 v192, s[20:21]
	s_add_i32 m0, s58, 0x2000
	s_nop 0
	global_load_lds_dwordx4 v196, s[20:21]
	s_mov_b32 m0, s3
	s_nop 0
	global_load_lds_dwordx4 v190, s[26:27]
	s_mov_b32 m0, s28
	s_nop 0
	global_load_lds_dwordx4 v194, s[26:27]
	s_waitcnt vmcnt(8)
	s_waitcnt lgkmcnt(0)
	s_barrier
	s_setprio 3
	s_waitcnt lgkmcnt(0)
	v_mfma_f32_16x16x32_bf16 v[62:65], v[98:101], v[154:157], v[62:65]
	v_mfma_f32_16x16x32_bf16 v[58:61], v[122:125], v[154:157], v[58:61]
	v_mfma_f32_16x16x32_bf16 v[46:49], v[98:101], v[170:173], v[46:49]
	v_mfma_f32_16x16x32_bf16 v[42:45], v[122:125], v[170:173], v[42:45]
	v_mfma_f32_16x16x32_bf16 v[30:33], v[98:101], v[178:181], v[30:33]
	v_mfma_f32_16x16x32_bf16 v[26:29], v[122:125], v[178:181], v[26:29]
	v_mfma_f32_16x16x32_bf16 v[14:17], v[98:101], v[186:189], v[14:17]
	v_mfma_f32_16x16x32_bf16 v[10:13], v[122:125], v[186:189], v[10:13]
	v_mfma_f32_16x16x32_bf16 v[62:65], v[110:113], v[166:169], v[62:65]
	v_mfma_f32_16x16x32_bf16 v[58:61], v[126:129], v[166:169], v[58:61]
	v_mfma_f32_16x16x32_bf16 v[46:49], v[110:113], v[174:177], v[46:49]
	v_mfma_f32_16x16x32_bf16 v[42:45], v[126:129], v[174:177], v[42:45]
	v_mfma_f32_16x16x32_bf16 v[30:33], v[110:113], v[182:185], v[30:33]
	v_mfma_f32_16x16x32_bf16 v[26:29], v[126:129], v[182:185], v[26:29]
	v_mfma_f32_16x16x32_bf16 v[14:17], v[110:113], v[206:209], v[14:17]
	v_mfma_f32_16x16x32_bf16 v[10:13], v[126:129], v[206:209], v[10:13]
	s_setprio 0
	s_setprio 3
	v_mfma_f32_16x16x32_bf16 v[54:57], v[138:141], v[154:157], v[54:57]
	v_mfma_f32_16x16x32_bf16 v[50:53], v[146:149], v[154:157], v[50:53]
	v_mfma_f32_16x16x32_bf16 v[38:41], v[138:141], v[170:173], v[38:41]
	v_mfma_f32_16x16x32_bf16 v[34:37], v[146:149], v[170:173], v[34:37]
	v_mfma_f32_16x16x32_bf16 v[22:25], v[138:141], v[178:181], v[22:25]
	v_mfma_f32_16x16x32_bf16 v[18:21], v[146:149], v[178:181], v[18:21]
	v_mfma_f32_16x16x32_bf16 v[6:9], v[138:141], v[186:189], v[6:9]
	v_mfma_f32_16x16x32_bf16 v[2:5], v[146:149], v[186:189], v[2:5]
	v_mfma_f32_16x16x32_bf16 v[54:57], v[142:145], v[166:169], v[54:57]
	v_mfma_f32_16x16x32_bf16 v[50:53], v[150:153], v[166:169], v[50:53]
	v_mfma_f32_16x16x32_bf16 v[38:41], v[142:145], v[174:177], v[38:41]
	v_mfma_f32_16x16x32_bf16 v[34:37], v[150:153], v[174:177], v[34:37]
	v_mfma_f32_16x16x32_bf16 v[22:25], v[142:145], v[182:185], v[22:25]
	v_mfma_f32_16x16x32_bf16 v[18:21], v[150:153], v[182:185], v[18:21]
	v_mfma_f32_16x16x32_bf16 v[6:9], v[142:145], v[206:209], v[6:9]
	v_mfma_f32_16x16x32_bf16 v[2:5], v[150:153], v[206:209], v[2:5]
	s_setprio 0
	s_barrier
; #define PG8_STAGE_A(b, h, ptr, NX) do { if constexpr (Sched::GATHER) { unsigned gs_[2]; gs_[0] = ((NX) && last_) ? gN[h][0] : gA[h][0]; gs_[1] = ((NX) && last_) ? gN[h][1] : gA[h][1]; PG8_STAGE(PG8_SA(b, h), ptr, gs_); } \
;         else PG8_STAGE(PG8_SA(b, h), (ptr) + ((h) ? hstep : (size_t)0), voffA); } while (0)
; #define PG8_STAGE(bufoff, gbase, voff) do { _Pragma("unroll") for (int _i = 0; _i < 2; ++_i) \
;         __builtin_amdgcn_global_load_lds((const unsigned*)((const char*)(gbase) + (voff)[_i]), (PG8_LAS unsigned*)(lds + (bufoff) + ldsw + _i * 8192), 16, 0, 0); } while (0)
; #define PG8_LDA(dst, b, h) do { _Pragma("unroll") for (int m = 0; m < 4; ++m) _Pragma("unroll") for (int k = 0; k < 2; ++k) dst[m][k] = *(const PG8_LAS bf16x8*)(lds + PG8_SA(b, h) + aoff + m * 2048 + k * 1024); } while (0)
; #define PG8_LDB(dst, b, h) do { _Pragma("unroll") for (int n = 0; n < 2; ++n) _Pragma("unroll") for (int k = 0; k < 2; ++k) dst[n][k] = *(const PG8_LAS bf16x8*)(lds + PG8_SB(b, h) + boff + n * 2048 + k * 1024); } while (0)
; #define PG8_MMA(ai, bj, At, Bt) do { __builtin_amdgcn_s_setprio(1); _Pragma("unroll") for (int m = 0; m < 4; ++m) _Pragma("unroll") for (int n = 0; n < 2; ++n) _Pragma("unroll") for (int k = 0; k < 2; ++k) \
;         acc[ai][bj][m][n] = __builtin_amdgcn_mfma_f32_16x16x32_bf16(Bt[n][k], At[m][k], acc[ai][bj][m][n], 0, 0, 0); __builtin_amdgcn_s_setprio(0); } while (0)
; #define PG8_WAIT_V(n) asm volatile("s_waitcnt vmcnt(" #n ")" ::: "memory")
; #define PG8_WAIT_L(n) asm volatile("s_waitcnt lgkmcnt(" #n ")" ::: "memory")
; #define PG8_BAR __builtin_amdgcn_s_barrier()
; template <class Epi, class Sched, bool ALIGN_EPI = false, bool SP2 = false>
; __device__ __forceinline__ void gemm_phase(PG8_LAS unsigned char* lds, const Gemm g, const Sched& S, const Epi& E, const bool skip_epi = false) {
;     ...
;             PG8_LDB(B0, 1, 0); PG8_LDB(B1, 1, 1); PG8_SCHED; PG8_LDA(At, 1, 0); PG8_STAGE_A(0, 1, a2, true);
;             PG8_WAIT_V(8); PG8_WAIT_L(0); PG8_BAR; PG8_MMA(0, 0, At, B0); PG8_MMA(0, 1, At, B1); PG8_BAR; PG8_SCHED;
;             PG8_LDA(At, 1, 1); PG8_STAGE(PG8_SB(1, 0), b3, voffB); PG8_STAGE(PG8_SB(1, 1), b3 + hstep, voffB); PG8_STAGE_A(1, 0, a3, true);
;             PG8_WAIT_V(8); PG8_WAIT_L(0); PG8_BAR; PG8_MMA(1, 0, At, B0); PG8_MMA(1, 1, At, B1); PG8_BAR; PG8_SCHED;
;     ...
;         if constexpr (ALIGN_EPI) { if (wr == 0) PG8_BAR; }
	s_add_i32 s58, 0, 0x18000
	s_add_i32 s59, 0, 0x1c000
	v_add_u32_e32 v126, s58, v229
	v_add_u32_e32 v150, s59, v229
	ds_read_b128 v[98:101], v126
	ds_read_b128 v[110:113], v126 offset:1024
	ds_read_b128 v[122:125], v126 offset:2048
	ds_read_b128 v[126:129], v126 offset:3072
	ds_read_b128 v[138:141], v150
	ds_read_b128 v[142:145], v150 offset:1024
	ds_read_b128 v[146:149], v150 offset:2048
	ds_read_b128 v[150:153], v150 offset:3072
	s_add_u32 s20, s26, 0xb0000
	s_addc_u32 s21, s27, 0
	s_mov_b32 m0, s29
	ds_read_b128 v[154:157], v236 offset:32768
	ds_read_b128 v[166:169], v236 offset:33792
	ds_read_b128 v[170:173], v236 offset:34816
	ds_read_b128 v[174:177], v236 offset:35840
	ds_read_b128 v[178:181], v236 offset:36864
	ds_read_b128 v[182:185], v236 offset:37888
	ds_read_b128 v[186:189], v236 offset:38912
	ds_read_b128 v[206:209], v236 offset:39936
	global_load_lds_dwordx4 v190, s[20:21]
	s_mov_b32 m0, s30
	s_nop 0
	global_load_lds_dwordx4 v194, s[20:21]
	s_waitcnt vmcnt(8)
	s_waitcnt lgkmcnt(0)
	s_barrier
	s_setprio 3
	s_waitcnt lgkmcnt(0)
	v_mfma_f32_16x16x32_bf16 v[162:165], v[98:101], v[154:157], v[162:165]
	v_mfma_f32_16x16x32_bf16 v[158:161], v[122:125], v[154:157], v[158:161]
	v_mfma_f32_16x16x32_bf16 v[118:121], v[98:101], v[170:173], v[118:121]
	v_mfma_f32_16x16x32_bf16 v[114:117], v[122:125], v[170:173], v[114:117]
	v_mfma_f32_16x16x32_bf16 v[94:97], v[98:101], v[178:181], v[94:97]
	v_mfma_f32_16x16x32_bf16 v[90:93], v[122:125], v[178:181], v[90:93]
	v_mfma_f32_16x16x32_bf16 v[78:81], v[98:101], v[186:189], v[78:81]
	v_mfma_f32_16x16x32_bf16 v[74:77], v[122:125], v[186:189], v[74:77]
	v_mfma_f32_16x16x32_bf16 v[162:165], v[110:113], v[166:169], v[162:165]
	v_mfma_f32_16x16x32_bf16 v[158:161], v[126:129], v[166:169], v[158:161]
	v_mfma_f32_16x16x32_bf16 v[118:121], v[110:113], v[174:177], v[118:121]
	v_mfma_f32_16x16x32_bf16 v[114:117], v[126:129], v[174:177], v[114:117]
	v_mfma_f32_16x16x32_bf16 v[94:97], v[110:113], v[182:185], v[94:97]
	v_mfma_f32_16x16x32_bf16 v[90:93], v[126:129], v[182:185], v[90:93]
	v_mfma_f32_16x16x32_bf16 v[78:81], v[110:113], v[206:209], v[78:81]
	v_mfma_f32_16x16x32_bf16 v[74:77], v[126:129], v[206:209], v[74:77]
	s_setprio 0
	s_setprio 3
	v_mfma_f32_16x16x32_bf16 v[134:137], v[138:141], v[154:157], v[134:137]
	v_mfma_f32_16x16x32_bf16 v[130:133], v[146:149], v[154:157], v[130:133]
	v_mfma_f32_16x16x32_bf16 v[106:109], v[138:141], v[170:173], v[106:109]
	v_mfma_f32_16x16x32_bf16 v[102:105], v[146:149], v[170:173], v[102:105]
	v_mfma_f32_16x16x32_bf16 v[86:89], v[138:141], v[178:181], v[86:89]
	v_mfma_f32_16x16x32_bf16 v[82:85], v[146:149], v[178:181], v[82:85]
	v_mfma_f32_16x16x32_bf16 v[70:73], v[138:141], v[186:189], v[70:73]
	v_mfma_f32_16x16x32_bf16 v[66:69], v[146:149], v[186:189], v[66:69]
	v_mfma_f32_16x16x32_bf16 v[134:137], v[142:145], v[166:169], v[134:137]
	v_mfma_f32_16x16x32_bf16 v[130:133], v[150:153], v[166:169], v[130:133]
	v_mfma_f32_16x16x32_bf16 v[106:109], v[142:145], v[174:177], v[106:109]
	v_mfma_f32_16x16x32_bf16 v[102:105], v[150:153], v[174:177], v[102:105]
	v_mfma_f32_16x16x32_bf16 v[86:89], v[142:145], v[182:185], v[86:89]
	v_mfma_f32_16x16x32_bf16 v[82:85], v[150:153], v[182:185], v[82:85]
	v_mfma_f32_16x16x32_bf16 v[70:73], v[142:145], v[206:209], v[70:73]
	v_mfma_f32_16x16x32_bf16 v[66:69], v[150:153], v[206:209], v[66:69]
	s_setprio 0
	s_barrier
	s_add_i32 s20, s58, s2
	s_add_i32 m0, s20, 0xffffff80
	ds_read_b128 v[154:157], v236 offset:49152
	ds_read_b128 v[166:169], v236 offset:50176
	ds_read_b128 v[170:173], v236 offset:51200
	ds_read_b128 v[174:177], v236 offset:52224
	ds_read_b128 v[178:181], v236 offset:53248
	ds_read_b128 v[182:185], v236 offset:54272
	ds_read_b128 v[186:189], v236 offset:55296
	ds_read_b128 v[206:209], v236 offset:56320
	global_load_lds_dwordx4 v192, s[24:25] offset:128
	s_add_i32 m0, s20, 0x1f80
	s_add_u32 s20, s24, 0xb0080
	s_addc_u32 s21, s25, 0
	s_add_i32 s24, s59, s2
	global_load_lds_dwordx4 v196, s[98:99] offset:128
	s_mov_b32 m0, s24
	s_nop 0
	global_load_lds_dwordx4 v192, s[20:21]
	s_add_i32 m0, s24, 0x2000
	s_nop 0
	global_load_lds_dwordx4 v196, s[20:21]
	s_add_i32 m0, s35, 0xffffff80
	s_nop 0
	global_load_lds_dwordx4 v190, s[26:27] offset:128
	s_add_i32 m0, s36, 0xffffff80
	s_nop 0
	global_load_lds_dwordx4 v194, s[26:27] offset:128
	s_waitcnt vmcnt(8)
	s_waitcnt lgkmcnt(0)
	s_barrier
	s_setprio 3
	s_waitcnt lgkmcnt(0)
	v_mfma_f32_16x16x32_bf16 v[62:65], v[98:101], v[154:157], v[62:65]
	v_mfma_f32_16x16x32_bf16 v[58:61], v[122:125], v[154:157], v[58:61]
	v_mfma_f32_16x16x32_bf16 v[46:49], v[98:101], v[170:173], v[46:49]
	v_mfma_f32_16x16x32_bf16 v[42:45], v[122:125], v[170:173], v[42:45]
	v_mfma_f32_16x16x32_bf16 v[30:33], v[98:101], v[178:181], v[30:33]
	v_mfma_f32_16x16x32_bf16 v[26:29], v[122:125], v[178:181], v[26:29]
	v_mfma_f32_16x16x32_bf16 v[14:17], v[98:101], v[186:189], v[14:17]
	v_mfma_f32_16x16x32_bf16 v[10:13], v[122:125], v[186:189], v[10:13]
	v_mfma_f32_16x16x32_bf16 v[62:65], v[110:113], v[166:169], v[62:65]
	v_mfma_f32_16x16x32_bf16 v[58:61], v[126:129], v[166:169], v[58:61]
	v_mfma_f32_16x16x32_bf16 v[46:49], v[110:113], v[174:177], v[46:49]
	v_mfma_f32_16x16x32_bf16 v[42:45], v[126:129], v[174:177], v[42:45]
	v_mfma_f32_16x16x32_bf16 v[30:33], v[110:113], v[182:185], v[30:33]
	v_mfma_f32_16x16x32_bf16 v[26:29], v[126:129], v[182:185], v[26:29]
	v_mfma_f32_16x16x32_bf16 v[14:17], v[110:113], v[206:209], v[14:17]
	v_mfma_f32_16x16x32_bf16 v[10:13], v[126:129], v[206:209], v[10:13]
	s_setprio 0
	s_setprio 3
	v_mfma_f32_16x16x32_bf16 v[54:57], v[138:141], v[154:157], v[54:57]
	v_mfma_f32_16x16x32_bf16 v[50:53], v[146:149], v[154:157], v[50:53]
	v_mfma_f32_16x16x32_bf16 v[38:41], v[138:141], v[170:173], v[38:41]
	v_mfma_f32_16x16x32_bf16 v[34:37], v[146:149], v[170:173], v[34:37]
	v_mfma_f32_16x16x32_bf16 v[22:25], v[138:141], v[178:181], v[22:25]
	v_mfma_f32_16x16x32_bf16 v[18:21], v[146:149], v[178:181], v[18:21]
	v_mfma_f32_16x16x32_bf16 v[6:9], v[138:141], v[186:189], v[6:9]
	v_mfma_f32_16x16x32_bf16 v[2:5], v[146:149], v[186:189], v[2:5]
	v_mfma_f32_16x16x32_bf16 v[54:57], v[142:145], v[166:169], v[54:57]
	v_mfma_f32_16x16x32_bf16 v[50:53], v[150:153], v[166:169], v[50:53]
	v_mfma_f32_16x16x32_bf16 v[38:41], v[142:145], v[174:177], v[38:41]
	v_mfma_f32_16x16x32_bf16 v[34:37], v[150:153], v[174:177], v[34:37]
	v_mfma_f32_16x16x32_bf16 v[22:25], v[142:145], v[182:185], v[22:25]
	v_mfma_f32_16x16x32_bf16 v[18:21], v[150:153], v[182:185], v[18:21]
	v_mfma_f32_16x16x32_bf16 v[6:9], v[142:145], v[206:209], v[6:9]
	v_mfma_f32_16x16x32_bf16 v[2:5], v[150:153], v[206:209], v[2:5]
	s_setprio 0
	s_barrier
	s_add_i32 s57, s57, 2
	s_add_u32 s55, s55, 0x100
	s_addc_u32 s56, s56, 0
	s_cmp_gt_u32 s57, 41
	s_mov_b64 s[20:21], s[22:23]
	s_cbranch_scc0 .LBB0_857
	s_and_b64 vcc, exec, s[16:17]
	s_cbranch_vccz .LBB0_860
	s_barrier

; #define PG8_STAGE_A(b, h, ptr, NX) do { if constexpr (Sched::GATHER) { unsigned gs_[2]; gs_[0] = ((NX) && last_) ? gN[h][0] : gA[h][0]; gs_[1] = ((NX) && last_) ? gN[h][1] : gA[h][1]; PG8_STAGE(PG8_SA(b, h), ptr, gs_); } \
;         else PG8_STAGE(PG8_SA(b, h), (ptr) + ((h) ? hstep : (size_t)0), voffA); } while (0)
; #define PG8_STAGE(bufoff, gbase, voff) do { _Pragma("unroll") for (int _i = 0; _i < 2; ++_i) \
;         __builtin_amdgcn_global_load_lds((const unsigned*)((const char*)(gbase) + (voff)[_i]), (PG8_LAS unsigned*)(lds + (bufoff) + ldsw + _i * 8192), 16, 0, 0); } while (0)
; #define PG8_LDA(dst, b, h) do { _Pragma("unroll") for (int m = 0; m < 4; ++m) _Pragma("unroll") for (int k = 0; k < 2; ++k) dst[m][k] = *(const PG8_LAS bf16x8*)(lds + PG8_SA(b, h) + aoff + m * 2048 + k * 1024); } while (0)
; #define PG8_LDB(dst, b, h) do { _Pragma("unroll") for (int n = 0; n < 2; ++n) _Pragma("unroll") for (int k = 0; k < 2; ++k) dst[n][k] = *(const PG8_LAS bf16x8*)(lds + PG8_SB(b, h) + boff + n * 2048 + k * 1024); } while (0)
; #define PG8_WAIT_V(n) asm volatile("s_waitcnt vmcnt(" #n ")" ::: "memory")
; template <class Epi, class Sched, bool ALIGN_EPI = false, bool SP2 = false>
; __device__ __forceinline__ void gemm_phase(PG8_LAS unsigned char* lds, const Gemm g, const Sched& S, const Epi& E, const bool skip_epi = false) {
;     ...
;         const char* nA = has_next ? (const char*)g.A + (size_t)nxt.pm * pmstepA + nxt.ko : cA; const char* nB = has_next ? (const char*)g.Bt + (size_t)nxt.pn * tstep + nxt.ko : cB;
;         for (int t = 0; t < nt; t += 2) {
;             const bool last = (t == nt - 2); last_ = last && has_next;
;             const char* a1 = cA + (size_t)(t + 1) * kstep;
;             const char* a2 = last ? nA : cA + (size_t)(t + 2) * kstep; const char* b2 = last ? nB : cB + (size_t)(t + 2) * kstep;
;             const char* a3 = a2 + kstep; const char* b3 = b2 + kstep;
;             if (last && has_next) S.a_ready(nxt);
;             if constexpr (SP2) {
;             PG8_LDB(B0, 0, 0); PG8_LDB(B1, 0, 1); PG8_SCHED; PG8_LDA(At, 0, 0); PG8_STAGE_A(1, 1, a1, false);
;             PG8_WAIT_V(8); PG8_WAIT_L(0); PG8_BAR; PG8_MMA(0, 0, At, B0); PG8_MMA(0, 1, At, B1); PG8_BAR; PG8_SCHED;
;             PG8_LDA(At, 0, 1); PG8_STAGE(PG8_SB(0, 0), b2, voffB); PG8_STAGE(PG8_SB(0, 1), b2 + hstep, voffB); PG8_STAGE_A(0, 0, a2, true);
.LBB0_943:
	s_ashr_i32 s15, s14, 31
	s_lshl_b64 s[16:17], s[14:15], 19
	s_add_u32 s16, s86, s16
	s_addc_u32 s17, s87, s17
	s_and_b64 s[18:19], s[4:5], exec
	s_cselect_b32 s15, s17, s23
	s_cselect_b32 s54, s16, s22
	s_ashr_i32 s13, s12, 31
	s_lshl_b64 s[18:19], s[12:13], 19
	s_add_u32 s18, s2, s18
	s_addc_u32 s19, s3, s19
	s_and_b64 s[26:27], s[4:5], exec
	s_cselect_b32 s13, s19, s25
	s_cselect_b32 s55, s18, s24
	s_add_u32 s22, s22, 0x40080
	s_addc_u32 s23, s23, 0
	s_add_u32 s56, s24, 0x100
	s_addc_u32 s57, s25, 0
	s_mov_b32 s58, -2
	s_waitcnt vmcnt(0)
	ds_read_b128 v[148:151], v170
	ds_read_b128 v[152:155], v170 offset:1024
	ds_read_b128 v[156:159], v170 offset:2048
	ds_read_b128 v[160:163], v170 offset:3072
	ds_read_b128 v[176:179], v171
	ds_read_b128 v[180:183], v171 offset:1024
	ds_read_b128 v[184:187], v171 offset:2048
	ds_read_b128 v[188:191], v171 offset:3072
	s_add_u32 s24, s22, 0xfffc0080
	s_addc_u32 s25, s23, -1
	s_cmp_eq_u32 s58, 12
	s_cselect_b32 s27, s15, s25
	s_cselect_b32 s26, s54, s24
	s_cselect_b32 s25, s13, s57
	s_cselect_b32 s24, s55, s56
	s_add_i32 m0, s21, 0xc000
	ds_read_b128 v[192:195], v172
	ds_read_b128 v[196:199], v172 offset:1024
	ds_read_b128 v[200:203], v172 offset:2048
	ds_read_b128 v[204:207], v172 offset:3072
	ds_read_b128 v[208:211], v172 offset:4096
	ds_read_b128 v[212:215], v172 offset:5120
	ds_read_b128 v[216:219], v172 offset:6144
	ds_read_b128 v[220:223], v172 offset:7168
	global_load_lds_dwordx4 v140, s[22:23]
	s_add_i32 m0, s21, 0xe000
	s_nop 0
	global_load_lds_dwordx4 v142, s[22:23]
	s_waitcnt vmcnt(8)
	s_waitcnt lgkmcnt(0)
	s_barrier
	s_setprio 3
	s_waitcnt lgkmcnt(0)
	v_mfma_f32_16x16x32_bf16 v[126:129], v[148:151], v[192:195], 0
	v_mfma_f32_16x16x32_bf16 v[122:125], v[156:159], v[192:195], 0
	v_mfma_f32_16x16x32_bf16 v[114:117], v[148:151], v[200:203], 0
	v_mfma_f32_16x16x32_bf16 v[106:109], v[156:159], v[200:203], 0
	v_mfma_f32_16x16x32_bf16 v[98:101], v[148:151], v[208:211], 0
	v_mfma_f32_16x16x32_bf16 v[90:93], v[156:159], v[208:211], 0
	v_mfma_f32_16x16x32_bf16 v[82:85], v[148:151], v[216:219], 0
	v_mfma_f32_16x16x32_bf16 v[74:77], v[156:159], v[216:219], 0
	v_mfma_f32_16x16x32_bf16 v[126:129], v[152:155], v[196:199], v[126:129]
	v_mfma_f32_16x16x32_bf16 v[122:125], v[160:163], v[196:199], v[122:125]
	v_mfma_f32_16x16x32_bf16 v[114:117], v[152:155], v[204:207], v[114:117]
	v_mfma_f32_16x16x32_bf16 v[106:109], v[160:163], v[204:207], v[106:109]
	v_mfma_f32_16x16x32_bf16 v[98:101], v[152:155], v[212:215], v[98:101]
	v_mfma_f32_16x16x32_bf16 v[90:93], v[160:163], v[212:215], v[90:93]
	v_mfma_f32_16x16x32_bf16 v[82:85], v[152:155], v[220:223], v[82:85]
	v_mfma_f32_16x16x32_bf16 v[74:77], v[160:163], v[220:223], v[74:77]
	s_setprio 0
	s_setprio 3
	v_mfma_f32_16x16x32_bf16 v[118:121], v[176:179], v[192:195], 0
	v_mfma_f32_16x16x32_bf16 v[110:113], v[184:187], v[192:195], 0
	v_mfma_f32_16x16x32_bf16 v[102:105], v[176:179], v[200:203], 0
	v_mfma_f32_16x16x32_bf16 v[94:97], v[184:187], v[200:203], 0
	v_mfma_f32_16x16x32_bf16 v[86:89], v[176:179], v[208:211], 0
	v_mfma_f32_16x16x32_bf16 v[78:81], v[184:187], v[208:211], 0
	v_mfma_f32_16x16x32_bf16 v[70:73], v[176:179], v[216:219], 0
	v_mfma_f32_16x16x32_bf16 v[66:69], v[184:187], v[216:219], 0
	v_mfma_f32_16x16x32_bf16 v[118:121], v[180:183], v[196:199], v[118:121]
	v_mfma_f32_16x16x32_bf16 v[110:113], v[188:191], v[196:199], v[110:113]
	v_mfma_f32_16x16x32_bf16 v[102:105], v[180:183], v[204:207], v[102:105]
	v_mfma_f32_16x16x32_bf16 v[94:97], v[188:191], v[204:207], v[94:97]
	v_mfma_f32_16x16x32_bf16 v[86:89], v[180:183], v[212:215], v[86:89]
	v_mfma_f32_16x16x32_bf16 v[78:81], v[188:191], v[212:215], v[78:81]
	v_mfma_f32_16x16x32_bf16 v[70:73], v[180:183], v[220:223], v[70:73]
	v_mfma_f32_16x16x32_bf16 v[66:69], v[188:191], v[220:223], v[66:69]
	s_setprio 0
	s_barrier
	s_add_i32 s59, s48, s28
	s_mov_b32 m0, s59
	ds_read_b128 v[192:195], v172 offset:16384
	ds_read_b128 v[196:199], v172 offset:17408
	ds_read_b128 v[200:203], v172 offset:18432
	ds_read_b128 v[204:207], v172 offset:19456
	ds_read_b128 v[208:211], v172 offset:20480
	ds_read_b128 v[212:215], v172 offset:21504
	ds_read_b128 v[216:219], v172 offset:22528
	ds_read_b128 v[220:223], v172 offset:23552
	global_load_lds_dwordx4 v134, s[24:25]
	s_add_i32 m0, s59, 0x2000
	s_add_u32 s60, s24, 0x40000
	s_addc_u32 s61, s25, 0
	s_add_i32 s59, s49, s28
	global_load_lds_dwordx4 v130, s[24:25]
	s_mov_b32 m0, s59
	s_mov_b64 s[98:99], s[26:27]
	global_load_lds_dwordx4 v134, s[60:61]
	s_add_i32 m0, s59, 0x2000
	s_nop 0
	global_load_lds_dwordx4 v130, s[60:61]
	s_mov_b32 m0, s21
	s_nop 0
	global_load_lds_dwordx4 v136, s[26:27]
	s_mov_b32 m0, s31
	s_nop 0
	global_load_lds_dwordx4 v132, s[26:27]
	s_waitcnt vmcnt(8)
	s_waitcnt lgkmcnt(0)
	s_barrier
; #define PG8_STAGE_A(b, h, ptr, NX) do { if constexpr (Sched::GATHER) { unsigned gs_[2]; gs_[0] = ((NX) && last_) ? gN[h][0] : gA[h][0]; gs_[1] = ((NX) && last_) ? gN[h][1] : gA[h][1]; PG8_STAGE(PG8_SA(b, h), ptr, gs_); } \
;         else PG8_STAGE(PG8_SA(b, h), (ptr) + ((h) ? hstep : (size_t)0), voffA); } while (0)
; #define PG8_STAGE(bufoff, gbase, voff) do { _Pragma("unroll") for (int _i = 0; _i < 2; ++_i) \
;         __builtin_amdgcn_global_load_lds((const unsigned*)((const char*)(gbase) + (voff)[_i]), (PG8_LAS unsigned*)(lds + (bufoff) + ldsw + _i * 8192), 16, 0, 0); } while (0)
; #define PG8_LDA(dst, b, h) do { _Pragma("unroll") for (int m = 0; m < 4; ++m) _Pragma("unroll") for (int k = 0; k < 2; ++k) dst[m][k] = *(const PG8_LAS bf16x8*)(lds + PG8_SA(b, h) + aoff + m * 2048 + k * 1024); } while (0)
; #define PG8_LDB(dst, b, h) do { _Pragma("unroll") for (int n = 0; n < 2; ++n) _Pragma("unroll") for (int k = 0; k < 2; ++k) dst[n][k] = *(const PG8_LAS bf16x8*)(lds + PG8_SB(b, h) + boff + n * 2048 + k * 1024); } while (0)
; #define PG8_MMA(ai, bj, At, Bt) do { __builtin_amdgcn_s_setprio(1); _Pragma("unroll") for (int m = 0; m < 4; ++m) _Pragma("unroll") for (int n = 0; n < 2; ++n) _Pragma("unroll") for (int k = 0; k < 2; ++k) \
;         acc[ai][bj][m][n] = __builtin_amdgcn_mfma_f32_16x16x32_bf16(Bt[n][k], At[m][k], acc[ai][bj][m][n], 0, 0, 0); __builtin_amdgcn_s_setprio(0); } while (0)
; #define PG8_WAIT_V(n) asm volatile("s_waitcnt vmcnt(" #n ")" ::: "memory")
; #define PG8_WAIT_L(n) asm volatile("s_waitcnt lgkmcnt(" #n ")" ::: "memory")
; #define PG8_BAR __builtin_amdgcn_s_barrier()
; #define PG8_SCHED __builtin_amdgcn_sched_barrier(0)
; template <class Epi, class Sched, bool ALIGN_EPI = false, bool SP2 = false>
; __device__ __forceinline__ void gemm_phase(PG8_LAS unsigned char* lds, const Gemm g, const Sched& S, const Epi& E, const bool skip_epi = false) {
;     ...
;             PG8_WAIT_V(8); PG8_WAIT_L(0); PG8_BAR; PG8_MMA(1, 0, At, B0); PG8_MMA(1, 1, At, B1); PG8_BAR; PG8_SCHED;
;             PG8_LDB(B0, 1, 0); PG8_LDB(B1, 1, 1); PG8_SCHED; PG8_LDA(At, 1, 0); PG8_STAGE_A(0, 1, a2, true);
;             PG8_WAIT_V(8); PG8_WAIT_L(0); PG8_BAR; PG8_MMA(0, 0, At, B0); PG8_MMA(0, 1, At, B1); PG8_BAR; PG8_SCHED;
;             PG8_LDA(At, 1, 1); PG8_STAGE(PG8_SB(1, 0), b3, voffB); PG8_STAGE(PG8_SB(1, 1), b3 + hstep, voffB); PG8_STAGE_A(1, 0, a3, true);
	s_setprio 3
	s_waitcnt lgkmcnt(0)
	v_mfma_f32_16x16x32_bf16 v[62:65], v[148:151], v[192:195], 0
	v_mfma_f32_16x16x32_bf16 v[58:61], v[156:159], v[192:195], 0
	v_mfma_f32_16x16x32_bf16 v[50:53], v[148:151], v[200:203], 0
	v_mfma_f32_16x16x32_bf16 v[42:45], v[156:159], v[200:203], 0
	v_mfma_f32_16x16x32_bf16 v[34:37], v[148:151], v[208:211], 0
	v_mfma_f32_16x16x32_bf16 v[26:29], v[156:159], v[208:211], 0
	v_mfma_f32_16x16x32_bf16 v[18:21], v[148:151], v[216:219], 0
	v_mfma_f32_16x16x32_bf16 v[10:13], v[156:159], v[216:219], 0
	v_mfma_f32_16x16x32_bf16 v[62:65], v[152:155], v[196:199], v[62:65]
	v_mfma_f32_16x16x32_bf16 v[58:61], v[160:163], v[196:199], v[58:61]
	v_mfma_f32_16x16x32_bf16 v[50:53], v[152:155], v[204:207], v[50:53]
	v_mfma_f32_16x16x32_bf16 v[42:45], v[160:163], v[204:207], v[42:45]
	v_mfma_f32_16x16x32_bf16 v[34:37], v[152:155], v[212:215], v[34:37]
	v_mfma_f32_16x16x32_bf16 v[26:29], v[160:163], v[212:215], v[26:29]
	v_mfma_f32_16x16x32_bf16 v[18:21], v[152:155], v[220:223], v[18:21]
	v_mfma_f32_16x16x32_bf16 v[10:13], v[160:163], v[220:223], v[10:13]
	s_setprio 0
	s_setprio 3
	v_mfma_f32_16x16x32_bf16 v[54:57], v[176:179], v[192:195], 0
	v_mfma_f32_16x16x32_bf16 v[46:49], v[184:187], v[192:195], 0
	v_mfma_f32_16x16x32_bf16 v[38:41], v[176:179], v[200:203], 0
	v_mfma_f32_16x16x32_bf16 v[30:33], v[184:187], v[200:203], 0
	v_mfma_f32_16x16x32_bf16 v[22:25], v[176:179], v[208:211], 0
	v_mfma_f32_16x16x32_bf16 v[14:17], v[184:187], v[208:211], 0
	v_mfma_f32_16x16x32_bf16 v[6:9], v[176:179], v[216:219], 0
	v_mfma_f32_16x16x32_bf16 v[2:5], v[184:187], v[216:219], 0
	v_mfma_f32_16x16x32_bf16 v[54:57], v[180:183], v[196:199], v[54:57]
	v_mfma_f32_16x16x32_bf16 v[46:49], v[188:191], v[196:199], v[46:49]
	v_mfma_f32_16x16x32_bf16 v[38:41], v[180:183], v[204:207], v[38:41]
	v_mfma_f32_16x16x32_bf16 v[30:33], v[188:191], v[204:207], v[30:33]
	v_mfma_f32_16x16x32_bf16 v[22:25], v[180:183], v[212:215], v[22:25]
	v_mfma_f32_16x16x32_bf16 v[14:17], v[188:191], v[212:215], v[14:17]
	v_mfma_f32_16x16x32_bf16 v[6:9], v[180:183], v[220:223], v[6:9]
	v_mfma_f32_16x16x32_bf16 v[2:5], v[188:191], v[220:223], v[2:5]
	s_setprio 0
	s_barrier
	s_add_i32 s59, 0, 0x18000
	s_add_i32 s60, 0, 0x1c000
	v_add_u32_e32 v160, s59, v1
	v_add_u32_e32 v188, s60, v1
	ds_read_b128 v[148:151], v160
	ds_read_b128 v[152:155], v160 offset:1024
	ds_read_b128 v[156:159], v160 offset:2048
	ds_read_b128 v[160:163], v160 offset:3072
	ds_read_b128 v[176:179], v188
	ds_read_b128 v[180:183], v188 offset:1024
	ds_read_b128 v[184:187], v188 offset:2048
	ds_read_b128 v[188:191], v188 offset:3072
	s_add_u32 s26, s26, 0x40000
	s_addc_u32 s27, s27, 0
	s_mov_b32 m0, s34
	ds_read_b128 v[192:195], v172 offset:32768
	ds_read_b128 v[196:199], v172 offset:33792
	ds_read_b128 v[200:203], v172 offset:34816
	ds_read_b128 v[204:207], v172 offset:35840
	ds_read_b128 v[208:211], v172 offset:36864
	ds_read_b128 v[212:215], v172 offset:37888
	ds_read_b128 v[216:219], v172 offset:38912
	ds_read_b128 v[220:223], v172 offset:39936
	global_load_lds_dwordx4 v136, s[26:27]
	s_mov_b32 m0, s35
	s_nop 0
	global_load_lds_dwordx4 v132, s[26:27]
	s_waitcnt vmcnt(8)
	s_waitcnt lgkmcnt(0)
	s_barrier
	s_setprio 3
	s_waitcnt lgkmcnt(0)
	v_mfma_f32_16x16x32_bf16 v[126:129], v[148:151], v[192:195], v[126:129]
	v_mfma_f32_16x16x32_bf16 v[122:125], v[156:159], v[192:195], v[122:125]
	v_mfma_f32_16x16x32_bf16 v[114:117], v[148:151], v[200:203], v[114:117]
	v_mfma_f32_16x16x32_bf16 v[106:109], v[156:159], v[200:203], v[106:109]
	v_mfma_f32_16x16x32_bf16 v[98:101], v[148:151], v[208:211], v[98:101]
	v_mfma_f32_16x16x32_bf16 v[90:93], v[156:159], v[208:211], v[90:93]
	v_mfma_f32_16x16x32_bf16 v[82:85], v[148:151], v[216:219], v[82:85]
	v_mfma_f32_16x16x32_bf16 v[74:77], v[156:159], v[216:219], v[74:77]
	v_mfma_f32_16x16x32_bf16 v[126:129], v[152:155], v[196:199], v[126:129]
	v_mfma_f32_16x16x32_bf16 v[122:125], v[160:163], v[196:199], v[122:125]
	v_mfma_f32_16x16x32_bf16 v[114:117], v[152:155], v[204:207], v[114:117]
	v_mfma_f32_16x16x32_bf16 v[106:109], v[160:163], v[204:207], v[106:109]
	v_mfma_f32_16x16x32_bf16 v[98:101], v[152:155], v[212:215], v[98:101]
	v_mfma_f32_16x16x32_bf16 v[90:93], v[160:163], v[212:215], v[90:93]
	v_mfma_f32_16x16x32_bf16 v[82:85], v[152:155], v[220:223], v[82:85]
	v_mfma_f32_16x16x32_bf16 v[74:77], v[160:163], v[220:223], v[74:77]
	s_setprio 0
	s_setprio 3
	v_mfma_f32_16x16x32_bf16 v[118:121], v[176:179], v[192:195], v[118:121]
	v_mfma_f32_16x16x32_bf16 v[110:113], v[184:187], v[192:195], v[110:113]
	v_mfma_f32_16x16x32_bf16 v[102:105], v[176:179], v[200:203], v[102:105]
	v_mfma_f32_16x16x32_bf16 v[94:97], v[184:187], v[200:203], v[94:97]
	v_mfma_f32_16x16x32_bf16 v[86:89], v[176:179], v[208:211], v[86:89]
	v_mfma_f32_16x16x32_bf16 v[78:81], v[184:187], v[208:211], v[78:81]
	v_mfma_f32_16x16x32_bf16 v[70:73], v[176:179], v[216:219], v[70:73]
	v_mfma_f32_16x16x32_bf16 v[66:69], v[184:187], v[216:219], v[66:69]
	v_mfma_f32_16x16x32_bf16 v[118:121], v[180:183], v[196:199], v[118:121]
	v_mfma_f32_16x16x32_bf16 v[110:113], v[188:191], v[196:199], v[110:113]
	v_mfma_f32_16x16x32_bf16 v[102:105], v[180:183], v[204:207], v[102:105]
	v_mfma_f32_16x16x32_bf16 v[94:97], v[188:191], v[204:207], v[94:97]
	v_mfma_f32_16x16x32_bf16 v[86:89], v[180:183], v[212:215], v[86:89]
	v_mfma_f32_16x16x32_bf16 v[78:81], v[188:191], v[212:215], v[78:81]
	v_mfma_f32_16x16x32_bf16 v[70:73], v[180:183], v[220:223], v[70:73]
	v_mfma_f32_16x16x32_bf16 v[66:69], v[188:191], v[220:223], v[66:69]
	s_setprio 0
	s_barrier
; #define PG8_STAGE_A(b, h, ptr, NX) do { if constexpr (Sched::GATHER) { unsigned gs_[2]; gs_[0] = ((NX) && last_) ? gN[h][0] : gA[h][0]; gs_[1] = ((NX) && last_) ? gN[h][1] : gA[h][1]; PG8_STAGE(PG8_SA(b, h), ptr, gs_); } \
;         else PG8_STAGE(PG8_SA(b, h), (ptr) + ((h) ? hstep : (size_t)0), voffA); } while (0)
; #define PG8_STAGE(bufoff, gbase, voff) do { _Pragma("unroll") for (int _i = 0; _i < 2; ++_i) \
;         __builtin_amdgcn_global_load_lds((const unsigned*)((const char*)(gbase) + (voff)[_i]), (PG8_LAS unsigned*)(lds + (bufoff) + ldsw + _i * 8192), 16, 0, 0); } while (0)
; #define PG8_LDA(dst, b, h) do { _Pragma("unroll") for (int m = 0; m < 4; ++m) _Pragma("unroll") for (int k = 0; k < 2; ++k) dst[m][k] = *(const PG8_LAS bf16x8*)(lds + PG8_SA(b, h) + aoff + m * 2048 + k * 1024); } while (0)
; #define PG8_LDB(dst, b, h) do { _Pragma("unroll") for (int n = 0; n < 2; ++n) _Pragma("unroll") for (int k = 0; k < 2; ++k) dst[n][k] = *(const PG8_LAS bf16x8*)(lds + PG8_SB(b, h) + boff + n * 2048 + k * 1024); } while (0)
; #define PG8_WAIT_V(n) asm volatile("s_waitcnt vmcnt(" #n ")" ::: "memory")
; #define PG8_WAIT_L(n) asm volatile("s_waitcnt lgkmcnt(" #n ")" ::: "memory")
; #define PG8_BAR __builtin_amdgcn_s_barrier()
; #define PG8_SCHED __builtin_amdgcn_sched_barrier(0)
; template <class Epi, class Sched, bool ALIGN_EPI = false, bool SP2 = false>
; __device__ __forceinline__ void gemm_phase(PG8_LAS unsigned char* lds, const Gemm g, const Sched& S, const Epi& E, const bool skip_epi = false) {
;     ...
;         for (int t = 0; t < nt; t += 2) {
;             const bool last = (t == nt - 2); last_ = last && has_next;
;             const char* a1 = cA + (size_t)(t + 1) * kstep;
;             const char* a2 = last ? nA : cA + (size_t)(t + 2) * kstep; const char* b2 = last ? nB : cB + (size_t)(t + 2) * kstep;
;             const char* a3 = a2 + kstep; const char* b3 = b2 + kstep;
;             if (last && has_next) S.a_ready(nxt);
;             if constexpr (SP2) {
;             PG8_LDB(B0, 0, 0); PG8_LDB(B1, 0, 1); PG8_SCHED; PG8_LDA(At, 0, 0); PG8_STAGE_A(1, 1, a1, false);
;     ...
;             PG8_LDA(At, 1, 1); PG8_STAGE(PG8_SB(1, 0), b3, voffB); PG8_STAGE(PG8_SB(1, 1), b3 + hstep, voffB); PG8_STAGE_A(1, 0, a3, true);
;             PG8_WAIT_V(8); PG8_WAIT_L(0); PG8_BAR; PG8_MMA(1, 0, At, B0); PG8_MMA(1, 1, At, B1); PG8_BAR; PG8_SCHED;
	s_add_i32 s26, s59, s28
	s_add_i32 m0, s26, 0xffffff80
	ds_read_b128 v[192:195], v172 offset:49152
	ds_read_b128 v[196:199], v172 offset:50176
	ds_read_b128 v[200:203], v172 offset:51200
	ds_read_b128 v[204:207], v172 offset:52224
	ds_read_b128 v[208:211], v172 offset:53248
	ds_read_b128 v[212:215], v172 offset:54272
	ds_read_b128 v[216:219], v172 offset:55296
	ds_read_b128 v[220:223], v172 offset:56320
	global_load_lds_dwordx4 v134, s[24:25] offset:128
	s_add_i32 m0, s26, 0x1f80
	s_add_i32 s26, s60, s28
	global_load_lds_dwordx4 v130, s[24:25] offset:128
	s_add_u32 s24, s24, 0x40080
	s_addc_u32 s25, s25, 0
	s_mov_b32 m0, s26
	s_nop 0
	global_load_lds_dwordx4 v134, s[24:25]
	s_add_i32 m0, s26, 0x2000
	s_nop 0
	global_load_lds_dwordx4 v130, s[24:25]
	s_add_i32 m0, s37, 0xffffff80
	s_nop 0
	global_load_lds_dwordx4 v136, s[98:99] offset:128
	s_add_i32 m0, s38, 0xffffff80
	s_nop 0
	global_load_lds_dwordx4 v132, s[98:99] offset:128
	s_waitcnt vmcnt(8)
	s_waitcnt lgkmcnt(0)
	s_barrier
	s_setprio 3
	s_waitcnt lgkmcnt(0)
	v_mfma_f32_16x16x32_bf16 v[62:65], v[148:151], v[192:195], v[62:65]
	v_mfma_f32_16x16x32_bf16 v[58:61], v[156:159], v[192:195], v[58:61]
	v_mfma_f32_16x16x32_bf16 v[50:53], v[148:151], v[200:203], v[50:53]
	v_mfma_f32_16x16x32_bf16 v[42:45], v[156:159], v[200:203], v[42:45]
	v_mfma_f32_16x16x32_bf16 v[34:37], v[148:151], v[208:211], v[34:37]
	v_mfma_f32_16x16x32_bf16 v[26:29], v[156:159], v[208:211], v[26:29]
	v_mfma_f32_16x16x32_bf16 v[18:21], v[148:151], v[216:219], v[18:21]
	v_mfma_f32_16x16x32_bf16 v[10:13], v[156:159], v[216:219], v[10:13]
	v_mfma_f32_16x16x32_bf16 v[62:65], v[152:155], v[196:199], v[62:65]
	v_mfma_f32_16x16x32_bf16 v[58:61], v[160:163], v[196:199], v[58:61]
	v_mfma_f32_16x16x32_bf16 v[50:53], v[152:155], v[204:207], v[50:53]
	v_mfma_f32_16x16x32_bf16 v[42:45], v[160:163], v[204:207], v[42:45]
	v_mfma_f32_16x16x32_bf16 v[34:37], v[152:155], v[212:215], v[34:37]
	v_mfma_f32_16x16x32_bf16 v[26:29], v[160:163], v[212:215], v[26:29]
	v_mfma_f32_16x16x32_bf16 v[18:21], v[152:155], v[220:223], v[18:21]
	v_mfma_f32_16x16x32_bf16 v[10:13], v[160:163], v[220:223], v[10:13]
	s_setprio 0
	s_setprio 3
	v_mfma_f32_16x16x32_bf16 v[54:57], v[176:179], v[192:195], v[54:57]
	v_mfma_f32_16x16x32_bf16 v[46:49], v[184:187], v[192:195], v[46:49]
	v_mfma_f32_16x16x32_bf16 v[38:41], v[176:179], v[200:203], v[38:41]
	v_mfma_f32_16x16x32_bf16 v[30:33], v[184:187], v[200:203], v[30:33]
	v_mfma_f32_16x16x32_bf16 v[22:25], v[176:179], v[208:211], v[22:25]
	v_mfma_f32_16x16x32_bf16 v[14:17], v[184:187], v[208:211], v[14:17]
	v_mfma_f32_16x16x32_bf16 v[6:9], v[176:179], v[216:219], v[6:9]
	v_mfma_f32_16x16x32_bf16 v[2:5], v[184:187], v[216:219], v[2:5]
	v_mfma_f32_16x16x32_bf16 v[54:57], v[180:183], v[196:199], v[54:57]
	v_mfma_f32_16x16x32_bf16 v[46:49], v[188:191], v[196:199], v[46:49]
	v_mfma_f32_16x16x32_bf16 v[38:41], v[180:183], v[204:207], v[38:41]
	v_mfma_f32_16x16x32_bf16 v[30:33], v[188:191], v[204:207], v[30:33]
	v_mfma_f32_16x16x32_bf16 v[22:25], v[180:183], v[212:215], v[22:25]
	v_mfma_f32_16x16x32_bf16 v[14:17], v[188:191], v[212:215], v[14:17]
	v_mfma_f32_16x16x32_bf16 v[6:9], v[180:183], v[220:223], v[6:9]
	v_mfma_f32_16x16x32_bf16 v[2:5], v[188:191], v[220:223], v[2:5]
	s_setprio 0
	s_barrier
	s_add_i32 s58, s58, 2
	s_add_u32 s22, s22, 0x100
	s_addc_u32 s23, s23, 0
	s_add_u32 s56, s56, 0x100
	s_addc_u32 s57, s57, 0
	s_cmp_gt_u32 s58, 13
.LBB0_944:
	ds_read_b128 v[148:151], v170
	ds_read_b128 v[152:155], v170 offset:1024
	ds_read_b128 v[156:159], v170 offset:2048
	ds_read_b128 v[160:163], v170 offset:3072
	ds_read_b128 v[176:179], v171
	ds_read_b128 v[180:183], v171 offset:1024
	ds_read_b128 v[184:187], v171 offset:2048
	ds_read_b128 v[188:191], v171 offset:3072
	s_add_u32 s24, s22, 0xfffc0080
	s_addc_u32 s25, s23, -1
	s_cmp_eq_u32 s58, 12
	s_cselect_b32 s27, s15, s25
	s_cselect_b32 s26, s54, s24
	s_cselect_b32 s25, s13, s57
	s_cselect_b32 s24, s55, s56
	s_add_i32 m0, s21, 0xc000
	ds_read_b128 v[192:195], v172
	ds_read_b128 v[196:199], v172 offset:1024
	ds_read_b128 v[200:203], v172 offset:2048
	ds_read_b128 v[204:207], v172 offset:3072
	ds_read_b128 v[208:211], v172 offset:4096
	ds_read_b128 v[212:215], v172 offset:5120
	ds_read_b128 v[216:219], v172 offset:6144
	ds_read_b128 v[220:223], v172 offset:7168
	global_load_lds_dwordx4 v140, s[22:23]
	s_add_i32 m0, s21, 0xe000
	s_nop 0
	global_load_lds_dwordx4 v142, s[22:23]
	s_waitcnt vmcnt(8)
	s_waitcnt lgkmcnt(0)
	s_barrier
; #define PG8_STAGE_A(b, h, ptr, NX) do { if constexpr (Sched::GATHER) { unsigned gs_[2]; gs_[0] = ((NX) && last_) ? gN[h][0] : gA[h][0]; gs_[1] = ((NX) && last_) ? gN[h][1] : gA[h][1]; PG8_STAGE(PG8_SA(b, h), ptr, gs_); } \
;         else PG8_STAGE(PG8_SA(b, h), (ptr) + ((h) ? hstep : (size_t)0), voffA); } while (0)
; #define PG8_STAGE(bufoff, gbase, voff) do { _Pragma("unroll") for (int _i = 0; _i < 2; ++_i) \
;         __builtin_amdgcn_global_load_lds((const unsigned*)((const char*)(gbase) + (voff)[_i]), (PG8_LAS unsigned*)(lds + (bufoff) + ldsw + _i * 8192), 16, 0, 0); } while (0)
; #define PG8_LDA(dst, b, h) do { _Pragma("unroll") for (int m = 0; m < 4; ++m) _Pragma("unroll") for (int k = 0; k < 2; ++k) dst[m][k] = *(const PG8_LAS bf16x8*)(lds + PG8_SA(b, h) + aoff + m * 2048 + k * 1024); } while (0)
; #define PG8_MMA(ai, bj, At, Bt) do { __builtin_amdgcn_s_setprio(1); _Pragma("unroll") for (int m = 0; m < 4; ++m) _Pragma("unroll") for (int n = 0; n < 2; ++n) _Pragma("unroll") for (int k = 0; k < 2; ++k) \
;         acc[ai][bj][m][n] = __builtin_amdgcn_mfma_f32_16x16x32_bf16(Bt[n][k], At[m][k], acc[ai][bj][m][n], 0, 0, 0); __builtin_amdgcn_s_setprio(0); } while (0)
; #define PG8_WAIT_V(n) asm volatile("s_waitcnt vmcnt(" #n ")" ::: "memory")
; #define PG8_WAIT_L(n) asm volatile("s_waitcnt lgkmcnt(" #n ")" ::: "memory")
; #define PG8_BAR __builtin_amdgcn_s_barrier()
; #define PG8_SCHED __builtin_amdgcn_sched_barrier(0)
; template <class Epi, class Sched, bool ALIGN_EPI = false, bool SP2 = false>
; __device__ __forceinline__ void gemm_phase(PG8_LAS unsigned char* lds, const Gemm g, const Sched& S, const Epi& E, const bool skip_epi = false) {
;     ...
;             PG8_WAIT_V(8); PG8_WAIT_L(0); PG8_BAR; PG8_MMA(0, 0, At, B0); PG8_MMA(0, 1, At, B1); PG8_BAR; PG8_SCHED;
;             PG8_LDA(At, 0, 1); PG8_STAGE(PG8_SB(0, 0), b2, voffB); PG8_STAGE(PG8_SB(0, 1), b2 + hstep, voffB); PG8_STAGE_A(0, 0, a2, true);
;             PG8_WAIT_V(8); PG8_WAIT_L(0); PG8_BAR; PG8_MMA(1, 0, At, B0); PG8_MMA(1, 1, At, B1); PG8_BAR; PG8_SCHED;
	s_setprio 3
	s_waitcnt lgkmcnt(0)
	v_mfma_f32_16x16x32_bf16 v[126:129], v[148:151], v[192:195], v[126:129]
	v_mfma_f32_16x16x32_bf16 v[122:125], v[156:159], v[192:195], v[122:125]
	v_mfma_f32_16x16x32_bf16 v[114:117], v[148:151], v[200:203], v[114:117]
	v_mfma_f32_16x16x32_bf16 v[106:109], v[156:159], v[200:203], v[106:109]
	v_mfma_f32_16x16x32_bf16 v[98:101], v[148:151], v[208:211], v[98:101]
	v_mfma_f32_16x16x32_bf16 v[90:93], v[156:159], v[208:211], v[90:93]
	v_mfma_f32_16x16x32_bf16 v[82:85], v[148:151], v[216:219], v[82:85]
	v_mfma_f32_16x16x32_bf16 v[74:77], v[156:159], v[216:219], v[74:77]
	v_mfma_f32_16x16x32_bf16 v[126:129], v[152:155], v[196:199], v[126:129]
	v_mfma_f32_16x16x32_bf16 v[122:125], v[160:163], v[196:199], v[122:125]
	v_mfma_f32_16x16x32_bf16 v[114:117], v[152:155], v[204:207], v[114:117]
	v_mfma_f32_16x16x32_bf16 v[106:109], v[160:163], v[204:207], v[106:109]
	v_mfma_f32_16x16x32_bf16 v[98:101], v[152:155], v[212:215], v[98:101]
	v_mfma_f32_16x16x32_bf16 v[90:93], v[160:163], v[212:215], v[90:93]
	v_mfma_f32_16x16x32_bf16 v[82:85], v[152:155], v[220:223], v[82:85]
	v_mfma_f32_16x16x32_bf16 v[74:77], v[160:163], v[220:223], v[74:77]
	s_setprio 0
	s_setprio 3
	v_mfma_f32_16x16x32_bf16 v[118:121], v[176:179], v[192:195], v[118:121]
	v_mfma_f32_16x16x32_bf16 v[110:113], v[184:187], v[192:195], v[110:113]
	v_mfma_f32_16x16x32_bf16 v[102:105], v[176:179], v[200:203], v[102:105]
	v_mfma_f32_16x16x32_bf16 v[94:97], v[184:187], v[200:203], v[94:97]
	v_mfma_f32_16x16x32_bf16 v[86:89], v[176:179], v[208:211], v[86:89]
	v_mfma_f32_16x16x32_bf16 v[78:81], v[184:187], v[208:211], v[78:81]
	v_mfma_f32_16x16x32_bf16 v[70:73], v[176:179], v[216:219], v[70:73]
	v_mfma_f32_16x16x32_bf16 v[66:69], v[184:187], v[216:219], v[66:69]
	v_mfma_f32_16x16x32_bf16 v[118:121], v[180:183], v[196:199], v[118:121]
	v_mfma_f32_16x16x32_bf16 v[110:113], v[188:191], v[196:199], v[110:113]
	v_mfma_f32_16x16x32_bf16 v[102:105], v[180:183], v[204:207], v[102:105]
	v_mfma_f32_16x16x32_bf16 v[94:97], v[188:191], v[204:207], v[94:97]
	v_mfma_f32_16x16x32_bf16 v[86:89], v[180:183], v[212:215], v[86:89]
	v_mfma_f32_16x16x32_bf16 v[78:81], v[188:191], v[212:215], v[78:81]
	v_mfma_f32_16x16x32_bf16 v[70:73], v[180:183], v[220:223], v[70:73]
	v_mfma_f32_16x16x32_bf16 v[66:69], v[188:191], v[220:223], v[66:69]
	s_setprio 0
	s_barrier
	s_add_i32 s59, s48, s28
	s_mov_b32 m0, s59
	ds_read_b128 v[192:195], v172 offset:16384
	ds_read_b128 v[196:199], v172 offset:17408
	ds_read_b128 v[200:203], v172 offset:18432
	ds_read_b128 v[204:207], v172 offset:19456
	ds_read_b128 v[208:211], v172 offset:20480
	ds_read_b128 v[212:215], v172 offset:21504
	ds_read_b128 v[216:219], v172 offset:22528
	ds_read_b128 v[220:223], v172 offset:23552
	global_load_lds_dwordx4 v134, s[24:25]
	s_add_i32 m0, s59, 0x2000
	s_add_u32 s60, s24, 0x40000
	s_addc_u32 s61, s25, 0
	s_add_i32 s59, s49, s28
	global_load_lds_dwordx4 v130, s[24:25]
	s_mov_b32 m0, s59
	s_mov_b64 s[98:99], s[26:27]
	global_load_lds_dwordx4 v134, s[60:61]
	s_add_i32 m0, s59, 0x2000
	s_nop 0
	global_load_lds_dwordx4 v130, s[60:61]
	s_mov_b32 m0, s21
	s_nop 0
	global_load_lds_dwordx4 v136, s[26:27]
	s_mov_b32 m0, s31
	s_nop 0
	global_load_lds_dwordx4 v132, s[26:27]
	s_waitcnt vmcnt(8)
	s_waitcnt lgkmcnt(0)
	s_barrier
	s_setprio 3
	s_waitcnt lgkmcnt(0)
	v_mfma_f32_16x16x32_bf16 v[62:65], v[148:151], v[192:195], v[62:65]
	v_mfma_f32_16x16x32_bf16 v[58:61], v[156:159], v[192:195], v[58:61]
	v_mfma_f32_16x16x32_bf16 v[50:53], v[148:151], v[200:203], v[50:53]
	v_mfma_f32_16x16x32_bf16 v[42:45], v[156:159], v[200:203], v[42:45]
	v_mfma_f32_16x16x32_bf16 v[34:37], v[148:151], v[208:211], v[34:37]
	v_mfma_f32_16x16x32_bf16 v[26:29], v[156:159], v[208:211], v[26:29]
	v_mfma_f32_16x16x32_bf16 v[18:21], v[148:151], v[216:219], v[18:21]
	v_mfma_f32_16x16x32_bf16 v[10:13], v[156:159], v[216:219], v[10:13]
	v_mfma_f32_16x16x32_bf16 v[62:65], v[152:155], v[196:199], v[62:65]
	v_mfma_f32_16x16x32_bf16 v[58:61], v[160:163], v[196:199], v[58:61]
	v_mfma_f32_16x16x32_bf16 v[50:53], v[152:155], v[204:207], v[50:53]
	v_mfma_f32_16x16x32_bf16 v[42:45], v[160:163], v[204:207], v[42:45]
	v_mfma_f32_16x16x32_bf16 v[34:37], v[152:155], v[212:215], v[34:37]
	v_mfma_f32_16x16x32_bf16 v[26:29], v[160:163], v[212:215], v[26:29]
	v_mfma_f32_16x16x32_bf16 v[18:21], v[152:155], v[220:223], v[18:21]
	v_mfma_f32_16x16x32_bf16 v[10:13], v[160:163], v[220:223], v[10:13]
	s_setprio 0
	s_setprio 3
	v_mfma_f32_16x16x32_bf16 v[54:57], v[176:179], v[192:195], v[54:57]
	v_mfma_f32_16x16x32_bf16 v[46:49], v[184:187], v[192:195], v[46:49]
	v_mfma_f32_16x16x32_bf16 v[38:41], v[176:179], v[200:203], v[38:41]
	v_mfma_f32_16x16x32_bf16 v[30:33], v[184:187], v[200:203], v[30:33]
	v_mfma_f32_16x16x32_bf16 v[22:25], v[176:179], v[208:211], v[22:25]
	v_mfma_f32_16x16x32_bf16 v[14:17], v[184:187], v[208:211], v[14:17]
	v_mfma_f32_16x16x32_bf16 v[6:9], v[176:179], v[216:219], v[6:9]
	v_mfma_f32_16x16x32_bf16 v[2:5], v[184:187], v[216:219], v[2:5]
	v_mfma_f32_16x16x32_bf16 v[54:57], v[180:183], v[196:199], v[54:57]
	v_mfma_f32_16x16x32_bf16 v[46:49], v[188:191], v[196:199], v[46:49]
	v_mfma_f32_16x16x32_bf16 v[38:41], v[180:183], v[204:207], v[38:41]
	v_mfma_f32_16x16x32_bf16 v[30:33], v[188:191], v[204:207], v[30:33]
	v_mfma_f32_16x16x32_bf16 v[22:25], v[180:183], v[212:215], v[22:25]
	v_mfma_f32_16x16x32_bf16 v[14:17], v[188:191], v[212:215], v[14:17]
	v_mfma_f32_16x16x32_bf16 v[6:9], v[180:183], v[220:223], v[6:9]
	v_mfma_f32_16x16x32_bf16 v[2:5], v[188:191], v[220:223], v[2:5]
	s_setprio 0
	s_barrier
; #define PG8_STAGE_A(b, h, ptr, NX) do { if constexpr (Sched::GATHER) { unsigned gs_[2]; gs_[0] = ((NX) && last_) ? gN[h][0] : gA[h][0]; gs_[1] = ((NX) && last_) ? gN[h][1] : gA[h][1]; PG8_STAGE(PG8_SA(b, h), ptr, gs_); } \
;         else PG8_STAGE(PG8_SA(b, h), (ptr) + ((h) ? hstep : (size_t)0), voffA); } while (0)
; #define PG8_LDA(dst, b, h) do { _Pragma("unroll") for (int m = 0; m < 4; ++m) _Pragma("unroll") for (int k = 0; k < 2; ++k) dst[m][k] = *(const PG8_LAS bf16x8*)(lds + PG8_SA(b, h) + aoff + m * 2048 + k * 1024); } while (0)
; #define PG8_LDB(dst, b, h) do { _Pragma("unroll") for (int n = 0; n < 2; ++n) _Pragma("unroll") for (int k = 0; k < 2; ++k) dst[n][k] = *(const PG8_LAS bf16x8*)(lds + PG8_SB(b, h) + boff + n * 2048 + k * 1024); } while (0)
; #define PG8_MMA(ai, bj, At, Bt) do { __builtin_amdgcn_s_setprio(1); _Pragma("unroll") for (int m = 0; m < 4; ++m) _Pragma("unroll") for (int n = 0; n < 2; ++n) _Pragma("unroll") for (int k = 0; k < 2; ++k) \
;         acc[ai][bj][m][n] = __builtin_amdgcn_mfma_f32_16x16x32_bf16(Bt[n][k], At[m][k], acc[ai][bj][m][n], 0, 0, 0); __builtin_amdgcn_s_setprio(0); } while (0)
; #define PG8_WAIT_V(n) asm volatile("s_waitcnt vmcnt(" #n ")" ::: "memory")
; #define PG8_WAIT_L(n) asm volatile("s_waitcnt lgkmcnt(" #n ")" ::: "memory")
; #define PG8_BAR __builtin_amdgcn_s_barrier()
; #define PG8_SCHED __builtin_amdgcn_sched_barrier(0)
; template <class Epi, class Sched, bool ALIGN_EPI = false, bool SP2 = false>
; __device__ __forceinline__ void gemm_phase(PG8_LAS unsigned char* lds, const Gemm g, const Sched& S, const Epi& E, const bool skip_epi = false) {
;     ...
;             PG8_LDB(B0, 1, 0); PG8_LDB(B1, 1, 1); PG8_SCHED; PG8_LDA(At, 1, 0); PG8_STAGE_A(0, 1, a2, true);
;             PG8_WAIT_V(8); PG8_WAIT_L(0); PG8_BAR; PG8_MMA(0, 0, At, B0); PG8_MMA(0, 1, At, B1); PG8_BAR; PG8_SCHED;
	s_add_i32 s59, 0, 0x18000
	s_add_i32 s60, 0, 0x1c000
	v_add_u32_e32 v160, s59, v1
	v_add_u32_e32 v188, s60, v1
	ds_read_b128 v[148:151], v160
	ds_read_b128 v[152:155], v160 offset:1024
	ds_read_b128 v[156:159], v160 offset:2048
	ds_read_b128 v[160:163], v160 offset:3072
	ds_read_b128 v[176:179], v188
	ds_read_b128 v[180:183], v188 offset:1024
	ds_read_b128 v[184:187], v188 offset:2048
	ds_read_b128 v[188:191], v188 offset:3072
	s_add_u32 s26, s26, 0x40000
	s_addc_u32 s27, s27, 0
	s_mov_b32 m0, s34
	ds_read_b128 v[192:195], v172 offset:32768
	ds_read_b128 v[196:199], v172 offset:33792
	ds_read_b128 v[200:203], v172 offset:34816
	ds_read_b128 v[204:207], v172 offset:35840
	ds_read_b128 v[208:211], v172 offset:36864
	ds_read_b128 v[212:215], v172 offset:37888
	ds_read_b128 v[216:219], v172 offset:38912
	ds_read_b128 v[220:223], v172 offset:39936
	global_load_lds_dwordx4 v136, s[26:27]
	s_mov_b32 m0, s35
	s_nop 0
	global_load_lds_dwordx4 v132, s[26:27]
	s_waitcnt vmcnt(8)
	s_waitcnt lgkmcnt(0)
	s_barrier
	s_setprio 3
	s_waitcnt lgkmcnt(0)
	v_mfma_f32_16x16x32_bf16 v[126:129], v[148:151], v[192:195], v[126:129]
	v_mfma_f32_16x16x32_bf16 v[122:125], v[156:159], v[192:195], v[122:125]
	v_mfma_f32_16x16x32_bf16 v[114:117], v[148:151], v[200:203], v[114:117]
	v_mfma_f32_16x16x32_bf16 v[106:109], v[156:159], v[200:203], v[106:109]
	v_mfma_f32_16x16x32_bf16 v[98:101], v[148:151], v[208:211], v[98:101]
	v_mfma_f32_16x16x32_bf16 v[90:93], v[156:159], v[208:211], v[90:93]
	v_mfma_f32_16x16x32_bf16 v[82:85], v[148:151], v[216:219], v[82:85]
	v_mfma_f32_16x16x32_bf16 v[74:77], v[156:159], v[216:219], v[74:77]
	v_mfma_f32_16x16x32_bf16 v[126:129], v[152:155], v[196:199], v[126:129]
	v_mfma_f32_16x16x32_bf16 v[122:125], v[160:163], v[196:199], v[122:125]
	v_mfma_f32_16x16x32_bf16 v[114:117], v[152:155], v[204:207], v[114:117]
	v_mfma_f32_16x16x32_bf16 v[106:109], v[160:163], v[204:207], v[106:109]
	v_mfma_f32_16x16x32_bf16 v[98:101], v[152:155], v[212:215], v[98:101]
	v_mfma_f32_16x16x32_bf16 v[90:93], v[160:163], v[212:215], v[90:93]
	v_mfma_f32_16x16x32_bf16 v[82:85], v[152:155], v[220:223], v[82:85]
	v_mfma_f32_16x16x32_bf16 v[74:77], v[160:163], v[220:223], v[74:77]
	s_setprio 0
	s_setprio 3
	v_mfma_f32_16x16x32_bf16 v[118:121], v[176:179], v[192:195], v[118:121]
	v_mfma_f32_16x16x32_bf16 v[110:113], v[184:187], v[192:195], v[110:113]
	v_mfma_f32_16x16x32_bf16 v[102:105], v[176:179], v[200:203], v[102:105]
	v_mfma_f32_16x16x32_bf16 v[94:97], v[184:187], v[200:203], v[94:97]
	v_mfma_f32_16x16x32_bf16 v[86:89], v[176:179], v[208:211], v[86:89]
	v_mfma_f32_16x16x32_bf16 v[78:81], v[184:187], v[208:211], v[78:81]
	v_mfma_f32_16x16x32_bf16 v[70:73], v[176:179], v[216:219], v[70:73]
	v_mfma_f32_16x16x32_bf16 v[66:69], v[184:187], v[216:219], v[66:69]
	v_mfma_f32_16x16x32_bf16 v[118:121], v[180:183], v[196:199], v[118:121]
	v_mfma_f32_16x16x32_bf16 v[110:113], v[188:191], v[196:199], v[110:113]
	v_mfma_f32_16x16x32_bf16 v[102:105], v[180:183], v[204:207], v[102:105]
	v_mfma_f32_16x16x32_bf16 v[94:97], v[188:191], v[204:207], v[94:97]
	v_mfma_f32_16x16x32_bf16 v[86:89], v[180:183], v[212:215], v[86:89]
	v_mfma_f32_16x16x32_bf16 v[78:81], v[188:191], v[212:215], v[78:81]
	v_mfma_f32_16x16x32_bf16 v[70:73], v[180:183], v[220:223], v[70:73]
	v_mfma_f32_16x16x32_bf16 v[66:69], v[188:191], v[220:223], v[66:69]
	s_setprio 0
	s_barrier
; #define PG8_STAGE_A(b, h, ptr, NX) do { if constexpr (Sched::GATHER) { unsigned gs_[2]; gs_[0] = ((NX) && last_) ? gN[h][0] : gA[h][0]; gs_[1] = ((NX) && last_) ? gN[h][1] : gA[h][1]; PG8_STAGE(PG8_SA(b, h), ptr, gs_); } \
;         else PG8_STAGE(PG8_SA(b, h), (ptr) + ((h) ? hstep : (size_t)0), voffA); } while (0)
; #define PG8_STAGE(bufoff, gbase, voff) do { _Pragma("unroll") for (int _i = 0; _i < 2; ++_i) \
;         __builtin_amdgcn_global_load_lds((const unsigned*)((const char*)(gbase) + (voff)[_i]), (PG8_LAS unsigned*)(lds + (bufoff) + ldsw + _i * 8192), 16, 0, 0); } while (0)
; #define PG8_LDA(dst, b, h) do { _Pragma("unroll") for (int m = 0; m < 4; ++m) _Pragma("unroll") for (int k = 0; k < 2; ++k) dst[m][k] = *(const PG8_LAS bf16x8*)(lds + PG8_SA(b, h) + aoff + m * 2048 + k * 1024); } while (0)
; #define PG8_MMA(ai, bj, At, Bt) do { __builtin_amdgcn_s_setprio(1); _Pragma("unroll") for (int m = 0; m < 4; ++m) _Pragma("unroll") for (int n = 0; n < 2; ++n) _Pragma("unroll") for (int k = 0; k < 2; ++k) \
;         acc[ai][bj][m][n] = __builtin_amdgcn_mfma_f32_16x16x32_bf16(Bt[n][k], At[m][k], acc[ai][bj][m][n], 0, 0, 0); __builtin_amdgcn_s_setprio(0); } while (0)
; #define PG8_WAIT_V(n) asm volatile("s_waitcnt vmcnt(" #n ")" ::: "memory")
; #define PG8_WAIT_L(n) asm volatile("s_waitcnt lgkmcnt(" #n ")" ::: "memory")
; #define PG8_BAR __builtin_amdgcn_s_barrier()
; __device__ __forceinline__ void rstd8(const float* SS, int rowb, int lane, float (&rs)[2][4]) {
;     f32x4 p[2][4];
; #pragma unroll
;     for (int ai = 0; ai < 2; ++ai)
; #pragma unroll
;         for (int m = 0; m < 4; ++m) p[ai][m] = *(const f32x4*)(SS + (size_t)(rowb + HALF * ai + 16 * m + (lane >> 2)) * 16 + 4 * (lane & 3));
;     asm volatile("" : "+v"(p[0][0]), "+v"(p[0][1]), "+v"(p[0][2]), "+v"(p[0][3]), "+v"(p[1][0]), "+v"(p[1][1]), "+v"(p[1][2]), "+v"(p[1][3]));
; template <class Epi, class Sched, bool ALIGN_EPI = false, bool SP2 = false>
; __device__ __forceinline__ void gemm_phase(PG8_LAS unsigned char* lds, const Gemm g, const Sched& S, const Epi& E, const bool skip_epi = false) {
;     ...
;             PG8_LDA(At, 1, 1); PG8_STAGE(PG8_SB(1, 0), b3, voffB); PG8_STAGE(PG8_SB(1, 1), b3 + hstep, voffB); PG8_STAGE_A(1, 0, a3, true);
;             PG8_WAIT_V(8); PG8_WAIT_L(0); PG8_BAR; PG8_MMA(1, 0, At, B0); PG8_MMA(1, 1, At, B1); PG8_BAR; PG8_SCHED;
	s_add_i32 s26, s59, s28
	s_add_i32 m0, s26, 0xffffff80
	ds_read_b128 v[192:195], v172 offset:49152
	ds_read_b128 v[196:199], v172 offset:50176
	ds_read_b128 v[200:203], v172 offset:51200
	ds_read_b128 v[204:207], v172 offset:52224
	ds_read_b128 v[208:211], v172 offset:53248
	ds_read_b128 v[212:215], v172 offset:54272
	ds_read_b128 v[216:219], v172 offset:55296
	ds_read_b128 v[220:223], v172 offset:56320
	global_load_lds_dwordx4 v134, s[24:25] offset:128
	s_add_i32 m0, s26, 0x1f80
	s_add_i32 s26, s60, s28
	global_load_lds_dwordx4 v130, s[24:25] offset:128
	s_add_u32 s24, s24, 0x40080
	s_addc_u32 s25, s25, 0
	s_mov_b32 m0, s26
	s_nop 0
	global_load_lds_dwordx4 v134, s[24:25]
	s_add_i32 m0, s26, 0x2000
	s_nop 0
	global_load_lds_dwordx4 v130, s[24:25]
	s_add_i32 m0, s37, 0xffffff80
	s_nop 0
	global_load_lds_dwordx4 v136, s[98:99] offset:128
	s_add_i32 m0, s38, 0xffffff80
	s_nop 0
	global_load_lds_dwordx4 v132, s[98:99] offset:128
	s_waitcnt vmcnt(8)
	s_waitcnt lgkmcnt(0)
	s_barrier
	s_setprio 3
	s_waitcnt lgkmcnt(0)
	v_mfma_f32_16x16x32_bf16 v[62:65], v[148:151], v[192:195], v[62:65]
	v_mfma_f32_16x16x32_bf16 v[58:61], v[156:159], v[192:195], v[58:61]
	v_mfma_f32_16x16x32_bf16 v[50:53], v[148:151], v[200:203], v[50:53]
	v_mfma_f32_16x16x32_bf16 v[42:45], v[156:159], v[200:203], v[42:45]
	v_mfma_f32_16x16x32_bf16 v[34:37], v[148:151], v[208:211], v[34:37]
	v_mfma_f32_16x16x32_bf16 v[26:29], v[156:159], v[208:211], v[26:29]
	v_mfma_f32_16x16x32_bf16 v[18:21], v[148:151], v[216:219], v[18:21]
	v_mfma_f32_16x16x32_bf16 v[10:13], v[156:159], v[216:219], v[10:13]
	v_mfma_f32_16x16x32_bf16 v[62:65], v[152:155], v[196:199], v[62:65]
	v_mfma_f32_16x16x32_bf16 v[58:61], v[160:163], v[196:199], v[58:61]
	v_mfma_f32_16x16x32_bf16 v[50:53], v[152:155], v[204:207], v[50:53]
	v_mfma_f32_16x16x32_bf16 v[42:45], v[160:163], v[204:207], v[42:45]
	v_mfma_f32_16x16x32_bf16 v[34:37], v[152:155], v[212:215], v[34:37]
	v_mfma_f32_16x16x32_bf16 v[26:29], v[160:163], v[212:215], v[26:29]
	v_mfma_f32_16x16x32_bf16 v[18:21], v[152:155], v[220:223], v[18:21]
	v_mfma_f32_16x16x32_bf16 v[10:13], v[160:163], v[220:223], v[10:13]
	s_setprio 0
	s_setprio 3
	v_mfma_f32_16x16x32_bf16 v[54:57], v[176:179], v[192:195], v[54:57]
	v_mfma_f32_16x16x32_bf16 v[46:49], v[184:187], v[192:195], v[46:49]
	v_mfma_f32_16x16x32_bf16 v[38:41], v[176:179], v[200:203], v[38:41]
	v_mfma_f32_16x16x32_bf16 v[30:33], v[184:187], v[200:203], v[30:33]
	v_mfma_f32_16x16x32_bf16 v[22:25], v[176:179], v[208:211], v[22:25]
	v_mfma_f32_16x16x32_bf16 v[14:17], v[184:187], v[208:211], v[14:17]
	v_mfma_f32_16x16x32_bf16 v[6:9], v[176:179], v[216:219], v[6:9]
	v_mfma_f32_16x16x32_bf16 v[2:5], v[184:187], v[216:219], v[2:5]
	v_mfma_f32_16x16x32_bf16 v[54:57], v[180:183], v[196:199], v[54:57]
	v_mfma_f32_16x16x32_bf16 v[46:49], v[188:191], v[196:199], v[46:49]
	v_mfma_f32_16x16x32_bf16 v[38:41], v[180:183], v[204:207], v[38:41]
	v_mfma_f32_16x16x32_bf16 v[30:33], v[188:191], v[204:207], v[30:33]
	v_mfma_f32_16x16x32_bf16 v[22:25], v[180:183], v[212:215], v[22:25]
	v_mfma_f32_16x16x32_bf16 v[14:17], v[188:191], v[212:215], v[14:17]
	v_mfma_f32_16x16x32_bf16 v[6:9], v[180:183], v[220:223], v[6:9]
	v_mfma_f32_16x16x32_bf16 v[2:5], v[188:191], v[220:223], v[2:5]
	s_setprio 0
	s_barrier
	s_add_i32 s58, s58, 2
	s_add_u32 s22, s22, 0x100
	s_addc_u32 s23, s23, 0
	s_add_u32 s56, s56, 0x100
	s_addc_u32 s57, s57, 0
	s_cmp_gt_u32 s58, 13
	s_cbranch_scc0 .LBB0_944
	v_lshl_add_u32 v164, s20, 8, v167
	v_ashrrev_i32_e32 v165, 31, v164
	v_lshlrev_b64 v[148:149], 6, v[164:165]
	v_lshl_add_u64 v[148:149], v[138:139], 0, v[148:149]
	v_add_co_u32_e32 v150, vcc, 0x2000, v148
	v_addc_co_u32_e32 v151, vcc, 0, v149, vcc
	global_load_dwordx4 v[176:179], v[148:149], off
	global_load_dwordx4 v[180:183], v[148:149], off offset:1024
	global_load_dwordx4 v[184:187], v[148:149], off offset:2048
	global_load_dwordx4 v[188:191], v[148:149], off offset:3072
	global_load_dwordx4 v[192:195], v[150:151], off
	global_load_dwordx4 v[196:199], v[150:151], off offset:1024
	global_load_dwordx4 v[200:203], v[150:151], off offset:2048
	global_load_dwordx4 v[204:207], v[150:151], off offset:3072
	s_and_b64 vcc, exec, s[10:11]
	s_cbranch_vccz .LBB0_947
	s_barrier

; #define PG8_STAGE_A(b, h, ptr, NX) do { if constexpr (Sched::GATHER) { unsigned gs_[2]; gs_[0] = ((NX) && last_) ? gN[h][0] : gA[h][0]; gs_[1] = ((NX) && last_) ? gN[h][1] : gA[h][1]; PG8_STAGE(PG8_SA(b, h), ptr, gs_); } \
;         else PG8_STAGE(PG8_SA(b, h), (ptr) + ((h) ? hstep : (size_t)0), voffA); } while (0)
; #define PG8_STAGE(bufoff, gbase, voff) do { _Pragma("unroll") for (int _i = 0; _i < 2; ++_i) \
;         __builtin_amdgcn_global_load_lds((const unsigned*)((const char*)(gbase) + (voff)[_i]), (PG8_LAS unsigned*)(lds + (bufoff) + ldsw + _i * 8192), 16, 0, 0); } while (0)
; #define PG8_LDA(dst, b, h) do { _Pragma("unroll") for (int m = 0; m < 4; ++m) _Pragma("unroll") for (int k = 0; k < 2; ++k) dst[m][k] = *(const PG8_LAS bf16x8*)(lds + PG8_SA(b, h) + aoff + m * 2048 + k * 1024); } while (0)
; #define PG8_LDB(dst, b, h) do { _Pragma("unroll") for (int n = 0; n < 2; ++n) _Pragma("unroll") for (int k = 0; k < 2; ++k) dst[n][k] = *(const PG8_LAS bf16x8*)(lds + PG8_SB(b, h) + boff + n * 2048 + k * 1024); } while (0)
; #define PG8_WAIT_V(n) asm volatile("s_waitcnt vmcnt(" #n ")" ::: "memory")
; template <class Epi, class Sched, bool ALIGN_EPI = false, bool SP2 = false>
; __device__ __forceinline__ void gemm_phase(PG8_LAS unsigned char* lds, const Gemm g, const Sched& S, const Epi& E, const bool skip_epi = false) {
;     ...
;         const char* nA = has_next ? (const char*)g.A + (size_t)nxt.pm * pmstepA + nxt.ko : cA; const char* nB = has_next ? (const char*)g.Bt + (size_t)nxt.pn * tstep + nxt.ko : cB;
;         for (int t = 0; t < nt; t += 2) {
;             const bool last = (t == nt - 2); last_ = last && has_next;
;             const char* a1 = cA + (size_t)(t + 1) * kstep;
;             const char* a2 = last ? nA : cA + (size_t)(t + 2) * kstep; const char* b2 = last ? nB : cB + (size_t)(t + 2) * kstep;
;             const char* a3 = a2 + kstep; const char* b3 = b2 + kstep;
;             if (last && has_next) S.a_ready(nxt);
;             if constexpr (SP2) {
;             PG8_LDB(B0, 0, 0); PG8_LDB(B1, 0, 1); PG8_SCHED; PG8_LDA(At, 0, 0); PG8_STAGE_A(1, 1, a1, false);
;             PG8_WAIT_V(8); PG8_WAIT_L(0); PG8_BAR; PG8_MMA(0, 0, At, B0); PG8_MMA(0, 1, At, B1); PG8_BAR; PG8_SCHED;
;             PG8_LDA(At, 0, 1); PG8_STAGE(PG8_SB(0, 0), b2, voffB); PG8_STAGE(PG8_SB(0, 1), b2 + hstep, voffB); PG8_STAGE_A(0, 0, a2, true);
.LBB0_1323:
	s_ashr_i32 s25, s24, 31
	s_lshl_b64 s[26:27], s[24:25], 19
	s_add_u32 s26, s46, s26
	s_addc_u32 s27, s47, s27
	s_and_b64 s[28:29], s[6:7], exec
	s_cselect_b32 s25, s27, s35
	s_cselect_b32 s31, s26, s34
	s_ashr_i32 s23, s22, 31
	s_lshl_b64 s[28:29], s[22:23], 19
	s_add_u32 s28, s2, s28
	s_addc_u32 s29, s3, s29
	s_and_b64 s[38:39], s[6:7], exec
	s_cselect_b32 s23, s29, s37
	s_cselect_b32 s60, s28, s36
	s_add_u32 s34, s34, 0x40080
	s_addc_u32 s35, s35, 0
	s_add_u32 s61, s36, 0x100
	s_addc_u32 s62, s37, 0
	s_mov_b32 s63, -2
	s_waitcnt vmcnt(0)
	s_waitcnt lgkmcnt(0)
	ds_read_b128 v[98:101], v225
	ds_read_b128 v[110:113], v225 offset:1024
	ds_read_b128 v[122:125], v225 offset:2048
	ds_read_b128 v[130:133], v225 offset:3072
	ds_read_b128 v[146:149], v226
	ds_read_b128 v[150:153], v226 offset:1024
	ds_read_b128 v[154:157], v226 offset:2048
	ds_read_b128 v[158:161], v226 offset:3072
	s_add_u32 s36, s34, 0xfffc0080
	s_addc_u32 s37, s35, -1
	s_cmp_eq_u32 s63, 12
	s_cselect_b32 s39, s25, s37
	s_cselect_b32 s38, s31, s36
	s_cselect_b32 s37, s23, s62
	s_cselect_b32 s36, s60, s61
	s_add_i32 m0, s41, 0xc000
	ds_read_b128 v[162:165], v227
	ds_read_b128 v[166:169], v227 offset:1024
	ds_read_b128 v[170:173], v227 offset:2048
	ds_read_b128 v[174:177], v227 offset:3072
	ds_read_b128 v[178:181], v227 offset:4096
	ds_read_b128 v[182:185], v227 offset:5120
	ds_read_b128 v[202:205], v227 offset:6144
	ds_read_b128 v[206:209], v227 offset:7168
	global_load_lds_dwordx4 v194, s[34:35]
	s_add_i32 m0, s41, 0xe000
	s_nop 0
	global_load_lds_dwordx4 v196, s[34:35]
	s_waitcnt vmcnt(8)
	s_waitcnt lgkmcnt(0)
	s_barrier
	s_setprio 3
	s_waitcnt lgkmcnt(0)
	v_mfma_f32_16x16x32_bf16 v[142:145], v[98:101], v[162:165], 0
	v_mfma_f32_16x16x32_bf16 v[138:141], v[122:125], v[162:165], 0
	v_mfma_f32_16x16x32_bf16 v[118:121], v[98:101], v[170:173], 0
	v_mfma_f32_16x16x32_bf16 v[114:117], v[122:125], v[170:173], 0
	v_mfma_f32_16x16x32_bf16 v[94:97], v[98:101], v[178:181], 0
	v_mfma_f32_16x16x32_bf16 v[90:93], v[122:125], v[178:181], 0
	v_mfma_f32_16x16x32_bf16 v[78:81], v[98:101], v[202:205], 0
	v_mfma_f32_16x16x32_bf16 v[74:77], v[122:125], v[202:205], 0
	v_mfma_f32_16x16x32_bf16 v[142:145], v[110:113], v[166:169], v[142:145]
	v_mfma_f32_16x16x32_bf16 v[138:141], v[130:133], v[166:169], v[138:141]
	v_mfma_f32_16x16x32_bf16 v[118:121], v[110:113], v[174:177], v[118:121]
	v_mfma_f32_16x16x32_bf16 v[114:117], v[130:133], v[174:177], v[114:117]
	v_mfma_f32_16x16x32_bf16 v[94:97], v[110:113], v[182:185], v[94:97]
	v_mfma_f32_16x16x32_bf16 v[90:93], v[130:133], v[182:185], v[90:93]
	v_mfma_f32_16x16x32_bf16 v[78:81], v[110:113], v[206:209], v[78:81]
	v_mfma_f32_16x16x32_bf16 v[74:77], v[130:133], v[206:209], v[74:77]
	s_setprio 0
	s_setprio 3
	v_mfma_f32_16x16x32_bf16 v[134:137], v[146:149], v[162:165], 0
	v_mfma_f32_16x16x32_bf16 v[126:129], v[154:157], v[162:165], 0
	v_mfma_f32_16x16x32_bf16 v[106:109], v[146:149], v[170:173], 0
	v_mfma_f32_16x16x32_bf16 v[102:105], v[154:157], v[170:173], 0
	v_mfma_f32_16x16x32_bf16 v[86:89], v[146:149], v[178:181], 0
	v_mfma_f32_16x16x32_bf16 v[82:85], v[154:157], v[178:181], 0
	v_mfma_f32_16x16x32_bf16 v[70:73], v[146:149], v[202:205], 0
	v_mfma_f32_16x16x32_bf16 v[66:69], v[154:157], v[202:205], 0
	v_mfma_f32_16x16x32_bf16 v[134:137], v[150:153], v[166:169], v[134:137]
	v_mfma_f32_16x16x32_bf16 v[126:129], v[158:161], v[166:169], v[126:129]
	v_mfma_f32_16x16x32_bf16 v[106:109], v[150:153], v[174:177], v[106:109]
	v_mfma_f32_16x16x32_bf16 v[102:105], v[158:161], v[174:177], v[102:105]
	v_mfma_f32_16x16x32_bf16 v[86:89], v[150:153], v[182:185], v[86:89]
	v_mfma_f32_16x16x32_bf16 v[82:85], v[158:161], v[182:185], v[82:85]
	v_mfma_f32_16x16x32_bf16 v[70:73], v[150:153], v[206:209], v[70:73]
	v_mfma_f32_16x16x32_bf16 v[66:69], v[158:161], v[206:209], v[66:69]
	s_setprio 0
	s_barrier
	s_add_i32 s64, s57, s40
	s_mov_b32 m0, s64
	ds_read_b128 v[162:165], v227 offset:16384
	ds_read_b128 v[166:169], v227 offset:17408
	ds_read_b128 v[170:173], v227 offset:18432
	ds_read_b128 v[174:177], v227 offset:19456
	ds_read_b128 v[178:181], v227 offset:20480
	ds_read_b128 v[182:185], v227 offset:21504
	ds_read_b128 v[202:205], v227 offset:22528
	ds_read_b128 v[206:209], v227 offset:23552
	global_load_lds_dwordx4 v188, s[36:37]
	s_add_i32 m0, s64, 0x2000
	s_add_u32 s64, s36, 0x40000
	s_addc_u32 s65, s37, 0
	s_add_i32 s66, s58, s40
	global_load_lds_dwordx4 v192, s[36:37]
	s_mov_b32 m0, s66
	s_mov_b64 s[98:99], s[38:39]
	global_load_lds_dwordx4 v188, s[64:65]
	s_add_i32 m0, s66, 0x2000
	s_nop 0
	global_load_lds_dwordx4 v192, s[64:65]
	s_mov_b32 m0, s41
	s_nop 0
	global_load_lds_dwordx4 v186, s[38:39]
	s_mov_b32 m0, s44
	s_nop 0
	global_load_lds_dwordx4 v190, s[38:39]
	s_waitcnt vmcnt(8)
	s_waitcnt lgkmcnt(0)
	s_barrier
; #define PG8_STAGE_A(b, h, ptr, NX) do { if constexpr (Sched::GATHER) { unsigned gs_[2]; gs_[0] = ((NX) && last_) ? gN[h][0] : gA[h][0]; gs_[1] = ((NX) && last_) ? gN[h][1] : gA[h][1]; PG8_STAGE(PG8_SA(b, h), ptr, gs_); } \
;         else PG8_STAGE(PG8_SA(b, h), (ptr) + ((h) ? hstep : (size_t)0), voffA); } while (0)
; #define PG8_STAGE(bufoff, gbase, voff) do { _Pragma("unroll") for (int _i = 0; _i < 2; ++_i) \
;         __builtin_amdgcn_global_load_lds((const unsigned*)((const char*)(gbase) + (voff)[_i]), (PG8_LAS unsigned*)(lds + (bufoff) + ldsw + _i * 8192), 16, 0, 0); } while (0)
; #define PG8_LDA(dst, b, h) do { _Pragma("unroll") for (int m = 0; m < 4; ++m) _Pragma("unroll") for (int k = 0; k < 2; ++k) dst[m][k] = *(const PG8_LAS bf16x8*)(lds + PG8_SA(b, h) + aoff + m * 2048 + k * 1024); } while (0)
; #define PG8_LDB(dst, b, h) do { _Pragma("unroll") for (int n = 0; n < 2; ++n) _Pragma("unroll") for (int k = 0; k < 2; ++k) dst[n][k] = *(const PG8_LAS bf16x8*)(lds + PG8_SB(b, h) + boff + n * 2048 + k * 1024); } while (0)
; #define PG8_MMA(ai, bj, At, Bt) do { __builtin_amdgcn_s_setprio(1); _Pragma("unroll") for (int m = 0; m < 4; ++m) _Pragma("unroll") for (int n = 0; n < 2; ++n) _Pragma("unroll") for (int k = 0; k < 2; ++k) \
;         acc[ai][bj][m][n] = __builtin_amdgcn_mfma_f32_16x16x32_bf16(Bt[n][k], At[m][k], acc[ai][bj][m][n], 0, 0, 0); __builtin_amdgcn_s_setprio(0); } while (0)
; #define PG8_WAIT_V(n) asm volatile("s_waitcnt vmcnt(" #n ")" ::: "memory")
; #define PG8_WAIT_L(n) asm volatile("s_waitcnt lgkmcnt(" #n ")" ::: "memory")
; #define PG8_BAR __builtin_amdgcn_s_barrier()
; #define PG8_SCHED __builtin_amdgcn_sched_barrier(0)
; template <class Epi, class Sched, bool ALIGN_EPI = false, bool SP2 = false>
; __device__ __forceinline__ void gemm_phase(PG8_LAS unsigned char* lds, const Gemm g, const Sched& S, const Epi& E, const bool skip_epi = false) {
;     ...
;             PG8_WAIT_V(8); PG8_WAIT_L(0); PG8_BAR; PG8_MMA(1, 0, At, B0); PG8_MMA(1, 1, At, B1); PG8_BAR; PG8_SCHED;
;             PG8_LDB(B0, 1, 0); PG8_LDB(B1, 1, 1); PG8_SCHED; PG8_LDA(At, 1, 0); PG8_STAGE_A(0, 1, a2, true);
;             PG8_WAIT_V(8); PG8_WAIT_L(0); PG8_BAR; PG8_MMA(0, 0, At, B0); PG8_MMA(0, 1, At, B1); PG8_BAR; PG8_SCHED;
;             PG8_LDA(At, 1, 1); PG8_STAGE(PG8_SB(1, 0), b3, voffB); PG8_STAGE(PG8_SB(1, 1), b3 + hstep, voffB); PG8_STAGE_A(1, 0, a3, true);
	s_setprio 3
	s_waitcnt lgkmcnt(0)
	v_mfma_f32_16x16x32_bf16 v[62:65], v[98:101], v[162:165], 0
	v_mfma_f32_16x16x32_bf16 v[58:61], v[122:125], v[162:165], 0
	v_mfma_f32_16x16x32_bf16 v[46:49], v[98:101], v[170:173], 0
	v_mfma_f32_16x16x32_bf16 v[42:45], v[122:125], v[170:173], 0
	v_mfma_f32_16x16x32_bf16 v[30:33], v[98:101], v[178:181], 0
	v_mfma_f32_16x16x32_bf16 v[26:29], v[122:125], v[178:181], 0
	v_mfma_f32_16x16x32_bf16 v[14:17], v[98:101], v[202:205], 0
	v_mfma_f32_16x16x32_bf16 v[10:13], v[122:125], v[202:205], 0
	v_mfma_f32_16x16x32_bf16 v[62:65], v[110:113], v[166:169], v[62:65]
	v_mfma_f32_16x16x32_bf16 v[58:61], v[130:133], v[166:169], v[58:61]
	v_mfma_f32_16x16x32_bf16 v[46:49], v[110:113], v[174:177], v[46:49]
	v_mfma_f32_16x16x32_bf16 v[42:45], v[130:133], v[174:177], v[42:45]
	v_mfma_f32_16x16x32_bf16 v[30:33], v[110:113], v[182:185], v[30:33]
	v_mfma_f32_16x16x32_bf16 v[26:29], v[130:133], v[182:185], v[26:29]
	v_mfma_f32_16x16x32_bf16 v[14:17], v[110:113], v[206:209], v[14:17]
	v_mfma_f32_16x16x32_bf16 v[10:13], v[130:133], v[206:209], v[10:13]
	s_setprio 0
	s_setprio 3
	v_mfma_f32_16x16x32_bf16 v[54:57], v[146:149], v[162:165], 0
	v_mfma_f32_16x16x32_bf16 v[50:53], v[154:157], v[162:165], 0
	v_mfma_f32_16x16x32_bf16 v[38:41], v[146:149], v[170:173], 0
	v_mfma_f32_16x16x32_bf16 v[34:37], v[154:157], v[170:173], 0
	v_mfma_f32_16x16x32_bf16 v[22:25], v[146:149], v[178:181], 0
	v_mfma_f32_16x16x32_bf16 v[18:21], v[154:157], v[178:181], 0
	v_mfma_f32_16x16x32_bf16 v[6:9], v[146:149], v[202:205], 0
	v_mfma_f32_16x16x32_bf16 v[2:5], v[154:157], v[202:205], 0
	v_mfma_f32_16x16x32_bf16 v[54:57], v[150:153], v[166:169], v[54:57]
	v_mfma_f32_16x16x32_bf16 v[50:53], v[158:161], v[166:169], v[50:53]
	v_mfma_f32_16x16x32_bf16 v[38:41], v[150:153], v[174:177], v[38:41]
	v_mfma_f32_16x16x32_bf16 v[34:37], v[158:161], v[174:177], v[34:37]
	v_mfma_f32_16x16x32_bf16 v[22:25], v[150:153], v[182:185], v[22:25]
	v_mfma_f32_16x16x32_bf16 v[18:21], v[158:161], v[182:185], v[18:21]
	v_mfma_f32_16x16x32_bf16 v[6:9], v[150:153], v[206:209], v[6:9]
	v_mfma_f32_16x16x32_bf16 v[2:5], v[158:161], v[206:209], v[2:5]
	s_setprio 0
	s_barrier
	s_add_i32 s64, 0, 0x18000
	s_add_i32 s65, 0, 0x1c000
	v_add_u32_e32 v130, s64, v220
	v_add_u32_e32 v158, s65, v220
	ds_read_b128 v[98:101], v130
	ds_read_b128 v[110:113], v130 offset:1024
	ds_read_b128 v[122:125], v130 offset:2048
	ds_read_b128 v[130:133], v130 offset:3072
	ds_read_b128 v[146:149], v158
	ds_read_b128 v[150:153], v158 offset:1024
	ds_read_b128 v[154:157], v158 offset:2048
	ds_read_b128 v[158:161], v158 offset:3072
	s_add_u32 s38, s38, 0x40000
	s_addc_u32 s39, s39, 0
	s_mov_b32 m0, s45
	ds_read_b128 v[162:165], v227 offset:32768
	ds_read_b128 v[166:169], v227 offset:33792
	ds_read_b128 v[170:173], v227 offset:34816
	ds_read_b128 v[174:177], v227 offset:35840
	ds_read_b128 v[178:181], v227 offset:36864
	ds_read_b128 v[182:185], v227 offset:37888
	ds_read_b128 v[202:205], v227 offset:38912
	ds_read_b128 v[206:209], v227 offset:39936
	global_load_lds_dwordx4 v186, s[38:39]
	s_mov_b32 m0, s48
	s_nop 0
	global_load_lds_dwordx4 v190, s[38:39]
	s_waitcnt vmcnt(8)
	s_waitcnt lgkmcnt(0)
	s_barrier
	s_setprio 3
	s_waitcnt lgkmcnt(0)
	v_mfma_f32_16x16x32_bf16 v[142:145], v[98:101], v[162:165], v[142:145]
	v_mfma_f32_16x16x32_bf16 v[138:141], v[122:125], v[162:165], v[138:141]
	v_mfma_f32_16x16x32_bf16 v[118:121], v[98:101], v[170:173], v[118:121]
	v_mfma_f32_16x16x32_bf16 v[114:117], v[122:125], v[170:173], v[114:117]
	v_mfma_f32_16x16x32_bf16 v[94:97], v[98:101], v[178:181], v[94:97]
	v_mfma_f32_16x16x32_bf16 v[90:93], v[122:125], v[178:181], v[90:93]
	v_mfma_f32_16x16x32_bf16 v[78:81], v[98:101], v[202:205], v[78:81]
	v_mfma_f32_16x16x32_bf16 v[74:77], v[122:125], v[202:205], v[74:77]
	v_mfma_f32_16x16x32_bf16 v[142:145], v[110:113], v[166:169], v[142:145]
	v_mfma_f32_16x16x32_bf16 v[138:141], v[130:133], v[166:169], v[138:141]
	v_mfma_f32_16x16x32_bf16 v[118:121], v[110:113], v[174:177], v[118:121]
	v_mfma_f32_16x16x32_bf16 v[114:117], v[130:133], v[174:177], v[114:117]
	v_mfma_f32_16x16x32_bf16 v[94:97], v[110:113], v[182:185], v[94:97]
	v_mfma_f32_16x16x32_bf16 v[90:93], v[130:133], v[182:185], v[90:93]
	v_mfma_f32_16x16x32_bf16 v[78:81], v[110:113], v[206:209], v[78:81]
	v_mfma_f32_16x16x32_bf16 v[74:77], v[130:133], v[206:209], v[74:77]
	s_setprio 0
	s_setprio 3
	v_mfma_f32_16x16x32_bf16 v[134:137], v[146:149], v[162:165], v[134:137]
	v_mfma_f32_16x16x32_bf16 v[126:129], v[154:157], v[162:165], v[126:129]
	v_mfma_f32_16x16x32_bf16 v[106:109], v[146:149], v[170:173], v[106:109]
	v_mfma_f32_16x16x32_bf16 v[102:105], v[154:157], v[170:173], v[102:105]
	v_mfma_f32_16x16x32_bf16 v[86:89], v[146:149], v[178:181], v[86:89]
	v_mfma_f32_16x16x32_bf16 v[82:85], v[154:157], v[178:181], v[82:85]
	v_mfma_f32_16x16x32_bf16 v[70:73], v[146:149], v[202:205], v[70:73]
	v_mfma_f32_16x16x32_bf16 v[66:69], v[154:157], v[202:205], v[66:69]
	v_mfma_f32_16x16x32_bf16 v[134:137], v[150:153], v[166:169], v[134:137]
	v_mfma_f32_16x16x32_bf16 v[126:129], v[158:161], v[166:169], v[126:129]
	v_mfma_f32_16x16x32_bf16 v[106:109], v[150:153], v[174:177], v[106:109]
	v_mfma_f32_16x16x32_bf16 v[102:105], v[158:161], v[174:177], v[102:105]
	v_mfma_f32_16x16x32_bf16 v[86:89], v[150:153], v[182:185], v[86:89]
	v_mfma_f32_16x16x32_bf16 v[82:85], v[158:161], v[182:185], v[82:85]
	v_mfma_f32_16x16x32_bf16 v[70:73], v[150:153], v[206:209], v[70:73]
	v_mfma_f32_16x16x32_bf16 v[66:69], v[158:161], v[206:209], v[66:69]
	s_setprio 0
	s_barrier
; #define PG8_STAGE_A(b, h, ptr, NX) do { if constexpr (Sched::GATHER) { unsigned gs_[2]; gs_[0] = ((NX) && last_) ? gN[h][0] : gA[h][0]; gs_[1] = ((NX) && last_) ? gN[h][1] : gA[h][1]; PG8_STAGE(PG8_SA(b, h), ptr, gs_); } \
;         else PG8_STAGE(PG8_SA(b, h), (ptr) + ((h) ? hstep : (size_t)0), voffA); } while (0)
; #define PG8_STAGE(bufoff, gbase, voff) do { _Pragma("unroll") for (int _i = 0; _i < 2; ++_i) \
;         __builtin_amdgcn_global_load_lds((const unsigned*)((const char*)(gbase) + (voff)[_i]), (PG8_LAS unsigned*)(lds + (bufoff) + ldsw + _i * 8192), 16, 0, 0); } while (0)
; #define PG8_WAIT_V(n) asm volatile("s_waitcnt vmcnt(" #n ")" ::: "memory")
; #define PG8_BAR __builtin_amdgcn_s_barrier()
; template <class Epi, class Sched, bool ALIGN_EPI = false, bool SP2 = false>
; __device__ __forceinline__ void gemm_phase(PG8_LAS unsigned char* lds, const Gemm g, const Sched& S, const Epi& E, const bool skip_epi = false) {
;     ...
;         for (int t = 0; t < nt; t += 2) {
;             const bool last = (t == nt - 2); last_ = last && has_next;
;             const char* a1 = cA + (size_t)(t + 1) * kstep;
;             const char* a2 = last ? nA : cA + (size_t)(t + 2) * kstep; const char* b2 = last ? nB : cB + (size_t)(t + 2) * kstep;
;             const char* a3 = a2 + kstep; const char* b3 = b2 + kstep;
;             if (last && has_next) S.a_ready(nxt);
;             if constexpr (SP2) {
;             PG8_LDB(B0, 0, 0); PG8_LDB(B1, 0, 1); PG8_SCHED; PG8_LDA(At, 0, 0); PG8_STAGE_A(1, 1, a1, false);
;             PG8_WAIT_V(8); PG8_WAIT_L(0); PG8_BAR; PG8_MMA(0, 0, At, B0); PG8_MMA(0, 1, At, B1); PG8_BAR; PG8_SCHED;
;             PG8_LDA(At, 0, 1); PG8_STAGE(PG8_SB(0, 0), b2, voffB); PG8_STAGE(PG8_SB(0, 1), b2 + hstep, voffB); PG8_STAGE_A(0, 0, a2, true);
;             PG8_WAIT_V(8); PG8_WAIT_L(0); PG8_BAR; PG8_MMA(1, 0, At, B0); PG8_MMA(1, 1, At, B1); PG8_BAR; PG8_SCHED;
;             PG8_LDB(B0, 1, 0); PG8_LDB(B1, 1, 1); PG8_SCHED; PG8_LDA(At, 1, 0); PG8_STAGE_A(0, 1, a2, true);
;             PG8_WAIT_V(8); PG8_WAIT_L(0); PG8_BAR; PG8_MMA(0, 0, At, B0); PG8_MMA(0, 1, At, B1); PG8_BAR; PG8_SCHED;
;             PG8_LDA(At, 1, 1); PG8_STAGE(PG8_SB(1, 0), b3, voffB); PG8_STAGE(PG8_SB(1, 1), b3 + hstep, voffB); PG8_STAGE_A(1, 0, a3, true);
;             PG8_WAIT_V(8); PG8_WAIT_L(0); PG8_BAR; PG8_MMA(1, 0, At, B0); PG8_MMA(1, 1, At, B1); PG8_BAR; PG8_SCHED;
	s_add_i32 s38, s64, s40
	s_add_i32 m0, s38, 0xffffff80
	ds_read_b128 v[162:165], v227 offset:49152
	ds_read_b128 v[166:169], v227 offset:50176
	ds_read_b128 v[170:173], v227 offset:51200
	ds_read_b128 v[174:177], v227 offset:52224
	ds_read_b128 v[178:181], v227 offset:53248
	ds_read_b128 v[182:185], v227 offset:54272
	ds_read_b128 v[202:205], v227 offset:55296
	ds_read_b128 v[206:209], v227 offset:56320
	global_load_lds_dwordx4 v188, s[36:37] offset:128
	s_add_i32 m0, s38, 0x1f80
	s_add_i32 s38, s65, s40
	global_load_lds_dwordx4 v192, s[36:37] offset:128
	s_add_u32 s36, s36, 0x40080
	s_addc_u32 s37, s37, 0
	s_mov_b32 m0, s38
	s_nop 0
	global_load_lds_dwordx4 v188, s[36:37]
	s_add_i32 m0, s38, 0x2000
	s_nop 0
	global_load_lds_dwordx4 v192, s[36:37]
	s_add_i32 m0, s53, 0xffffff80
	s_nop 0
	global_load_lds_dwordx4 v186, s[98:99] offset:128
	s_add_i32 m0, s54, 0xffffff80
	s_nop 0
	global_load_lds_dwordx4 v190, s[98:99] offset:128
	s_waitcnt vmcnt(8)
	s_waitcnt lgkmcnt(0)
	s_barrier
	s_setprio 3
	s_waitcnt lgkmcnt(0)
	v_mfma_f32_16x16x32_bf16 v[62:65], v[98:101], v[162:165], v[62:65]
	v_mfma_f32_16x16x32_bf16 v[58:61], v[122:125], v[162:165], v[58:61]
	v_mfma_f32_16x16x32_bf16 v[46:49], v[98:101], v[170:173], v[46:49]
	v_mfma_f32_16x16x32_bf16 v[42:45], v[122:125], v[170:173], v[42:45]
	v_mfma_f32_16x16x32_bf16 v[30:33], v[98:101], v[178:181], v[30:33]
	v_mfma_f32_16x16x32_bf16 v[26:29], v[122:125], v[178:181], v[26:29]
	v_mfma_f32_16x16x32_bf16 v[14:17], v[98:101], v[202:205], v[14:17]
	v_mfma_f32_16x16x32_bf16 v[10:13], v[122:125], v[202:205], v[10:13]
	v_mfma_f32_16x16x32_bf16 v[62:65], v[110:113], v[166:169], v[62:65]
	v_mfma_f32_16x16x32_bf16 v[58:61], v[130:133], v[166:169], v[58:61]
	v_mfma_f32_16x16x32_bf16 v[46:49], v[110:113], v[174:177], v[46:49]
	v_mfma_f32_16x16x32_bf16 v[42:45], v[130:133], v[174:177], v[42:45]
	v_mfma_f32_16x16x32_bf16 v[30:33], v[110:113], v[182:185], v[30:33]
	v_mfma_f32_16x16x32_bf16 v[26:29], v[130:133], v[182:185], v[26:29]
	v_mfma_f32_16x16x32_bf16 v[14:17], v[110:113], v[206:209], v[14:17]
	v_mfma_f32_16x16x32_bf16 v[10:13], v[130:133], v[206:209], v[10:13]
	s_setprio 0
	s_setprio 3
	v_mfma_f32_16x16x32_bf16 v[54:57], v[146:149], v[162:165], v[54:57]
	v_mfma_f32_16x16x32_bf16 v[50:53], v[154:157], v[162:165], v[50:53]
	v_mfma_f32_16x16x32_bf16 v[38:41], v[146:149], v[170:173], v[38:41]
	v_mfma_f32_16x16x32_bf16 v[34:37], v[154:157], v[170:173], v[34:37]
	v_mfma_f32_16x16x32_bf16 v[22:25], v[146:149], v[178:181], v[22:25]
	v_mfma_f32_16x16x32_bf16 v[18:21], v[154:157], v[178:181], v[18:21]
	v_mfma_f32_16x16x32_bf16 v[6:9], v[146:149], v[202:205], v[6:9]
	v_mfma_f32_16x16x32_bf16 v[2:5], v[154:157], v[202:205], v[2:5]
	v_mfma_f32_16x16x32_bf16 v[54:57], v[150:153], v[166:169], v[54:57]
	v_mfma_f32_16x16x32_bf16 v[50:53], v[158:161], v[166:169], v[50:53]
	v_mfma_f32_16x16x32_bf16 v[38:41], v[150:153], v[174:177], v[38:41]
	v_mfma_f32_16x16x32_bf16 v[34:37], v[158:161], v[174:177], v[34:37]
	v_mfma_f32_16x16x32_bf16 v[22:25], v[150:153], v[182:185], v[22:25]
	v_mfma_f32_16x16x32_bf16 v[18:21], v[158:161], v[182:185], v[18:21]
	v_mfma_f32_16x16x32_bf16 v[6:9], v[150:153], v[206:209], v[6:9]
	v_mfma_f32_16x16x32_bf16 v[2:5], v[158:161], v[206:209], v[2:5]
	s_setprio 0
	s_barrier
	s_add_i32 s63, s63, 2
	s_add_u32 s34, s34, 0x100
	s_addc_u32 s35, s35, 0
	s_add_u32 s61, s61, 0x100
	s_addc_u32 s62, s62, 0
	s_cmp_gt_u32 s63, 13
.LBB0_1324:
	ds_read_b128 v[98:101], v225
	ds_read_b128 v[110:113], v225 offset:1024
	ds_read_b128 v[122:125], v225 offset:2048
	ds_read_b128 v[130:133], v225 offset:3072
	ds_read_b128 v[146:149], v226
	ds_read_b128 v[150:153], v226 offset:1024
	ds_read_b128 v[154:157], v226 offset:2048
	ds_read_b128 v[158:161], v226 offset:3072
	s_add_u32 s36, s34, 0xfffc0080
	s_addc_u32 s37, s35, -1
	s_cmp_eq_u32 s63, 12
	s_cselect_b32 s39, s25, s37
	s_cselect_b32 s38, s31, s36
	s_cselect_b32 s37, s23, s62
	s_cselect_b32 s36, s60, s61
	s_add_i32 m0, s41, 0xc000
	ds_read_b128 v[162:165], v227
	ds_read_b128 v[166:169], v227 offset:1024
	ds_read_b128 v[170:173], v227 offset:2048
	ds_read_b128 v[174:177], v227 offset:3072
	ds_read_b128 v[178:181], v227 offset:4096
	ds_read_b128 v[182:185], v227 offset:5120
	ds_read_b128 v[202:205], v227 offset:6144
	ds_read_b128 v[206:209], v227 offset:7168
	global_load_lds_dwordx4 v194, s[34:35]
	s_add_i32 m0, s41, 0xe000
	s_nop 0
	global_load_lds_dwordx4 v196, s[34:35]
	s_waitcnt vmcnt(8)
	s_waitcnt lgkmcnt(0)
	s_barrier
; #define PG8_STAGE_A(b, h, ptr, NX) do { if constexpr (Sched::GATHER) { unsigned gs_[2]; gs_[0] = ((NX) && last_) ? gN[h][0] : gA[h][0]; gs_[1] = ((NX) && last_) ? gN[h][1] : gA[h][1]; PG8_STAGE(PG8_SA(b, h), ptr, gs_); } \
;         else PG8_STAGE(PG8_SA(b, h), (ptr) + ((h) ? hstep : (size_t)0), voffA); } while (0)
; #define PG8_STAGE(bufoff, gbase, voff) do { _Pragma("unroll") for (int _i = 0; _i < 2; ++_i) \
;         __builtin_amdgcn_global_load_lds((const unsigned*)((const char*)(gbase) + (voff)[_i]), (PG8_LAS unsigned*)(lds + (bufoff) + ldsw + _i * 8192), 16, 0, 0); } while (0)
; #define PG8_LDA(dst, b, h) do { _Pragma("unroll") for (int m = 0; m < 4; ++m) _Pragma("unroll") for (int k = 0; k < 2; ++k) dst[m][k] = *(const PG8_LAS bf16x8*)(lds + PG8_SA(b, h) + aoff + m * 2048 + k * 1024); } while (0)
; #define PG8_LDB(dst, b, h) do { _Pragma("unroll") for (int n = 0; n < 2; ++n) _Pragma("unroll") for (int k = 0; k < 2; ++k) dst[n][k] = *(const PG8_LAS bf16x8*)(lds + PG8_SB(b, h) + boff + n * 2048 + k * 1024); } while (0)
; #define PG8_MMA(ai, bj, At, Bt) do { __builtin_amdgcn_s_setprio(1); _Pragma("unroll") for (int m = 0; m < 4; ++m) _Pragma("unroll") for (int n = 0; n < 2; ++n) _Pragma("unroll") for (int k = 0; k < 2; ++k) \
;         acc[ai][bj][m][n] = __builtin_amdgcn_mfma_f32_16x16x32_bf16(Bt[n][k], At[m][k], acc[ai][bj][m][n], 0, 0, 0); __builtin_amdgcn_s_setprio(0); } while (0)
; #define PG8_WAIT_V(n) asm volatile("s_waitcnt vmcnt(" #n ")" ::: "memory")
; #define PG8_WAIT_L(n) asm volatile("s_waitcnt lgkmcnt(" #n ")" ::: "memory")
; #define PG8_BAR __builtin_amdgcn_s_barrier()
; #define PG8_SCHED __builtin_amdgcn_sched_barrier(0)
; template <class Epi, class Sched, bool ALIGN_EPI = false, bool SP2 = false>
; __device__ __forceinline__ void gemm_phase(PG8_LAS unsigned char* lds, const Gemm g, const Sched& S, const Epi& E, const bool skip_epi = false) {
;     ...
;             PG8_LDB(B0, 0, 0); PG8_LDB(B1, 0, 1); PG8_SCHED; PG8_LDA(At, 0, 0); PG8_STAGE_A(1, 1, a1, false);
;             PG8_WAIT_V(8); PG8_WAIT_L(0); PG8_BAR; PG8_MMA(0, 0, At, B0); PG8_MMA(0, 1, At, B1); PG8_BAR; PG8_SCHED;
;             PG8_LDA(At, 0, 1); PG8_STAGE(PG8_SB(0, 0), b2, voffB); PG8_STAGE(PG8_SB(0, 1), b2 + hstep, voffB); PG8_STAGE_A(0, 0, a2, true);
;             PG8_WAIT_V(8); PG8_WAIT_L(0); PG8_BAR; PG8_MMA(1, 0, At, B0); PG8_MMA(1, 1, At, B1); PG8_BAR; PG8_SCHED;
	s_setprio 3
	s_waitcnt lgkmcnt(0)
	v_mfma_f32_16x16x32_bf16 v[142:145], v[98:101], v[162:165], v[142:145]
	v_mfma_f32_16x16x32_bf16 v[138:141], v[122:125], v[162:165], v[138:141]
	v_mfma_f32_16x16x32_bf16 v[118:121], v[98:101], v[170:173], v[118:121]
	v_mfma_f32_16x16x32_bf16 v[114:117], v[122:125], v[170:173], v[114:117]
	v_mfma_f32_16x16x32_bf16 v[94:97], v[98:101], v[178:181], v[94:97]
	v_mfma_f32_16x16x32_bf16 v[90:93], v[122:125], v[178:181], v[90:93]
	v_mfma_f32_16x16x32_bf16 v[78:81], v[98:101], v[202:205], v[78:81]
	v_mfma_f32_16x16x32_bf16 v[74:77], v[122:125], v[202:205], v[74:77]
	v_mfma_f32_16x16x32_bf16 v[142:145], v[110:113], v[166:169], v[142:145]
	v_mfma_f32_16x16x32_bf16 v[138:141], v[130:133], v[166:169], v[138:141]
	v_mfma_f32_16x16x32_bf16 v[118:121], v[110:113], v[174:177], v[118:121]
	v_mfma_f32_16x16x32_bf16 v[114:117], v[130:133], v[174:177], v[114:117]
	v_mfma_f32_16x16x32_bf16 v[94:97], v[110:113], v[182:185], v[94:97]
	v_mfma_f32_16x16x32_bf16 v[90:93], v[130:133], v[182:185], v[90:93]
	v_mfma_f32_16x16x32_bf16 v[78:81], v[110:113], v[206:209], v[78:81]
	v_mfma_f32_16x16x32_bf16 v[74:77], v[130:133], v[206:209], v[74:77]
	s_setprio 0
	s_setprio 3
	v_mfma_f32_16x16x32_bf16 v[134:137], v[146:149], v[162:165], v[134:137]
	v_mfma_f32_16x16x32_bf16 v[126:129], v[154:157], v[162:165], v[126:129]
	v_mfma_f32_16x16x32_bf16 v[106:109], v[146:149], v[170:173], v[106:109]
	v_mfma_f32_16x16x32_bf16 v[102:105], v[154:157], v[170:173], v[102:105]
	v_mfma_f32_16x16x32_bf16 v[86:89], v[146:149], v[178:181], v[86:89]
	v_mfma_f32_16x16x32_bf16 v[82:85], v[154:157], v[178:181], v[82:85]
	v_mfma_f32_16x16x32_bf16 v[70:73], v[146:149], v[202:205], v[70:73]
	v_mfma_f32_16x16x32_bf16 v[66:69], v[154:157], v[202:205], v[66:69]
	v_mfma_f32_16x16x32_bf16 v[134:137], v[150:153], v[166:169], v[134:137]
	v_mfma_f32_16x16x32_bf16 v[126:129], v[158:161], v[166:169], v[126:129]
	v_mfma_f32_16x16x32_bf16 v[106:109], v[150:153], v[174:177], v[106:109]
	v_mfma_f32_16x16x32_bf16 v[102:105], v[158:161], v[174:177], v[102:105]
	v_mfma_f32_16x16x32_bf16 v[86:89], v[150:153], v[182:185], v[86:89]
	v_mfma_f32_16x16x32_bf16 v[82:85], v[158:161], v[182:185], v[82:85]
	v_mfma_f32_16x16x32_bf16 v[70:73], v[150:153], v[206:209], v[70:73]
	v_mfma_f32_16x16x32_bf16 v[66:69], v[158:161], v[206:209], v[66:69]
	s_setprio 0
	s_barrier
	s_add_i32 s64, s57, s40
	s_mov_b32 m0, s64
	ds_read_b128 v[162:165], v227 offset:16384
	ds_read_b128 v[166:169], v227 offset:17408
	ds_read_b128 v[170:173], v227 offset:18432
	ds_read_b128 v[174:177], v227 offset:19456
	ds_read_b128 v[178:181], v227 offset:20480
	ds_read_b128 v[182:185], v227 offset:21504
	ds_read_b128 v[202:205], v227 offset:22528
	ds_read_b128 v[206:209], v227 offset:23552
	global_load_lds_dwordx4 v188, s[36:37]
	s_add_i32 m0, s64, 0x2000
	s_add_u32 s64, s36, 0x40000
	s_addc_u32 s65, s37, 0
	s_add_i32 s66, s58, s40
	global_load_lds_dwordx4 v192, s[36:37]
	s_mov_b32 m0, s66
	s_mov_b64 s[98:99], s[38:39]
	global_load_lds_dwordx4 v188, s[64:65]
	s_add_i32 m0, s66, 0x2000
	s_nop 0
	global_load_lds_dwordx4 v192, s[64:65]
	s_mov_b32 m0, s41
	s_nop 0
	global_load_lds_dwordx4 v186, s[38:39]
	s_mov_b32 m0, s44
	s_nop 0
	global_load_lds_dwordx4 v190, s[38:39]
	s_waitcnt vmcnt(8)
	s_waitcnt lgkmcnt(0)
	s_barrier
	s_setprio 3
	s_waitcnt lgkmcnt(0)
	v_mfma_f32_16x16x32_bf16 v[62:65], v[98:101], v[162:165], v[62:65]
	v_mfma_f32_16x16x32_bf16 v[58:61], v[122:125], v[162:165], v[58:61]
	v_mfma_f32_16x16x32_bf16 v[46:49], v[98:101], v[170:173], v[46:49]
	v_mfma_f32_16x16x32_bf16 v[42:45], v[122:125], v[170:173], v[42:45]
	v_mfma_f32_16x16x32_bf16 v[30:33], v[98:101], v[178:181], v[30:33]
	v_mfma_f32_16x16x32_bf16 v[26:29], v[122:125], v[178:181], v[26:29]
	v_mfma_f32_16x16x32_bf16 v[14:17], v[98:101], v[202:205], v[14:17]
	v_mfma_f32_16x16x32_bf16 v[10:13], v[122:125], v[202:205], v[10:13]
	v_mfma_f32_16x16x32_bf16 v[62:65], v[110:113], v[166:169], v[62:65]
	v_mfma_f32_16x16x32_bf16 v[58:61], v[130:133], v[166:169], v[58:61]
	v_mfma_f32_16x16x32_bf16 v[46:49], v[110:113], v[174:177], v[46:49]
	v_mfma_f32_16x16x32_bf16 v[42:45], v[130:133], v[174:177], v[42:45]
	v_mfma_f32_16x16x32_bf16 v[30:33], v[110:113], v[182:185], v[30:33]
	v_mfma_f32_16x16x32_bf16 v[26:29], v[130:133], v[182:185], v[26:29]
	v_mfma_f32_16x16x32_bf16 v[14:17], v[110:113], v[206:209], v[14:17]
	v_mfma_f32_16x16x32_bf16 v[10:13], v[130:133], v[206:209], v[10:13]
	s_setprio 0
	s_setprio 3
	v_mfma_f32_16x16x32_bf16 v[54:57], v[146:149], v[162:165], v[54:57]
	v_mfma_f32_16x16x32_bf16 v[50:53], v[154:157], v[162:165], v[50:53]
	v_mfma_f32_16x16x32_bf16 v[38:41], v[146:149], v[170:173], v[38:41]
	v_mfma_f32_16x16x32_bf16 v[34:37], v[154:157], v[170:173], v[34:37]
	v_mfma_f32_16x16x32_bf16 v[22:25], v[146:149], v[178:181], v[22:25]
	v_mfma_f32_16x16x32_bf16 v[18:21], v[154:157], v[178:181], v[18:21]
	v_mfma_f32_16x16x32_bf16 v[6:9], v[146:149], v[202:205], v[6:9]
	v_mfma_f32_16x16x32_bf16 v[2:5], v[154:157], v[202:205], v[2:5]
	v_mfma_f32_16x16x32_bf16 v[54:57], v[150:153], v[166:169], v[54:57]
	v_mfma_f32_16x16x32_bf16 v[50:53], v[158:161], v[166:169], v[50:53]
	v_mfma_f32_16x16x32_bf16 v[38:41], v[150:153], v[174:177], v[38:41]
	v_mfma_f32_16x16x32_bf16 v[34:37], v[158:161], v[174:177], v[34:37]
	v_mfma_f32_16x16x32_bf16 v[22:25], v[150:153], v[182:185], v[22:25]
	v_mfma_f32_16x16x32_bf16 v[18:21], v[158:161], v[182:185], v[18:21]
	v_mfma_f32_16x16x32_bf16 v[6:9], v[150:153], v[206:209], v[6:9]
	v_mfma_f32_16x16x32_bf16 v[2:5], v[158:161], v[206:209], v[2:5]
	s_setprio 0
	s_barrier
; #define PG8_STAGE_A(b, h, ptr, NX) do { if constexpr (Sched::GATHER) { unsigned gs_[2]; gs_[0] = ((NX) && last_) ? gN[h][0] : gA[h][0]; gs_[1] = ((NX) && last_) ? gN[h][1] : gA[h][1]; PG8_STAGE(PG8_SA(b, h), ptr, gs_); } \
;         else PG8_STAGE(PG8_SA(b, h), (ptr) + ((h) ? hstep : (size_t)0), voffA); } while (0)
; #define PG8_STAGE(bufoff, gbase, voff) do { _Pragma("unroll") for (int _i = 0; _i < 2; ++_i) \
;         __builtin_amdgcn_global_load_lds((const unsigned*)((const char*)(gbase) + (voff)[_i]), (PG8_LAS unsigned*)(lds + (bufoff) + ldsw + _i * 8192), 16, 0, 0); } while (0)
; #define PG8_LDA(dst, b, h) do { _Pragma("unroll") for (int m = 0; m < 4; ++m) _Pragma("unroll") for (int k = 0; k < 2; ++k) dst[m][k] = *(const PG8_LAS bf16x8*)(lds + PG8_SA(b, h) + aoff + m * 2048 + k * 1024); } while (0)
; #define PG8_LDB(dst, b, h) do { _Pragma("unroll") for (int n = 0; n < 2; ++n) _Pragma("unroll") for (int k = 0; k < 2; ++k) dst[n][k] = *(const PG8_LAS bf16x8*)(lds + PG8_SB(b, h) + boff + n * 2048 + k * 1024); } while (0)
; #define PG8_MMA(ai, bj, At, Bt) do { __builtin_amdgcn_s_setprio(1); _Pragma("unroll") for (int m = 0; m < 4; ++m) _Pragma("unroll") for (int n = 0; n < 2; ++n) _Pragma("unroll") for (int k = 0; k < 2; ++k) \
;         acc[ai][bj][m][n] = __builtin_amdgcn_mfma_f32_16x16x32_bf16(Bt[n][k], At[m][k], acc[ai][bj][m][n], 0, 0, 0); __builtin_amdgcn_s_setprio(0); } while (0)
; #define PG8_WAIT_V(n) asm volatile("s_waitcnt vmcnt(" #n ")" ::: "memory")
; #define PG8_WAIT_L(n) asm volatile("s_waitcnt lgkmcnt(" #n ")" ::: "memory")
; #define PG8_BAR __builtin_amdgcn_s_barrier()
; #define PG8_SCHED __builtin_amdgcn_sched_barrier(0)
; template <class Epi, class Sched, bool ALIGN_EPI = false, bool SP2 = false>
; __device__ __forceinline__ void gemm_phase(PG8_LAS unsigned char* lds, const Gemm g, const Sched& S, const Epi& E, const bool skip_epi = false) {
;     ...
;             PG8_LDB(B0, 1, 0); PG8_LDB(B1, 1, 1); PG8_SCHED; PG8_LDA(At, 1, 0); PG8_STAGE_A(0, 1, a2, true);
;             PG8_WAIT_V(8); PG8_WAIT_L(0); PG8_BAR; PG8_MMA(0, 0, At, B0); PG8_MMA(0, 1, At, B1); PG8_BAR; PG8_SCHED;
;             PG8_LDA(At, 1, 1); PG8_STAGE(PG8_SB(1, 0), b3, voffB); PG8_STAGE(PG8_SB(1, 1), b3 + hstep, voffB); PG8_STAGE_A(1, 0, a3, true);
;             PG8_WAIT_V(8); PG8_WAIT_L(0); PG8_BAR; PG8_MMA(1, 0, At, B0); PG8_MMA(1, 1, At, B1); PG8_BAR; PG8_SCHED;
	s_add_i32 s64, 0, 0x18000
	s_add_i32 s65, 0, 0x1c000
	v_add_u32_e32 v130, s64, v220
	v_add_u32_e32 v158, s65, v220
	ds_read_b128 v[98:101], v130
	ds_read_b128 v[110:113], v130 offset:1024
	ds_read_b128 v[122:125], v130 offset:2048
	ds_read_b128 v[130:133], v130 offset:3072
	ds_read_b128 v[146:149], v158
	ds_read_b128 v[150:153], v158 offset:1024
	ds_read_b128 v[154:157], v158 offset:2048
	ds_read_b128 v[158:161], v158 offset:3072
	s_add_u32 s38, s38, 0x40000
	s_addc_u32 s39, s39, 0
	s_mov_b32 m0, s45
	ds_read_b128 v[162:165], v227 offset:32768
	ds_read_b128 v[166:169], v227 offset:33792
	ds_read_b128 v[170:173], v227 offset:34816
	ds_read_b128 v[174:177], v227 offset:35840
	ds_read_b128 v[178:181], v227 offset:36864
	ds_read_b128 v[182:185], v227 offset:37888
	ds_read_b128 v[202:205], v227 offset:38912
	ds_read_b128 v[206:209], v227 offset:39936
	global_load_lds_dwordx4 v186, s[38:39]
	s_mov_b32 m0, s48
	s_nop 0
	global_load_lds_dwordx4 v190, s[38:39]
	s_waitcnt vmcnt(8)
	s_waitcnt lgkmcnt(0)
	s_barrier
	s_setprio 3
	s_waitcnt lgkmcnt(0)
	v_mfma_f32_16x16x32_bf16 v[142:145], v[98:101], v[162:165], v[142:145]
	v_mfma_f32_16x16x32_bf16 v[138:141], v[122:125], v[162:165], v[138:141]
	v_mfma_f32_16x16x32_bf16 v[118:121], v[98:101], v[170:173], v[118:121]
	v_mfma_f32_16x16x32_bf16 v[114:117], v[122:125], v[170:173], v[114:117]
	v_mfma_f32_16x16x32_bf16 v[94:97], v[98:101], v[178:181], v[94:97]
	v_mfma_f32_16x16x32_bf16 v[90:93], v[122:125], v[178:181], v[90:93]
	v_mfma_f32_16x16x32_bf16 v[78:81], v[98:101], v[202:205], v[78:81]
	v_mfma_f32_16x16x32_bf16 v[74:77], v[122:125], v[202:205], v[74:77]
	v_mfma_f32_16x16x32_bf16 v[142:145], v[110:113], v[166:169], v[142:145]
	v_mfma_f32_16x16x32_bf16 v[138:141], v[130:133], v[166:169], v[138:141]
	v_mfma_f32_16x16x32_bf16 v[118:121], v[110:113], v[174:177], v[118:121]
	v_mfma_f32_16x16x32_bf16 v[114:117], v[130:133], v[174:177], v[114:117]
	v_mfma_f32_16x16x32_bf16 v[94:97], v[110:113], v[182:185], v[94:97]
	v_mfma_f32_16x16x32_bf16 v[90:93], v[130:133], v[182:185], v[90:93]
	v_mfma_f32_16x16x32_bf16 v[78:81], v[110:113], v[206:209], v[78:81]
	v_mfma_f32_16x16x32_bf16 v[74:77], v[130:133], v[206:209], v[74:77]
	s_setprio 0
	s_setprio 3
	v_mfma_f32_16x16x32_bf16 v[134:137], v[146:149], v[162:165], v[134:137]
	v_mfma_f32_16x16x32_bf16 v[126:129], v[154:157], v[162:165], v[126:129]
	v_mfma_f32_16x16x32_bf16 v[106:109], v[146:149], v[170:173], v[106:109]
	v_mfma_f32_16x16x32_bf16 v[102:105], v[154:157], v[170:173], v[102:105]
	v_mfma_f32_16x16x32_bf16 v[86:89], v[146:149], v[178:181], v[86:89]
	v_mfma_f32_16x16x32_bf16 v[82:85], v[154:157], v[178:181], v[82:85]
	v_mfma_f32_16x16x32_bf16 v[70:73], v[146:149], v[202:205], v[70:73]
	v_mfma_f32_16x16x32_bf16 v[66:69], v[154:157], v[202:205], v[66:69]
	v_mfma_f32_16x16x32_bf16 v[134:137], v[150:153], v[166:169], v[134:137]
	v_mfma_f32_16x16x32_bf16 v[126:129], v[158:161], v[166:169], v[126:129]
	v_mfma_f32_16x16x32_bf16 v[106:109], v[150:153], v[174:177], v[106:109]
	v_mfma_f32_16x16x32_bf16 v[102:105], v[158:161], v[174:177], v[102:105]
	v_mfma_f32_16x16x32_bf16 v[86:89], v[150:153], v[182:185], v[86:89]
	v_mfma_f32_16x16x32_bf16 v[82:85], v[158:161], v[182:185], v[82:85]
	v_mfma_f32_16x16x32_bf16 v[70:73], v[150:153], v[206:209], v[70:73]
	v_mfma_f32_16x16x32_bf16 v[66:69], v[158:161], v[206:209], v[66:69]
	s_setprio 0
	s_barrier
	s_add_i32 s38, s64, s40
	s_add_i32 m0, s38, 0xffffff80
	ds_read_b128 v[162:165], v227 offset:49152
	ds_read_b128 v[166:169], v227 offset:50176
	ds_read_b128 v[170:173], v227 offset:51200
	ds_read_b128 v[174:177], v227 offset:52224
	ds_read_b128 v[178:181], v227 offset:53248
	ds_read_b128 v[182:185], v227 offset:54272
	ds_read_b128 v[202:205], v227 offset:55296
	ds_read_b128 v[206:209], v227 offset:56320
	global_load_lds_dwordx4 v188, s[36:37] offset:128
	s_add_i32 m0, s38, 0x1f80
	s_add_i32 s38, s65, s40
	global_load_lds_dwordx4 v192, s[36:37] offset:128
	s_add_u32 s36, s36, 0x40080
	s_addc_u32 s37, s37, 0
	s_mov_b32 m0, s38
	s_nop 0
	global_load_lds_dwordx4 v188, s[36:37]
	s_add_i32 m0, s38, 0x2000
	s_nop 0
	global_load_lds_dwordx4 v192, s[36:37]
	s_add_i32 m0, s53, 0xffffff80
	s_nop 0
	global_load_lds_dwordx4 v186, s[98:99] offset:128
	s_add_i32 m0, s54, 0xffffff80
	s_nop 0
	global_load_lds_dwordx4 v190, s[98:99] offset:128
	s_waitcnt vmcnt(8)
	s_waitcnt lgkmcnt(0)
	s_barrier
	s_setprio 3
	s_waitcnt lgkmcnt(0)
	v_mfma_f32_16x16x32_bf16 v[62:65], v[98:101], v[162:165], v[62:65]
	v_mfma_f32_16x16x32_bf16 v[58:61], v[122:125], v[162:165], v[58:61]
	v_mfma_f32_16x16x32_bf16 v[46:49], v[98:101], v[170:173], v[46:49]
	v_mfma_f32_16x16x32_bf16 v[42:45], v[122:125], v[170:173], v[42:45]
	v_mfma_f32_16x16x32_bf16 v[30:33], v[98:101], v[178:181], v[30:33]
	v_mfma_f32_16x16x32_bf16 v[26:29], v[122:125], v[178:181], v[26:29]
	v_mfma_f32_16x16x32_bf16 v[14:17], v[98:101], v[202:205], v[14:17]
	v_mfma_f32_16x16x32_bf16 v[10:13], v[122:125], v[202:205], v[10:13]
	v_mfma_f32_16x16x32_bf16 v[62:65], v[110:113], v[166:169], v[62:65]
	v_mfma_f32_16x16x32_bf16 v[58:61], v[130:133], v[166:169], v[58:61]
	v_mfma_f32_16x16x32_bf16 v[46:49], v[110:113], v[174:177], v[46:49]
	v_mfma_f32_16x16x32_bf16 v[42:45], v[130:133], v[174:177], v[42:45]
	v_mfma_f32_16x16x32_bf16 v[30:33], v[110:113], v[182:185], v[30:33]
	v_mfma_f32_16x16x32_bf16 v[26:29], v[130:133], v[182:185], v[26:29]
	v_mfma_f32_16x16x32_bf16 v[14:17], v[110:113], v[206:209], v[14:17]
	v_mfma_f32_16x16x32_bf16 v[10:13], v[130:133], v[206:209], v[10:13]
	s_setprio 0
	s_setprio 3
	v_mfma_f32_16x16x32_bf16 v[54:57], v[146:149], v[162:165], v[54:57]
	v_mfma_f32_16x16x32_bf16 v[50:53], v[154:157], v[162:165], v[50:53]
	v_mfma_f32_16x16x32_bf16 v[38:41], v[146:149], v[170:173], v[38:41]
	v_mfma_f32_16x16x32_bf16 v[34:37], v[154:157], v[170:173], v[34:37]
	v_mfma_f32_16x16x32_bf16 v[22:25], v[146:149], v[178:181], v[22:25]
	v_mfma_f32_16x16x32_bf16 v[18:21], v[154:157], v[178:181], v[18:21]
	v_mfma_f32_16x16x32_bf16 v[6:9], v[146:149], v[202:205], v[6:9]
	v_mfma_f32_16x16x32_bf16 v[2:5], v[154:157], v[202:205], v[2:5]
	v_mfma_f32_16x16x32_bf16 v[54:57], v[150:153], v[166:169], v[54:57]
	v_mfma_f32_16x16x32_bf16 v[50:53], v[158:161], v[166:169], v[50:53]
	v_mfma_f32_16x16x32_bf16 v[38:41], v[150:153], v[174:177], v[38:41]
	v_mfma_f32_16x16x32_bf16 v[34:37], v[158:161], v[174:177], v[34:37]
	v_mfma_f32_16x16x32_bf16 v[22:25], v[150:153], v[182:185], v[22:25]
	v_mfma_f32_16x16x32_bf16 v[18:21], v[158:161], v[182:185], v[18:21]
	v_mfma_f32_16x16x32_bf16 v[6:9], v[150:153], v[206:209], v[6:9]
	v_mfma_f32_16x16x32_bf16 v[2:5], v[158:161], v[206:209], v[2:5]
	s_setprio 0
	s_barrier
	s_add_i32 s63, s63, 2
	s_add_u32 s34, s34, 0x100
	s_addc_u32 s35, s35, 0
	s_add_u32 s61, s61, 0x100
	s_addc_u32 s62, s62, 0
	s_cmp_gt_u32 s63, 13
	s_cbranch_scc0 .LBB0_1324
	s_and_b64 vcc, exec, s[14:15]
	s_cbranch_vccz .LBB0_1327
	s_barrier

; #define PG8_STAGE_A(b, h, ptr, NX) do { if constexpr (Sched::GATHER) { unsigned gs_[2]; gs_[0] = ((NX) && last_) ? gN[h][0] : gA[h][0]; gs_[1] = ((NX) && last_) ? gN[h][1] : gA[h][1]; PG8_STAGE(PG8_SA(b, h), ptr, gs_); } \
;         else PG8_STAGE(PG8_SA(b, h), (ptr) + ((h) ? hstep : (size_t)0), voffA); } while (0)
; #define PG8_STAGE(bufoff, gbase, voff) do { _Pragma("unroll") for (int _i = 0; _i < 2; ++_i) \
;         __builtin_amdgcn_global_load_lds((const unsigned*)((const char*)(gbase) + (voff)[_i]), (PG8_LAS unsigned*)(lds + (bufoff) + ldsw + _i * 8192), 16, 0, 0); } while (0)
; #define PG8_LDA(dst, b, h) do { _Pragma("unroll") for (int m = 0; m < 4; ++m) _Pragma("unroll") for (int k = 0; k < 2; ++k) dst[m][k] = *(const PG8_LAS bf16x8*)(lds + PG8_SA(b, h) + aoff + m * 2048 + k * 1024); } while (0)
; #define PG8_LDB(dst, b, h) do { _Pragma("unroll") for (int n = 0; n < 2; ++n) _Pragma("unroll") for (int k = 0; k < 2; ++k) dst[n][k] = *(const PG8_LAS bf16x8*)(lds + PG8_SB(b, h) + boff + n * 2048 + k * 1024); } while (0)
; #define PG8_WAIT_V(n) asm volatile("s_waitcnt vmcnt(" #n ")" ::: "memory")
; #define PG8_WAIT_L(n) asm volatile("s_waitcnt lgkmcnt(" #n ")" ::: "memory")
; template <class Epi, class Sched, bool ALIGN_EPI = false, bool SP2 = false>
; __device__ __forceinline__ void gemm_phase(PG8_LAS unsigned char* lds, const Gemm g, const Sched& S, const Epi& E, const bool skip_epi = false) {
;     ...
;         for (int t = 0; t < nt; t += 2) {
;             const bool last = (t == nt - 2); last_ = last && has_next;
;             const char* a1 = cA + (size_t)(t + 1) * kstep;
;             const char* a2 = last ? nA : cA + (size_t)(t + 2) * kstep; const char* b2 = last ? nB : cB + (size_t)(t + 2) * kstep;
;             const char* a3 = a2 + kstep; const char* b3 = b2 + kstep;
;             if (last && has_next) S.a_ready(nxt);
;             if constexpr (SP2) {
;             PG8_LDB(B0, 0, 0); PG8_LDB(B1, 0, 1); PG8_SCHED; PG8_LDA(At, 0, 0); PG8_STAGE_A(1, 1, a1, false);
;             PG8_WAIT_V(8); PG8_WAIT_L(0); PG8_BAR; PG8_MMA(0, 0, At, B0); PG8_MMA(0, 1, At, B1); PG8_BAR; PG8_SCHED;
;             PG8_LDA(At, 0, 1); PG8_STAGE(PG8_SB(0, 0), b2, voffB); PG8_STAGE(PG8_SB(0, 1), b2 + hstep, voffB); PG8_STAGE_A(0, 0, a2, true);
;             PG8_WAIT_V(8); PG8_WAIT_L(0); PG8_BAR; PG8_MMA(1, 0, At, B0); PG8_MMA(1, 1, At, B1); PG8_BAR; PG8_SCHED;
.Lg5_zero:
.LBB0_1727:
	s_mov_b32 s29, s41
	s_mov_b32 s31, s40
	v_mov_b32_e32 v143, v133
	v_mov_b32_e32 v141, v133
	s_add_u32 s61, s40, 0x100
	v_lshl_add_u64 v[146:147], s[24:25], 0, v[140:141]
	v_lshl_add_u64 v[148:149], s[24:25], 0, v[142:143]
	s_addc_u32 s62, s41, 0
	s_mov_b32 s63, -2
	s_mov_b64 s[40:41], 0
	ds_read_b128 v[166:169], v158
	ds_read_b128 v[170:173], v158 offset:1024
	ds_read_b128 v[174:177], v158 offset:2048
	ds_read_b128 v[178:181], v158 offset:3072
	ds_read_b128 v[182:185], v159
	ds_read_b128 v[186:189], v159 offset:1024
	ds_read_b128 v[190:193], v159 offset:2048
	ds_read_b128 v[194:197], v159 offset:3072
	s_add_u32 s42, s78, s40
	s_addc_u32 s43, s79, s41
	s_add_u32 s44, s42, 0x1aa00100
	s_addc_u32 s45, s43, 0
	s_add_u32 s66, s61, s40
	s_addc_u32 s67, s62, s41
	s_cmpk_eq_i32 s40, 0x700
	s_cselect_b64 s[64:65], -1, 0
	s_and_b64 s[42:43], s[64:65], exec
	s_cselect_b32 s45, s87, s45
	s_cselect_b32 s44, s86, s44
	s_cselect_b32 s42, s31, s66
	s_cselect_b32 s43, s29, s67
	s_and_b64 vcc, s[6:7], s[64:65]
	v_lshl_add_u64 v[226:227], v[148:149], 0, s[40:41]
	s_add_i32 m0, s37, 0xc000
	ds_read_b128 v[198:201], v160
	ds_read_b128 v[202:205], v160 offset:1024
	ds_read_b128 v[206:209], v160 offset:2048
	ds_read_b128 v[210:213], v160 offset:3072
	ds_read_b128 v[214:217], v160 offset:4096
	ds_read_b128 v[218:221], v160 offset:5120
	ds_read_b128 v[222:225], v160 offset:6144
	ds_read_b128 v[230:233], v160 offset:7168
	global_load_lds_dwordx4 v[226:227], off
	v_lshl_add_u64 v[226:227], v[146:147], 0, s[40:41]
	s_add_i32 m0, s37, 0xe000
	s_nop 0
	global_load_lds_dwordx4 v[226:227], off
	s_waitcnt vmcnt(8)
	s_waitcnt lgkmcnt(0)
	s_barrier
	s_setprio 3
	s_waitcnt lgkmcnt(0)
	v_mfma_f32_16x16x32_bf16 v[126:129], v[166:169], v[198:201], 0
	v_mfma_f32_16x16x32_bf16 v[122:125], v[174:177], v[198:201], 0
	v_mfma_f32_16x16x32_bf16 v[110:113], v[166:169], v[206:209], 0
	v_mfma_f32_16x16x32_bf16 v[106:109], v[174:177], v[206:209], 0
	v_mfma_f32_16x16x32_bf16 v[94:97], v[166:169], v[214:217], 0
	v_mfma_f32_16x16x32_bf16 v[90:93], v[174:177], v[214:217], 0
	v_mfma_f32_16x16x32_bf16 v[78:81], v[166:169], v[222:225], 0
	v_mfma_f32_16x16x32_bf16 v[74:77], v[174:177], v[222:225], 0
	v_mfma_f32_16x16x32_bf16 v[126:129], v[170:173], v[202:205], v[126:129]
	v_mfma_f32_16x16x32_bf16 v[122:125], v[178:181], v[202:205], v[122:125]
	v_mfma_f32_16x16x32_bf16 v[110:113], v[170:173], v[210:213], v[110:113]
	v_mfma_f32_16x16x32_bf16 v[106:109], v[178:181], v[210:213], v[106:109]
	v_mfma_f32_16x16x32_bf16 v[94:97], v[170:173], v[218:221], v[94:97]
	v_mfma_f32_16x16x32_bf16 v[90:93], v[178:181], v[218:221], v[90:93]
	v_mfma_f32_16x16x32_bf16 v[78:81], v[170:173], v[230:233], v[78:81]
	v_mfma_f32_16x16x32_bf16 v[74:77], v[178:181], v[230:233], v[74:77]
	s_setprio 0
	s_setprio 3
	v_mfma_f32_16x16x32_bf16 v[118:121], v[182:185], v[198:201], 0
	v_mfma_f32_16x16x32_bf16 v[114:117], v[190:193], v[198:201], 0
	v_mfma_f32_16x16x32_bf16 v[102:105], v[182:185], v[206:209], 0
	v_mfma_f32_16x16x32_bf16 v[98:101], v[190:193], v[206:209], 0
	v_mfma_f32_16x16x32_bf16 v[86:89], v[182:185], v[214:217], 0
	v_mfma_f32_16x16x32_bf16 v[82:85], v[190:193], v[214:217], 0
	v_mfma_f32_16x16x32_bf16 v[70:73], v[182:185], v[222:225], 0
	v_mfma_f32_16x16x32_bf16 v[66:69], v[190:193], v[222:225], 0
	v_mfma_f32_16x16x32_bf16 v[118:121], v[186:189], v[202:205], v[118:121]
	v_mfma_f32_16x16x32_bf16 v[114:117], v[194:197], v[202:205], v[114:117]
	v_mfma_f32_16x16x32_bf16 v[102:105], v[186:189], v[210:213], v[102:105]
	v_mfma_f32_16x16x32_bf16 v[98:101], v[194:197], v[210:213], v[98:101]
	v_mfma_f32_16x16x32_bf16 v[86:89], v[186:189], v[218:221], v[86:89]
	v_mfma_f32_16x16x32_bf16 v[82:85], v[194:197], v[218:221], v[82:85]
	v_mfma_f32_16x16x32_bf16 v[70:73], v[186:189], v[230:233], v[70:73]
	v_mfma_f32_16x16x32_bf16 v[66:69], v[194:197], v[230:233], v[66:69]
	s_setprio 0
	s_barrier
	s_add_i32 s64, s58, s50
	s_mov_b32 m0, s64
	ds_read_b128 v[198:201], v160 offset:16384
	ds_read_b128 v[202:205], v160 offset:17408
	ds_read_b128 v[206:209], v160 offset:18432
	ds_read_b128 v[210:213], v160 offset:19456
	ds_read_b128 v[214:217], v160 offset:20480
	ds_read_b128 v[218:221], v160 offset:21504
	ds_read_b128 v[222:225], v160 offset:22528
	ds_read_b128 v[230:233], v160 offset:23552
	global_load_lds_dwordx4 v134, s[42:43]
	s_add_i32 m0, s64, 0x2000
	s_add_u32 s64, s42, 0x40000
	s_addc_u32 s65, s43, 0
	s_add_i32 s66, s59, s50
	global_load_lds_dwordx4 v136, s[42:43]
	s_mov_b32 m0, s66
	v_cndmask_b32_e32 v132, v130, v164, vcc
	global_load_lds_dwordx4 v134, s[64:65]
	s_add_i32 m0, s66, 0x2000
	v_lshl_add_u64 v[238:239], s[44:45], 0, v[132:133]
	global_load_lds_dwordx4 v136, s[64:65]
	s_mov_b32 m0, s37
	v_cndmask_b32_e32 v236, v144, v163, vcc
	global_load_lds_dwordx4 v132, s[44:45]
	s_mov_b32 m0, s39
	v_mov_b32_e32 v237, v133
	global_load_lds_dwordx4 v236, s[44:45]
	s_waitcnt vmcnt(8)
	s_waitcnt lgkmcnt(0)
	v_lshl_add_u64 v[236:237], s[44:45], 0, v[236:237]
	s_barrier
; #define PG8_STAGE_A(b, h, ptr, NX) do { if constexpr (Sched::GATHER) { unsigned gs_[2]; gs_[0] = ((NX) && last_) ? gN[h][0] : gA[h][0]; gs_[1] = ((NX) && last_) ? gN[h][1] : gA[h][1]; PG8_STAGE(PG8_SA(b, h), ptr, gs_); } \
;         else PG8_STAGE(PG8_SA(b, h), (ptr) + ((h) ? hstep : (size_t)0), voffA); } while (0)
; #define PG8_STAGE(bufoff, gbase, voff) do { _Pragma("unroll") for (int _i = 0; _i < 2; ++_i) \
;         __builtin_amdgcn_global_load_lds((const unsigned*)((const char*)(gbase) + (voff)[_i]), (PG8_LAS unsigned*)(lds + (bufoff) + ldsw + _i * 8192), 16, 0, 0); } while (0)
; #define PG8_LDA(dst, b, h) do { _Pragma("unroll") for (int m = 0; m < 4; ++m) _Pragma("unroll") for (int k = 0; k < 2; ++k) dst[m][k] = *(const PG8_LAS bf16x8*)(lds + PG8_SA(b, h) + aoff + m * 2048 + k * 1024); } while (0)
; #define PG8_LDB(dst, b, h) do { _Pragma("unroll") for (int n = 0; n < 2; ++n) _Pragma("unroll") for (int k = 0; k < 2; ++k) dst[n][k] = *(const PG8_LAS bf16x8*)(lds + PG8_SB(b, h) + boff + n * 2048 + k * 1024); } while (0)
; #define PG8_MMA(ai, bj, At, Bt) do { __builtin_amdgcn_s_setprio(1); _Pragma("unroll") for (int m = 0; m < 4; ++m) _Pragma("unroll") for (int n = 0; n < 2; ++n) _Pragma("unroll") for (int k = 0; k < 2; ++k) \
;         acc[ai][bj][m][n] = __builtin_amdgcn_mfma_f32_16x16x32_bf16(Bt[n][k], At[m][k], acc[ai][bj][m][n], 0, 0, 0); __builtin_amdgcn_s_setprio(0); } while (0)
; #define PG8_WAIT_V(n) asm volatile("s_waitcnt vmcnt(" #n ")" ::: "memory")
; #define PG8_BAR __builtin_amdgcn_s_barrier()
; template <class Epi, class Sched, bool ALIGN_EPI = false, bool SP2 = false>
; __device__ __forceinline__ void gemm_phase(PG8_LAS unsigned char* lds, const Gemm g, const Sched& S, const Epi& E, const bool skip_epi = false) {
;     ...
;             PG8_WAIT_V(8); PG8_WAIT_L(0); PG8_BAR; PG8_MMA(0, 0, At, B0); PG8_MMA(0, 1, At, B1); PG8_BAR; PG8_SCHED;
;             PG8_LDA(At, 0, 1); PG8_STAGE(PG8_SB(0, 0), b2, voffB); PG8_STAGE(PG8_SB(0, 1), b2 + hstep, voffB); PG8_STAGE_A(0, 0, a2, true);
;             PG8_WAIT_V(8); PG8_WAIT_L(0); PG8_BAR; PG8_MMA(1, 0, At, B0); PG8_MMA(1, 1, At, B1); PG8_BAR; PG8_SCHED;
;             PG8_LDB(B0, 1, 0); PG8_LDB(B1, 1, 1); PG8_SCHED; PG8_LDA(At, 1, 0); PG8_STAGE_A(0, 1, a2, true);
;             PG8_WAIT_V(8); PG8_WAIT_L(0); PG8_BAR; PG8_MMA(0, 0, At, B0); PG8_MMA(0, 1, At, B1); PG8_BAR; PG8_SCHED;
	s_setprio 3
	s_waitcnt lgkmcnt(0)
	v_mfma_f32_16x16x32_bf16 v[62:65], v[166:169], v[198:201], 0
	v_mfma_f32_16x16x32_bf16 v[58:61], v[174:177], v[198:201], 0
	v_mfma_f32_16x16x32_bf16 v[38:41], v[166:169], v[206:209], 0
	v_mfma_f32_16x16x32_bf16 v[34:37], v[174:177], v[206:209], 0
	v_mfma_f32_16x16x32_bf16 v[22:25], v[166:169], v[214:217], 0
	v_mfma_f32_16x16x32_bf16 v[18:21], v[174:177], v[214:217], 0
	v_mfma_f32_16x16x32_bf16 v[6:9], v[166:169], v[222:225], 0
	v_mfma_f32_16x16x32_bf16 v[2:5], v[174:177], v[222:225], 0
	v_mfma_f32_16x16x32_bf16 v[62:65], v[170:173], v[202:205], v[62:65]
	v_mfma_f32_16x16x32_bf16 v[58:61], v[178:181], v[202:205], v[58:61]
	v_mfma_f32_16x16x32_bf16 v[38:41], v[170:173], v[210:213], v[38:41]
	v_mfma_f32_16x16x32_bf16 v[34:37], v[178:181], v[210:213], v[34:37]
	v_mfma_f32_16x16x32_bf16 v[22:25], v[170:173], v[218:221], v[22:25]
	v_mfma_f32_16x16x32_bf16 v[18:21], v[178:181], v[218:221], v[18:21]
	v_mfma_f32_16x16x32_bf16 v[6:9], v[170:173], v[230:233], v[6:9]
	v_mfma_f32_16x16x32_bf16 v[2:5], v[178:181], v[230:233], v[2:5]
	s_setprio 0
	s_setprio 3
	v_mfma_f32_16x16x32_bf16 v[50:53], v[182:185], v[198:201], 0
	v_mfma_f32_16x16x32_bf16 v[42:45], v[190:193], v[198:201], 0
	v_mfma_f32_16x16x32_bf16 v[54:57], v[182:185], v[206:209], 0
	v_mfma_f32_16x16x32_bf16 v[46:49], v[190:193], v[206:209], 0
	v_mfma_f32_16x16x32_bf16 v[30:33], v[182:185], v[214:217], 0
	v_mfma_f32_16x16x32_bf16 v[26:29], v[190:193], v[214:217], 0
	v_mfma_f32_16x16x32_bf16 v[14:17], v[182:185], v[222:225], 0
	v_mfma_f32_16x16x32_bf16 v[10:13], v[190:193], v[222:225], 0
	v_mfma_f32_16x16x32_bf16 v[50:53], v[186:189], v[202:205], v[50:53]
	v_mfma_f32_16x16x32_bf16 v[42:45], v[194:197], v[202:205], v[42:45]
	v_mfma_f32_16x16x32_bf16 v[54:57], v[186:189], v[210:213], v[54:57]
	v_mfma_f32_16x16x32_bf16 v[46:49], v[194:197], v[210:213], v[46:49]
	v_mfma_f32_16x16x32_bf16 v[30:33], v[186:189], v[218:221], v[30:33]
	v_mfma_f32_16x16x32_bf16 v[26:29], v[194:197], v[218:221], v[26:29]
	v_mfma_f32_16x16x32_bf16 v[14:17], v[186:189], v[230:233], v[14:17]
	v_mfma_f32_16x16x32_bf16 v[10:13], v[194:197], v[230:233], v[10:13]
	s_setprio 0
	s_barrier
	s_add_i32 s64, 0, 0x18000
	v_add_u32_e32 v132, s64, v154
	s_add_i32 s65, 0, 0x1c000
	ds_read_b128 v[166:169], v132
	ds_read_b128 v[170:173], v132 offset:1024
	ds_read_b128 v[174:177], v132 offset:2048
	ds_read_b128 v[178:181], v132 offset:3072
	v_add_u32_e32 v132, s65, v154
	ds_read_b128 v[182:185], v132
	ds_read_b128 v[186:189], v132 offset:1024
	ds_read_b128 v[190:193], v132 offset:2048
	ds_read_b128 v[194:197], v132 offset:3072
	s_mov_b32 m0, s51
	v_cndmask_b32_e32 v132, v142, v162, vcc
	ds_read_b128 v[198:201], v160 offset:32768
	ds_read_b128 v[202:205], v160 offset:33792
	ds_read_b128 v[206:209], v160 offset:34816
	ds_read_b128 v[210:213], v160 offset:35840
	ds_read_b128 v[214:217], v160 offset:36864
	ds_read_b128 v[218:221], v160 offset:37888
	ds_read_b128 v[222:225], v160 offset:38912
	ds_read_b128 v[230:233], v160 offset:39936
	v_cndmask_b32_e32 v141, v140, v161, vcc
	global_load_lds_dwordx4 v132, s[44:45]
	s_mov_b32 m0, s52
	s_nop 0
	global_load_lds_dwordx4 v141, s[44:45]
	s_waitcnt vmcnt(8)
	s_waitcnt lgkmcnt(0)
	s_barrier
	s_setprio 3
	s_waitcnt lgkmcnt(0)
	v_mfma_f32_16x16x32_bf16 v[126:129], v[166:169], v[198:201], v[126:129]
	v_mfma_f32_16x16x32_bf16 v[122:125], v[174:177], v[198:201], v[122:125]
	v_mfma_f32_16x16x32_bf16 v[110:113], v[166:169], v[206:209], v[110:113]
	v_mfma_f32_16x16x32_bf16 v[106:109], v[174:177], v[206:209], v[106:109]
	v_mfma_f32_16x16x32_bf16 v[94:97], v[166:169], v[214:217], v[94:97]
	v_mfma_f32_16x16x32_bf16 v[90:93], v[174:177], v[214:217], v[90:93]
	v_mfma_f32_16x16x32_bf16 v[78:81], v[166:169], v[222:225], v[78:81]
	v_mfma_f32_16x16x32_bf16 v[74:77], v[174:177], v[222:225], v[74:77]
	v_mfma_f32_16x16x32_bf16 v[126:129], v[170:173], v[202:205], v[126:129]
	v_mfma_f32_16x16x32_bf16 v[122:125], v[178:181], v[202:205], v[122:125]
	v_mfma_f32_16x16x32_bf16 v[110:113], v[170:173], v[210:213], v[110:113]
	v_mfma_f32_16x16x32_bf16 v[106:109], v[178:181], v[210:213], v[106:109]
	v_mfma_f32_16x16x32_bf16 v[94:97], v[170:173], v[218:221], v[94:97]
	v_mfma_f32_16x16x32_bf16 v[90:93], v[178:181], v[218:221], v[90:93]
	v_mfma_f32_16x16x32_bf16 v[78:81], v[170:173], v[230:233], v[78:81]
	v_mfma_f32_16x16x32_bf16 v[74:77], v[178:181], v[230:233], v[74:77]
	s_setprio 0
	s_setprio 3
	v_mfma_f32_16x16x32_bf16 v[118:121], v[182:185], v[198:201], v[118:121]
	v_mfma_f32_16x16x32_bf16 v[114:117], v[190:193], v[198:201], v[114:117]
	v_mfma_f32_16x16x32_bf16 v[102:105], v[182:185], v[206:209], v[102:105]
	v_mfma_f32_16x16x32_bf16 v[98:101], v[190:193], v[206:209], v[98:101]
	v_mfma_f32_16x16x32_bf16 v[86:89], v[182:185], v[214:217], v[86:89]
	v_mfma_f32_16x16x32_bf16 v[82:85], v[190:193], v[214:217], v[82:85]
	v_mfma_f32_16x16x32_bf16 v[70:73], v[182:185], v[222:225], v[70:73]
	v_mfma_f32_16x16x32_bf16 v[66:69], v[190:193], v[222:225], v[66:69]
	v_mfma_f32_16x16x32_bf16 v[118:121], v[186:189], v[202:205], v[118:121]
	v_mfma_f32_16x16x32_bf16 v[114:117], v[194:197], v[202:205], v[114:117]
	v_mfma_f32_16x16x32_bf16 v[102:105], v[186:189], v[210:213], v[102:105]
	v_mfma_f32_16x16x32_bf16 v[98:101], v[194:197], v[210:213], v[98:101]
	v_mfma_f32_16x16x32_bf16 v[86:89], v[186:189], v[218:221], v[86:89]
	v_mfma_f32_16x16x32_bf16 v[82:85], v[194:197], v[218:221], v[82:85]
	v_mfma_f32_16x16x32_bf16 v[70:73], v[186:189], v[230:233], v[70:73]
	v_mfma_f32_16x16x32_bf16 v[66:69], v[194:197], v[230:233], v[66:69]
	s_setprio 0
	s_barrier
; #define PG8_STAGE_A(b, h, ptr, NX) do { if constexpr (Sched::GATHER) { unsigned gs_[2]; gs_[0] = ((NX) && last_) ? gN[h][0] : gA[h][0]; gs_[1] = ((NX) && last_) ? gN[h][1] : gA[h][1]; PG8_STAGE(PG8_SA(b, h), ptr, gs_); } \
;         else PG8_STAGE(PG8_SA(b, h), (ptr) + ((h) ? hstep : (size_t)0), voffA); } while (0)
; #define PG8_STAGE(bufoff, gbase, voff) do { _Pragma("unroll") for (int _i = 0; _i < 2; ++_i) \
;         __builtin_amdgcn_global_load_lds((const unsigned*)((const char*)(gbase) + (voff)[_i]), (PG8_LAS unsigned*)(lds + (bufoff) + ldsw + _i * 8192), 16, 0, 0); } while (0)
; #define PG8_WAIT_V(n) asm volatile("s_waitcnt vmcnt(" #n ")" ::: "memory")
; #define PG8_BAR __builtin_amdgcn_s_barrier()
; template <class Epi, class Sched, bool ALIGN_EPI = false, bool SP2 = false>
; __device__ __forceinline__ void gemm_phase(PG8_LAS unsigned char* lds, const Gemm g, const Sched& S, const Epi& E, const bool skip_epi = false) {
;     ...
;         for (int t = 0; t < nt; t += 2) {
;             const bool last = (t == nt - 2); last_ = last && has_next;
;             const char* a1 = cA + (size_t)(t + 1) * kstep;
;             const char* a2 = last ? nA : cA + (size_t)(t + 2) * kstep; const char* b2 = last ? nB : cB + (size_t)(t + 2) * kstep;
;             const char* a3 = a2 + kstep; const char* b3 = b2 + kstep;
;             if (last && has_next) S.a_ready(nxt);
;             if constexpr (SP2) {
;             PG8_LDB(B0, 0, 0); PG8_LDB(B1, 0, 1); PG8_SCHED; PG8_LDA(At, 0, 0); PG8_STAGE_A(1, 1, a1, false);
;             PG8_WAIT_V(8); PG8_WAIT_L(0); PG8_BAR; PG8_MMA(0, 0, At, B0); PG8_MMA(0, 1, At, B1); PG8_BAR; PG8_SCHED;
;             PG8_LDA(At, 0, 1); PG8_STAGE(PG8_SB(0, 0), b2, voffB); PG8_STAGE(PG8_SB(0, 1), b2 + hstep, voffB); PG8_STAGE_A(0, 0, a2, true);
;             PG8_WAIT_V(8); PG8_WAIT_L(0); PG8_BAR; PG8_MMA(1, 0, At, B0); PG8_MMA(1, 1, At, B1); PG8_BAR; PG8_SCHED;
;             PG8_LDB(B0, 1, 0); PG8_LDB(B1, 1, 1); PG8_SCHED; PG8_LDA(At, 1, 0); PG8_STAGE_A(0, 1, a2, true);
;             PG8_WAIT_V(8); PG8_WAIT_L(0); PG8_BAR; PG8_MMA(0, 0, At, B0); PG8_MMA(0, 1, At, B1); PG8_BAR; PG8_SCHED;
;             PG8_LDA(At, 1, 1); PG8_STAGE(PG8_SB(1, 0), b3, voffB); PG8_STAGE(PG8_SB(1, 1), b3 + hstep, voffB); PG8_STAGE_A(1, 0, a3, true);
;             PG8_WAIT_V(8); PG8_WAIT_L(0); PG8_BAR; PG8_MMA(1, 0, At, B0); PG8_MMA(1, 1, At, B1); PG8_BAR; PG8_SCHED;
	s_add_i32 s44, s64, s50
	s_add_i32 m0, s44, 0xffffff80
	ds_read_b128 v[198:201], v160 offset:49152
	ds_read_b128 v[202:205], v160 offset:50176
	ds_read_b128 v[206:209], v160 offset:51200
	ds_read_b128 v[210:213], v160 offset:52224
	ds_read_b128 v[214:217], v160 offset:53248
	ds_read_b128 v[218:221], v160 offset:54272
	ds_read_b128 v[222:225], v160 offset:55296
	ds_read_b128 v[230:233], v160 offset:56320
	global_load_lds_dwordx4 v134, s[42:43] offset:128
	s_add_i32 m0, s44, 0x1f80
	s_add_i32 s44, s65, s50
	global_load_lds_dwordx4 v136, s[42:43] offset:128
	s_add_u32 s42, s42, 0x40080
	s_addc_u32 s43, s43, 0
	s_mov_b32 m0, s44
	s_nop 0
	global_load_lds_dwordx4 v134, s[42:43]
	s_add_i32 m0, s44, 0x2000
	s_nop 0
	global_load_lds_dwordx4 v136, s[42:43]
	s_add_i32 m0, s55, 0xffffff80
	s_nop 0
	global_load_lds_dwordx4 v[238:239], off offset:128
	s_add_i32 m0, s56, 0xffffff80
	s_nop 0
	global_load_lds_dwordx4 v[236:237], off offset:128
	s_waitcnt vmcnt(8)
	s_waitcnt lgkmcnt(0)
	s_barrier
	s_setprio 3
	s_waitcnt lgkmcnt(0)
	v_mfma_f32_16x16x32_bf16 v[62:65], v[166:169], v[198:201], v[62:65]
	v_mfma_f32_16x16x32_bf16 v[58:61], v[174:177], v[198:201], v[58:61]
	v_mfma_f32_16x16x32_bf16 v[38:41], v[166:169], v[206:209], v[38:41]
	v_mfma_f32_16x16x32_bf16 v[34:37], v[174:177], v[206:209], v[34:37]
	v_mfma_f32_16x16x32_bf16 v[22:25], v[166:169], v[214:217], v[22:25]
	v_mfma_f32_16x16x32_bf16 v[18:21], v[174:177], v[214:217], v[18:21]
	v_mfma_f32_16x16x32_bf16 v[6:9], v[166:169], v[222:225], v[6:9]
	v_mfma_f32_16x16x32_bf16 v[2:5], v[174:177], v[222:225], v[2:5]
	v_mfma_f32_16x16x32_bf16 v[62:65], v[170:173], v[202:205], v[62:65]
	v_mfma_f32_16x16x32_bf16 v[58:61], v[178:181], v[202:205], v[58:61]
	v_mfma_f32_16x16x32_bf16 v[38:41], v[170:173], v[210:213], v[38:41]
	v_mfma_f32_16x16x32_bf16 v[34:37], v[178:181], v[210:213], v[34:37]
	v_mfma_f32_16x16x32_bf16 v[22:25], v[170:173], v[218:221], v[22:25]
	v_mfma_f32_16x16x32_bf16 v[18:21], v[178:181], v[218:221], v[18:21]
	v_mfma_f32_16x16x32_bf16 v[6:9], v[170:173], v[230:233], v[6:9]
	v_mfma_f32_16x16x32_bf16 v[2:5], v[178:181], v[230:233], v[2:5]
	s_setprio 0
	s_setprio 3
	v_mfma_f32_16x16x32_bf16 v[50:53], v[182:185], v[198:201], v[50:53]
	v_mfma_f32_16x16x32_bf16 v[42:45], v[190:193], v[198:201], v[42:45]
	v_mfma_f32_16x16x32_bf16 v[54:57], v[182:185], v[206:209], v[54:57]
	v_mfma_f32_16x16x32_bf16 v[46:49], v[190:193], v[206:209], v[46:49]
	v_mfma_f32_16x16x32_bf16 v[30:33], v[182:185], v[214:217], v[30:33]
	v_mfma_f32_16x16x32_bf16 v[26:29], v[190:193], v[214:217], v[26:29]
	v_mfma_f32_16x16x32_bf16 v[14:17], v[182:185], v[222:225], v[14:17]
	v_mfma_f32_16x16x32_bf16 v[10:13], v[190:193], v[222:225], v[10:13]
	v_mfma_f32_16x16x32_bf16 v[50:53], v[186:189], v[202:205], v[50:53]
	v_mfma_f32_16x16x32_bf16 v[42:45], v[194:197], v[202:205], v[42:45]
	v_mfma_f32_16x16x32_bf16 v[54:57], v[186:189], v[210:213], v[54:57]
	v_mfma_f32_16x16x32_bf16 v[46:49], v[194:197], v[210:213], v[46:49]
	v_mfma_f32_16x16x32_bf16 v[30:33], v[186:189], v[218:221], v[30:33]
	v_mfma_f32_16x16x32_bf16 v[26:29], v[194:197], v[218:221], v[26:29]
	v_mfma_f32_16x16x32_bf16 v[14:17], v[186:189], v[230:233], v[14:17]
	v_mfma_f32_16x16x32_bf16 v[10:13], v[194:197], v[230:233], v[10:13]
	s_setprio 0
	s_barrier
	s_add_i32 s63, s63, 2
	s_add_u32 s40, s40, 0x100
	s_addc_u32 s41, s41, 0
	s_cmp_gt_u32 s63, 13
	s_andn2_b64 vcc, exec, s[6:7]
	s_cbranch_vccnz .Lg5_nonext
	s_waitcnt vmcnt(8)
	v_readfirstlane_b32 s34, v250
	v_lshl_add_u32 v164, v229, 11, v152
	v_lshl_add_u32 v163, v251, 11, v153
	v_lshl_add_u32 v162, v252, 11, v152
	v_lshl_add_u32 v161, v253, 11, v153
	s_mul_i32 s34, s34, 28
	s_add_i32 s30, s34, s30
	s_ashr_i32 s31, s30, 31
	s_lshl_b64 s[34:35], s[30:31], 19
	v_readlane_b32 s42, v254, 29
	v_readlane_b32 s43, v254, 30
	s_add_u32 s34, s42, s34
	s_addc_u32 s35, s43, s35
	s_mov_b32 s29, s35
	s_mov_b32 s31, s34
.Lg5_nonext:
.LBB0_1728:
	ds_read_b128 v[166:169], v158
	ds_read_b128 v[170:173], v158 offset:1024
	ds_read_b128 v[174:177], v158 offset:2048
	ds_read_b128 v[178:181], v158 offset:3072
	ds_read_b128 v[182:185], v159
	ds_read_b128 v[186:189], v159 offset:1024
	ds_read_b128 v[190:193], v159 offset:2048
	ds_read_b128 v[194:197], v159 offset:3072
	s_add_u32 s42, s78, s40
	s_addc_u32 s43, s79, s41
	s_add_u32 s44, s42, 0x1aa00100
	s_addc_u32 s45, s43, 0
	s_add_u32 s66, s61, s40
	s_addc_u32 s67, s62, s41
	s_cmpk_eq_i32 s40, 0x700
	s_cselect_b64 s[64:65], -1, 0
	s_and_b64 s[42:43], s[64:65], exec
	s_cselect_b32 s45, s87, s45
	s_cselect_b32 s44, s86, s44
	s_cselect_b32 s42, s31, s66
	s_cselect_b32 s43, s29, s67
	s_and_b64 vcc, s[6:7], s[64:65]
	v_lshl_add_u64 v[226:227], v[148:149], 0, s[40:41]
	s_add_i32 m0, s37, 0xc000
	ds_read_b128 v[198:201], v160
	ds_read_b128 v[202:205], v160 offset:1024
	ds_read_b128 v[206:209], v160 offset:2048
	ds_read_b128 v[210:213], v160 offset:3072
	ds_read_b128 v[214:217], v160 offset:4096
	ds_read_b128 v[218:221], v160 offset:5120
	ds_read_b128 v[222:225], v160 offset:6144
	ds_read_b128 v[230:233], v160 offset:7168
	global_load_lds_dwordx4 v[226:227], off
	v_lshl_add_u64 v[226:227], v[146:147], 0, s[40:41]
	s_add_i32 m0, s37, 0xe000
	s_nop 0
	global_load_lds_dwordx4 v[226:227], off
	s_waitcnt vmcnt(8)
	s_waitcnt lgkmcnt(0)
	s_barrier
; #define PG8_STAGE_A(b, h, ptr, NX) do { if constexpr (Sched::GATHER) { unsigned gs_[2]; gs_[0] = ((NX) && last_) ? gN[h][0] : gA[h][0]; gs_[1] = ((NX) && last_) ? gN[h][1] : gA[h][1]; PG8_STAGE(PG8_SA(b, h), ptr, gs_); } \
;         else PG8_STAGE(PG8_SA(b, h), (ptr) + ((h) ? hstep : (size_t)0), voffA); } while (0)
; #define PG8_STAGE(bufoff, gbase, voff) do { _Pragma("unroll") for (int _i = 0; _i < 2; ++_i) \
;         __builtin_amdgcn_global_load_lds((const unsigned*)((const char*)(gbase) + (voff)[_i]), (PG8_LAS unsigned*)(lds + (bufoff) + ldsw + _i * 8192), 16, 0, 0); } while (0)
; #define PG8_LDA(dst, b, h) do { _Pragma("unroll") for (int m = 0; m < 4; ++m) _Pragma("unroll") for (int k = 0; k < 2; ++k) dst[m][k] = *(const PG8_LAS bf16x8*)(lds + PG8_SA(b, h) + aoff + m * 2048 + k * 1024); } while (0)
; #define PG8_MMA(ai, bj, At, Bt) do { __builtin_amdgcn_s_setprio(1); _Pragma("unroll") for (int m = 0; m < 4; ++m) _Pragma("unroll") for (int n = 0; n < 2; ++n) _Pragma("unroll") for (int k = 0; k < 2; ++k) \
;         acc[ai][bj][m][n] = __builtin_amdgcn_mfma_f32_16x16x32_bf16(Bt[n][k], At[m][k], acc[ai][bj][m][n], 0, 0, 0); __builtin_amdgcn_s_setprio(0); } while (0)
; #define PG8_WAIT_V(n) asm volatile("s_waitcnt vmcnt(" #n ")" ::: "memory")
; #define PG8_WAIT_L(n) asm volatile("s_waitcnt lgkmcnt(" #n ")" ::: "memory")
; #define PG8_BAR __builtin_amdgcn_s_barrier()
; #define PG8_SCHED __builtin_amdgcn_sched_barrier(0)
; template <class Epi, class Sched, bool ALIGN_EPI = false, bool SP2 = false>
; __device__ __forceinline__ void gemm_phase(PG8_LAS unsigned char* lds, const Gemm g, const Sched& S, const Epi& E, const bool skip_epi = false) {
;     ...
;             PG8_WAIT_V(8); PG8_WAIT_L(0); PG8_BAR; PG8_MMA(0, 0, At, B0); PG8_MMA(0, 1, At, B1); PG8_BAR; PG8_SCHED;
;             PG8_LDA(At, 0, 1); PG8_STAGE(PG8_SB(0, 0), b2, voffB); PG8_STAGE(PG8_SB(0, 1), b2 + hstep, voffB); PG8_STAGE_A(0, 0, a2, true);
;             PG8_WAIT_V(8); PG8_WAIT_L(0); PG8_BAR; PG8_MMA(1, 0, At, B0); PG8_MMA(1, 1, At, B1); PG8_BAR; PG8_SCHED;
	s_setprio 3
	s_waitcnt lgkmcnt(0)
	v_mfma_f32_16x16x32_bf16 v[126:129], v[166:169], v[198:201], v[126:129]
	v_mfma_f32_16x16x32_bf16 v[122:125], v[174:177], v[198:201], v[122:125]
	v_mfma_f32_16x16x32_bf16 v[110:113], v[166:169], v[206:209], v[110:113]
	v_mfma_f32_16x16x32_bf16 v[106:109], v[174:177], v[206:209], v[106:109]
	v_mfma_f32_16x16x32_bf16 v[94:97], v[166:169], v[214:217], v[94:97]
	v_mfma_f32_16x16x32_bf16 v[90:93], v[174:177], v[214:217], v[90:93]
	v_mfma_f32_16x16x32_bf16 v[78:81], v[166:169], v[222:225], v[78:81]
	v_mfma_f32_16x16x32_bf16 v[74:77], v[174:177], v[222:225], v[74:77]
	v_mfma_f32_16x16x32_bf16 v[126:129], v[170:173], v[202:205], v[126:129]
	v_mfma_f32_16x16x32_bf16 v[122:125], v[178:181], v[202:205], v[122:125]
	v_mfma_f32_16x16x32_bf16 v[110:113], v[170:173], v[210:213], v[110:113]
	v_mfma_f32_16x16x32_bf16 v[106:109], v[178:181], v[210:213], v[106:109]
	v_mfma_f32_16x16x32_bf16 v[94:97], v[170:173], v[218:221], v[94:97]
	v_mfma_f32_16x16x32_bf16 v[90:93], v[178:181], v[218:221], v[90:93]
	v_mfma_f32_16x16x32_bf16 v[78:81], v[170:173], v[230:233], v[78:81]
	v_mfma_f32_16x16x32_bf16 v[74:77], v[178:181], v[230:233], v[74:77]
	s_setprio 0
	s_setprio 3
	v_mfma_f32_16x16x32_bf16 v[118:121], v[182:185], v[198:201], v[118:121]
	v_mfma_f32_16x16x32_bf16 v[114:117], v[190:193], v[198:201], v[114:117]
	v_mfma_f32_16x16x32_bf16 v[102:105], v[182:185], v[206:209], v[102:105]
	v_mfma_f32_16x16x32_bf16 v[98:101], v[190:193], v[206:209], v[98:101]
	v_mfma_f32_16x16x32_bf16 v[86:89], v[182:185], v[214:217], v[86:89]
	v_mfma_f32_16x16x32_bf16 v[82:85], v[190:193], v[214:217], v[82:85]
	v_mfma_f32_16x16x32_bf16 v[70:73], v[182:185], v[222:225], v[70:73]
	v_mfma_f32_16x16x32_bf16 v[66:69], v[190:193], v[222:225], v[66:69]
	v_mfma_f32_16x16x32_bf16 v[118:121], v[186:189], v[202:205], v[118:121]
	v_mfma_f32_16x16x32_bf16 v[114:117], v[194:197], v[202:205], v[114:117]
	v_mfma_f32_16x16x32_bf16 v[102:105], v[186:189], v[210:213], v[102:105]
	v_mfma_f32_16x16x32_bf16 v[98:101], v[194:197], v[210:213], v[98:101]
	v_mfma_f32_16x16x32_bf16 v[86:89], v[186:189], v[218:221], v[86:89]
	v_mfma_f32_16x16x32_bf16 v[82:85], v[194:197], v[218:221], v[82:85]
	v_mfma_f32_16x16x32_bf16 v[70:73], v[186:189], v[230:233], v[70:73]
	v_mfma_f32_16x16x32_bf16 v[66:69], v[194:197], v[230:233], v[66:69]
	s_setprio 0
	s_barrier
	s_add_i32 s64, s58, s50
	s_mov_b32 m0, s64
	ds_read_b128 v[198:201], v160 offset:16384
	ds_read_b128 v[202:205], v160 offset:17408
	ds_read_b128 v[206:209], v160 offset:18432
	ds_read_b128 v[210:213], v160 offset:19456
	ds_read_b128 v[214:217], v160 offset:20480
	ds_read_b128 v[218:221], v160 offset:21504
	ds_read_b128 v[222:225], v160 offset:22528
	ds_read_b128 v[230:233], v160 offset:23552
	global_load_lds_dwordx4 v134, s[42:43]
	s_add_i32 m0, s64, 0x2000
	s_add_u32 s64, s42, 0x40000
	s_addc_u32 s65, s43, 0
	s_add_i32 s66, s59, s50
	global_load_lds_dwordx4 v136, s[42:43]
	s_mov_b32 m0, s66
	v_cndmask_b32_e32 v132, v130, v164, vcc
	global_load_lds_dwordx4 v134, s[64:65]
	s_add_i32 m0, s66, 0x2000
	v_lshl_add_u64 v[238:239], s[44:45], 0, v[132:133]
	global_load_lds_dwordx4 v136, s[64:65]
	s_mov_b32 m0, s37
	v_cndmask_b32_e32 v236, v144, v163, vcc
	global_load_lds_dwordx4 v132, s[44:45]
	s_mov_b32 m0, s39
	v_mov_b32_e32 v237, v133
	global_load_lds_dwordx4 v236, s[44:45]
	s_waitcnt vmcnt(8)
	s_waitcnt lgkmcnt(0)
	v_lshl_add_u64 v[236:237], s[44:45], 0, v[236:237]
	s_barrier
	s_setprio 3
	s_waitcnt lgkmcnt(0)
	v_mfma_f32_16x16x32_bf16 v[62:65], v[166:169], v[198:201], v[62:65]
	v_mfma_f32_16x16x32_bf16 v[58:61], v[174:177], v[198:201], v[58:61]
	v_mfma_f32_16x16x32_bf16 v[38:41], v[166:169], v[206:209], v[38:41]
	v_mfma_f32_16x16x32_bf16 v[34:37], v[174:177], v[206:209], v[34:37]
	v_mfma_f32_16x16x32_bf16 v[22:25], v[166:169], v[214:217], v[22:25]
	v_mfma_f32_16x16x32_bf16 v[18:21], v[174:177], v[214:217], v[18:21]
	v_mfma_f32_16x16x32_bf16 v[6:9], v[166:169], v[222:225], v[6:9]
	v_mfma_f32_16x16x32_bf16 v[2:5], v[174:177], v[222:225], v[2:5]
	v_mfma_f32_16x16x32_bf16 v[62:65], v[170:173], v[202:205], v[62:65]
	v_mfma_f32_16x16x32_bf16 v[58:61], v[178:181], v[202:205], v[58:61]
	v_mfma_f32_16x16x32_bf16 v[38:41], v[170:173], v[210:213], v[38:41]
	v_mfma_f32_16x16x32_bf16 v[34:37], v[178:181], v[210:213], v[34:37]
	v_mfma_f32_16x16x32_bf16 v[22:25], v[170:173], v[218:221], v[22:25]
	v_mfma_f32_16x16x32_bf16 v[18:21], v[178:181], v[218:221], v[18:21]
	v_mfma_f32_16x16x32_bf16 v[6:9], v[170:173], v[230:233], v[6:9]
	v_mfma_f32_16x16x32_bf16 v[2:5], v[178:181], v[230:233], v[2:5]
	s_setprio 0
	s_setprio 3
	v_mfma_f32_16x16x32_bf16 v[50:53], v[182:185], v[198:201], v[50:53]
	v_mfma_f32_16x16x32_bf16 v[42:45], v[190:193], v[198:201], v[42:45]
	v_mfma_f32_16x16x32_bf16 v[54:57], v[182:185], v[206:209], v[54:57]
	v_mfma_f32_16x16x32_bf16 v[46:49], v[190:193], v[206:209], v[46:49]
	v_mfma_f32_16x16x32_bf16 v[30:33], v[182:185], v[214:217], v[30:33]
	v_mfma_f32_16x16x32_bf16 v[26:29], v[190:193], v[214:217], v[26:29]
	v_mfma_f32_16x16x32_bf16 v[14:17], v[182:185], v[222:225], v[14:17]
	v_mfma_f32_16x16x32_bf16 v[10:13], v[190:193], v[222:225], v[10:13]
	v_mfma_f32_16x16x32_bf16 v[50:53], v[186:189], v[202:205], v[50:53]
	v_mfma_f32_16x16x32_bf16 v[42:45], v[194:197], v[202:205], v[42:45]
	v_mfma_f32_16x16x32_bf16 v[54:57], v[186:189], v[210:213], v[54:57]
	v_mfma_f32_16x16x32_bf16 v[46:49], v[194:197], v[210:213], v[46:49]
	v_mfma_f32_16x16x32_bf16 v[30:33], v[186:189], v[218:221], v[30:33]
	v_mfma_f32_16x16x32_bf16 v[26:29], v[194:197], v[218:221], v[26:29]
	v_mfma_f32_16x16x32_bf16 v[14:17], v[186:189], v[230:233], v[14:17]
	v_mfma_f32_16x16x32_bf16 v[10:13], v[194:197], v[230:233], v[10:13]
	s_setprio 0
	s_barrier
; #define PG8_STAGE_A(b, h, ptr, NX) do { if constexpr (Sched::GATHER) { unsigned gs_[2]; gs_[0] = ((NX) && last_) ? gN[h][0] : gA[h][0]; gs_[1] = ((NX) && last_) ? gN[h][1] : gA[h][1]; PG8_STAGE(PG8_SA(b, h), ptr, gs_); } \
;         else PG8_STAGE(PG8_SA(b, h), (ptr) + ((h) ? hstep : (size_t)0), voffA); } while (0)
; #define PG8_STAGE(bufoff, gbase, voff) do { _Pragma("unroll") for (int _i = 0; _i < 2; ++_i) \
;         __builtin_amdgcn_global_load_lds((const unsigned*)((const char*)(gbase) + (voff)[_i]), (PG8_LAS unsigned*)(lds + (bufoff) + ldsw + _i * 8192), 16, 0, 0); } while (0)
; #define PG8_LDA(dst, b, h) do { _Pragma("unroll") for (int m = 0; m < 4; ++m) _Pragma("unroll") for (int k = 0; k < 2; ++k) dst[m][k] = *(const PG8_LAS bf16x8*)(lds + PG8_SA(b, h) + aoff + m * 2048 + k * 1024); } while (0)
; #define PG8_LDB(dst, b, h) do { _Pragma("unroll") for (int n = 0; n < 2; ++n) _Pragma("unroll") for (int k = 0; k < 2; ++k) dst[n][k] = *(const PG8_LAS bf16x8*)(lds + PG8_SB(b, h) + boff + n * 2048 + k * 1024); } while (0)
; #define PG8_MMA(ai, bj, At, Bt) do { __builtin_amdgcn_s_setprio(1); _Pragma("unroll") for (int m = 0; m < 4; ++m) _Pragma("unroll") for (int n = 0; n < 2; ++n) _Pragma("unroll") for (int k = 0; k < 2; ++k) \
;         acc[ai][bj][m][n] = __builtin_amdgcn_mfma_f32_16x16x32_bf16(Bt[n][k], At[m][k], acc[ai][bj][m][n], 0, 0, 0); __builtin_amdgcn_s_setprio(0); } while (0)
; #define PG8_WAIT_V(n) asm volatile("s_waitcnt vmcnt(" #n ")" ::: "memory")
; #define PG8_WAIT_L(n) asm volatile("s_waitcnt lgkmcnt(" #n ")" ::: "memory")
; #define PG8_BAR __builtin_amdgcn_s_barrier()
; #define PG8_SCHED __builtin_amdgcn_sched_barrier(0)
; template <class Epi, class Sched, bool ALIGN_EPI = false, bool SP2 = false>
; __device__ __forceinline__ void gemm_phase(PG8_LAS unsigned char* lds, const Gemm g, const Sched& S, const Epi& E, const bool skip_epi = false) {
;     ...
;             PG8_LDB(B0, 1, 0); PG8_LDB(B1, 1, 1); PG8_SCHED; PG8_LDA(At, 1, 0); PG8_STAGE_A(0, 1, a2, true);
;             PG8_WAIT_V(8); PG8_WAIT_L(0); PG8_BAR; PG8_MMA(0, 0, At, B0); PG8_MMA(0, 1, At, B1); PG8_BAR; PG8_SCHED;
;             PG8_LDA(At, 1, 1); PG8_STAGE(PG8_SB(1, 0), b3, voffB); PG8_STAGE(PG8_SB(1, 1), b3 + hstep, voffB); PG8_STAGE_A(1, 0, a3, true);
;             PG8_WAIT_V(8); PG8_WAIT_L(0); PG8_BAR; PG8_MMA(1, 0, At, B0); PG8_MMA(1, 1, At, B1); PG8_BAR; PG8_SCHED;
	s_add_i32 s64, 0, 0x18000
	v_add_u32_e32 v132, s64, v154
	s_add_i32 s65, 0, 0x1c000
	ds_read_b128 v[166:169], v132
	ds_read_b128 v[170:173], v132 offset:1024
	ds_read_b128 v[174:177], v132 offset:2048
	ds_read_b128 v[178:181], v132 offset:3072
	v_add_u32_e32 v132, s65, v154
	ds_read_b128 v[182:185], v132
	ds_read_b128 v[186:189], v132 offset:1024
	ds_read_b128 v[190:193], v132 offset:2048
	ds_read_b128 v[194:197], v132 offset:3072
	s_mov_b32 m0, s51
	v_cndmask_b32_e32 v132, v142, v162, vcc
	ds_read_b128 v[198:201], v160 offset:32768
	ds_read_b128 v[202:205], v160 offset:33792
	ds_read_b128 v[206:209], v160 offset:34816
	ds_read_b128 v[210:213], v160 offset:35840
	ds_read_b128 v[214:217], v160 offset:36864
	ds_read_b128 v[218:221], v160 offset:37888
	ds_read_b128 v[222:225], v160 offset:38912
	ds_read_b128 v[230:233], v160 offset:39936
	v_cndmask_b32_e32 v141, v140, v161, vcc
	global_load_lds_dwordx4 v132, s[44:45]
	s_mov_b32 m0, s52
	s_nop 0
	global_load_lds_dwordx4 v141, s[44:45]
	s_waitcnt vmcnt(8)
	s_waitcnt lgkmcnt(0)
	s_barrier
	s_setprio 3
	s_waitcnt lgkmcnt(0)
	v_mfma_f32_16x16x32_bf16 v[126:129], v[166:169], v[198:201], v[126:129]
	v_mfma_f32_16x16x32_bf16 v[122:125], v[174:177], v[198:201], v[122:125]
	v_mfma_f32_16x16x32_bf16 v[110:113], v[166:169], v[206:209], v[110:113]
	v_mfma_f32_16x16x32_bf16 v[106:109], v[174:177], v[206:209], v[106:109]
	v_mfma_f32_16x16x32_bf16 v[94:97], v[166:169], v[214:217], v[94:97]
	v_mfma_f32_16x16x32_bf16 v[90:93], v[174:177], v[214:217], v[90:93]
	v_mfma_f32_16x16x32_bf16 v[78:81], v[166:169], v[222:225], v[78:81]
	v_mfma_f32_16x16x32_bf16 v[74:77], v[174:177], v[222:225], v[74:77]
	v_mfma_f32_16x16x32_bf16 v[126:129], v[170:173], v[202:205], v[126:129]
	v_mfma_f32_16x16x32_bf16 v[122:125], v[178:181], v[202:205], v[122:125]
	v_mfma_f32_16x16x32_bf16 v[110:113], v[170:173], v[210:213], v[110:113]
	v_mfma_f32_16x16x32_bf16 v[106:109], v[178:181], v[210:213], v[106:109]
	v_mfma_f32_16x16x32_bf16 v[94:97], v[170:173], v[218:221], v[94:97]
	v_mfma_f32_16x16x32_bf16 v[90:93], v[178:181], v[218:221], v[90:93]
	v_mfma_f32_16x16x32_bf16 v[78:81], v[170:173], v[230:233], v[78:81]
	v_mfma_f32_16x16x32_bf16 v[74:77], v[178:181], v[230:233], v[74:77]
	s_setprio 0
	s_setprio 3
	v_mfma_f32_16x16x32_bf16 v[118:121], v[182:185], v[198:201], v[118:121]
	v_mfma_f32_16x16x32_bf16 v[114:117], v[190:193], v[198:201], v[114:117]
	v_mfma_f32_16x16x32_bf16 v[102:105], v[182:185], v[206:209], v[102:105]
	v_mfma_f32_16x16x32_bf16 v[98:101], v[190:193], v[206:209], v[98:101]
	v_mfma_f32_16x16x32_bf16 v[86:89], v[182:185], v[214:217], v[86:89]
	v_mfma_f32_16x16x32_bf16 v[82:85], v[190:193], v[214:217], v[82:85]
	v_mfma_f32_16x16x32_bf16 v[70:73], v[182:185], v[222:225], v[70:73]
	v_mfma_f32_16x16x32_bf16 v[66:69], v[190:193], v[222:225], v[66:69]
	v_mfma_f32_16x16x32_bf16 v[118:121], v[186:189], v[202:205], v[118:121]
	v_mfma_f32_16x16x32_bf16 v[114:117], v[194:197], v[202:205], v[114:117]
	v_mfma_f32_16x16x32_bf16 v[102:105], v[186:189], v[210:213], v[102:105]
	v_mfma_f32_16x16x32_bf16 v[98:101], v[194:197], v[210:213], v[98:101]
	v_mfma_f32_16x16x32_bf16 v[86:89], v[186:189], v[218:221], v[86:89]
	v_mfma_f32_16x16x32_bf16 v[82:85], v[194:197], v[218:221], v[82:85]
	v_mfma_f32_16x16x32_bf16 v[70:73], v[186:189], v[230:233], v[70:73]
	v_mfma_f32_16x16x32_bf16 v[66:69], v[194:197], v[230:233], v[66:69]
	s_setprio 0
	s_barrier
	s_add_i32 s44, s64, s50
	s_add_i32 m0, s44, 0xffffff80
	ds_read_b128 v[198:201], v160 offset:49152
	ds_read_b128 v[202:205], v160 offset:50176
	ds_read_b128 v[206:209], v160 offset:51200
	ds_read_b128 v[210:213], v160 offset:52224
	ds_read_b128 v[214:217], v160 offset:53248
	ds_read_b128 v[218:221], v160 offset:54272
	ds_read_b128 v[222:225], v160 offset:55296
	ds_read_b128 v[230:233], v160 offset:56320
	global_load_lds_dwordx4 v134, s[42:43] offset:128
	s_add_i32 m0, s44, 0x1f80
	s_add_i32 s44, s65, s50
	global_load_lds_dwordx4 v136, s[42:43] offset:128
	s_add_u32 s42, s42, 0x40080
	s_addc_u32 s43, s43, 0
	s_mov_b32 m0, s44
	s_nop 0
	global_load_lds_dwordx4 v134, s[42:43]
	s_add_i32 m0, s44, 0x2000
	s_nop 0
	global_load_lds_dwordx4 v136, s[42:43]
	s_add_i32 m0, s55, 0xffffff80
	s_nop 0
	global_load_lds_dwordx4 v[238:239], off offset:128
	s_add_i32 m0, s56, 0xffffff80
	s_nop 0
	global_load_lds_dwordx4 v[236:237], off offset:128
	s_waitcnt vmcnt(8)
	s_waitcnt lgkmcnt(0)
	s_barrier
	s_setprio 3
	s_waitcnt lgkmcnt(0)
	v_mfma_f32_16x16x32_bf16 v[62:65], v[166:169], v[198:201], v[62:65]
	v_mfma_f32_16x16x32_bf16 v[58:61], v[174:177], v[198:201], v[58:61]
	v_mfma_f32_16x16x32_bf16 v[38:41], v[166:169], v[206:209], v[38:41]
	v_mfma_f32_16x16x32_bf16 v[34:37], v[174:177], v[206:209], v[34:37]
	v_mfma_f32_16x16x32_bf16 v[22:25], v[166:169], v[214:217], v[22:25]
	v_mfma_f32_16x16x32_bf16 v[18:21], v[174:177], v[214:217], v[18:21]
	v_mfma_f32_16x16x32_bf16 v[6:9], v[166:169], v[222:225], v[6:9]
	v_mfma_f32_16x16x32_bf16 v[2:5], v[174:177], v[222:225], v[2:5]
	v_mfma_f32_16x16x32_bf16 v[62:65], v[170:173], v[202:205], v[62:65]
	v_mfma_f32_16x16x32_bf16 v[58:61], v[178:181], v[202:205], v[58:61]
	v_mfma_f32_16x16x32_bf16 v[38:41], v[170:173], v[210:213], v[38:41]
	v_mfma_f32_16x16x32_bf16 v[34:37], v[178:181], v[210:213], v[34:37]
	v_mfma_f32_16x16x32_bf16 v[22:25], v[170:173], v[218:221], v[22:25]
	v_mfma_f32_16x16x32_bf16 v[18:21], v[178:181], v[218:221], v[18:21]
	v_mfma_f32_16x16x32_bf16 v[6:9], v[170:173], v[230:233], v[6:9]
	v_mfma_f32_16x16x32_bf16 v[2:5], v[178:181], v[230:233], v[2:5]
	s_setprio 0
	s_setprio 3
	v_mfma_f32_16x16x32_bf16 v[50:53], v[182:185], v[198:201], v[50:53]
	v_mfma_f32_16x16x32_bf16 v[42:45], v[190:193], v[198:201], v[42:45]
	v_mfma_f32_16x16x32_bf16 v[54:57], v[182:185], v[206:209], v[54:57]
	v_mfma_f32_16x16x32_bf16 v[46:49], v[190:193], v[206:209], v[46:49]
	v_mfma_f32_16x16x32_bf16 v[30:33], v[182:185], v[214:217], v[30:33]
	v_mfma_f32_16x16x32_bf16 v[26:29], v[190:193], v[214:217], v[26:29]
	v_mfma_f32_16x16x32_bf16 v[14:17], v[182:185], v[222:225], v[14:17]
	v_mfma_f32_16x16x32_bf16 v[10:13], v[190:193], v[222:225], v[10:13]
	v_mfma_f32_16x16x32_bf16 v[50:53], v[186:189], v[202:205], v[50:53]
	v_mfma_f32_16x16x32_bf16 v[42:45], v[194:197], v[202:205], v[42:45]
	v_mfma_f32_16x16x32_bf16 v[54:57], v[186:189], v[210:213], v[54:57]
	v_mfma_f32_16x16x32_bf16 v[46:49], v[194:197], v[210:213], v[46:49]
	v_mfma_f32_16x16x32_bf16 v[30:33], v[186:189], v[218:221], v[30:33]
	v_mfma_f32_16x16x32_bf16 v[26:29], v[194:197], v[218:221], v[26:29]
	v_mfma_f32_16x16x32_bf16 v[14:17], v[186:189], v[230:233], v[14:17]
	v_mfma_f32_16x16x32_bf16 v[10:13], v[194:197], v[230:233], v[10:13]
	s_setprio 0
	s_barrier
	s_add_i32 s63, s63, 2
	s_add_u32 s40, s40, 0x100
	s_addc_u32 s41, s41, 0
	s_cmp_gt_u32 s63, 13
	s_cbranch_scc0 .LBB0_1728
	s_and_b64 vcc, exec, s[26:27]
	s_cbranch_vccz .LBB0_1731
	s_barrier

; #define PG8_STAGE_A(b, h, ptr, NX) do { if constexpr (Sched::GATHER) { unsigned gs_[2]; gs_[0] = ((NX) && last_) ? gN[h][0] : gA[h][0]; gs_[1] = ((NX) && last_) ? gN[h][1] : gA[h][1]; PG8_STAGE(PG8_SA(b, h), ptr, gs_); } \
;         else PG8_STAGE(PG8_SA(b, h), (ptr) + ((h) ? hstep : (size_t)0), voffA); } while (0)
; #define PG8_STAGE(bufoff, gbase, voff) do { _Pragma("unroll") for (int _i = 0; _i < 2; ++_i) \
;         __builtin_amdgcn_global_load_lds((const unsigned*)((const char*)(gbase) + (voff)[_i]), (PG8_LAS unsigned*)(lds + (bufoff) + ldsw + _i * 8192), 16, 0, 0); } while (0)
; #define PG8_LDA(dst, b, h) do { _Pragma("unroll") for (int m = 0; m < 4; ++m) _Pragma("unroll") for (int k = 0; k < 2; ++k) dst[m][k] = *(const PG8_LAS bf16x8*)(lds + PG8_SA(b, h) + aoff + m * 2048 + k * 1024); } while (0)
; #define PG8_LDB(dst, b, h) do { _Pragma("unroll") for (int n = 0; n < 2; ++n) _Pragma("unroll") for (int k = 0; k < 2; ++k) dst[n][k] = *(const PG8_LAS bf16x8*)(lds + PG8_SB(b, h) + boff + n * 2048 + k * 1024); } while (0)
; #define PG8_WAIT_V(n) asm volatile("s_waitcnt vmcnt(" #n ")" ::: "memory")
; #define PG8_WAIT_L(n) asm volatile("s_waitcnt lgkmcnt(" #n ")" ::: "memory")
; template <class Epi, class Sched, bool ALIGN_EPI = false, bool SP2 = false>
; __device__ __forceinline__ void gemm_phase(PG8_LAS unsigned char* lds, const Gemm g, const Sched& S, const Epi& E, const bool skip_epi = false) {
;     ...
;         for (int t = 0; t < nt; t += 2) {
;             const bool last = (t == nt - 2); last_ = last && has_next;
;             const char* a1 = cA + (size_t)(t + 1) * kstep;
;             const char* a2 = last ? nA : cA + (size_t)(t + 2) * kstep; const char* b2 = last ? nB : cB + (size_t)(t + 2) * kstep;
;             const char* a3 = a2 + kstep; const char* b3 = b2 + kstep;
;             if (last && has_next) S.a_ready(nxt);
;             if constexpr (SP2) {
;             PG8_LDB(B0, 0, 0); PG8_LDB(B1, 0, 1); PG8_SCHED; PG8_LDA(At, 0, 0); PG8_STAGE_A(1, 1, a1, false);
;             PG8_WAIT_V(8); PG8_WAIT_L(0); PG8_BAR; PG8_MMA(0, 0, At, B0); PG8_MMA(0, 1, At, B1); PG8_BAR; PG8_SCHED;
;             PG8_LDA(At, 0, 1); PG8_STAGE(PG8_SB(0, 0), b2, voffB); PG8_STAGE(PG8_SB(0, 1), b2 + hstep, voffB); PG8_STAGE_A(0, 0, a2, true);
;             PG8_WAIT_V(8); PG8_WAIT_L(0); PG8_BAR; PG8_MMA(1, 0, At, B0); PG8_MMA(1, 1, At, B1); PG8_BAR; PG8_SCHED;
.LBB0_1822:
	s_add_u32 s67, s40, 0x100
	s_addc_u32 s68, s41, 0
	s_mov_b32 s69, -2
	ds_read_b128 v[160:163], v157
	ds_read_b128 v[164:167], v157 offset:1024
	ds_read_b128 v[168:171], v157 offset:2048
	ds_read_b128 v[172:175], v157 offset:3072
	ds_read_b128 v[176:179], v158
	ds_read_b128 v[180:183], v158 offset:1024
	ds_read_b128 v[184:187], v158 offset:2048
	ds_read_b128 v[188:191], v158 offset:3072
	s_add_u32 s40, s38, 0x100
	s_addc_u32 s41, s39, 0
	s_cmp_eq_u32 s69, 52
	s_cselect_b32 s45, s7, s41
	s_cselect_b32 s44, s6, s40
	s_cselect_b32 s43, s35, s68
	s_cselect_b32 s42, s34, s67
	v_lshl_add_u64 v[152:153], s[38:39], 0, v[140:141]
	s_add_i32 m0, s37, 0xc000
	ds_read_b128 v[192:195], v159
	ds_read_b128 v[196:199], v159 offset:1024
	ds_read_b128 v[200:203], v159 offset:2048
	ds_read_b128 v[204:207], v159 offset:3072
	ds_read_b128 v[208:211], v159 offset:4096
	ds_read_b128 v[212:215], v159 offset:5120
	ds_read_b128 v[216:219], v159 offset:6144
	ds_read_b128 v[220:223], v159 offset:7168
	global_load_lds_dwordx4 v[152:153], off
	v_lshl_add_u64 v[152:153], s[38:39], 0, v[142:143]
	s_add_i32 m0, s37, 0xe000
	s_nop 0
	global_load_lds_dwordx4 v[152:153], off
	s_waitcnt vmcnt(8)
	s_waitcnt lgkmcnt(0)
	s_barrier
	s_setprio 3
	s_waitcnt lgkmcnt(0)
	v_mfma_f32_16x16x32_bf16 v[126:129], v[160:163], v[192:195], 0
	v_mfma_f32_16x16x32_bf16 v[122:125], v[168:171], v[192:195], 0
	v_mfma_f32_16x16x32_bf16 v[118:121], v[160:163], v[200:203], 0
	v_mfma_f32_16x16x32_bf16 v[114:117], v[168:171], v[200:203], 0
	v_mfma_f32_16x16x32_bf16 v[106:109], v[160:163], v[208:211], 0
	v_mfma_f32_16x16x32_bf16 v[98:101], v[168:171], v[208:211], 0
	v_mfma_f32_16x16x32_bf16 v[78:81], v[160:163], v[216:219], 0
	v_mfma_f32_16x16x32_bf16 v[74:77], v[168:171], v[216:219], 0
	v_mfma_f32_16x16x32_bf16 v[126:129], v[164:167], v[196:199], v[126:129]
	v_mfma_f32_16x16x32_bf16 v[122:125], v[172:175], v[196:199], v[122:125]
	v_mfma_f32_16x16x32_bf16 v[118:121], v[164:167], v[204:207], v[118:121]
	v_mfma_f32_16x16x32_bf16 v[114:117], v[172:175], v[204:207], v[114:117]
	v_mfma_f32_16x16x32_bf16 v[106:109], v[164:167], v[212:215], v[106:109]
	v_mfma_f32_16x16x32_bf16 v[98:101], v[172:175], v[212:215], v[98:101]
	v_mfma_f32_16x16x32_bf16 v[78:81], v[164:167], v[220:223], v[78:81]
	v_mfma_f32_16x16x32_bf16 v[74:77], v[172:175], v[220:223], v[74:77]
	s_setprio 0
	s_setprio 3
	v_mfma_f32_16x16x32_bf16 v[110:113], v[176:179], v[192:195], 0
	v_mfma_f32_16x16x32_bf16 v[102:105], v[184:187], v[192:195], 0
	v_mfma_f32_16x16x32_bf16 v[94:97], v[176:179], v[200:203], 0
	v_mfma_f32_16x16x32_bf16 v[90:93], v[184:187], v[200:203], 0
	v_mfma_f32_16x16x32_bf16 v[86:89], v[176:179], v[208:211], 0
	v_mfma_f32_16x16x32_bf16 v[82:85], v[184:187], v[208:211], 0
	v_mfma_f32_16x16x32_bf16 v[70:73], v[176:179], v[216:219], 0
	v_mfma_f32_16x16x32_bf16 v[66:69], v[184:187], v[216:219], 0
	v_mfma_f32_16x16x32_bf16 v[110:113], v[180:183], v[196:199], v[110:113]
	v_mfma_f32_16x16x32_bf16 v[102:105], v[188:191], v[196:199], v[102:105]
	v_mfma_f32_16x16x32_bf16 v[94:97], v[180:183], v[204:207], v[94:97]
	v_mfma_f32_16x16x32_bf16 v[90:93], v[188:191], v[204:207], v[90:93]
	v_mfma_f32_16x16x32_bf16 v[86:89], v[180:183], v[212:215], v[86:89]
	v_mfma_f32_16x16x32_bf16 v[82:85], v[188:191], v[212:215], v[82:85]
	v_mfma_f32_16x16x32_bf16 v[70:73], v[180:183], v[220:223], v[70:73]
	v_mfma_f32_16x16x32_bf16 v[66:69], v[188:191], v[220:223], v[66:69]
	s_setprio 0
	s_barrier
	s_add_i32 s38, s60, s51
	s_mov_b64 s[98:99], s[42:43]
	s_mov_b32 m0, s38
	ds_read_b128 v[192:195], v159 offset:16384
	ds_read_b128 v[196:199], v159 offset:17408
	ds_read_b128 v[200:203], v159 offset:18432
	ds_read_b128 v[204:207], v159 offset:19456
	ds_read_b128 v[208:211], v159 offset:20480
	ds_read_b128 v[212:215], v159 offset:21504
	ds_read_b128 v[216:219], v159 offset:22528
	ds_read_b128 v[220:223], v159 offset:23552
	global_load_lds_dwordx4 v134, s[42:43]
	s_add_i32 m0, s38, 0x2000
	s_add_u32 s38, s42, 0xe0000
	s_addc_u32 s39, s43, 0
	s_add_i32 s70, s61, s51
	global_load_lds_dwordx4 v138, s[42:43]
	s_mov_b32 m0, s70
	s_nop 0
	global_load_lds_dwordx4 v134, s[38:39]
	s_add_i32 m0, s70, 0x2000
	s_nop 0
	global_load_lds_dwordx4 v138, s[38:39]
	s_mov_b32 m0, s37
	s_nop 0
	global_load_lds_dwordx4 v132, s[44:45]
	s_mov_b32 m0, s52
	s_nop 0
	global_load_lds_dwordx4 v136, s[44:45]
	s_waitcnt vmcnt(8)
	s_waitcnt lgkmcnt(0)
	s_barrier
	s_setprio 3
	s_waitcnt lgkmcnt(0)
	v_mfma_f32_16x16x32_bf16 v[62:65], v[160:163], v[192:195], 0
	v_mfma_f32_16x16x32_bf16 v[58:61], v[168:171], v[192:195], 0
	v_mfma_f32_16x16x32_bf16 v[50:53], v[160:163], v[200:203], 0
	v_mfma_f32_16x16x32_bf16 v[42:45], v[168:171], v[200:203], 0
	v_mfma_f32_16x16x32_bf16 v[34:37], v[160:163], v[208:211], 0
	v_mfma_f32_16x16x32_bf16 v[26:29], v[168:171], v[208:211], 0
	v_mfma_f32_16x16x32_bf16 v[18:21], v[160:163], v[216:219], 0
	v_mfma_f32_16x16x32_bf16 v[10:13], v[168:171], v[216:219], 0
	v_mfma_f32_16x16x32_bf16 v[62:65], v[164:167], v[196:199], v[62:65]
	v_mfma_f32_16x16x32_bf16 v[58:61], v[172:175], v[196:199], v[58:61]
	v_mfma_f32_16x16x32_bf16 v[50:53], v[164:167], v[204:207], v[50:53]
	v_mfma_f32_16x16x32_bf16 v[42:45], v[172:175], v[204:207], v[42:45]
	v_mfma_f32_16x16x32_bf16 v[34:37], v[164:167], v[212:215], v[34:37]
	v_mfma_f32_16x16x32_bf16 v[26:29], v[172:175], v[212:215], v[26:29]
	v_mfma_f32_16x16x32_bf16 v[18:21], v[164:167], v[220:223], v[18:21]
	v_mfma_f32_16x16x32_bf16 v[10:13], v[172:175], v[220:223], v[10:13]
	s_setprio 0
	s_setprio 3
	v_mfma_f32_16x16x32_bf16 v[54:57], v[176:179], v[192:195], 0
	v_mfma_f32_16x16x32_bf16 v[46:49], v[184:187], v[192:195], 0
	v_mfma_f32_16x16x32_bf16 v[38:41], v[176:179], v[200:203], 0
	v_mfma_f32_16x16x32_bf16 v[30:33], v[184:187], v[200:203], 0
	v_mfma_f32_16x16x32_bf16 v[22:25], v[176:179], v[208:211], 0
	v_mfma_f32_16x16x32_bf16 v[14:17], v[184:187], v[208:211], 0
	v_mfma_f32_16x16x32_bf16 v[6:9], v[176:179], v[216:219], 0
	v_mfma_f32_16x16x32_bf16 v[2:5], v[184:187], v[216:219], 0
	v_mfma_f32_16x16x32_bf16 v[54:57], v[180:183], v[196:199], v[54:57]
	v_mfma_f32_16x16x32_bf16 v[46:49], v[188:191], v[196:199], v[46:49]
	v_mfma_f32_16x16x32_bf16 v[38:41], v[180:183], v[204:207], v[38:41]
	v_mfma_f32_16x16x32_bf16 v[30:33], v[188:191], v[204:207], v[30:33]
	v_mfma_f32_16x16x32_bf16 v[22:25], v[180:183], v[212:215], v[22:25]
	v_mfma_f32_16x16x32_bf16 v[14:17], v[188:191], v[212:215], v[14:17]
	v_mfma_f32_16x16x32_bf16 v[6:9], v[180:183], v[220:223], v[6:9]
	v_mfma_f32_16x16x32_bf16 v[2:5], v[188:191], v[220:223], v[2:5]
	s_setprio 0
	s_barrier
; #define PG8_STAGE_A(b, h, ptr, NX) do { if constexpr (Sched::GATHER) { unsigned gs_[2]; gs_[0] = ((NX) && last_) ? gN[h][0] : gA[h][0]; gs_[1] = ((NX) && last_) ? gN[h][1] : gA[h][1]; PG8_STAGE(PG8_SA(b, h), ptr, gs_); } \
;         else PG8_STAGE(PG8_SA(b, h), (ptr) + ((h) ? hstep : (size_t)0), voffA); } while (0)
; #define PG8_STAGE(bufoff, gbase, voff) do { _Pragma("unroll") for (int _i = 0; _i < 2; ++_i) \
;         __builtin_amdgcn_global_load_lds((const unsigned*)((const char*)(gbase) + (voff)[_i]), (PG8_LAS unsigned*)(lds + (bufoff) + ldsw + _i * 8192), 16, 0, 0); } while (0)
; #define PG8_LDA(dst, b, h) do { _Pragma("unroll") for (int m = 0; m < 4; ++m) _Pragma("unroll") for (int k = 0; k < 2; ++k) dst[m][k] = *(const PG8_LAS bf16x8*)(lds + PG8_SA(b, h) + aoff + m * 2048 + k * 1024); } while (0)
; #define PG8_LDB(dst, b, h) do { _Pragma("unroll") for (int n = 0; n < 2; ++n) _Pragma("unroll") for (int k = 0; k < 2; ++k) dst[n][k] = *(const PG8_LAS bf16x8*)(lds + PG8_SB(b, h) + boff + n * 2048 + k * 1024); } while (0)
; #define PG8_MMA(ai, bj, At, Bt) do { __builtin_amdgcn_s_setprio(1); _Pragma("unroll") for (int m = 0; m < 4; ++m) _Pragma("unroll") for (int n = 0; n < 2; ++n) _Pragma("unroll") for (int k = 0; k < 2; ++k) \
;         acc[ai][bj][m][n] = __builtin_amdgcn_mfma_f32_16x16x32_bf16(Bt[n][k], At[m][k], acc[ai][bj][m][n], 0, 0, 0); __builtin_amdgcn_s_setprio(0); } while (0)
; #define PG8_WAIT_V(n) asm volatile("s_waitcnt vmcnt(" #n ")" ::: "memory")
; #define PG8_WAIT_L(n) asm volatile("s_waitcnt lgkmcnt(" #n ")" ::: "memory")
; #define PG8_BAR __builtin_amdgcn_s_barrier()
; #define PG8_SCHED __builtin_amdgcn_sched_barrier(0)
; template <class Epi, class Sched, bool ALIGN_EPI = false, bool SP2 = false>
; __device__ __forceinline__ void gemm_phase(PG8_LAS unsigned char* lds, const Gemm g, const Sched& S, const Epi& E, const bool skip_epi = false) {
;     ...
;             PG8_LDB(B0, 1, 0); PG8_LDB(B1, 1, 1); PG8_SCHED; PG8_LDA(At, 1, 0); PG8_STAGE_A(0, 1, a2, true);
;             PG8_WAIT_V(8); PG8_WAIT_L(0); PG8_BAR; PG8_MMA(0, 0, At, B0); PG8_MMA(0, 1, At, B1); PG8_BAR; PG8_SCHED;
;             PG8_LDA(At, 1, 1); PG8_STAGE(PG8_SB(1, 0), b3, voffB); PG8_STAGE(PG8_SB(1, 1), b3 + hstep, voffB); PG8_STAGE_A(1, 0, a3, true);
;             PG8_WAIT_V(8); PG8_WAIT_L(0); PG8_BAR; PG8_MMA(1, 0, At, B0); PG8_MMA(1, 1, At, B1); PG8_BAR; PG8_SCHED;
	s_add_i32 s70, 0, 0x18000
	v_add_u32_e32 v130, s70, v147
	s_add_i32 s71, 0, 0x1c000
	ds_read_b128 v[160:163], v130
	ds_read_b128 v[164:167], v130 offset:1024
	ds_read_b128 v[168:171], v130 offset:2048
	ds_read_b128 v[172:175], v130 offset:3072
	v_add_u32_e32 v130, s71, v147
	ds_read_b128 v[176:179], v130
	ds_read_b128 v[180:183], v130 offset:1024
	ds_read_b128 v[184:187], v130 offset:2048
	ds_read_b128 v[188:191], v130 offset:3072
	s_add_u32 s38, s44, 0xe0000
	s_addc_u32 s39, s45, 0
	s_mov_b32 m0, s53
	ds_read_b128 v[192:195], v159 offset:32768
	ds_read_b128 v[196:199], v159 offset:33792
	ds_read_b128 v[200:203], v159 offset:34816
	ds_read_b128 v[204:207], v159 offset:35840
	ds_read_b128 v[208:211], v159 offset:36864
	ds_read_b128 v[212:215], v159 offset:37888
	ds_read_b128 v[216:219], v159 offset:38912
	ds_read_b128 v[220:223], v159 offset:39936
	global_load_lds_dwordx4 v132, s[38:39]
	s_mov_b32 m0, s54
	s_nop 0
	global_load_lds_dwordx4 v136, s[38:39]
	s_waitcnt vmcnt(8)
	s_waitcnt lgkmcnt(0)
	s_barrier
	s_setprio 3
	s_waitcnt lgkmcnt(0)
	v_mfma_f32_16x16x32_bf16 v[126:129], v[160:163], v[192:195], v[126:129]
	v_mfma_f32_16x16x32_bf16 v[122:125], v[168:171], v[192:195], v[122:125]
	v_mfma_f32_16x16x32_bf16 v[118:121], v[160:163], v[200:203], v[118:121]
	v_mfma_f32_16x16x32_bf16 v[114:117], v[168:171], v[200:203], v[114:117]
	v_mfma_f32_16x16x32_bf16 v[106:109], v[160:163], v[208:211], v[106:109]
	v_mfma_f32_16x16x32_bf16 v[98:101], v[168:171], v[208:211], v[98:101]
	v_mfma_f32_16x16x32_bf16 v[78:81], v[160:163], v[216:219], v[78:81]
	v_mfma_f32_16x16x32_bf16 v[74:77], v[168:171], v[216:219], v[74:77]
	v_mfma_f32_16x16x32_bf16 v[126:129], v[164:167], v[196:199], v[126:129]
	v_mfma_f32_16x16x32_bf16 v[122:125], v[172:175], v[196:199], v[122:125]
	v_mfma_f32_16x16x32_bf16 v[118:121], v[164:167], v[204:207], v[118:121]
	v_mfma_f32_16x16x32_bf16 v[114:117], v[172:175], v[204:207], v[114:117]
	v_mfma_f32_16x16x32_bf16 v[106:109], v[164:167], v[212:215], v[106:109]
	v_mfma_f32_16x16x32_bf16 v[98:101], v[172:175], v[212:215], v[98:101]
	v_mfma_f32_16x16x32_bf16 v[78:81], v[164:167], v[220:223], v[78:81]
	v_mfma_f32_16x16x32_bf16 v[74:77], v[172:175], v[220:223], v[74:77]
	s_setprio 0
	s_setprio 3
	v_mfma_f32_16x16x32_bf16 v[110:113], v[176:179], v[192:195], v[110:113]
	v_mfma_f32_16x16x32_bf16 v[102:105], v[184:187], v[192:195], v[102:105]
	v_mfma_f32_16x16x32_bf16 v[94:97], v[176:179], v[200:203], v[94:97]
	v_mfma_f32_16x16x32_bf16 v[90:93], v[184:187], v[200:203], v[90:93]
	v_mfma_f32_16x16x32_bf16 v[86:89], v[176:179], v[208:211], v[86:89]
	v_mfma_f32_16x16x32_bf16 v[82:85], v[184:187], v[208:211], v[82:85]
	v_mfma_f32_16x16x32_bf16 v[70:73], v[176:179], v[216:219], v[70:73]
	v_mfma_f32_16x16x32_bf16 v[66:69], v[184:187], v[216:219], v[66:69]
	v_mfma_f32_16x16x32_bf16 v[110:113], v[180:183], v[196:199], v[110:113]
	v_mfma_f32_16x16x32_bf16 v[102:105], v[188:191], v[196:199], v[102:105]
	v_mfma_f32_16x16x32_bf16 v[94:97], v[180:183], v[204:207], v[94:97]
	v_mfma_f32_16x16x32_bf16 v[90:93], v[188:191], v[204:207], v[90:93]
	v_mfma_f32_16x16x32_bf16 v[86:89], v[180:183], v[212:215], v[86:89]
	v_mfma_f32_16x16x32_bf16 v[82:85], v[188:191], v[212:215], v[82:85]
	v_mfma_f32_16x16x32_bf16 v[70:73], v[180:183], v[220:223], v[70:73]
	v_mfma_f32_16x16x32_bf16 v[66:69], v[188:191], v[220:223], v[66:69]
	s_setprio 0
	s_barrier
	s_add_i32 s38, s70, s51
	s_add_i32 m0, s38, 0xffffff80
	ds_read_b128 v[192:195], v159 offset:49152
	ds_read_b128 v[196:199], v159 offset:50176
	ds_read_b128 v[200:203], v159 offset:51200
	ds_read_b128 v[204:207], v159 offset:52224
	ds_read_b128 v[208:211], v159 offset:53248
	ds_read_b128 v[212:215], v159 offset:54272
	ds_read_b128 v[216:219], v159 offset:55296
	ds_read_b128 v[220:223], v159 offset:56320
	global_load_lds_dwordx4 v134, s[42:43] offset:128
	s_add_i32 m0, s38, 0x1f80
	s_add_u32 s38, s42, 0xe0080
	s_addc_u32 s39, s43, 0
	s_add_i32 s42, s71, s51
	global_load_lds_dwordx4 v138, s[98:99] offset:128
	s_mov_b32 m0, s42
	s_nop 0
	global_load_lds_dwordx4 v134, s[38:39]
	s_add_i32 m0, s42, 0x2000
	s_nop 0
	global_load_lds_dwordx4 v138, s[38:39]
	s_add_i32 m0, s57, 0xffffff80
	s_nop 0
	global_load_lds_dwordx4 v132, s[44:45] offset:128
	s_add_i32 m0, s58, 0xffffff80
	s_nop 0
	global_load_lds_dwordx4 v136, s[44:45] offset:128
	s_waitcnt vmcnt(8)
	s_waitcnt lgkmcnt(0)
	s_barrier
	s_setprio 3
	s_waitcnt lgkmcnt(0)
	v_mfma_f32_16x16x32_bf16 v[62:65], v[160:163], v[192:195], v[62:65]
	v_mfma_f32_16x16x32_bf16 v[58:61], v[168:171], v[192:195], v[58:61]
	v_mfma_f32_16x16x32_bf16 v[50:53], v[160:163], v[200:203], v[50:53]
	v_mfma_f32_16x16x32_bf16 v[42:45], v[168:171], v[200:203], v[42:45]
	v_mfma_f32_16x16x32_bf16 v[34:37], v[160:163], v[208:211], v[34:37]
	v_mfma_f32_16x16x32_bf16 v[26:29], v[168:171], v[208:211], v[26:29]
	v_mfma_f32_16x16x32_bf16 v[18:21], v[160:163], v[216:219], v[18:21]
	v_mfma_f32_16x16x32_bf16 v[10:13], v[168:171], v[216:219], v[10:13]
	v_mfma_f32_16x16x32_bf16 v[62:65], v[164:167], v[196:199], v[62:65]
	v_mfma_f32_16x16x32_bf16 v[58:61], v[172:175], v[196:199], v[58:61]
	v_mfma_f32_16x16x32_bf16 v[50:53], v[164:167], v[204:207], v[50:53]
	v_mfma_f32_16x16x32_bf16 v[42:45], v[172:175], v[204:207], v[42:45]
	v_mfma_f32_16x16x32_bf16 v[34:37], v[164:167], v[212:215], v[34:37]
	v_mfma_f32_16x16x32_bf16 v[26:29], v[172:175], v[212:215], v[26:29]
	v_mfma_f32_16x16x32_bf16 v[18:21], v[164:167], v[220:223], v[18:21]
	v_mfma_f32_16x16x32_bf16 v[10:13], v[172:175], v[220:223], v[10:13]
	s_setprio 0
	s_setprio 3
	v_mfma_f32_16x16x32_bf16 v[54:57], v[176:179], v[192:195], v[54:57]
	v_mfma_f32_16x16x32_bf16 v[46:49], v[184:187], v[192:195], v[46:49]
	v_mfma_f32_16x16x32_bf16 v[38:41], v[176:179], v[200:203], v[38:41]
	v_mfma_f32_16x16x32_bf16 v[30:33], v[184:187], v[200:203], v[30:33]
	v_mfma_f32_16x16x32_bf16 v[22:25], v[176:179], v[208:211], v[22:25]
	v_mfma_f32_16x16x32_bf16 v[14:17], v[184:187], v[208:211], v[14:17]
	v_mfma_f32_16x16x32_bf16 v[6:9], v[176:179], v[216:219], v[6:9]
	v_mfma_f32_16x16x32_bf16 v[2:5], v[184:187], v[216:219], v[2:5]
	v_mfma_f32_16x16x32_bf16 v[54:57], v[180:183], v[196:199], v[54:57]
	v_mfma_f32_16x16x32_bf16 v[46:49], v[188:191], v[196:199], v[46:49]
	v_mfma_f32_16x16x32_bf16 v[38:41], v[180:183], v[204:207], v[38:41]
	v_mfma_f32_16x16x32_bf16 v[30:33], v[188:191], v[204:207], v[30:33]
	v_mfma_f32_16x16x32_bf16 v[22:25], v[180:183], v[212:215], v[22:25]
	v_mfma_f32_16x16x32_bf16 v[14:17], v[188:191], v[212:215], v[14:17]
	v_mfma_f32_16x16x32_bf16 v[6:9], v[180:183], v[220:223], v[6:9]
	v_mfma_f32_16x16x32_bf16 v[2:5], v[188:191], v[220:223], v[2:5]
	s_setprio 0
	s_barrier
	s_add_i32 s69, s69, 2
	s_add_u32 s67, s67, 0x100
	s_addc_u32 s68, s68, 0
	s_cmp_gt_u32 s69, 53
	s_mov_b64 s[38:39], s[40:41]
; #define PG8_STAGE_A(b, h, ptr, NX) do { if constexpr (Sched::GATHER) { unsigned gs_[2]; gs_[0] = ((NX) && last_) ? gN[h][0] : gA[h][0]; gs_[1] = ((NX) && last_) ? gN[h][1] : gA[h][1]; PG8_STAGE(PG8_SA(b, h), ptr, gs_); } \
;         else PG8_STAGE(PG8_SA(b, h), (ptr) + ((h) ? hstep : (size_t)0), voffA); } while (0)
; #define PG8_STAGE(bufoff, gbase, voff) do { _Pragma("unroll") for (int _i = 0; _i < 2; ++_i) \
;         __builtin_amdgcn_global_load_lds((const unsigned*)((const char*)(gbase) + (voff)[_i]), (PG8_LAS unsigned*)(lds + (bufoff) + ldsw + _i * 8192), 16, 0, 0); } while (0)
; #define PG8_LDA(dst, b, h) do { _Pragma("unroll") for (int m = 0; m < 4; ++m) _Pragma("unroll") for (int k = 0; k < 2; ++k) dst[m][k] = *(const PG8_LAS bf16x8*)(lds + PG8_SA(b, h) + aoff + m * 2048 + k * 1024); } while (0)
; #define PG8_LDB(dst, b, h) do { _Pragma("unroll") for (int n = 0; n < 2; ++n) _Pragma("unroll") for (int k = 0; k < 2; ++k) dst[n][k] = *(const PG8_LAS bf16x8*)(lds + PG8_SB(b, h) + boff + n * 2048 + k * 1024); } while (0)
; #define PG8_WAIT_V(n) asm volatile("s_waitcnt vmcnt(" #n ")" ::: "memory")
; #define PG8_WAIT_L(n) asm volatile("s_waitcnt lgkmcnt(" #n ")" ::: "memory")
; template <class Epi, class Sched, bool ALIGN_EPI = false, bool SP2 = false>
; __device__ __forceinline__ void gemm_phase(PG8_LAS unsigned char* lds, const Gemm g, const Sched& S, const Epi& E, const bool skip_epi = false) {
;     ...
;         for (int t = 0; t < nt; t += 2) {
;             const bool last = (t == nt - 2); last_ = last && has_next;
;             const char* a1 = cA + (size_t)(t + 1) * kstep;
;             const char* a2 = last ? nA : cA + (size_t)(t + 2) * kstep; const char* b2 = last ? nB : cB + (size_t)(t + 2) * kstep;
;             const char* a3 = a2 + kstep; const char* b3 = b2 + kstep;
;             if (last && has_next) S.a_ready(nxt);
;             if constexpr (SP2) {
;             PG8_LDB(B0, 0, 0); PG8_LDB(B1, 0, 1); PG8_SCHED; PG8_LDA(At, 0, 0); PG8_STAGE_A(1, 1, a1, false);
;             PG8_WAIT_V(8); PG8_WAIT_L(0); PG8_BAR; PG8_MMA(0, 0, At, B0); PG8_MMA(0, 1, At, B1); PG8_BAR; PG8_SCHED;
;             PG8_LDA(At, 0, 1); PG8_STAGE(PG8_SB(0, 0), b2, voffB); PG8_STAGE(PG8_SB(0, 1), b2 + hstep, voffB); PG8_STAGE_A(0, 0, a2, true);
;             PG8_WAIT_V(8); PG8_WAIT_L(0); PG8_BAR; PG8_MMA(1, 0, At, B0); PG8_MMA(1, 1, At, B1); PG8_BAR; PG8_SCHED;
.LBB0_1823:
	ds_read_b128 v[160:163], v157
	ds_read_b128 v[164:167], v157 offset:1024
	ds_read_b128 v[168:171], v157 offset:2048
	ds_read_b128 v[172:175], v157 offset:3072
	ds_read_b128 v[176:179], v158
	ds_read_b128 v[180:183], v158 offset:1024
	ds_read_b128 v[184:187], v158 offset:2048
	ds_read_b128 v[188:191], v158 offset:3072
	s_add_u32 s40, s38, 0x100
	s_addc_u32 s41, s39, 0
	s_cmp_eq_u32 s69, 52
	s_cselect_b32 s45, s7, s41
	s_cselect_b32 s44, s6, s40
	s_cselect_b32 s43, s35, s68
	s_cselect_b32 s42, s34, s67
	v_lshl_add_u64 v[152:153], s[38:39], 0, v[140:141]
	s_add_i32 m0, s37, 0xc000
	ds_read_b128 v[192:195], v159
	ds_read_b128 v[196:199], v159 offset:1024
	ds_read_b128 v[200:203], v159 offset:2048
	ds_read_b128 v[204:207], v159 offset:3072
	ds_read_b128 v[208:211], v159 offset:4096
	ds_read_b128 v[212:215], v159 offset:5120
	ds_read_b128 v[216:219], v159 offset:6144
	ds_read_b128 v[220:223], v159 offset:7168
	global_load_lds_dwordx4 v[152:153], off
	v_lshl_add_u64 v[152:153], s[38:39], 0, v[142:143]
	s_add_i32 m0, s37, 0xe000
	s_nop 0
	global_load_lds_dwordx4 v[152:153], off
	s_waitcnt vmcnt(8)
	s_waitcnt lgkmcnt(0)
	s_barrier
	s_setprio 3
	s_waitcnt lgkmcnt(0)
	v_mfma_f32_16x16x32_bf16 v[126:129], v[160:163], v[192:195], v[126:129]
	v_mfma_f32_16x16x32_bf16 v[122:125], v[168:171], v[192:195], v[122:125]
	v_mfma_f32_16x16x32_bf16 v[118:121], v[160:163], v[200:203], v[118:121]
	v_mfma_f32_16x16x32_bf16 v[114:117], v[168:171], v[200:203], v[114:117]
	v_mfma_f32_16x16x32_bf16 v[106:109], v[160:163], v[208:211], v[106:109]
	v_mfma_f32_16x16x32_bf16 v[98:101], v[168:171], v[208:211], v[98:101]
	v_mfma_f32_16x16x32_bf16 v[78:81], v[160:163], v[216:219], v[78:81]
	v_mfma_f32_16x16x32_bf16 v[74:77], v[168:171], v[216:219], v[74:77]
	v_mfma_f32_16x16x32_bf16 v[126:129], v[164:167], v[196:199], v[126:129]
	v_mfma_f32_16x16x32_bf16 v[122:125], v[172:175], v[196:199], v[122:125]
	v_mfma_f32_16x16x32_bf16 v[118:121], v[164:167], v[204:207], v[118:121]
	v_mfma_f32_16x16x32_bf16 v[114:117], v[172:175], v[204:207], v[114:117]
	v_mfma_f32_16x16x32_bf16 v[106:109], v[164:167], v[212:215], v[106:109]
	v_mfma_f32_16x16x32_bf16 v[98:101], v[172:175], v[212:215], v[98:101]
	v_mfma_f32_16x16x32_bf16 v[78:81], v[164:167], v[220:223], v[78:81]
	v_mfma_f32_16x16x32_bf16 v[74:77], v[172:175], v[220:223], v[74:77]
	s_setprio 0
	s_setprio 3
	v_mfma_f32_16x16x32_bf16 v[110:113], v[176:179], v[192:195], v[110:113]
	v_mfma_f32_16x16x32_bf16 v[102:105], v[184:187], v[192:195], v[102:105]
	v_mfma_f32_16x16x32_bf16 v[94:97], v[176:179], v[200:203], v[94:97]
	v_mfma_f32_16x16x32_bf16 v[90:93], v[184:187], v[200:203], v[90:93]
	v_mfma_f32_16x16x32_bf16 v[86:89], v[176:179], v[208:211], v[86:89]
	v_mfma_f32_16x16x32_bf16 v[82:85], v[184:187], v[208:211], v[82:85]
	v_mfma_f32_16x16x32_bf16 v[70:73], v[176:179], v[216:219], v[70:73]
	v_mfma_f32_16x16x32_bf16 v[66:69], v[184:187], v[216:219], v[66:69]
	v_mfma_f32_16x16x32_bf16 v[110:113], v[180:183], v[196:199], v[110:113]
	v_mfma_f32_16x16x32_bf16 v[102:105], v[188:191], v[196:199], v[102:105]
	v_mfma_f32_16x16x32_bf16 v[94:97], v[180:183], v[204:207], v[94:97]
	v_mfma_f32_16x16x32_bf16 v[90:93], v[188:191], v[204:207], v[90:93]
	v_mfma_f32_16x16x32_bf16 v[86:89], v[180:183], v[212:215], v[86:89]
	v_mfma_f32_16x16x32_bf16 v[82:85], v[188:191], v[212:215], v[82:85]
	v_mfma_f32_16x16x32_bf16 v[70:73], v[180:183], v[220:223], v[70:73]
	v_mfma_f32_16x16x32_bf16 v[66:69], v[188:191], v[220:223], v[66:69]
	s_setprio 0
	s_barrier
	s_add_i32 s38, s60, s51
	s_mov_b64 s[98:99], s[42:43]
	s_mov_b32 m0, s38
	ds_read_b128 v[192:195], v159 offset:16384
	ds_read_b128 v[196:199], v159 offset:17408
	ds_read_b128 v[200:203], v159 offset:18432
	ds_read_b128 v[204:207], v159 offset:19456
	ds_read_b128 v[208:211], v159 offset:20480
	ds_read_b128 v[212:215], v159 offset:21504
	ds_read_b128 v[216:219], v159 offset:22528
	ds_read_b128 v[220:223], v159 offset:23552
	global_load_lds_dwordx4 v134, s[42:43]
	s_add_i32 m0, s38, 0x2000
	s_add_u32 s38, s42, 0xe0000
	s_addc_u32 s39, s43, 0
	s_add_i32 s70, s61, s51
	global_load_lds_dwordx4 v138, s[42:43]
	s_mov_b32 m0, s70
	s_nop 0
	global_load_lds_dwordx4 v134, s[38:39]
	s_add_i32 m0, s70, 0x2000
	s_nop 0
	global_load_lds_dwordx4 v138, s[38:39]
	s_mov_b32 m0, s37
	s_nop 0
	global_load_lds_dwordx4 v132, s[44:45]
	s_mov_b32 m0, s52
	s_nop 0
	global_load_lds_dwordx4 v136, s[44:45]
	s_waitcnt vmcnt(8)
	s_waitcnt lgkmcnt(0)
	s_barrier
	s_setprio 3
	s_waitcnt lgkmcnt(0)
	v_mfma_f32_16x16x32_bf16 v[62:65], v[160:163], v[192:195], v[62:65]
	v_mfma_f32_16x16x32_bf16 v[58:61], v[168:171], v[192:195], v[58:61]
	v_mfma_f32_16x16x32_bf16 v[50:53], v[160:163], v[200:203], v[50:53]
	v_mfma_f32_16x16x32_bf16 v[42:45], v[168:171], v[200:203], v[42:45]
	v_mfma_f32_16x16x32_bf16 v[34:37], v[160:163], v[208:211], v[34:37]
	v_mfma_f32_16x16x32_bf16 v[26:29], v[168:171], v[208:211], v[26:29]
	v_mfma_f32_16x16x32_bf16 v[18:21], v[160:163], v[216:219], v[18:21]
	v_mfma_f32_16x16x32_bf16 v[10:13], v[168:171], v[216:219], v[10:13]
	v_mfma_f32_16x16x32_bf16 v[62:65], v[164:167], v[196:199], v[62:65]
	v_mfma_f32_16x16x32_bf16 v[58:61], v[172:175], v[196:199], v[58:61]
	v_mfma_f32_16x16x32_bf16 v[50:53], v[164:167], v[204:207], v[50:53]
	v_mfma_f32_16x16x32_bf16 v[42:45], v[172:175], v[204:207], v[42:45]
	v_mfma_f32_16x16x32_bf16 v[34:37], v[164:167], v[212:215], v[34:37]
	v_mfma_f32_16x16x32_bf16 v[26:29], v[172:175], v[212:215], v[26:29]
	v_mfma_f32_16x16x32_bf16 v[18:21], v[164:167], v[220:223], v[18:21]
	v_mfma_f32_16x16x32_bf16 v[10:13], v[172:175], v[220:223], v[10:13]
	s_setprio 0
	s_setprio 3
	v_mfma_f32_16x16x32_bf16 v[54:57], v[176:179], v[192:195], v[54:57]
	v_mfma_f32_16x16x32_bf16 v[46:49], v[184:187], v[192:195], v[46:49]
	v_mfma_f32_16x16x32_bf16 v[38:41], v[176:179], v[200:203], v[38:41]
	v_mfma_f32_16x16x32_bf16 v[30:33], v[184:187], v[200:203], v[30:33]
	v_mfma_f32_16x16x32_bf16 v[22:25], v[176:179], v[208:211], v[22:25]
	v_mfma_f32_16x16x32_bf16 v[14:17], v[184:187], v[208:211], v[14:17]
	v_mfma_f32_16x16x32_bf16 v[6:9], v[176:179], v[216:219], v[6:9]
	v_mfma_f32_16x16x32_bf16 v[2:5], v[184:187], v[216:219], v[2:5]
	v_mfma_f32_16x16x32_bf16 v[54:57], v[180:183], v[196:199], v[54:57]
	v_mfma_f32_16x16x32_bf16 v[46:49], v[188:191], v[196:199], v[46:49]
	v_mfma_f32_16x16x32_bf16 v[38:41], v[180:183], v[204:207], v[38:41]
	v_mfma_f32_16x16x32_bf16 v[30:33], v[188:191], v[204:207], v[30:33]
	v_mfma_f32_16x16x32_bf16 v[22:25], v[180:183], v[212:215], v[22:25]
	v_mfma_f32_16x16x32_bf16 v[14:17], v[188:191], v[212:215], v[14:17]
	v_mfma_f32_16x16x32_bf16 v[6:9], v[180:183], v[220:223], v[6:9]
	v_mfma_f32_16x16x32_bf16 v[2:5], v[188:191], v[220:223], v[2:5]
	s_setprio 0
	s_barrier
; #define PG8_STAGE_A(b, h, ptr, NX) do { if constexpr (Sched::GATHER) { unsigned gs_[2]; gs_[0] = ((NX) && last_) ? gN[h][0] : gA[h][0]; gs_[1] = ((NX) && last_) ? gN[h][1] : gA[h][1]; PG8_STAGE(PG8_SA(b, h), ptr, gs_); } \
;         else PG8_STAGE(PG8_SA(b, h), (ptr) + ((h) ? hstep : (size_t)0), voffA); } while (0)
; #define PG8_STAGE(bufoff, gbase, voff) do { _Pragma("unroll") for (int _i = 0; _i < 2; ++_i) \
;         __builtin_amdgcn_global_load_lds((const unsigned*)((const char*)(gbase) + (voff)[_i]), (PG8_LAS unsigned*)(lds + (bufoff) + ldsw + _i * 8192), 16, 0, 0); } while (0)
; #define PG8_LDA(dst, b, h) do { _Pragma("unroll") for (int m = 0; m < 4; ++m) _Pragma("unroll") for (int k = 0; k < 2; ++k) dst[m][k] = *(const PG8_LAS bf16x8*)(lds + PG8_SA(b, h) + aoff + m * 2048 + k * 1024); } while (0)
; #define PG8_LDB(dst, b, h) do { _Pragma("unroll") for (int n = 0; n < 2; ++n) _Pragma("unroll") for (int k = 0; k < 2; ++k) dst[n][k] = *(const PG8_LAS bf16x8*)(lds + PG8_SB(b, h) + boff + n * 2048 + k * 1024); } while (0)
; #define PG8_MMA(ai, bj, At, Bt) do { __builtin_amdgcn_s_setprio(1); _Pragma("unroll") for (int m = 0; m < 4; ++m) _Pragma("unroll") for (int n = 0; n < 2; ++n) _Pragma("unroll") for (int k = 0; k < 2; ++k) \
;         acc[ai][bj][m][n] = __builtin_amdgcn_mfma_f32_16x16x32_bf16(Bt[n][k], At[m][k], acc[ai][bj][m][n], 0, 0, 0); __builtin_amdgcn_s_setprio(0); } while (0)
; #define PG8_WAIT_V(n) asm volatile("s_waitcnt vmcnt(" #n ")" ::: "memory")
; #define PG8_WAIT_L(n) asm volatile("s_waitcnt lgkmcnt(" #n ")" ::: "memory")
; #define PG8_BAR __builtin_amdgcn_s_barrier()
; #define PG8_SCHED __builtin_amdgcn_sched_barrier(0)
; template <class Epi, class Sched, bool ALIGN_EPI = false, bool SP2 = false>
; __device__ __forceinline__ void gemm_phase(PG8_LAS unsigned char* lds, const Gemm g, const Sched& S, const Epi& E, const bool skip_epi = false) {
;     ...
;             PG8_LDB(B0, 1, 0); PG8_LDB(B1, 1, 1); PG8_SCHED; PG8_LDA(At, 1, 0); PG8_STAGE_A(0, 1, a2, true);
;             PG8_WAIT_V(8); PG8_WAIT_L(0); PG8_BAR; PG8_MMA(0, 0, At, B0); PG8_MMA(0, 1, At, B1); PG8_BAR; PG8_SCHED;
;             PG8_LDA(At, 1, 1); PG8_STAGE(PG8_SB(1, 0), b3, voffB); PG8_STAGE(PG8_SB(1, 1), b3 + hstep, voffB); PG8_STAGE_A(1, 0, a3, true);
;             PG8_WAIT_V(8); PG8_WAIT_L(0); PG8_BAR; PG8_MMA(1, 0, At, B0); PG8_MMA(1, 1, At, B1); PG8_BAR; PG8_SCHED;
	s_add_i32 s70, 0, 0x18000
	v_add_u32_e32 v130, s70, v147
	s_add_i32 s71, 0, 0x1c000
	ds_read_b128 v[160:163], v130
	ds_read_b128 v[164:167], v130 offset:1024
	ds_read_b128 v[168:171], v130 offset:2048
	ds_read_b128 v[172:175], v130 offset:3072
	v_add_u32_e32 v130, s71, v147
	ds_read_b128 v[176:179], v130
	ds_read_b128 v[180:183], v130 offset:1024
	ds_read_b128 v[184:187], v130 offset:2048
	ds_read_b128 v[188:191], v130 offset:3072
	s_add_u32 s38, s44, 0xe0000
	s_addc_u32 s39, s45, 0
	s_mov_b32 m0, s53
	ds_read_b128 v[192:195], v159 offset:32768
	ds_read_b128 v[196:199], v159 offset:33792
	ds_read_b128 v[200:203], v159 offset:34816
	ds_read_b128 v[204:207], v159 offset:35840
	ds_read_b128 v[208:211], v159 offset:36864
	ds_read_b128 v[212:215], v159 offset:37888
	ds_read_b128 v[216:219], v159 offset:38912
	ds_read_b128 v[220:223], v159 offset:39936
	global_load_lds_dwordx4 v132, s[38:39]
	s_mov_b32 m0, s54
	s_nop 0
	global_load_lds_dwordx4 v136, s[38:39]
	s_waitcnt vmcnt(8)
	s_waitcnt lgkmcnt(0)
	s_barrier
	s_setprio 3
	s_waitcnt lgkmcnt(0)
	v_mfma_f32_16x16x32_bf16 v[126:129], v[160:163], v[192:195], v[126:129]
	v_mfma_f32_16x16x32_bf16 v[122:125], v[168:171], v[192:195], v[122:125]
	v_mfma_f32_16x16x32_bf16 v[118:121], v[160:163], v[200:203], v[118:121]
	v_mfma_f32_16x16x32_bf16 v[114:117], v[168:171], v[200:203], v[114:117]
	v_mfma_f32_16x16x32_bf16 v[106:109], v[160:163], v[208:211], v[106:109]
	v_mfma_f32_16x16x32_bf16 v[98:101], v[168:171], v[208:211], v[98:101]
	v_mfma_f32_16x16x32_bf16 v[78:81], v[160:163], v[216:219], v[78:81]
	v_mfma_f32_16x16x32_bf16 v[74:77], v[168:171], v[216:219], v[74:77]
	v_mfma_f32_16x16x32_bf16 v[126:129], v[164:167], v[196:199], v[126:129]
	v_mfma_f32_16x16x32_bf16 v[122:125], v[172:175], v[196:199], v[122:125]
	v_mfma_f32_16x16x32_bf16 v[118:121], v[164:167], v[204:207], v[118:121]
	v_mfma_f32_16x16x32_bf16 v[114:117], v[172:175], v[204:207], v[114:117]
	v_mfma_f32_16x16x32_bf16 v[106:109], v[164:167], v[212:215], v[106:109]
	v_mfma_f32_16x16x32_bf16 v[98:101], v[172:175], v[212:215], v[98:101]
	v_mfma_f32_16x16x32_bf16 v[78:81], v[164:167], v[220:223], v[78:81]
	v_mfma_f32_16x16x32_bf16 v[74:77], v[172:175], v[220:223], v[74:77]
	s_setprio 0
	s_setprio 3
	v_mfma_f32_16x16x32_bf16 v[110:113], v[176:179], v[192:195], v[110:113]
	v_mfma_f32_16x16x32_bf16 v[102:105], v[184:187], v[192:195], v[102:105]
	v_mfma_f32_16x16x32_bf16 v[94:97], v[176:179], v[200:203], v[94:97]
	v_mfma_f32_16x16x32_bf16 v[90:93], v[184:187], v[200:203], v[90:93]
	v_mfma_f32_16x16x32_bf16 v[86:89], v[176:179], v[208:211], v[86:89]
	v_mfma_f32_16x16x32_bf16 v[82:85], v[184:187], v[208:211], v[82:85]
	v_mfma_f32_16x16x32_bf16 v[70:73], v[176:179], v[216:219], v[70:73]
	v_mfma_f32_16x16x32_bf16 v[66:69], v[184:187], v[216:219], v[66:69]
	v_mfma_f32_16x16x32_bf16 v[110:113], v[180:183], v[196:199], v[110:113]
	v_mfma_f32_16x16x32_bf16 v[102:105], v[188:191], v[196:199], v[102:105]
	v_mfma_f32_16x16x32_bf16 v[94:97], v[180:183], v[204:207], v[94:97]
	v_mfma_f32_16x16x32_bf16 v[90:93], v[188:191], v[204:207], v[90:93]
	v_mfma_f32_16x16x32_bf16 v[86:89], v[180:183], v[212:215], v[86:89]
	v_mfma_f32_16x16x32_bf16 v[82:85], v[188:191], v[212:215], v[82:85]
	v_mfma_f32_16x16x32_bf16 v[70:73], v[180:183], v[220:223], v[70:73]
	v_mfma_f32_16x16x32_bf16 v[66:69], v[188:191], v[220:223], v[66:69]
	s_setprio 0
	s_barrier
	s_add_i32 s38, s70, s51
	s_add_i32 m0, s38, 0xffffff80
	ds_read_b128 v[192:195], v159 offset:49152
	ds_read_b128 v[196:199], v159 offset:50176
	ds_read_b128 v[200:203], v159 offset:51200
	ds_read_b128 v[204:207], v159 offset:52224
	ds_read_b128 v[208:211], v159 offset:53248
	ds_read_b128 v[212:215], v159 offset:54272
	ds_read_b128 v[216:219], v159 offset:55296
	ds_read_b128 v[220:223], v159 offset:56320
	global_load_lds_dwordx4 v134, s[42:43] offset:128
	s_add_i32 m0, s38, 0x1f80
	s_add_u32 s38, s42, 0xe0080
	s_addc_u32 s39, s43, 0
	s_add_i32 s42, s71, s51
	global_load_lds_dwordx4 v138, s[98:99] offset:128
	s_mov_b32 m0, s42
	s_nop 0
	global_load_lds_dwordx4 v134, s[38:39]
	s_add_i32 m0, s42, 0x2000
	s_nop 0
	global_load_lds_dwordx4 v138, s[38:39]
	s_add_i32 m0, s57, 0xffffff80
	s_nop 0
	global_load_lds_dwordx4 v132, s[44:45] offset:128
	s_add_i32 m0, s58, 0xffffff80
	s_nop 0
	global_load_lds_dwordx4 v136, s[44:45] offset:128
	s_waitcnt vmcnt(8)
	s_waitcnt lgkmcnt(0)
	s_barrier
	s_setprio 3
	s_waitcnt lgkmcnt(0)
	v_mfma_f32_16x16x32_bf16 v[62:65], v[160:163], v[192:195], v[62:65]
	v_mfma_f32_16x16x32_bf16 v[58:61], v[168:171], v[192:195], v[58:61]
	v_mfma_f32_16x16x32_bf16 v[50:53], v[160:163], v[200:203], v[50:53]
	v_mfma_f32_16x16x32_bf16 v[42:45], v[168:171], v[200:203], v[42:45]
	v_mfma_f32_16x16x32_bf16 v[34:37], v[160:163], v[208:211], v[34:37]
	v_mfma_f32_16x16x32_bf16 v[26:29], v[168:171], v[208:211], v[26:29]
	v_mfma_f32_16x16x32_bf16 v[18:21], v[160:163], v[216:219], v[18:21]
	v_mfma_f32_16x16x32_bf16 v[10:13], v[168:171], v[216:219], v[10:13]
	v_mfma_f32_16x16x32_bf16 v[62:65], v[164:167], v[196:199], v[62:65]
	v_mfma_f32_16x16x32_bf16 v[58:61], v[172:175], v[196:199], v[58:61]
	v_mfma_f32_16x16x32_bf16 v[50:53], v[164:167], v[204:207], v[50:53]
	v_mfma_f32_16x16x32_bf16 v[42:45], v[172:175], v[204:207], v[42:45]
	v_mfma_f32_16x16x32_bf16 v[34:37], v[164:167], v[212:215], v[34:37]
	v_mfma_f32_16x16x32_bf16 v[26:29], v[172:175], v[212:215], v[26:29]
	v_mfma_f32_16x16x32_bf16 v[18:21], v[164:167], v[220:223], v[18:21]
	v_mfma_f32_16x16x32_bf16 v[10:13], v[172:175], v[220:223], v[10:13]
	s_setprio 0
	s_setprio 3
	v_mfma_f32_16x16x32_bf16 v[54:57], v[176:179], v[192:195], v[54:57]
	v_mfma_f32_16x16x32_bf16 v[46:49], v[184:187], v[192:195], v[46:49]
	v_mfma_f32_16x16x32_bf16 v[38:41], v[176:179], v[200:203], v[38:41]
	v_mfma_f32_16x16x32_bf16 v[30:33], v[184:187], v[200:203], v[30:33]
	v_mfma_f32_16x16x32_bf16 v[22:25], v[176:179], v[208:211], v[22:25]
	v_mfma_f32_16x16x32_bf16 v[14:17], v[184:187], v[208:211], v[14:17]
	v_mfma_f32_16x16x32_bf16 v[6:9], v[176:179], v[216:219], v[6:9]
	v_mfma_f32_16x16x32_bf16 v[2:5], v[184:187], v[216:219], v[2:5]
	v_mfma_f32_16x16x32_bf16 v[54:57], v[180:183], v[196:199], v[54:57]
	v_mfma_f32_16x16x32_bf16 v[46:49], v[188:191], v[196:199], v[46:49]
	v_mfma_f32_16x16x32_bf16 v[38:41], v[180:183], v[204:207], v[38:41]
	v_mfma_f32_16x16x32_bf16 v[30:33], v[188:191], v[204:207], v[30:33]
	v_mfma_f32_16x16x32_bf16 v[22:25], v[180:183], v[212:215], v[22:25]
	v_mfma_f32_16x16x32_bf16 v[14:17], v[188:191], v[212:215], v[14:17]
	v_mfma_f32_16x16x32_bf16 v[6:9], v[180:183], v[220:223], v[6:9]
	v_mfma_f32_16x16x32_bf16 v[2:5], v[188:191], v[220:223], v[2:5]
	s_setprio 0
	s_barrier
	s_add_i32 s69, s69, 2
	s_add_u32 s67, s67, 0x100
	s_addc_u32 s68, s68, 0
	s_cmp_gt_u32 s69, 53
	s_mov_b64 s[38:39], s[40:41]
	s_cbranch_scc0 .LBB0_1823
	s_and_b64 vcc, exec, s[20:21]
	s_cbranch_vccz .LBB0_1826
	s_barrier

; #define PG8_STAGE_A(b, h, ptr, NX) do { if constexpr (Sched::GATHER) { unsigned gs_[2]; gs_[0] = ((NX) && last_) ? gN[h][0] : gA[h][0]; gs_[1] = ((NX) && last_) ? gN[h][1] : gA[h][1]; PG8_STAGE(PG8_SA(b, h), ptr, gs_); } \
;         else PG8_STAGE(PG8_SA(b, h), (ptr) + ((h) ? hstep : (size_t)0), voffA); } while (0)
; #define PG8_STAGE(bufoff, gbase, voff) do { _Pragma("unroll") for (int _i = 0; _i < 2; ++_i) \
;         __builtin_amdgcn_global_load_lds((const unsigned*)((const char*)(gbase) + (voff)[_i]), (PG8_LAS unsigned*)(lds + (bufoff) + ldsw + _i * 8192), 16, 0, 0); } while (0)
; #define PG8_LDA(dst, b, h) do { _Pragma("unroll") for (int m = 0; m < 4; ++m) _Pragma("unroll") for (int k = 0; k < 2; ++k) dst[m][k] = *(const PG8_LAS bf16x8*)(lds + PG8_SA(b, h) + aoff + m * 2048 + k * 1024); } while (0)
; #define PG8_LDB(dst, b, h) do { _Pragma("unroll") for (int n = 0; n < 2; ++n) _Pragma("unroll") for (int k = 0; k < 2; ++k) dst[n][k] = *(const PG8_LAS bf16x8*)(lds + PG8_SB(b, h) + boff + n * 2048 + k * 1024); } while (0)
; #define PG8_WAIT_V(n) asm volatile("s_waitcnt vmcnt(" #n ")" ::: "memory")
; #define PG8_WAIT_L(n) asm volatile("s_waitcnt lgkmcnt(" #n ")" ::: "memory")
; template <class Epi, class Sched, bool ALIGN_EPI = false, bool SP2 = false>
; __device__ __forceinline__ void gemm_phase(PG8_LAS unsigned char* lds, const Gemm g, const Sched& S, const Epi& E, const bool skip_epi = false) {
;     ...
;         for (int t = 0; t < nt; t += 2) {
;             const bool last = (t == nt - 2); last_ = last && has_next;
;             const char* a1 = cA + (size_t)(t + 1) * kstep;
;             const char* a2 = last ? nA : cA + (size_t)(t + 2) * kstep; const char* b2 = last ? nB : cB + (size_t)(t + 2) * kstep;
;             const char* a3 = a2 + kstep; const char* b3 = b2 + kstep;
;             if (last && has_next) S.a_ready(nxt);
;             if constexpr (SP2) {
;             PG8_LDB(B0, 0, 0); PG8_LDB(B1, 0, 1); PG8_SCHED; PG8_LDA(At, 0, 0); PG8_STAGE_A(1, 1, a1, false);
;             PG8_WAIT_V(8); PG8_WAIT_L(0); PG8_BAR; PG8_MMA(0, 0, At, B0); PG8_MMA(0, 1, At, B1); PG8_BAR; PG8_SCHED;
;             PG8_LDA(At, 0, 1); PG8_STAGE(PG8_SB(0, 0), b2, voffB); PG8_STAGE(PG8_SB(0, 1), b2 + hstep, voffB); PG8_STAGE_A(0, 0, a2, true);
;             PG8_WAIT_V(8); PG8_WAIT_L(0); PG8_BAR; PG8_MMA(1, 0, At, B0); PG8_MMA(1, 1, At, B1); PG8_BAR; PG8_SCHED;
.LBB0_1843:
	s_add_u32 s54, s30, 0x100
	s_addc_u32 s55, s31, 0
	s_mov_b32 s56, -2
	ds_read_b128 v[142:145], v150
	ds_read_b128 v[154:157], v150 offset:1024
	ds_read_b128 v[158:161], v150 offset:2048
	ds_read_b128 v[162:165], v150 offset:3072
	ds_read_b128 v[166:169], v151
	ds_read_b128 v[170:173], v151 offset:1024
	ds_read_b128 v[174:177], v151 offset:2048
	ds_read_b128 v[178:181], v151 offset:3072
	s_add_u32 s30, s28, 0x100
	s_addc_u32 s31, s29, 0
	s_cmp_eq_u32 s56, 10
	s_cselect_b32 s37, s7, s31
	s_cselect_b32 s36, s6, s30
	s_cselect_b32 s35, s25, s55
	s_cselect_b32 s34, s24, s54
	v_lshl_add_u64 v[214:215], s[28:29], 0, v[136:137]
	s_add_i32 m0, s38, 0xc000
	ds_read_b128 v[182:185], v152
	ds_read_b128 v[186:189], v152 offset:1024
	ds_read_b128 v[190:193], v152 offset:2048
	ds_read_b128 v[194:197], v152 offset:3072
	ds_read_b128 v[198:201], v152 offset:4096
	ds_read_b128 v[202:205], v152 offset:5120
	ds_read_b128 v[206:209], v152 offset:6144
	ds_read_b128 v[210:213], v152 offset:7168
	global_load_lds_dwordx4 v[214:215], off
	v_lshl_add_u64 v[214:215], s[28:29], 0, v[138:139]
	s_add_i32 m0, s38, 0xe000
	s_nop 0
	global_load_lds_dwordx4 v[214:215], off
	s_waitcnt vmcnt(8)
	s_waitcnt lgkmcnt(0)
	s_barrier
	s_setprio 3
	s_waitcnt lgkmcnt(0)
	v_mfma_f32_16x16x32_bf16 v[126:129], v[142:145], v[182:185], 0
	v_mfma_f32_16x16x32_bf16 v[122:125], v[158:161], v[182:185], 0
	v_mfma_f32_16x16x32_bf16 v[110:113], v[142:145], v[190:193], 0
	v_mfma_f32_16x16x32_bf16 v[106:109], v[158:161], v[190:193], 0
	v_mfma_f32_16x16x32_bf16 v[94:97], v[142:145], v[198:201], 0
	v_mfma_f32_16x16x32_bf16 v[90:93], v[158:161], v[198:201], 0
	v_mfma_f32_16x16x32_bf16 v[78:81], v[142:145], v[206:209], 0
	v_mfma_f32_16x16x32_bf16 v[74:77], v[158:161], v[206:209], 0
	v_mfma_f32_16x16x32_bf16 v[126:129], v[154:157], v[186:189], v[126:129]
	v_mfma_f32_16x16x32_bf16 v[122:125], v[162:165], v[186:189], v[122:125]
	v_mfma_f32_16x16x32_bf16 v[110:113], v[154:157], v[194:197], v[110:113]
	v_mfma_f32_16x16x32_bf16 v[106:109], v[162:165], v[194:197], v[106:109]
	v_mfma_f32_16x16x32_bf16 v[94:97], v[154:157], v[202:205], v[94:97]
	v_mfma_f32_16x16x32_bf16 v[90:93], v[162:165], v[202:205], v[90:93]
	v_mfma_f32_16x16x32_bf16 v[78:81], v[154:157], v[210:213], v[78:81]
	v_mfma_f32_16x16x32_bf16 v[74:77], v[162:165], v[210:213], v[74:77]
	s_setprio 0
	s_setprio 3
	v_mfma_f32_16x16x32_bf16 v[118:121], v[166:169], v[182:185], 0
	v_mfma_f32_16x16x32_bf16 v[114:117], v[174:177], v[182:185], 0
	v_mfma_f32_16x16x32_bf16 v[102:105], v[166:169], v[190:193], 0
	v_mfma_f32_16x16x32_bf16 v[98:101], v[174:177], v[190:193], 0
	v_mfma_f32_16x16x32_bf16 v[86:89], v[166:169], v[198:201], 0
	v_mfma_f32_16x16x32_bf16 v[82:85], v[174:177], v[198:201], 0
	v_mfma_f32_16x16x32_bf16 v[70:73], v[166:169], v[206:209], 0
	v_mfma_f32_16x16x32_bf16 v[66:69], v[174:177], v[206:209], 0
	v_mfma_f32_16x16x32_bf16 v[118:121], v[170:173], v[186:189], v[118:121]
	v_mfma_f32_16x16x32_bf16 v[114:117], v[178:181], v[186:189], v[114:117]
	v_mfma_f32_16x16x32_bf16 v[102:105], v[170:173], v[194:197], v[102:105]
	v_mfma_f32_16x16x32_bf16 v[98:101], v[178:181], v[194:197], v[98:101]
	v_mfma_f32_16x16x32_bf16 v[86:89], v[170:173], v[202:205], v[86:89]
	v_mfma_f32_16x16x32_bf16 v[82:85], v[178:181], v[202:205], v[82:85]
	v_mfma_f32_16x16x32_bf16 v[70:73], v[170:173], v[210:213], v[70:73]
	v_mfma_f32_16x16x32_bf16 v[66:69], v[178:181], v[210:213], v[66:69]
	s_setprio 0
	s_barrier
	s_add_i32 s28, s50, s3
	s_mov_b64 s[98:99], s[34:35]
	s_mov_b32 m0, s28
	ds_read_b128 v[182:185], v152 offset:16384
	ds_read_b128 v[186:189], v152 offset:17408
	ds_read_b128 v[190:193], v152 offset:18432
	ds_read_b128 v[194:197], v152 offset:19456
	ds_read_b128 v[198:201], v152 offset:20480
	ds_read_b128 v[202:205], v152 offset:21504
	ds_read_b128 v[206:209], v152 offset:22528
	ds_read_b128 v[210:213], v152 offset:23552
	global_load_lds_dwordx4 v132, s[34:35]
	s_add_i32 m0, s28, 0x2000
	s_add_u32 s28, s34, 0xe0000
	s_addc_u32 s29, s35, 0
	s_add_i32 s57, s51, s3
	global_load_lds_dwordx4 v134, s[34:35]
	s_mov_b32 m0, s57
	s_nop 0
	global_load_lds_dwordx4 v132, s[28:29]
	s_add_i32 m0, s57, 0x2000
	s_nop 0
	global_load_lds_dwordx4 v134, s[28:29]
	s_mov_b32 m0, s38
	s_nop 0
	global_load_lds_dwordx4 v132, s[36:37]
	s_mov_b32 m0, s39
	s_nop 0
	global_load_lds_dwordx4 v134, s[36:37]
	s_waitcnt vmcnt(8)
	s_waitcnt lgkmcnt(0)
	s_barrier
	s_setprio 3
	s_waitcnt lgkmcnt(0)
	v_mfma_f32_16x16x32_bf16 v[62:65], v[142:145], v[182:185], 0
	v_mfma_f32_16x16x32_bf16 v[58:61], v[158:161], v[182:185], 0
	v_mfma_f32_16x16x32_bf16 v[46:49], v[142:145], v[190:193], 0
	v_mfma_f32_16x16x32_bf16 v[42:45], v[158:161], v[190:193], 0
	v_mfma_f32_16x16x32_bf16 v[30:33], v[142:145], v[198:201], 0
	v_mfma_f32_16x16x32_bf16 v[26:29], v[158:161], v[198:201], 0
	v_mfma_f32_16x16x32_bf16 v[14:17], v[142:145], v[206:209], 0
	v_mfma_f32_16x16x32_bf16 v[10:13], v[158:161], v[206:209], 0
	v_mfma_f32_16x16x32_bf16 v[62:65], v[154:157], v[186:189], v[62:65]
	v_mfma_f32_16x16x32_bf16 v[58:61], v[162:165], v[186:189], v[58:61]
	v_mfma_f32_16x16x32_bf16 v[46:49], v[154:157], v[194:197], v[46:49]
	v_mfma_f32_16x16x32_bf16 v[42:45], v[162:165], v[194:197], v[42:45]
	v_mfma_f32_16x16x32_bf16 v[30:33], v[154:157], v[202:205], v[30:33]
	v_mfma_f32_16x16x32_bf16 v[26:29], v[162:165], v[202:205], v[26:29]
	v_mfma_f32_16x16x32_bf16 v[14:17], v[154:157], v[210:213], v[14:17]
	v_mfma_f32_16x16x32_bf16 v[10:13], v[162:165], v[210:213], v[10:13]
	s_setprio 0
	s_setprio 3
	v_mfma_f32_16x16x32_bf16 v[54:57], v[166:169], v[182:185], 0
	v_mfma_f32_16x16x32_bf16 v[50:53], v[174:177], v[182:185], 0
	v_mfma_f32_16x16x32_bf16 v[38:41], v[166:169], v[190:193], 0
	v_mfma_f32_16x16x32_bf16 v[34:37], v[174:177], v[190:193], 0
	v_mfma_f32_16x16x32_bf16 v[22:25], v[166:169], v[198:201], 0
	v_mfma_f32_16x16x32_bf16 v[18:21], v[174:177], v[198:201], 0
	v_mfma_f32_16x16x32_bf16 v[6:9], v[166:169], v[206:209], 0
	v_mfma_f32_16x16x32_bf16 v[2:5], v[174:177], v[206:209], 0
	v_mfma_f32_16x16x32_bf16 v[54:57], v[170:173], v[186:189], v[54:57]
	v_mfma_f32_16x16x32_bf16 v[50:53], v[178:181], v[186:189], v[50:53]
	v_mfma_f32_16x16x32_bf16 v[38:41], v[170:173], v[194:197], v[38:41]
	v_mfma_f32_16x16x32_bf16 v[34:37], v[178:181], v[194:197], v[34:37]
	v_mfma_f32_16x16x32_bf16 v[22:25], v[170:173], v[202:205], v[22:25]
	v_mfma_f32_16x16x32_bf16 v[18:21], v[178:181], v[202:205], v[18:21]
	v_mfma_f32_16x16x32_bf16 v[6:9], v[170:173], v[210:213], v[6:9]
	v_mfma_f32_16x16x32_bf16 v[2:5], v[178:181], v[210:213], v[2:5]
	s_setprio 0
	s_barrier
; #define PG8_STAGE_A(b, h, ptr, NX) do { if constexpr (Sched::GATHER) { unsigned gs_[2]; gs_[0] = ((NX) && last_) ? gN[h][0] : gA[h][0]; gs_[1] = ((NX) && last_) ? gN[h][1] : gA[h][1]; PG8_STAGE(PG8_SA(b, h), ptr, gs_); } \
;         else PG8_STAGE(PG8_SA(b, h), (ptr) + ((h) ? hstep : (size_t)0), voffA); } while (0)
; #define PG8_STAGE(bufoff, gbase, voff) do { _Pragma("unroll") for (int _i = 0; _i < 2; ++_i) \
;         __builtin_amdgcn_global_load_lds((const unsigned*)((const char*)(gbase) + (voff)[_i]), (PG8_LAS unsigned*)(lds + (bufoff) + ldsw + _i * 8192), 16, 0, 0); } while (0)
; #define PG8_LDA(dst, b, h) do { _Pragma("unroll") for (int m = 0; m < 4; ++m) _Pragma("unroll") for (int k = 0; k < 2; ++k) dst[m][k] = *(const PG8_LAS bf16x8*)(lds + PG8_SA(b, h) + aoff + m * 2048 + k * 1024); } while (0)
; #define PG8_LDB(dst, b, h) do { _Pragma("unroll") for (int n = 0; n < 2; ++n) _Pragma("unroll") for (int k = 0; k < 2; ++k) dst[n][k] = *(const PG8_LAS bf16x8*)(lds + PG8_SB(b, h) + boff + n * 2048 + k * 1024); } while (0)
; #define PG8_MMA(ai, bj, At, Bt) do { __builtin_amdgcn_s_setprio(1); _Pragma("unroll") for (int m = 0; m < 4; ++m) _Pragma("unroll") for (int n = 0; n < 2; ++n) _Pragma("unroll") for (int k = 0; k < 2; ++k) \
;         acc[ai][bj][m][n] = __builtin_amdgcn_mfma_f32_16x16x32_bf16(Bt[n][k], At[m][k], acc[ai][bj][m][n], 0, 0, 0); __builtin_amdgcn_s_setprio(0); } while (0)
; #define PG8_WAIT_V(n) asm volatile("s_waitcnt vmcnt(" #n ")" ::: "memory")
; #define PG8_WAIT_L(n) asm volatile("s_waitcnt lgkmcnt(" #n ")" ::: "memory")
; #define PG8_BAR __builtin_amdgcn_s_barrier()
; #define PG8_SCHED __builtin_amdgcn_sched_barrier(0)
; template <class Epi, class Sched, bool ALIGN_EPI = false, bool SP2 = false>
; __device__ __forceinline__ void gemm_phase(PG8_LAS unsigned char* lds, const Gemm g, const Sched& S, const Epi& E, const bool skip_epi = false) {
;     ...
;             PG8_LDB(B0, 1, 0); PG8_LDB(B1, 1, 1); PG8_SCHED; PG8_LDA(At, 1, 0); PG8_STAGE_A(0, 1, a2, true);
;             PG8_WAIT_V(8); PG8_WAIT_L(0); PG8_BAR; PG8_MMA(0, 0, At, B0); PG8_MMA(0, 1, At, B1); PG8_BAR; PG8_SCHED;
;             PG8_LDA(At, 1, 1); PG8_STAGE(PG8_SB(1, 0), b3, voffB); PG8_STAGE(PG8_SB(1, 1), b3 + hstep, voffB); PG8_STAGE_A(1, 0, a3, true);
;             PG8_WAIT_V(8); PG8_WAIT_L(0); PG8_BAR; PG8_MMA(1, 0, At, B0); PG8_MMA(1, 1, At, B1); PG8_BAR; PG8_SCHED;
	s_add_i32 s57, 0, 0x18000
	v_add_u32_e32 v130, s57, v146
	s_add_i32 s58, 0, 0x1c000
	ds_read_b128 v[142:145], v130
	ds_read_b128 v[154:157], v130 offset:1024
	ds_read_b128 v[158:161], v130 offset:2048
	ds_read_b128 v[162:165], v130 offset:3072
	v_add_u32_e32 v130, s58, v146
	ds_read_b128 v[166:169], v130
	ds_read_b128 v[170:173], v130 offset:1024
	ds_read_b128 v[174:177], v130 offset:2048
	ds_read_b128 v[178:181], v130 offset:3072
	s_add_u32 s28, s36, 0xe0000
	s_addc_u32 s29, s37, 0
	s_mov_b32 m0, s40
	ds_read_b128 v[182:185], v152 offset:32768
	ds_read_b128 v[186:189], v152 offset:33792
	ds_read_b128 v[190:193], v152 offset:34816
	ds_read_b128 v[194:197], v152 offset:35840
	ds_read_b128 v[198:201], v152 offset:36864
	ds_read_b128 v[202:205], v152 offset:37888
	ds_read_b128 v[206:209], v152 offset:38912
	ds_read_b128 v[210:213], v152 offset:39936
	global_load_lds_dwordx4 v132, s[28:29]
	s_mov_b32 m0, s41
	s_nop 0
	global_load_lds_dwordx4 v134, s[28:29]
	s_waitcnt vmcnt(8)
	s_waitcnt lgkmcnt(0)
	s_barrier
	s_setprio 3
	s_waitcnt lgkmcnt(0)
	v_mfma_f32_16x16x32_bf16 v[126:129], v[142:145], v[182:185], v[126:129]
	v_mfma_f32_16x16x32_bf16 v[122:125], v[158:161], v[182:185], v[122:125]
	v_mfma_f32_16x16x32_bf16 v[110:113], v[142:145], v[190:193], v[110:113]
	v_mfma_f32_16x16x32_bf16 v[106:109], v[158:161], v[190:193], v[106:109]
	v_mfma_f32_16x16x32_bf16 v[94:97], v[142:145], v[198:201], v[94:97]
	v_mfma_f32_16x16x32_bf16 v[90:93], v[158:161], v[198:201], v[90:93]
	v_mfma_f32_16x16x32_bf16 v[78:81], v[142:145], v[206:209], v[78:81]
	v_mfma_f32_16x16x32_bf16 v[74:77], v[158:161], v[206:209], v[74:77]
	v_mfma_f32_16x16x32_bf16 v[126:129], v[154:157], v[186:189], v[126:129]
	v_mfma_f32_16x16x32_bf16 v[122:125], v[162:165], v[186:189], v[122:125]
	v_mfma_f32_16x16x32_bf16 v[110:113], v[154:157], v[194:197], v[110:113]
	v_mfma_f32_16x16x32_bf16 v[106:109], v[162:165], v[194:197], v[106:109]
	v_mfma_f32_16x16x32_bf16 v[94:97], v[154:157], v[202:205], v[94:97]
	v_mfma_f32_16x16x32_bf16 v[90:93], v[162:165], v[202:205], v[90:93]
	v_mfma_f32_16x16x32_bf16 v[78:81], v[154:157], v[210:213], v[78:81]
	v_mfma_f32_16x16x32_bf16 v[74:77], v[162:165], v[210:213], v[74:77]
	s_setprio 0
	s_setprio 3
	v_mfma_f32_16x16x32_bf16 v[118:121], v[166:169], v[182:185], v[118:121]
	v_mfma_f32_16x16x32_bf16 v[114:117], v[174:177], v[182:185], v[114:117]
	v_mfma_f32_16x16x32_bf16 v[102:105], v[166:169], v[190:193], v[102:105]
	v_mfma_f32_16x16x32_bf16 v[98:101], v[174:177], v[190:193], v[98:101]
	v_mfma_f32_16x16x32_bf16 v[86:89], v[166:169], v[198:201], v[86:89]
	v_mfma_f32_16x16x32_bf16 v[82:85], v[174:177], v[198:201], v[82:85]
	v_mfma_f32_16x16x32_bf16 v[70:73], v[166:169], v[206:209], v[70:73]
	v_mfma_f32_16x16x32_bf16 v[66:69], v[174:177], v[206:209], v[66:69]
	v_mfma_f32_16x16x32_bf16 v[118:121], v[170:173], v[186:189], v[118:121]
	v_mfma_f32_16x16x32_bf16 v[114:117], v[178:181], v[186:189], v[114:117]
	v_mfma_f32_16x16x32_bf16 v[102:105], v[170:173], v[194:197], v[102:105]
	v_mfma_f32_16x16x32_bf16 v[98:101], v[178:181], v[194:197], v[98:101]
	v_mfma_f32_16x16x32_bf16 v[86:89], v[170:173], v[202:205], v[86:89]
	v_mfma_f32_16x16x32_bf16 v[82:85], v[178:181], v[202:205], v[82:85]
	v_mfma_f32_16x16x32_bf16 v[70:73], v[170:173], v[210:213], v[70:73]
	v_mfma_f32_16x16x32_bf16 v[66:69], v[178:181], v[210:213], v[66:69]
	s_setprio 0
	s_barrier
	s_add_i32 s28, s57, s3
	s_add_i32 m0, s28, 0xffffff80
	ds_read_b128 v[182:185], v152 offset:49152
	ds_read_b128 v[186:189], v152 offset:50176
	ds_read_b128 v[190:193], v152 offset:51200
	ds_read_b128 v[194:197], v152 offset:52224
	ds_read_b128 v[198:201], v152 offset:53248
	ds_read_b128 v[202:205], v152 offset:54272
	ds_read_b128 v[206:209], v152 offset:55296
	ds_read_b128 v[210:213], v152 offset:56320
	global_load_lds_dwordx4 v132, s[34:35] offset:128
	s_add_i32 m0, s28, 0x1f80
	s_add_u32 s28, s34, 0xe0080
	s_addc_u32 s29, s35, 0
	s_add_i32 s34, s58, s3
	global_load_lds_dwordx4 v134, s[98:99] offset:128
	s_mov_b32 m0, s34
	s_nop 0
	global_load_lds_dwordx4 v132, s[28:29]
	s_add_i32 m0, s34, 0x2000
	s_nop 0
	global_load_lds_dwordx4 v134, s[28:29]
	s_add_i32 m0, s46, 0xffffff80
	s_nop 0
	global_load_lds_dwordx4 v132, s[36:37] offset:128
	s_add_i32 m0, s47, 0xffffff80
	s_nop 0
	global_load_lds_dwordx4 v134, s[36:37] offset:128
	s_waitcnt vmcnt(8)
	s_waitcnt lgkmcnt(0)
	s_barrier
	s_setprio 3
	s_waitcnt lgkmcnt(0)
	v_mfma_f32_16x16x32_bf16 v[62:65], v[142:145], v[182:185], v[62:65]
	v_mfma_f32_16x16x32_bf16 v[58:61], v[158:161], v[182:185], v[58:61]
	v_mfma_f32_16x16x32_bf16 v[46:49], v[142:145], v[190:193], v[46:49]
	v_mfma_f32_16x16x32_bf16 v[42:45], v[158:161], v[190:193], v[42:45]
	v_mfma_f32_16x16x32_bf16 v[30:33], v[142:145], v[198:201], v[30:33]
	v_mfma_f32_16x16x32_bf16 v[26:29], v[158:161], v[198:201], v[26:29]
	v_mfma_f32_16x16x32_bf16 v[14:17], v[142:145], v[206:209], v[14:17]
	v_mfma_f32_16x16x32_bf16 v[10:13], v[158:161], v[206:209], v[10:13]
	v_mfma_f32_16x16x32_bf16 v[62:65], v[154:157], v[186:189], v[62:65]
	v_mfma_f32_16x16x32_bf16 v[58:61], v[162:165], v[186:189], v[58:61]
	v_mfma_f32_16x16x32_bf16 v[46:49], v[154:157], v[194:197], v[46:49]
	v_mfma_f32_16x16x32_bf16 v[42:45], v[162:165], v[194:197], v[42:45]
	v_mfma_f32_16x16x32_bf16 v[30:33], v[154:157], v[202:205], v[30:33]
	v_mfma_f32_16x16x32_bf16 v[26:29], v[162:165], v[202:205], v[26:29]
	v_mfma_f32_16x16x32_bf16 v[14:17], v[154:157], v[210:213], v[14:17]
	v_mfma_f32_16x16x32_bf16 v[10:13], v[162:165], v[210:213], v[10:13]
	s_setprio 0
	s_setprio 3
	v_mfma_f32_16x16x32_bf16 v[54:57], v[166:169], v[182:185], v[54:57]
	v_mfma_f32_16x16x32_bf16 v[50:53], v[174:177], v[182:185], v[50:53]
	v_mfma_f32_16x16x32_bf16 v[38:41], v[166:169], v[190:193], v[38:41]
	v_mfma_f32_16x16x32_bf16 v[34:37], v[174:177], v[190:193], v[34:37]
	v_mfma_f32_16x16x32_bf16 v[22:25], v[166:169], v[198:201], v[22:25]
	v_mfma_f32_16x16x32_bf16 v[18:21], v[174:177], v[198:201], v[18:21]
	v_mfma_f32_16x16x32_bf16 v[6:9], v[166:169], v[206:209], v[6:9]
	v_mfma_f32_16x16x32_bf16 v[2:5], v[174:177], v[206:209], v[2:5]
	v_mfma_f32_16x16x32_bf16 v[54:57], v[170:173], v[186:189], v[54:57]
	v_mfma_f32_16x16x32_bf16 v[50:53], v[178:181], v[186:189], v[50:53]
	v_mfma_f32_16x16x32_bf16 v[38:41], v[170:173], v[194:197], v[38:41]
	v_mfma_f32_16x16x32_bf16 v[34:37], v[178:181], v[194:197], v[34:37]
	v_mfma_f32_16x16x32_bf16 v[22:25], v[170:173], v[202:205], v[22:25]
	v_mfma_f32_16x16x32_bf16 v[18:21], v[178:181], v[202:205], v[18:21]
	v_mfma_f32_16x16x32_bf16 v[6:9], v[170:173], v[210:213], v[6:9]
	v_mfma_f32_16x16x32_bf16 v[2:5], v[178:181], v[210:213], v[2:5]
	s_setprio 0
	s_barrier
	s_add_i32 s56, s56, 2
	s_add_u32 s54, s54, 0x100
	s_addc_u32 s55, s55, 0
	s_cmp_gt_u32 s56, 11
	s_mov_b64 s[28:29], s[30:31]
; #define PG8_STAGE_A(b, h, ptr, NX) do { if constexpr (Sched::GATHER) { unsigned gs_[2]; gs_[0] = ((NX) && last_) ? gN[h][0] : gA[h][0]; gs_[1] = ((NX) && last_) ? gN[h][1] : gA[h][1]; PG8_STAGE(PG8_SA(b, h), ptr, gs_); } \
;         else PG8_STAGE(PG8_SA(b, h), (ptr) + ((h) ? hstep : (size_t)0), voffA); } while (0)
; #define PG8_STAGE(bufoff, gbase, voff) do { _Pragma("unroll") for (int _i = 0; _i < 2; ++_i) \
;         __builtin_amdgcn_global_load_lds((const unsigned*)((const char*)(gbase) + (voff)[_i]), (PG8_LAS unsigned*)(lds + (bufoff) + ldsw + _i * 8192), 16, 0, 0); } while (0)
; #define PG8_LDA(dst, b, h) do { _Pragma("unroll") for (int m = 0; m < 4; ++m) _Pragma("unroll") for (int k = 0; k < 2; ++k) dst[m][k] = *(const PG8_LAS bf16x8*)(lds + PG8_SA(b, h) + aoff + m * 2048 + k * 1024); } while (0)
; #define PG8_LDB(dst, b, h) do { _Pragma("unroll") for (int n = 0; n < 2; ++n) _Pragma("unroll") for (int k = 0; k < 2; ++k) dst[n][k] = *(const PG8_LAS bf16x8*)(lds + PG8_SB(b, h) + boff + n * 2048 + k * 1024); } while (0)
; #define PG8_WAIT_V(n) asm volatile("s_waitcnt vmcnt(" #n ")" ::: "memory")
; #define PG8_WAIT_L(n) asm volatile("s_waitcnt lgkmcnt(" #n ")" ::: "memory")
; template <class Epi, class Sched, bool ALIGN_EPI = false, bool SP2 = false>
; __device__ __forceinline__ void gemm_phase(PG8_LAS unsigned char* lds, const Gemm g, const Sched& S, const Epi& E, const bool skip_epi = false) {
;     ...
;         for (int t = 0; t < nt; t += 2) {
;             const bool last = (t == nt - 2); last_ = last && has_next;
;             const char* a1 = cA + (size_t)(t + 1) * kstep;
;             const char* a2 = last ? nA : cA + (size_t)(t + 2) * kstep; const char* b2 = last ? nB : cB + (size_t)(t + 2) * kstep;
;             const char* a3 = a2 + kstep; const char* b3 = b2 + kstep;
;             if (last && has_next) S.a_ready(nxt);
;             if constexpr (SP2) {
;             PG8_LDB(B0, 0, 0); PG8_LDB(B1, 0, 1); PG8_SCHED; PG8_LDA(At, 0, 0); PG8_STAGE_A(1, 1, a1, false);
;             PG8_WAIT_V(8); PG8_WAIT_L(0); PG8_BAR; PG8_MMA(0, 0, At, B0); PG8_MMA(0, 1, At, B1); PG8_BAR; PG8_SCHED;
;             PG8_LDA(At, 0, 1); PG8_STAGE(PG8_SB(0, 0), b2, voffB); PG8_STAGE(PG8_SB(0, 1), b2 + hstep, voffB); PG8_STAGE_A(0, 0, a2, true);
;             PG8_WAIT_V(8); PG8_WAIT_L(0); PG8_BAR; PG8_MMA(1, 0, At, B0); PG8_MMA(1, 1, At, B1); PG8_BAR; PG8_SCHED;
.LBB0_1844:
	ds_read_b128 v[142:145], v150
	ds_read_b128 v[154:157], v150 offset:1024
	ds_read_b128 v[158:161], v150 offset:2048
	ds_read_b128 v[162:165], v150 offset:3072
	ds_read_b128 v[166:169], v151
	ds_read_b128 v[170:173], v151 offset:1024
	ds_read_b128 v[174:177], v151 offset:2048
	ds_read_b128 v[178:181], v151 offset:3072
	s_add_u32 s30, s28, 0x100
	s_addc_u32 s31, s29, 0
	s_cmp_eq_u32 s56, 10
	s_cselect_b32 s37, s7, s31
	s_cselect_b32 s36, s6, s30
	s_cselect_b32 s35, s25, s55
	s_cselect_b32 s34, s24, s54
	v_lshl_add_u64 v[214:215], s[28:29], 0, v[136:137]
	s_add_i32 m0, s38, 0xc000
	ds_read_b128 v[182:185], v152
	ds_read_b128 v[186:189], v152 offset:1024
	ds_read_b128 v[190:193], v152 offset:2048
	ds_read_b128 v[194:197], v152 offset:3072
	ds_read_b128 v[198:201], v152 offset:4096
	ds_read_b128 v[202:205], v152 offset:5120
	ds_read_b128 v[206:209], v152 offset:6144
	ds_read_b128 v[210:213], v152 offset:7168
	global_load_lds_dwordx4 v[214:215], off
	v_lshl_add_u64 v[214:215], s[28:29], 0, v[138:139]
	s_add_i32 m0, s38, 0xe000
	s_nop 0
	global_load_lds_dwordx4 v[214:215], off
	s_waitcnt vmcnt(8)
	s_waitcnt lgkmcnt(0)
	s_barrier
	s_setprio 3
	s_waitcnt lgkmcnt(0)
	v_mfma_f32_16x16x32_bf16 v[126:129], v[142:145], v[182:185], v[126:129]
	v_mfma_f32_16x16x32_bf16 v[122:125], v[158:161], v[182:185], v[122:125]
	v_mfma_f32_16x16x32_bf16 v[110:113], v[142:145], v[190:193], v[110:113]
	v_mfma_f32_16x16x32_bf16 v[106:109], v[158:161], v[190:193], v[106:109]
	v_mfma_f32_16x16x32_bf16 v[94:97], v[142:145], v[198:201], v[94:97]
	v_mfma_f32_16x16x32_bf16 v[90:93], v[158:161], v[198:201], v[90:93]
	v_mfma_f32_16x16x32_bf16 v[78:81], v[142:145], v[206:209], v[78:81]
	v_mfma_f32_16x16x32_bf16 v[74:77], v[158:161], v[206:209], v[74:77]
	v_mfma_f32_16x16x32_bf16 v[126:129], v[154:157], v[186:189], v[126:129]
	v_mfma_f32_16x16x32_bf16 v[122:125], v[162:165], v[186:189], v[122:125]
	v_mfma_f32_16x16x32_bf16 v[110:113], v[154:157], v[194:197], v[110:113]
	v_mfma_f32_16x16x32_bf16 v[106:109], v[162:165], v[194:197], v[106:109]
	v_mfma_f32_16x16x32_bf16 v[94:97], v[154:157], v[202:205], v[94:97]
	v_mfma_f32_16x16x32_bf16 v[90:93], v[162:165], v[202:205], v[90:93]
	v_mfma_f32_16x16x32_bf16 v[78:81], v[154:157], v[210:213], v[78:81]
	v_mfma_f32_16x16x32_bf16 v[74:77], v[162:165], v[210:213], v[74:77]
	s_setprio 0
	s_setprio 3
	v_mfma_f32_16x16x32_bf16 v[118:121], v[166:169], v[182:185], v[118:121]
	v_mfma_f32_16x16x32_bf16 v[114:117], v[174:177], v[182:185], v[114:117]
	v_mfma_f32_16x16x32_bf16 v[102:105], v[166:169], v[190:193], v[102:105]
	v_mfma_f32_16x16x32_bf16 v[98:101], v[174:177], v[190:193], v[98:101]
	v_mfma_f32_16x16x32_bf16 v[86:89], v[166:169], v[198:201], v[86:89]
	v_mfma_f32_16x16x32_bf16 v[82:85], v[174:177], v[198:201], v[82:85]
	v_mfma_f32_16x16x32_bf16 v[70:73], v[166:169], v[206:209], v[70:73]
	v_mfma_f32_16x16x32_bf16 v[66:69], v[174:177], v[206:209], v[66:69]
	v_mfma_f32_16x16x32_bf16 v[118:121], v[170:173], v[186:189], v[118:121]
	v_mfma_f32_16x16x32_bf16 v[114:117], v[178:181], v[186:189], v[114:117]
	v_mfma_f32_16x16x32_bf16 v[102:105], v[170:173], v[194:197], v[102:105]
	v_mfma_f32_16x16x32_bf16 v[98:101], v[178:181], v[194:197], v[98:101]
	v_mfma_f32_16x16x32_bf16 v[86:89], v[170:173], v[202:205], v[86:89]
	v_mfma_f32_16x16x32_bf16 v[82:85], v[178:181], v[202:205], v[82:85]
	v_mfma_f32_16x16x32_bf16 v[70:73], v[170:173], v[210:213], v[70:73]
	v_mfma_f32_16x16x32_bf16 v[66:69], v[178:181], v[210:213], v[66:69]
	s_setprio 0
	s_barrier
	s_add_i32 s28, s50, s3
	s_mov_b64 s[98:99], s[34:35]
	s_mov_b32 m0, s28
	ds_read_b128 v[182:185], v152 offset:16384
	ds_read_b128 v[186:189], v152 offset:17408
	ds_read_b128 v[190:193], v152 offset:18432
	ds_read_b128 v[194:197], v152 offset:19456
	ds_read_b128 v[198:201], v152 offset:20480
	ds_read_b128 v[202:205], v152 offset:21504
	ds_read_b128 v[206:209], v152 offset:22528
	ds_read_b128 v[210:213], v152 offset:23552
	global_load_lds_dwordx4 v132, s[34:35]
	s_add_i32 m0, s28, 0x2000
	s_add_u32 s28, s34, 0xe0000
	s_addc_u32 s29, s35, 0
	s_add_i32 s57, s51, s3
	global_load_lds_dwordx4 v134, s[34:35]
	s_mov_b32 m0, s57
	s_nop 0
	global_load_lds_dwordx4 v132, s[28:29]
	s_add_i32 m0, s57, 0x2000
	s_nop 0
	global_load_lds_dwordx4 v134, s[28:29]
	s_mov_b32 m0, s38
	s_nop 0
	global_load_lds_dwordx4 v132, s[36:37]
	s_mov_b32 m0, s39
	s_nop 0
	global_load_lds_dwordx4 v134, s[36:37]
	s_waitcnt vmcnt(8)
	s_waitcnt lgkmcnt(0)
	s_barrier
	s_setprio 3
	s_waitcnt lgkmcnt(0)
	v_mfma_f32_16x16x32_bf16 v[62:65], v[142:145], v[182:185], v[62:65]
	v_mfma_f32_16x16x32_bf16 v[58:61], v[158:161], v[182:185], v[58:61]
	v_mfma_f32_16x16x32_bf16 v[46:49], v[142:145], v[190:193], v[46:49]
	v_mfma_f32_16x16x32_bf16 v[42:45], v[158:161], v[190:193], v[42:45]
	v_mfma_f32_16x16x32_bf16 v[30:33], v[142:145], v[198:201], v[30:33]
	v_mfma_f32_16x16x32_bf16 v[26:29], v[158:161], v[198:201], v[26:29]
	v_mfma_f32_16x16x32_bf16 v[14:17], v[142:145], v[206:209], v[14:17]
	v_mfma_f32_16x16x32_bf16 v[10:13], v[158:161], v[206:209], v[10:13]
	v_mfma_f32_16x16x32_bf16 v[62:65], v[154:157], v[186:189], v[62:65]
	v_mfma_f32_16x16x32_bf16 v[58:61], v[162:165], v[186:189], v[58:61]
	v_mfma_f32_16x16x32_bf16 v[46:49], v[154:157], v[194:197], v[46:49]
	v_mfma_f32_16x16x32_bf16 v[42:45], v[162:165], v[194:197], v[42:45]
	v_mfma_f32_16x16x32_bf16 v[30:33], v[154:157], v[202:205], v[30:33]
	v_mfma_f32_16x16x32_bf16 v[26:29], v[162:165], v[202:205], v[26:29]
	v_mfma_f32_16x16x32_bf16 v[14:17], v[154:157], v[210:213], v[14:17]
	v_mfma_f32_16x16x32_bf16 v[10:13], v[162:165], v[210:213], v[10:13]
	s_setprio 0
	s_setprio 3
	v_mfma_f32_16x16x32_bf16 v[54:57], v[166:169], v[182:185], v[54:57]
	v_mfma_f32_16x16x32_bf16 v[50:53], v[174:177], v[182:185], v[50:53]
	v_mfma_f32_16x16x32_bf16 v[38:41], v[166:169], v[190:193], v[38:41]
	v_mfma_f32_16x16x32_bf16 v[34:37], v[174:177], v[190:193], v[34:37]
	v_mfma_f32_16x16x32_bf16 v[22:25], v[166:169], v[198:201], v[22:25]
	v_mfma_f32_16x16x32_bf16 v[18:21], v[174:177], v[198:201], v[18:21]
	v_mfma_f32_16x16x32_bf16 v[6:9], v[166:169], v[206:209], v[6:9]
	v_mfma_f32_16x16x32_bf16 v[2:5], v[174:177], v[206:209], v[2:5]
	v_mfma_f32_16x16x32_bf16 v[54:57], v[170:173], v[186:189], v[54:57]
	v_mfma_f32_16x16x32_bf16 v[50:53], v[178:181], v[186:189], v[50:53]
	v_mfma_f32_16x16x32_bf16 v[38:41], v[170:173], v[194:197], v[38:41]
	v_mfma_f32_16x16x32_bf16 v[34:37], v[178:181], v[194:197], v[34:37]
	v_mfma_f32_16x16x32_bf16 v[22:25], v[170:173], v[202:205], v[22:25]
	v_mfma_f32_16x16x32_bf16 v[18:21], v[178:181], v[202:205], v[18:21]
	v_mfma_f32_16x16x32_bf16 v[6:9], v[170:173], v[210:213], v[6:9]
	v_mfma_f32_16x16x32_bf16 v[2:5], v[178:181], v[210:213], v[2:5]
	s_setprio 0
	s_barrier
; #define PG8_STAGE_A(b, h, ptr, NX) do { if constexpr (Sched::GATHER) { unsigned gs_[2]; gs_[0] = ((NX) && last_) ? gN[h][0] : gA[h][0]; gs_[1] = ((NX) && last_) ? gN[h][1] : gA[h][1]; PG8_STAGE(PG8_SA(b, h), ptr, gs_); } \
;         else PG8_STAGE(PG8_SA(b, h), (ptr) + ((h) ? hstep : (size_t)0), voffA); } while (0)
; #define PG8_STAGE(bufoff, gbase, voff) do { _Pragma("unroll") for (int _i = 0; _i < 2; ++_i) \
;         __builtin_amdgcn_global_load_lds((const unsigned*)((const char*)(gbase) + (voff)[_i]), (PG8_LAS unsigned*)(lds + (bufoff) + ldsw + _i * 8192), 16, 0, 0); } while (0)
; #define PG8_LDA(dst, b, h) do { _Pragma("unroll") for (int m = 0; m < 4; ++m) _Pragma("unroll") for (int k = 0; k < 2; ++k) dst[m][k] = *(const PG8_LAS bf16x8*)(lds + PG8_SA(b, h) + aoff + m * 2048 + k * 1024); } while (0)
; #define PG8_LDB(dst, b, h) do { _Pragma("unroll") for (int n = 0; n < 2; ++n) _Pragma("unroll") for (int k = 0; k < 2; ++k) dst[n][k] = *(const PG8_LAS bf16x8*)(lds + PG8_SB(b, h) + boff + n * 2048 + k * 1024); } while (0)
; #define PG8_MMA(ai, bj, At, Bt) do { __builtin_amdgcn_s_setprio(1); _Pragma("unroll") for (int m = 0; m < 4; ++m) _Pragma("unroll") for (int n = 0; n < 2; ++n) _Pragma("unroll") for (int k = 0; k < 2; ++k) \
;         acc[ai][bj][m][n] = __builtin_amdgcn_mfma_f32_16x16x32_bf16(Bt[n][k], At[m][k], acc[ai][bj][m][n], 0, 0, 0); __builtin_amdgcn_s_setprio(0); } while (0)
; #define PG8_WAIT_V(n) asm volatile("s_waitcnt vmcnt(" #n ")" ::: "memory")
; #define PG8_WAIT_L(n) asm volatile("s_waitcnt lgkmcnt(" #n ")" ::: "memory")
; #define PG8_BAR __builtin_amdgcn_s_barrier()
; #define PG8_SCHED __builtin_amdgcn_sched_barrier(0)
; template <class Epi, class Sched, bool ALIGN_EPI = false, bool SP2 = false>
; __device__ __forceinline__ void gemm_phase(PG8_LAS unsigned char* lds, const Gemm g, const Sched& S, const Epi& E, const bool skip_epi = false) {
;     ...
;             PG8_LDB(B0, 1, 0); PG8_LDB(B1, 1, 1); PG8_SCHED; PG8_LDA(At, 1, 0); PG8_STAGE_A(0, 1, a2, true);
;             PG8_WAIT_V(8); PG8_WAIT_L(0); PG8_BAR; PG8_MMA(0, 0, At, B0); PG8_MMA(0, 1, At, B1); PG8_BAR; PG8_SCHED;
;             PG8_LDA(At, 1, 1); PG8_STAGE(PG8_SB(1, 0), b3, voffB); PG8_STAGE(PG8_SB(1, 1), b3 + hstep, voffB); PG8_STAGE_A(1, 0, a3, true);
;             PG8_WAIT_V(8); PG8_WAIT_L(0); PG8_BAR; PG8_MMA(1, 0, At, B0); PG8_MMA(1, 1, At, B1); PG8_BAR; PG8_SCHED;
	s_add_i32 s57, 0, 0x18000
	v_add_u32_e32 v130, s57, v146
	s_add_i32 s58, 0, 0x1c000
	ds_read_b128 v[142:145], v130
	ds_read_b128 v[154:157], v130 offset:1024
	ds_read_b128 v[158:161], v130 offset:2048
	ds_read_b128 v[162:165], v130 offset:3072
	v_add_u32_e32 v130, s58, v146
	ds_read_b128 v[166:169], v130
	ds_read_b128 v[170:173], v130 offset:1024
	ds_read_b128 v[174:177], v130 offset:2048
	ds_read_b128 v[178:181], v130 offset:3072
	s_add_u32 s28, s36, 0xe0000
	s_addc_u32 s29, s37, 0
	s_mov_b32 m0, s40
	ds_read_b128 v[182:185], v152 offset:32768
	ds_read_b128 v[186:189], v152 offset:33792
	ds_read_b128 v[190:193], v152 offset:34816
	ds_read_b128 v[194:197], v152 offset:35840
	ds_read_b128 v[198:201], v152 offset:36864
	ds_read_b128 v[202:205], v152 offset:37888
	ds_read_b128 v[206:209], v152 offset:38912
	ds_read_b128 v[210:213], v152 offset:39936
	global_load_lds_dwordx4 v132, s[28:29]
	s_mov_b32 m0, s41
	s_nop 0
	global_load_lds_dwordx4 v134, s[28:29]
	s_waitcnt vmcnt(8)
	s_waitcnt lgkmcnt(0)
	s_barrier
	s_setprio 3
	s_waitcnt lgkmcnt(0)
	v_mfma_f32_16x16x32_bf16 v[126:129], v[142:145], v[182:185], v[126:129]
	v_mfma_f32_16x16x32_bf16 v[122:125], v[158:161], v[182:185], v[122:125]
	v_mfma_f32_16x16x32_bf16 v[110:113], v[142:145], v[190:193], v[110:113]
	v_mfma_f32_16x16x32_bf16 v[106:109], v[158:161], v[190:193], v[106:109]
	v_mfma_f32_16x16x32_bf16 v[94:97], v[142:145], v[198:201], v[94:97]
	v_mfma_f32_16x16x32_bf16 v[90:93], v[158:161], v[198:201], v[90:93]
	v_mfma_f32_16x16x32_bf16 v[78:81], v[142:145], v[206:209], v[78:81]
	v_mfma_f32_16x16x32_bf16 v[74:77], v[158:161], v[206:209], v[74:77]
	v_mfma_f32_16x16x32_bf16 v[126:129], v[154:157], v[186:189], v[126:129]
	v_mfma_f32_16x16x32_bf16 v[122:125], v[162:165], v[186:189], v[122:125]
	v_mfma_f32_16x16x32_bf16 v[110:113], v[154:157], v[194:197], v[110:113]
	v_mfma_f32_16x16x32_bf16 v[106:109], v[162:165], v[194:197], v[106:109]
	v_mfma_f32_16x16x32_bf16 v[94:97], v[154:157], v[202:205], v[94:97]
	v_mfma_f32_16x16x32_bf16 v[90:93], v[162:165], v[202:205], v[90:93]
	v_mfma_f32_16x16x32_bf16 v[78:81], v[154:157], v[210:213], v[78:81]
	v_mfma_f32_16x16x32_bf16 v[74:77], v[162:165], v[210:213], v[74:77]
	s_setprio 0
	s_setprio 3
	v_mfma_f32_16x16x32_bf16 v[118:121], v[166:169], v[182:185], v[118:121]
	v_mfma_f32_16x16x32_bf16 v[114:117], v[174:177], v[182:185], v[114:117]
	v_mfma_f32_16x16x32_bf16 v[102:105], v[166:169], v[190:193], v[102:105]
	v_mfma_f32_16x16x32_bf16 v[98:101], v[174:177], v[190:193], v[98:101]
	v_mfma_f32_16x16x32_bf16 v[86:89], v[166:169], v[198:201], v[86:89]
	v_mfma_f32_16x16x32_bf16 v[82:85], v[174:177], v[198:201], v[82:85]
	v_mfma_f32_16x16x32_bf16 v[70:73], v[166:169], v[206:209], v[70:73]
	v_mfma_f32_16x16x32_bf16 v[66:69], v[174:177], v[206:209], v[66:69]
	v_mfma_f32_16x16x32_bf16 v[118:121], v[170:173], v[186:189], v[118:121]
	v_mfma_f32_16x16x32_bf16 v[114:117], v[178:181], v[186:189], v[114:117]
	v_mfma_f32_16x16x32_bf16 v[102:105], v[170:173], v[194:197], v[102:105]
	v_mfma_f32_16x16x32_bf16 v[98:101], v[178:181], v[194:197], v[98:101]
	v_mfma_f32_16x16x32_bf16 v[86:89], v[170:173], v[202:205], v[86:89]
	v_mfma_f32_16x16x32_bf16 v[82:85], v[178:181], v[202:205], v[82:85]
	v_mfma_f32_16x16x32_bf16 v[70:73], v[170:173], v[210:213], v[70:73]
	v_mfma_f32_16x16x32_bf16 v[66:69], v[178:181], v[210:213], v[66:69]
	s_setprio 0
	s_barrier
	s_add_i32 s28, s57, s3
	s_add_i32 m0, s28, 0xffffff80
	ds_read_b128 v[182:185], v152 offset:49152
	ds_read_b128 v[186:189], v152 offset:50176
	ds_read_b128 v[190:193], v152 offset:51200
	ds_read_b128 v[194:197], v152 offset:52224
	ds_read_b128 v[198:201], v152 offset:53248
	ds_read_b128 v[202:205], v152 offset:54272
	ds_read_b128 v[206:209], v152 offset:55296
	ds_read_b128 v[210:213], v152 offset:56320
	global_load_lds_dwordx4 v132, s[34:35] offset:128
	s_add_i32 m0, s28, 0x1f80
	s_add_u32 s28, s34, 0xe0080
	s_addc_u32 s29, s35, 0
	s_add_i32 s34, s58, s3
	global_load_lds_dwordx4 v134, s[98:99] offset:128
	s_mov_b32 m0, s34
	s_nop 0
	global_load_lds_dwordx4 v132, s[28:29]
	s_add_i32 m0, s34, 0x2000
	s_nop 0
	global_load_lds_dwordx4 v134, s[28:29]
	s_add_i32 m0, s46, 0xffffff80
	s_nop 0
	global_load_lds_dwordx4 v132, s[36:37] offset:128
	s_add_i32 m0, s47, 0xffffff80
	s_nop 0
	global_load_lds_dwordx4 v134, s[36:37] offset:128
	s_waitcnt vmcnt(8)
	s_waitcnt lgkmcnt(0)
	s_barrier
	s_setprio 3
	s_waitcnt lgkmcnt(0)
	v_mfma_f32_16x16x32_bf16 v[62:65], v[142:145], v[182:185], v[62:65]
	v_mfma_f32_16x16x32_bf16 v[58:61], v[158:161], v[182:185], v[58:61]
	v_mfma_f32_16x16x32_bf16 v[46:49], v[142:145], v[190:193], v[46:49]
	v_mfma_f32_16x16x32_bf16 v[42:45], v[158:161], v[190:193], v[42:45]
	v_mfma_f32_16x16x32_bf16 v[30:33], v[142:145], v[198:201], v[30:33]
	v_mfma_f32_16x16x32_bf16 v[26:29], v[158:161], v[198:201], v[26:29]
	v_mfma_f32_16x16x32_bf16 v[14:17], v[142:145], v[206:209], v[14:17]
	v_mfma_f32_16x16x32_bf16 v[10:13], v[158:161], v[206:209], v[10:13]
	v_mfma_f32_16x16x32_bf16 v[62:65], v[154:157], v[186:189], v[62:65]
	v_mfma_f32_16x16x32_bf16 v[58:61], v[162:165], v[186:189], v[58:61]
	v_mfma_f32_16x16x32_bf16 v[46:49], v[154:157], v[194:197], v[46:49]
	v_mfma_f32_16x16x32_bf16 v[42:45], v[162:165], v[194:197], v[42:45]
	v_mfma_f32_16x16x32_bf16 v[30:33], v[154:157], v[202:205], v[30:33]
	v_mfma_f32_16x16x32_bf16 v[26:29], v[162:165], v[202:205], v[26:29]
	v_mfma_f32_16x16x32_bf16 v[14:17], v[154:157], v[210:213], v[14:17]
	v_mfma_f32_16x16x32_bf16 v[10:13], v[162:165], v[210:213], v[10:13]
	s_setprio 0
	s_setprio 3
	v_mfma_f32_16x16x32_bf16 v[54:57], v[166:169], v[182:185], v[54:57]
	v_mfma_f32_16x16x32_bf16 v[50:53], v[174:177], v[182:185], v[50:53]
	v_mfma_f32_16x16x32_bf16 v[38:41], v[166:169], v[190:193], v[38:41]
	v_mfma_f32_16x16x32_bf16 v[34:37], v[174:177], v[190:193], v[34:37]
	v_mfma_f32_16x16x32_bf16 v[22:25], v[166:169], v[198:201], v[22:25]
	v_mfma_f32_16x16x32_bf16 v[18:21], v[174:177], v[198:201], v[18:21]
	v_mfma_f32_16x16x32_bf16 v[6:9], v[166:169], v[206:209], v[6:9]
	v_mfma_f32_16x16x32_bf16 v[2:5], v[174:177], v[206:209], v[2:5]
	v_mfma_f32_16x16x32_bf16 v[54:57], v[170:173], v[186:189], v[54:57]
	v_mfma_f32_16x16x32_bf16 v[50:53], v[178:181], v[186:189], v[50:53]
	v_mfma_f32_16x16x32_bf16 v[38:41], v[170:173], v[194:197], v[38:41]
	v_mfma_f32_16x16x32_bf16 v[34:37], v[178:181], v[194:197], v[34:37]
	v_mfma_f32_16x16x32_bf16 v[22:25], v[170:173], v[202:205], v[22:25]
	v_mfma_f32_16x16x32_bf16 v[18:21], v[178:181], v[202:205], v[18:21]
	v_mfma_f32_16x16x32_bf16 v[6:9], v[170:173], v[210:213], v[6:9]
	v_mfma_f32_16x16x32_bf16 v[2:5], v[178:181], v[210:213], v[2:5]
	s_setprio 0
	s_barrier
	s_add_i32 s56, s56, 2
	s_add_u32 s54, s54, 0x100
	s_addc_u32 s55, s55, 0
	s_cmp_gt_u32 s56, 11
	s_mov_b64 s[28:29], s[30:31]
	s_cbranch_scc0 .LBB0_1844
	s_and_b64 vcc, exec, s[20:21]
	s_cbranch_vccz .LBB0_1847
	s_barrier
